# non-temporal (nt) cache hints on read-once streaming loads: expert f32 weight conversion loads+stores, gather-LayerNorm row loads + f32 output stores, LayerNorm residual/delta loads, x/mem f32 input l
# speedup vs baseline: 1.0158x; 1.0158x over previous
.LBB0_219:
	v_lshl_add_u64 v[12:13], s[40:41], 0, v[24:25]
	global_load_dwordx4 v[12:15], v[12:13], off nt
	s_mov_b64 s[58:59], s[54:55]
	s_mov_b64 s[56:57], s[52:53]
	s_mov_b64 s[54:55], s[50:51]
	s_mov_b64 s[52:53], s[48:49]
	s_mov_b64 s[48:49], s[44:45]
	v_lshl_add_u64 v[36:37], s[2:3], 0, v[34:35]
	s_mov_b64 s[46:47], s[42:43]
	s_mov_b64 s[44:45], s[40:41]
	v_cmp_gt_u64_e64 s[4:5], s[12:13], v[36:37]
	s_and_saveexec_b64 s[0:1], s[4:5]
	s_cbranch_execz .LBB0_221
	v_lshl_add_u64 v[0:1], s[44:45], 0, v[22:23]
	global_load_dwordx4 v[0:3], v[0:1], off nt
.LBB0_221:
	s_or_b64 exec, exec, s[0:1]
	v_lshl_add_u64 v[36:37], s[20:21], 0, v[34:35]
	v_cmp_gt_u64_e64 s[0:1], s[12:13], v[36:37]
	s_and_saveexec_b64 s[30:31], s[0:1]
	s_cbranch_execz .LBB0_223
	s_waitcnt lgkmcnt(0)
	v_lshl_add_u64 v[4:5], s[44:45], 0, v[26:27]
	global_load_dwordx4 v[4:7], v[4:5], off nt
.LBB0_223:
	s_or_b64 exec, exec, s[30:31]
	v_lshl_add_u64 v[36:37], s[24:25], 0, v[34:35]
	v_cmp_gt_u64_e32 vcc, s[12:13], v[36:37]
	s_and_saveexec_b64 s[30:31], vcc
	s_cbranch_execz .LBB0_225
	v_lshl_add_u64 v[8:9], s[44:45], 0, v[30:31]
	global_load_dwordx4 v[8:11], v[8:9], off nt

.LBB0_233:
	v_lshl_add_u64 v[16:17], v[16:17], 0, s[2:3]
	s_waitcnt lgkmcnt(0)
	global_load_dwordx4 v[4:7], v[2:3], off nt
	v_cmp_lt_u64_e32 vcc, s[12:13], v[16:17]
	v_lshl_add_u64 v[2:3], v[2:3], 0, s[8:9]
	s_or_b64 s[10:11], vcc, s[10:11]
	s_waitcnt vmcnt(0)
	v_cvt_pk_bf16_f32 v4, v4, v5
	v_cvt_pk_bf16_f32 v5, v6, v7
	global_store_dwordx2 v[0:1], v[4:5], off
	v_lshl_add_u64 v[0:1], v[0:1], 0, s[4:5]
	s_andn2_b64 exec, exec, s[10:11]
	s_cbranch_execnz .LBB0_233

.LBB0_601:
	s_add_i32 s29, s38, s23
	s_cmp_lt_i32 s29, 0x8000
	s_cselect_b64 s[2:3], -1, 0
	s_ashr_i32 s0, s23, 31
	s_lshr_b32 s0, s0, 25
	s_add_i32 s0, s23, s0
	s_ashr_i32 s6, s0, 7
	s_and_b32 s0, s0, 0xff80
	s_sub_i32 s0, s23, s0
	s_bfe_i32 s1, s0, 0x80000
	s_bfe_u32 s1, s1, 0x3000c
	s_add_i32 s1, s0, s1
	s_bfe_i32 s4, s1, 0x80000
	s_and_b32 s1, s1, 0xf8
	s_sub_i32 s0, s0, s1
	s_sext_i32_i8 s0, s0
	s_lshl_b32 s5, s0, 6
	s_lshl_b32 s0, s0, 5
	s_and_b32 s1, s5, 0xc0
	s_and_b32 s0, s0, 0xffffff80
	s_or_b32 s7, s0, s1
	s_add_i32 s0, s1, s0
	s_addk_i32 s0, 0x80
	s_cmpk_lt_u32 s1, 0x80
	s_cselect_b32 s0, s7, s0
	s_ashr_i32 s7, s6, 31
	s_lshl_b64 s[34:35], s[6:7], 21
	s_sext_i32_i16 s4, s4
	s_add_u32 s34, s8, s34
	s_addc_u32 s35, s9, s35
	s_lshl_b32 s1, s4, 3
	s_and_b32 s4, s1, 0xffffffc0
	v_add_u32_e32 v132, s4, v221
	v_ashrrev_i32_e32 v133, 31, v132
	v_lshlrev_b64 v[132:133], 11, v[132:133]
	s_ashr_i32 s1, s0, 31
	v_lshl_add_u64 v[132:133], s[34:35], 0, v[132:133]
	v_lshl_add_u64 v[132:133], s[0:1], 2, v[132:133]
	v_lshl_add_u64 v[180:181], v[132:133], 0, v[2:3]
	s_movk_i32 s0, 0x1000
	v_add_co_u32_e32 v148, vcc, s0, v180
	global_load_dwordx4 v[132:135], v[180:181], off nt
	global_load_dwordx4 v[136:139], v[180:181], off offset:2048 nt
	v_addc_co_u32_e32 v149, vcc, 0, v181, vcc
	v_add_co_u32_e32 v188, vcc, s83, v180
	s_cmpk_gt_i32 s29, 0x7fff
	s_nop 0
	v_addc_co_u32_e32 v189, vcc, 0, v181, vcc
	v_add_co_u32_e32 v152, vcc, 0x3000, v180
	global_load_dwordx4 v[140:143], v[188:189], off nt
	global_load_dwordx4 v[144:147], v[188:189], off offset:2048 nt
	v_addc_co_u32_e32 v153, vcc, 0, v181, vcc
	v_add_co_u32_e32 v164, vcc, s62, v180
	global_load_dwordx4 v[156:159], v[148:149], off offset:2048 nt
	s_nop 0
	global_load_dwordx4 v[148:151], v[152:153], off nt
	v_addc_co_u32_e32 v165, vcc, 0, v181, vcc
	v_add_co_u32_e32 v172, vcc, 0x5000, v180
	global_load_dwordx4 v[160:163], v[152:153], off offset:2048 nt
	s_nop 0
	global_load_dwordx4 v[152:155], v[164:165], off nt
	v_addc_co_u32_e32 v173, vcc, 0, v181, vcc
	v_add_co_u32_e32 v182, vcc, 0x6000, v180
	global_load_dwordx4 v[164:167], v[164:165], off offset:2048 nt
	s_nop 0
	global_load_dwordx4 v[168:171], v[172:173], off nt
	v_addc_co_u32_e32 v183, vcc, 0, v181, vcc
	v_add_co_u32_e32 v190, vcc, 0x7000, v180
	global_load_dwordx4 v[172:175], v[172:173], off offset:2048 nt
	s_nop 0
	global_load_dwordx4 v[176:179], v[182:183], off nt
	v_addc_co_u32_e32 v191, vcc, 0, v181, vcc
	global_load_dwordx4 v[180:183], v[182:183], off offset:2048 nt
	s_nop 0
	global_load_dwordx4 v[184:187], v[190:191], off nt
	global_load_dwordx4 v[192:195], v[188:189], off offset:-4096 nt
	s_nop 0
	global_load_dwordx4 v[188:191], v[190:191], off offset:2048 nt
	s_cbranch_scc1 .LBB0_603
	s_ashr_i32 s0, s29, 31
	s_lshr_b32 s0, s0, 25
	s_add_i32 s1, s29, s0
	s_and_b32 s0, s1, 0x80
	s_sub_i32 s0, s29, s0
	s_bfe_i32 s14, s0, 0x80000
	s_bfe_u32 s14, s14, 0x3000c
	s_add_i32 s14, s0, s14
	s_bfe_i32 s28, s14, 0x80000
	s_and_b32 s14, s14, 0xf8
	s_sub_i32 s0, s0, s14
	s_sext_i32_i8 s14, s0
	s_lshl_b32 s0, s0, 6
	s_lshl_b32 s14, s14, 5
	s_and_b32 s0, s0, 0xc0
	s_and_b32 s14, s14, 0xffffff80
	s_or_b32 s30, s14, s0
	s_add_i32 s14, s0, s14
	s_addk_i32 s14, 0x80
	s_cmpk_lt_u32 s0, 0x80
	s_cselect_b32 s0, s30, s14
	s_ashr_i32 s34, s1, 7
	s_ashr_i32 s35, s34, 31
	s_lshl_b64 s[34:35], s[34:35], 21
	s_sext_i32_i16 s28, s28
	s_add_u32 s34, s8, s34
	s_addc_u32 s35, s9, s35
	s_lshl_b32 s1, s28, 3
	s_andn2_b32 s1, s1, 63
	v_add_u32_e32 v4, s1, v221
	v_ashrrev_i32_e32 v5, 31, v4
	v_lshlrev_b64 v[4:5], 11, v[4:5]
	v_lshl_add_u64 v[4:5], s[34:35], 0, v[4:5]
	s_ashr_i32 s1, s0, 31
	v_lshl_add_u64 v[4:5], s[0:1], 2, v[4:5]
	v_lshl_add_u64 v[84:85], v[4:5], 0, v[2:3]
	s_movk_i32 s0, 0x1000
	v_add_co_u32_e32 v28, vcc, s0, v84
	global_load_dwordx4 v[8:11], v[84:85], off nt
	global_load_dwordx4 v[4:7], v[84:85], off offset:2048 nt
	v_addc_co_u32_e32 v29, vcc, 0, v85, vcc
	v_add_co_u32_e32 v92, vcc, s83, v84
	s_nop 1
	v_addc_co_u32_e32 v93, vcc, 0, v85, vcc
	v_add_co_u32_e32 v36, vcc, 0x3000, v84
	global_load_dwordx4 v[16:19], v[92:93], off nt
	global_load_dwordx4 v[12:15], v[92:93], off offset:2048 nt
	v_addc_co_u32_e32 v37, vcc, 0, v85, vcc
	v_add_co_u32_e32 v52, vcc, s62, v84
	global_load_dwordx4 v[32:35], v[28:29], off offset:2048 nt
	s_nop 0
	global_load_dwordx4 v[28:31], v[36:37], off nt
	v_addc_co_u32_e32 v53, vcc, 0, v85, vcc
	v_add_co_u32_e32 v68, vcc, 0x5000, v84
	global_load_dwordx4 v[36:39], v[36:37], off offset:2048 nt
	s_nop 0
	global_load_dwordx4 v[40:43], v[52:53], off nt
	v_addc_co_u32_e32 v69, vcc, 0, v85, vcc
	v_add_co_u32_e32 v86, vcc, 0x6000, v84
	global_load_dwordx4 v[52:55], v[52:53], off offset:2048 nt
	s_nop 0
	global_load_dwordx4 v[56:59], v[68:69], off nt
	v_addc_co_u32_e32 v87, vcc, 0, v85, vcc
	v_add_co_u32_e32 v94, vcc, 0x7000, v84
	global_load_dwordx4 v[68:71], v[68:69], off offset:2048 nt
	s_nop 0
	global_load_dwordx4 v[72:75], v[86:87], off nt
	v_addc_co_u32_e32 v95, vcc, 0, v85, vcc
	global_load_dwordx4 v[84:87], v[86:87], off offset:2048 nt
	s_nop 0
	global_load_dwordx4 v[88:91], v[94:95], off nt
	global_load_dwordx4 v[112:115], v[92:93], off offset:-4096 nt
	s_nop 0
	global_load_dwordx4 v[92:95], v[94:95], off offset:2048 nt
.LBB0_603:
	s_add_i32 s28, s22, s23
	s_cmp_lt_i32 s28, 0x8000
	s_cselect_b64 s[0:1], -1, 0
	s_cmpk_gt_i32 s28, 0x7fff
	s_cbranch_scc1 .LBB0_605
	s_ashr_i32 s14, s28, 31
	s_lshr_b32 s14, s14, 25
	s_add_i32 s14, s28, s14
	s_and_b32 s30, s14, 0x80
	s_sub_i32 s30, s28, s30
	s_bfe_i32 s34, s30, 0x80000
	s_bfe_u32 s34, s34, 0x3000c
	s_add_i32 s34, s30, s34
	s_bfe_i32 s35, s34, 0x80000
	s_and_b32 s34, s34, 0xf8
	s_sub_i32 s30, s30, s34
	s_sext_i32_i8 s34, s30
	s_lshl_b32 s30, s30, 6
	s_lshl_b32 s34, s34, 5
	s_and_b32 s30, s30, 0xc0
	s_and_b32 s34, s34, 0xffffff80
	s_or_b32 s36, s34, s30
	s_add_i32 s34, s30, s34
	s_addk_i32 s34, 0x80
	s_cmpk_lt_u32 s30, 0x80
	s_cselect_b32 s34, s36, s34
	s_ashr_i32 s36, s14, 7
	s_ashr_i32 s37, s36, 31
	s_lshl_b64 s[36:37], s[36:37], 21
	s_sext_i32_i16 s35, s35
	s_add_u32 s36, s8, s36
	s_addc_u32 s37, s9, s37
	s_lshl_b32 s14, s35, 3
	s_andn2_b32 s14, s14, 63
	v_add_u32_e32 v20, s14, v221
	v_ashrrev_i32_e32 v21, 31, v20
	v_lshlrev_b64 v[20:21], 11, v[20:21]
	v_lshl_add_u64 v[20:21], s[36:37], 0, v[20:21]
	s_ashr_i32 s35, s34, 31
	v_lshl_add_u64 v[20:21], s[34:35], 2, v[20:21]
	v_lshl_add_u64 v[116:117], v[20:21], 0, v[2:3]
	s_movk_i32 s14, 0x1000
	v_add_co_u32_e32 v60, vcc, s14, v116
	global_load_dwordx4 v[24:27], v[116:117], off nt
	global_load_dwordx4 v[20:23], v[116:117], off offset:2048 nt
	v_addc_co_u32_e32 v61, vcc, 0, v117, vcc
	v_add_co_u32_e32 v124, vcc, s83, v116
	s_nop 1
	v_addc_co_u32_e32 v125, vcc, 0, v117, vcc
	v_add_co_u32_e32 v76, vcc, 0x3000, v116
	global_load_dwordx4 v[48:51], v[124:125], off nt
	global_load_dwordx4 v[44:47], v[124:125], off offset:2048 nt
	v_addc_co_u32_e32 v77, vcc, 0, v117, vcc
	v_add_co_u32_e32 v96, vcc, s62, v116
	global_load_dwordx4 v[64:67], v[60:61], off offset:2048 nt
	s_nop 0
	global_load_dwordx4 v[60:63], v[76:77], off nt
	v_addc_co_u32_e32 v97, vcc, 0, v117, vcc
	v_add_co_u32_e32 v104, vcc, 0x5000, v116
	global_load_dwordx4 v[76:79], v[76:77], off offset:2048 nt
	s_nop 0
	global_load_dwordx4 v[80:83], v[96:97], off nt
	v_addc_co_u32_e32 v105, vcc, 0, v117, vcc
	v_add_co_u32_e32 v118, vcc, 0x6000, v116
	global_load_dwordx4 v[96:99], v[96:97], off offset:2048 nt
	s_nop 0
	global_load_dwordx4 v[100:103], v[104:105], off nt
	v_addc_co_u32_e32 v119, vcc, 0, v117, vcc
	v_add_co_u32_e32 v126, vcc, 0x7000, v116
	global_load_dwordx4 v[104:107], v[104:105], off offset:2048 nt
	s_nop 0
	global_load_dwordx4 v[108:111], v[118:119], off nt
	v_addc_co_u32_e32 v127, vcc, 0, v117, vcc
	global_load_dwordx4 v[116:119], v[118:119], off offset:2048 nt
	s_nop 0
	global_load_dwordx4 v[120:123], v[126:127], off nt
	global_load_dwordx4 v[128:131], v[124:125], off offset:-4096 nt
	s_nop 0
	global_load_dwordx4 v[124:127], v[126:127], off offset:2048 nt
.LBB0_605:
	s_waitcnt vmcnt(14)
	v_cvt_pk_bf16_f32 v240, v132, v136
	s_waitcnt vmcnt(1)
	v_cvt_pk_bf16_f32 v241, v192, v156
	v_cvt_pk_bf16_f32 v242, v140, v144
	v_cvt_pk_bf16_f32 v243, v148, v160
	ds_write_b128 v223, v[240:243]
	v_cvt_pk_bf16_f32 v240, v152, v164
	v_cvt_pk_bf16_f32 v241, v168, v172
	v_cvt_pk_bf16_f32 v242, v176, v180
	s_waitcnt vmcnt(0)
	v_cvt_pk_bf16_f32 v243, v184, v188
	ds_write_b128 v224, v[240:243]
	v_cvt_pk_bf16_f32 v240, v133, v137
	v_cvt_pk_bf16_f32 v241, v193, v157
	v_cvt_pk_bf16_f32 v242, v141, v145
	v_cvt_pk_bf16_f32 v243, v149, v161
	ds_write_b128 v223, v[240:243] offset:128
	v_cvt_pk_bf16_f32 v240, v153, v165
	v_cvt_pk_bf16_f32 v241, v169, v173
	v_cvt_pk_bf16_f32 v242, v177, v181
	v_cvt_pk_bf16_f32 v243, v185, v189
	ds_write_b128 v224, v[240:243] offset:128
	v_cvt_pk_bf16_f32 v240, v134, v138
	v_cvt_pk_bf16_f32 v241, v194, v158
	v_cvt_pk_bf16_f32 v242, v142, v146
	v_cvt_pk_bf16_f32 v243, v150, v162
	ds_write_b128 v223, v[240:243] offset:256
	v_cvt_pk_bf16_f32 v240, v154, v166
	v_cvt_pk_bf16_f32 v241, v170, v174
	v_cvt_pk_bf16_f32 v242, v178, v182
	v_cvt_pk_bf16_f32 v243, v186, v190
	ds_write_b128 v224, v[240:243] offset:256
	v_cvt_pk_bf16_f32 v132, v135, v139
	v_cvt_pk_bf16_f32 v133, v195, v159
	v_cvt_pk_bf16_f32 v134, v143, v147
	v_cvt_pk_bf16_f32 v135, v151, v163
	s_lshl_b64 s[6:7], s[6:7], 19
	ds_write_b128 v223, v[132:135] offset:384
	v_cvt_pk_bf16_f32 v132, v155, v167
	v_cvt_pk_bf16_f32 v133, v171, v175
	v_cvt_pk_bf16_f32 v134, v179, v183
	v_cvt_pk_bf16_f32 v135, v187, v191
	ds_write_b128 v224, v[132:135] offset:384
	s_lshl_b64 s[6:7], s[6:7], 1
	v_add_u32_e32 v132, s5, v222
	v_add_u32_e32 v135, v225, v226
	s_add_u32 s6, s12, s6
	v_ashrrev_i32_e32 v133, 31, v132
	ds_read_b128 v[136:139], v135
	s_addc_u32 s7, s21, s7
	v_lshlrev_b64 v[132:133], 11, v[132:133]
	v_lshl_add_u64 v[132:133], s[6:7], 0, v[132:133]
	s_ashr_i32 s5, s4, 31
	v_lshl_add_u64 v[132:133], s[4:5], 1, v[132:133]
	v_mov_b32_e32 v1, v3
	v_lshl_add_u64 v[152:153], v[132:133], 0, v[0:1]
	s_waitcnt lgkmcnt(0)
	global_store_dwordx4 v[152:153], v[136:139], off nt
	v_add_co_u32_e32 v132, vcc, s62, v152
	s_nop 0
	v_add_u32_e32 v137, v227, v228
	ds_read_b128 v[144:147], v137
	v_add_u32_e32 v136, v229, v230
	ds_read_b128 v[148:151], v136
	v_addc_co_u32_e32 v133, vcc, 0, v153, vcc
	v_add_u32_e32 v138, v231, v232
	s_waitcnt lgkmcnt(1)
	global_store_dwordx4 v[132:133], v[144:147], off nt
	ds_read_b128 v[144:147], v138
	v_add_co_u32_e32 v132, vcc, s88, v152
	ds_read_b128 v[140:143], v135 offset:4096
	s_nop 0
	v_addc_co_u32_e32 v133, vcc, 0, v153, vcc
	s_waitcnt lgkmcnt(2)
	global_store_dwordx4 v[132:133], v[148:151], off nt
	v_add_co_u32_e32 v132, vcc, s66, v152
	v_add_u32_e32 v134, v233, v234
	s_nop 0
	v_addc_co_u32_e32 v133, vcc, 0, v153, vcc
	ds_read_b128 v[148:151], v134
	s_waitcnt lgkmcnt(2)
	global_store_dwordx4 v[132:133], v[144:147], off nt
	v_add_co_u32_e32 v132, vcc, s82, v152
	s_mov_b32 s4, 0x14000
	s_nop 0
	v_addc_co_u32_e32 v133, vcc, 0, v153, vcc
	s_waitcnt lgkmcnt(1)
	global_store_dwordx4 v[132:133], v[140:143], off nt
	v_add_co_u32_e32 v132, vcc, s4, v152
	s_nop 1
	v_addc_co_u32_e32 v133, vcc, 0, v153, vcc
	s_waitcnt lgkmcnt(0)
	global_store_dwordx4 v[132:133], v[148:151], off nt
	v_add_u32_e32 v133, v235, v236
	ds_read_b128 v[140:143], v133
	v_add_u32_e32 v132, v237, v238
	v_add_co_u32_e32 v148, vcc, 0x18000, v152
	ds_read_b128 v[144:147], v132
	s_nop 0
	v_addc_co_u32_e32 v149, vcc, 0, v153, vcc
	s_waitcnt lgkmcnt(1)
	global_store_dwordx4 v[148:149], v[140:143], off nt
	s_nop 1
	v_add_co_u32_e32 v140, vcc, 0x1c000, v152
	s_nop 1
	v_addc_co_u32_e32 v141, vcc, 0, v153, vcc
	s_andn2_b64 vcc, exec, s[2:3]
	s_waitcnt lgkmcnt(0)
	global_store_dwordx4 v[140:141], v[144:147], off nt
	s_cbranch_vccz .LBB0_607
	s_andn2_b64 vcc, exec, s[0:1]
	s_cbranch_vccnz .LBB0_600
	s_branch .LBB0_608
.LBB0_607:
	s_ashr_i32 s2, s29, 31
	s_lshr_b32 s2, s2, 25
	s_add_i32 s3, s29, s2
	s_ashr_i32 s2, s3, 7
	s_and_b32 s3, s3, 0xff80
	v_cvt_pk_bf16_f32 v140, v8, v4
	s_sub_i32 s3, s29, s3
	v_cvt_pk_bf16_f32 v141, v112, v32
	v_cvt_pk_bf16_f32 v142, v16, v12
	v_cvt_pk_bf16_f32 v143, v28, v36
	ds_write_b128 v223, v[140:143]
	v_cvt_pk_bf16_f32 v140, v40, v52
	s_bfe_i32 s4, s3, 0x80000
	v_cvt_pk_bf16_f32 v141, v56, v68
	v_cvt_pk_bf16_f32 v142, v72, v84
	v_cvt_pk_bf16_f32 v143, v88, v92
	ds_write_b128 v224, v[140:143]
	v_cvt_pk_bf16_f32 v140, v9, v5
	s_bfe_u32 s4, s4, 0x3000c
	v_cvt_pk_bf16_f32 v141, v113, v33
	v_cvt_pk_bf16_f32 v142, v17, v13
	v_cvt_pk_bf16_f32 v143, v29, v37
	ds_write_b128 v223, v[140:143] offset:128
	v_cvt_pk_bf16_f32 v140, v41, v53
	s_add_i32 s4, s3, s4
	v_cvt_pk_bf16_f32 v141, v57, v69
	v_cvt_pk_bf16_f32 v142, v73, v85
	v_cvt_pk_bf16_f32 v143, v89, v93
	ds_write_b128 v224, v[140:143] offset:128
	v_cvt_pk_bf16_f32 v140, v10, v6
	s_bfe_i32 s5, s4, 0x80000
	s_and_b32 s4, s4, 0xf8
	v_cvt_pk_bf16_f32 v141, v114, v34
	v_cvt_pk_bf16_f32 v142, v18, v14
	v_cvt_pk_bf16_f32 v143, v30, v38
	ds_write_b128 v223, v[140:143] offset:256
	v_cvt_pk_bf16_f32 v140, v42, v54
	s_sub_i32 s3, s3, s4
	v_cvt_pk_bf16_f32 v141, v58, v70
	v_cvt_pk_bf16_f32 v142, v74, v86
	v_cvt_pk_bf16_f32 v143, v90, v94
	ds_write_b128 v224, v[140:143] offset:256
	v_cvt_pk_bf16_f32 v140, v11, v7
	v_cvt_pk_bf16_f32 v141, v115, v35
	v_cvt_pk_bf16_f32 v142, v19, v15
	v_cvt_pk_bf16_f32 v143, v31, v39
	ds_write_b128 v223, v[140:143] offset:384
	v_cvt_pk_bf16_f32 v140, v43, v55
	s_sext_i32_i8 s4, s3
	s_ashr_i32 s3, s2, 31
	v_cvt_pk_bf16_f32 v141, v59, v71
	v_cvt_pk_bf16_f32 v142, v75, v87
	v_cvt_pk_bf16_f32 v143, v91, v95
	ds_write_b128 v224, v[140:143] offset:384
	s_lshl_b64 s[2:3], s[2:3], 20
	v_lshl_add_u32 v140, s4, 6, v222
	s_add_u32 s2, s12, s2
	v_ashrrev_i32_e32 v141, 31, v140
	s_sext_i32_i16 s5, s5
	s_addc_u32 s3, s21, s3
	v_lshlrev_b64 v[140:141], 11, v[140:141]
	v_lshl_add_u64 v[140:141], s[2:3], 0, v[140:141]
	s_lshl_b32 s2, s5, 3
	s_andn2_b32 s2, s2, 63
	s_ashr_i32 s3, s2, 31
	v_lshl_add_u64 v[140:141], s[2:3], 1, v[140:141]
	v_lshl_add_u64 v[144:145], v[140:141], 0, v[0:1]
	ds_read_b128 v[140:143], v135
	v_add_co_u32_e32 v146, vcc, s62, v144
	s_waitcnt lgkmcnt(0)
	global_store_dwordx4 v[144:145], v[140:143], off nt
	ds_read_b128 v[140:143], v137
	v_addc_co_u32_e32 v147, vcc, 0, v145, vcc
	s_waitcnt lgkmcnt(0)
	global_store_dwordx4 v[146:147], v[140:143], off nt
	ds_read_b128 v[140:143], v136
	v_add_co_u32_e32 v146, vcc, 0x8000, v144
	s_nop 1
	v_addc_co_u32_e32 v147, vcc, 0, v145, vcc
	s_waitcnt lgkmcnt(0)
	global_store_dwordx4 v[146:147], v[140:143], off nt
	ds_read_b128 v[140:143], v138
	v_add_co_u32_e32 v146, vcc, 0xc000, v144
	s_nop 1
	v_addc_co_u32_e32 v147, vcc, 0, v145, vcc
	s_waitcnt lgkmcnt(0)
	global_store_dwordx4 v[146:147], v[140:143], off nt
	ds_read_b128 v[140:143], v135 offset:4096
	v_add_co_u32_e32 v146, vcc, s82, v144
	s_nop 1
	v_addc_co_u32_e32 v147, vcc, 0, v145, vcc
	s_waitcnt lgkmcnt(0)
	global_store_dwordx4 v[146:147], v[140:143], off nt
	ds_read_b128 v[140:143], v134
	v_add_co_u32_e32 v146, vcc, 0x14000, v144
	s_nop 1
	v_addc_co_u32_e32 v147, vcc, 0, v145, vcc
	s_waitcnt lgkmcnt(0)
	global_store_dwordx4 v[146:147], v[140:143], off nt
	ds_read_b128 v[140:143], v133
	v_add_co_u32_e32 v146, vcc, 0x18000, v144
	s_nop 1
	v_addc_co_u32_e32 v147, vcc, 0, v145, vcc
	s_waitcnt lgkmcnt(0)
	global_store_dwordx4 v[146:147], v[140:143], off nt
	ds_read_b128 v[140:143], v132
	v_add_co_u32_e32 v144, vcc, 0x1c000, v144
	s_nop 1
	v_addc_co_u32_e32 v145, vcc, 0, v145, vcc
	s_waitcnt lgkmcnt(0)
	global_store_dwordx4 v[144:145], v[140:143], off nt
	s_andn2_b64 vcc, exec, s[0:1]
	s_cbranch_vccnz .LBB0_600
.LBB0_608:
	s_ashr_i32 s0, s28, 31
	s_lshr_b32 s0, s0, 25
	s_add_i32 s1, s28, s0
	s_ashr_i32 s0, s1, 7
	s_and_b32 s1, s1, 0xff80
	v_cvt_pk_bf16_f32 v140, v24, v20
	s_sub_i32 s1, s28, s1
	v_cvt_pk_bf16_f32 v141, v128, v64
	v_cvt_pk_bf16_f32 v142, v48, v44
	v_cvt_pk_bf16_f32 v143, v60, v76
	ds_write_b128 v223, v[140:143]
	v_cvt_pk_bf16_f32 v140, v80, v96
	s_bfe_i32 s2, s1, 0x80000
	v_cvt_pk_bf16_f32 v141, v100, v104
	v_cvt_pk_bf16_f32 v142, v108, v116
	v_cvt_pk_bf16_f32 v143, v120, v124
	ds_write_b128 v224, v[140:143]
	v_cvt_pk_bf16_f32 v140, v25, v21
	s_bfe_u32 s2, s2, 0x3000c
	v_cvt_pk_bf16_f32 v141, v129, v65
	v_cvt_pk_bf16_f32 v142, v49, v45
	v_cvt_pk_bf16_f32 v143, v61, v77
	ds_write_b128 v223, v[140:143] offset:128
	v_cvt_pk_bf16_f32 v140, v81, v97
	s_add_i32 s2, s1, s2
	v_cvt_pk_bf16_f32 v141, v101, v105
	v_cvt_pk_bf16_f32 v142, v109, v117
	v_cvt_pk_bf16_f32 v143, v121, v125
	ds_write_b128 v224, v[140:143] offset:128
	v_cvt_pk_bf16_f32 v140, v26, v22
	s_bfe_i32 s3, s2, 0x80000
	s_and_b32 s2, s2, 0xf8
	v_cvt_pk_bf16_f32 v141, v130, v66
	v_cvt_pk_bf16_f32 v142, v50, v46
	v_cvt_pk_bf16_f32 v143, v62, v78
	ds_write_b128 v223, v[140:143] offset:256
	v_cvt_pk_bf16_f32 v140, v82, v98
	s_sub_i32 s1, s1, s2
	v_cvt_pk_bf16_f32 v141, v102, v106
	v_cvt_pk_bf16_f32 v142, v110, v118
	v_cvt_pk_bf16_f32 v143, v122, v126
	ds_write_b128 v224, v[140:143] offset:256
	v_cvt_pk_bf16_f32 v140, v27, v23
	v_cvt_pk_bf16_f32 v141, v131, v67
	v_cvt_pk_bf16_f32 v142, v51, v47
	v_cvt_pk_bf16_f32 v143, v63, v79
	ds_write_b128 v223, v[140:143] offset:384
	v_cvt_pk_bf16_f32 v140, v83, v99
	s_sext_i32_i8 s2, s1
	s_ashr_i32 s1, s0, 31
	v_cvt_pk_bf16_f32 v141, v103, v107
	v_cvt_pk_bf16_f32 v142, v111, v119
	v_cvt_pk_bf16_f32 v143, v123, v127
	ds_write_b128 v224, v[140:143] offset:384
	s_lshl_b64 s[0:1], s[0:1], 20
	v_lshl_add_u32 v140, s2, 6, v222
	s_add_u32 s0, s12, s0
	v_ashrrev_i32_e32 v141, 31, v140
	s_sext_i32_i16 s3, s3
	s_addc_u32 s1, s21, s1
	v_lshlrev_b64 v[140:141], 11, v[140:141]
	v_lshl_add_u64 v[140:141], s[0:1], 0, v[140:141]
	s_lshl_b32 s0, s3, 3
	s_andn2_b32 s0, s0, 63
	s_ashr_i32 s1, s0, 31
	v_lshl_add_u64 v[140:141], s[0:1], 1, v[140:141]
	v_mov_b32_e32 v1, v3
	v_lshl_add_u64 v[144:145], v[140:141], 0, v[0:1]
	ds_read_b128 v[140:143], v135
	v_add_co_u32_e32 v146, vcc, s62, v144
	s_waitcnt lgkmcnt(0)
	global_store_dwordx4 v[144:145], v[140:143], off nt
	ds_read_b128 v[140:143], v137
	v_addc_co_u32_e32 v147, vcc, 0, v145, vcc
	s_waitcnt lgkmcnt(0)
	global_store_dwordx4 v[146:147], v[140:143], off nt
	ds_read_b128 v[140:143], v136
	v_add_co_u32_e32 v136, vcc, 0x8000, v144
	s_nop 1
	v_addc_co_u32_e32 v137, vcc, 0, v145, vcc
	s_waitcnt lgkmcnt(0)
	global_store_dwordx4 v[136:137], v[140:143], off nt
	ds_read_b128 v[136:139], v138
	s_nop 0
	v_add_co_u32_e32 v140, vcc, 0xc000, v144
	s_nop 1
	v_addc_co_u32_e32 v141, vcc, 0, v145, vcc
	s_waitcnt lgkmcnt(0)
	global_store_dwordx4 v[140:141], v[136:139], off nt
	ds_read_b128 v[136:139], v135 offset:4096
	v_add_co_u32_e32 v140, vcc, s82, v144
	s_nop 1
	v_addc_co_u32_e32 v141, vcc, 0, v145, vcc
	s_waitcnt lgkmcnt(0)
	global_store_dwordx4 v[140:141], v[136:139], off nt
	ds_read_b128 v[134:137], v134
	s_nop 0
	v_add_co_u32_e32 v138, vcc, 0x14000, v144
	s_nop 1
	v_addc_co_u32_e32 v139, vcc, 0, v145, vcc
	s_waitcnt lgkmcnt(0)
	global_store_dwordx4 v[138:139], v[134:137], off nt
	ds_read_b128 v[134:137], v133
	v_add_co_u32_e32 v138, vcc, 0x18000, v144
	s_nop 1
	v_addc_co_u32_e32 v139, vcc, 0, v145, vcc
	s_waitcnt lgkmcnt(0)
	global_store_dwordx4 v[138:139], v[134:137], off nt
	ds_read_b128 v[132:135], v132
	s_nop 0
	v_add_co_u32_e32 v136, vcc, 0x1c000, v144
	s_nop 1
	v_addc_co_u32_e32 v137, vcc, 0, v145, vcc
	s_waitcnt lgkmcnt(0)
	global_store_dwordx4 v[136:137], v[132:135], off nt
	s_branch .LBB0_600

.LBB0_613:
	s_add_i32 s30, s38, s29
	s_cmpk_lt_i32 s30, 0x4000
	s_cselect_b64 s[2:3], -1, 0
	s_ashr_i32 s0, s29, 31
	s_lshr_b32 s0, s0, 26
	s_add_i32 s0, s29, s0
	s_ashr_i32 s8, s0, 6
	s_and_b32 s0, s0, 0xffc0
	s_sub_i32 s0, s29, s0
	s_bfe_i32 s1, s0, 0x80000
	s_bfe_u32 s1, s1, 0x4000b
	s_add_i32 s1, s0, s1
	s_bfe_i32 s4, s1, 0x80000
	s_and_b32 s1, s1, 0xf0
	s_sub_i32 s0, s0, s1
	s_sext_i32_i8 s0, s0
	s_ashr_i32 s9, s8, 31
	s_lshl_b32 s6, s0, 6
	s_lshl_b64 s[0:1], s[8:9], 20
	s_sext_i32_i16 s4, s4
	s_add_u32 s0, s12, s0
	s_addc_u32 s1, s21, s1
	s_lshl_b32 s4, s4, 2
	s_andn2_b32 s4, s4, 63
	v_add_u32_e32 v132, s4, v221
	v_ashrrev_i32_e32 v133, 31, v132
	v_lshlrev_b64 v[132:133], 12, v[132:133]
	s_ashr_i32 s7, s6, 31
	v_lshl_add_u64 v[132:133], s[0:1], 0, v[132:133]
	v_lshl_add_u64 v[132:133], s[6:7], 2, v[132:133]
	v_lshl_add_u64 v[188:189], v[132:133], 0, v[2:3]
	v_add_co_u32_e32 v132, vcc, s83, v188
	s_cmpk_gt_i32 s30, 0x3fff
	s_nop 0
	v_addc_co_u32_e32 v133, vcc, 0, v189, vcc
	v_add_co_u32_e32 v140, vcc, s62, v188
	global_load_dwordx4 v[136:139], v[132:133], off offset:-4096 nt
	s_nop 0
	global_load_dwordx4 v[132:135], v[132:133], off nt
	v_addc_co_u32_e32 v141, vcc, 0, v189, vcc
	v_add_co_u32_e32 v148, vcc, s77, v188
	global_load_dwordx4 v[144:147], v[140:141], off offset:-4096 nt
	s_nop 0
	global_load_dwordx4 v[140:143], v[140:141], off nt
	v_addc_co_u32_e32 v149, vcc, 0, v189, vcc
	v_add_co_u32_e32 v152, vcc, s88, v188
	global_load_dwordx4 v[156:159], v[148:149], off offset:-4096 nt
	s_nop 0
	global_load_dwordx4 v[148:151], v[148:149], off nt
	v_addc_co_u32_e32 v153, vcc, 0, v189, vcc
	v_add_co_u32_e32 v160, vcc, s72, v188
	global_load_dwordx4 v[164:167], v[152:153], off offset:-4096 nt
	s_nop 0
	global_load_dwordx4 v[152:155], v[152:153], off nt
	v_addc_co_u32_e32 v161, vcc, 0, v189, vcc
	v_add_co_u32_e32 v172, vcc, 0xb000, v188
	global_load_dwordx4 v[168:171], v[160:161], off offset:-4096 nt
	s_nop 0
	global_load_dwordx4 v[160:163], v[160:161], off nt
	v_addc_co_u32_e32 v173, vcc, 0, v189, vcc
	v_add_co_u32_e32 v176, vcc, s66, v188
	global_load_dwordx4 v[184:187], v[188:189], off nt
	s_nop 0
	global_load_dwordx4 v[172:175], v[172:173], off nt
	v_addc_co_u32_e32 v177, vcc, 0, v189, vcc
	v_add_co_u32_e32 v180, vcc, 0xd000, v188
	s_nop 1
	v_addc_co_u32_e32 v181, vcc, 0, v189, vcc
	v_add_co_u32_e32 v190, vcc, 0xe000, v188
	global_load_dwordx4 v[176:179], v[176:177], off nt
	s_nop 0
	global_load_dwordx4 v[180:183], v[180:181], off nt
	v_addc_co_u32_e32 v191, vcc, 0, v189, vcc
	v_add_co_u32_e32 v192, vcc, 0xf000, v188
	s_nop 1
	v_addc_co_u32_e32 v193, vcc, 0, v189, vcc
	global_load_dwordx4 v[188:191], v[190:191], off nt
	s_nop 0
	global_load_dwordx4 v[192:195], v[192:193], off nt
	s_cbranch_scc1 .LBB0_615
	s_ashr_i32 s0, s30, 31
	s_lshr_b32 s0, s0, 26
	s_add_i32 s1, s30, s0
	s_and_b32 s0, s1, 0xc0
	s_sub_i32 s0, s30, s0
	s_bfe_i32 s5, s0, 0x80000
	s_bfe_u32 s5, s5, 0x4000b
	s_add_i32 s5, s0, s5
	s_bfe_i32 s7, s5, 0x80000
	s_and_b32 s5, s5, 0xf0
	s_sub_i32 s0, s0, s5
	s_ashr_i32 s34, s1, 6
	s_sext_i32_i8 s0, s0
	s_ashr_i32 s35, s34, 31
	s_lshl_b32 s0, s0, 6
	s_lshl_b64 s[34:35], s[34:35], 20
	s_sext_i32_i16 s7, s7
	s_add_u32 s34, s12, s34
	s_addc_u32 s35, s21, s35
	s_lshl_b32 s1, s7, 2
	s_andn2_b32 s1, s1, 63
	v_add_u32_e32 v4, s1, v221
	v_ashrrev_i32_e32 v5, 31, v4
	v_lshlrev_b64 v[4:5], 12, v[4:5]
	v_lshl_add_u64 v[4:5], s[34:35], 0, v[4:5]
	s_ashr_i32 s1, s0, 31
	v_lshl_add_u64 v[4:5], s[0:1], 2, v[4:5]
	v_lshl_add_u64 v[108:109], v[4:5], 0, v[2:3]
	v_add_co_u32_e32 v4, vcc, s83, v108
	s_nop 1
	v_addc_co_u32_e32 v5, vcc, 0, v109, vcc
	v_add_co_u32_e32 v12, vcc, s62, v108
	global_load_dwordx4 v[8:11], v[4:5], off offset:-4096 nt
	s_nop 0
	global_load_dwordx4 v[4:7], v[4:5], off nt
	v_addc_co_u32_e32 v13, vcc, 0, v109, vcc
	v_add_co_u32_e32 v20, vcc, s77, v108
	global_load_dwordx4 v[16:19], v[12:13], off offset:-4096 nt
	s_nop 0
	global_load_dwordx4 v[12:15], v[12:13], off nt
	v_addc_co_u32_e32 v21, vcc, 0, v109, vcc
	v_add_co_u32_e32 v28, vcc, s88, v108
	global_load_dwordx4 v[24:27], v[20:21], off offset:-4096 nt
	s_nop 0
	global_load_dwordx4 v[20:23], v[20:21], off nt
	v_addc_co_u32_e32 v29, vcc, 0, v109, vcc
	v_add_co_u32_e32 v52, vcc, 0x9000, v108
	global_load_dwordx4 v[32:35], v[28:29], off offset:-4096 nt
	s_nop 0
	global_load_dwordx4 v[28:31], v[28:29], off nt
	v_addc_co_u32_e32 v53, vcc, 0, v109, vcc
	v_add_co_u32_e32 v68, vcc, s72, v108
	global_load_dwordx4 v[64:67], v[108:109], off nt
	s_nop 0
	global_load_dwordx4 v[52:55], v[52:53], off nt
	v_addc_co_u32_e32 v69, vcc, 0, v109, vcc
	v_add_co_u32_e32 v80, vcc, 0xb000, v108
	s_nop 1
	v_addc_co_u32_e32 v81, vcc, 0, v109, vcc
	v_add_co_u32_e32 v88, vcc, 0xc000, v108
	global_load_dwordx4 v[68:71], v[68:69], off nt
	s_nop 0
	global_load_dwordx4 v[80:83], v[80:81], off nt
	v_addc_co_u32_e32 v89, vcc, 0, v109, vcc
	v_add_co_u32_e32 v96, vcc, 0xd000, v108
	s_nop 1
	v_addc_co_u32_e32 v97, vcc, 0, v109, vcc
	v_add_co_u32_e32 v110, vcc, 0xe000, v108
	global_load_dwordx4 v[88:91], v[88:89], off nt
	s_nop 0
	global_load_dwordx4 v[96:99], v[96:97], off nt
	v_addc_co_u32_e32 v111, vcc, 0, v109, vcc
	v_add_co_u32_e32 v112, vcc, 0xf000, v108
	s_nop 1
	v_addc_co_u32_e32 v113, vcc, 0, v109, vcc
	global_load_dwordx4 v[108:111], v[110:111], off nt
	s_nop 0
	global_load_dwordx4 v[112:115], v[112:113], off nt
.LBB0_615:
	s_add_i32 s7, s28, s29
	s_cmpk_lt_i32 s7, 0x4000
	s_cselect_b64 s[0:1], -1, 0
	s_cmpk_gt_i32 s7, 0x3fff
	s_cbranch_scc1 .LBB0_617
	s_ashr_i32 s5, s7, 31
	s_lshr_b32 s5, s5, 26
	s_add_i32 s5, s7, s5
	s_and_b32 s14, s5, 0xc0
	s_sub_i32 s14, s7, s14
	s_bfe_i32 s34, s14, 0x80000
	s_bfe_u32 s34, s34, 0x4000b
	s_add_i32 s34, s14, s34
	s_bfe_i32 s35, s34, 0x80000
	s_and_b32 s34, s34, 0xf0
	s_sub_i32 s14, s14, s34
	s_ashr_i32 s36, s5, 6
	s_sext_i32_i8 s14, s14
	s_ashr_i32 s37, s36, 31
	s_lshl_b32 s34, s14, 6
	s_lshl_b64 s[36:37], s[36:37], 20
	s_sext_i32_i16 s35, s35
	s_add_u32 s36, s12, s36
	s_addc_u32 s37, s21, s37
	s_lshl_b32 s5, s35, 2
	s_andn2_b32 s5, s5, 63
	v_add_u32_e32 v36, s5, v221
	v_ashrrev_i32_e32 v37, 31, v36
	v_lshlrev_b64 v[36:37], 12, v[36:37]
	v_lshl_add_u64 v[36:37], s[36:37], 0, v[36:37]
	s_ashr_i32 s35, s34, 31
	v_lshl_add_u64 v[36:37], s[34:35], 2, v[36:37]
	v_lshl_add_u64 v[124:125], v[36:37], 0, v[2:3]
	v_add_co_u32_e32 v36, vcc, s83, v124
	s_nop 1
	v_addc_co_u32_e32 v37, vcc, 0, v125, vcc
	v_add_co_u32_e32 v44, vcc, s62, v124
	global_load_dwordx4 v[40:43], v[36:37], off offset:-4096 nt
	s_nop 0
	global_load_dwordx4 v[36:39], v[36:37], off nt
	v_addc_co_u32_e32 v45, vcc, 0, v125, vcc
	v_add_co_u32_e32 v56, vcc, s77, v124
	global_load_dwordx4 v[48:51], v[44:45], off offset:-4096 nt
	s_nop 0
	global_load_dwordx4 v[44:47], v[44:45], off nt
	v_addc_co_u32_e32 v57, vcc, 0, v125, vcc
	v_add_co_u32_e32 v72, vcc, s88, v124
	global_load_dwordx4 v[60:63], v[56:57], off offset:-4096 nt
	s_nop 0
	global_load_dwordx4 v[56:59], v[56:57], off nt
	v_addc_co_u32_e32 v73, vcc, 0, v125, vcc
	v_add_co_u32_e32 v84, vcc, 0x9000, v124
	global_load_dwordx4 v[76:79], v[72:73], off offset:-4096 nt
	s_nop 0
	global_load_dwordx4 v[72:75], v[72:73], off nt
	v_addc_co_u32_e32 v85, vcc, 0, v125, vcc
	v_add_co_u32_e32 v100, vcc, s72, v124
	global_load_dwordx4 v[92:95], v[124:125], off nt
	s_nop 0
	global_load_dwordx4 v[84:87], v[84:85], off nt
	v_addc_co_u32_e32 v101, vcc, 0, v125, vcc
	v_add_co_u32_e32 v104, vcc, 0xb000, v124
	s_nop 1
	v_addc_co_u32_e32 v105, vcc, 0, v125, vcc
	v_add_co_u32_e32 v116, vcc, 0xc000, v124
	global_load_dwordx4 v[100:103], v[100:101], off nt
	s_nop 0
	global_load_dwordx4 v[104:107], v[104:105], off nt
	v_addc_co_u32_e32 v117, vcc, 0, v125, vcc
	v_add_co_u32_e32 v120, vcc, 0xd000, v124
	s_nop 1
	v_addc_co_u32_e32 v121, vcc, 0, v125, vcc
	v_add_co_u32_e32 v126, vcc, 0xe000, v124
	global_load_dwordx4 v[116:119], v[116:117], off nt
	s_nop 0
	global_load_dwordx4 v[120:123], v[120:121], off nt
	v_addc_co_u32_e32 v127, vcc, 0, v125, vcc
	v_add_co_u32_e32 v128, vcc, 0xf000, v124
	s_nop 1
	v_addc_co_u32_e32 v129, vcc, 0, v125, vcc
	global_load_dwordx4 v[124:127], v[126:127], off nt
	s_nop 0
	global_load_dwordx4 v[128:131], v[128:129], off nt
.LBB0_617:
	s_waitcnt vmcnt(5)
	v_cvt_pk_bf16_f32 v240, v184, v136
	v_cvt_pk_bf16_f32 v241, v132, v144
	v_cvt_pk_bf16_f32 v242, v140, v156
	v_cvt_pk_bf16_f32 v243, v148, v164
	ds_write_b128 v223, v[240:243]
	v_cvt_pk_bf16_f32 v240, v152, v168
	s_waitcnt vmcnt(4)
	v_cvt_pk_bf16_f32 v241, v160, v172
	s_waitcnt vmcnt(2)
	v_cvt_pk_bf16_f32 v242, v176, v180
	s_waitcnt vmcnt(0)
	v_cvt_pk_bf16_f32 v243, v188, v192
	ds_write_b128 v224, v[240:243]
	v_cvt_pk_bf16_f32 v240, v185, v137
	v_cvt_pk_bf16_f32 v241, v133, v145
	v_cvt_pk_bf16_f32 v242, v141, v157
	v_cvt_pk_bf16_f32 v243, v149, v165
	ds_write_b128 v223, v[240:243] offset:128
	v_cvt_pk_bf16_f32 v240, v153, v169
	v_cvt_pk_bf16_f32 v241, v161, v173
	v_cvt_pk_bf16_f32 v242, v177, v181
	v_cvt_pk_bf16_f32 v243, v189, v193
	ds_write_b128 v224, v[240:243] offset:128
	v_cvt_pk_bf16_f32 v240, v186, v138
	v_cvt_pk_bf16_f32 v241, v134, v146
	v_cvt_pk_bf16_f32 v242, v142, v158
	v_cvt_pk_bf16_f32 v243, v150, v166
	ds_write_b128 v223, v[240:243] offset:256
	v_cvt_pk_bf16_f32 v240, v154, v170
	v_cvt_pk_bf16_f32 v241, v162, v174
	v_cvt_pk_bf16_f32 v242, v178, v182
	v_cvt_pk_bf16_f32 v243, v190, v194
	ds_write_b128 v224, v[240:243] offset:256
	v_cvt_pk_bf16_f32 v132, v187, v139
	v_cvt_pk_bf16_f32 v133, v135, v147
	v_cvt_pk_bf16_f32 v134, v143, v159
	v_cvt_pk_bf16_f32 v135, v151, v167
	s_lshl_b64 s[8:9], s[8:9], 18
	ds_write_b128 v223, v[132:135] offset:384
	v_cvt_pk_bf16_f32 v132, v155, v171
	v_cvt_pk_bf16_f32 v133, v163, v175
	v_cvt_pk_bf16_f32 v134, v179, v183
	v_cvt_pk_bf16_f32 v135, v191, v195
	ds_write_b128 v224, v[132:135] offset:384
	s_lshl_b64 s[8:9], s[8:9], 1
	v_add_u32_e32 v132, s6, v222
	v_add_u32_e32 v135, v225, v226
	s_add_u32 s8, s22, s8
	v_ashrrev_i32_e32 v133, 31, v132
	ds_read_b128 v[136:139], v135
	ds_read_b128 v[140:143], v135 offset:4096
	s_addc_u32 s9, s23, s9
	v_lshlrev_b64 v[132:133], 9, v[132:133]
	v_lshl_add_u64 v[132:133], s[8:9], 0, v[132:133]
	s_ashr_i32 s5, s4, 31
	v_lshl_add_u64 v[132:133], s[4:5], 1, v[132:133]
	v_mov_b32_e32 v1, v3
	v_lshl_add_u64 v[152:153], v[132:133], 0, v[0:1]
	s_waitcnt lgkmcnt(1)
	global_store_dwordx4 v[152:153], v[136:139], off nt
	v_add_co_u32_e32 v132, vcc, s83, v152
	s_nop 0
	v_add_u32_e32 v137, v227, v228
	v_add_u32_e32 v136, v229, v230
	ds_read_b128 v[144:147], v137
	ds_read_b128 v[148:151], v136
	v_addc_co_u32_e32 v133, vcc, 0, v153, vcc
	s_waitcnt lgkmcnt(1)
	global_store_dwordx4 v[132:133], v[144:147], off offset:-4096 nt
	s_waitcnt lgkmcnt(0)
	global_store_dwordx4 v[132:133], v[148:151], off nt
	v_add_u32_e32 v138, v231, v232
	ds_read_b128 v[144:147], v138
	v_add_u32_e32 v134, v233, v234
	ds_read_b128 v[148:151], v134
	v_add_co_u32_e32 v132, vcc, s62, v152
	s_nop 1
	v_addc_co_u32_e32 v133, vcc, 0, v153, vcc
	s_waitcnt lgkmcnt(1)
	global_store_dwordx4 v[132:133], v[144:147], off offset:-4096 nt
	global_store_dwordx4 v[132:133], v[140:143], off nt
	v_add_co_u32_e32 v132, vcc, 0x5000, v152
	s_nop 1
	v_addc_co_u32_e32 v133, vcc, 0, v153, vcc
	s_waitcnt lgkmcnt(0)
	global_store_dwordx4 v[132:133], v[148:151], off nt
	v_add_u32_e32 v133, v235, v236
	ds_read_b128 v[140:143], v133
	v_add_u32_e32 v132, v237, v238
	v_add_co_u32_e32 v148, vcc, 0x6000, v152
	ds_read_b128 v[144:147], v132
	s_nop 0
	v_addc_co_u32_e32 v149, vcc, 0, v153, vcc
	s_waitcnt lgkmcnt(1)
	global_store_dwordx4 v[148:149], v[140:143], off nt
	s_nop 1
	v_add_co_u32_e32 v140, vcc, 0x7000, v152
	s_nop 1
	v_addc_co_u32_e32 v141, vcc, 0, v153, vcc
	s_andn2_b64 vcc, exec, s[2:3]
	s_waitcnt lgkmcnt(0)
	global_store_dwordx4 v[140:141], v[144:147], off nt
	s_cbranch_vccz .LBB0_619
	s_andn2_b64 vcc, exec, s[0:1]
	s_cbranch_vccnz .LBB0_612
	s_branch .LBB0_620
.LBB0_619:
	s_ashr_i32 s2, s30, 31
	s_lshr_b32 s2, s2, 26
	s_add_i32 s3, s30, s2
	s_ashr_i32 s2, s3, 6
	s_and_b32 s3, s3, 0xffc0
	v_cvt_pk_bf16_f32 v140, v64, v8
	s_sub_i32 s3, s30, s3
	v_cvt_pk_bf16_f32 v141, v4, v16
	v_cvt_pk_bf16_f32 v142, v12, v24
	v_cvt_pk_bf16_f32 v143, v20, v32
	ds_write_b128 v223, v[140:143]
	v_cvt_pk_bf16_f32 v140, v28, v52
	s_bfe_i32 s4, s3, 0x80000
	v_cvt_pk_bf16_f32 v141, v68, v80
	v_cvt_pk_bf16_f32 v142, v88, v96
	v_cvt_pk_bf16_f32 v143, v108, v112
	ds_write_b128 v224, v[140:143]
	v_cvt_pk_bf16_f32 v140, v65, v9
	s_bfe_u32 s4, s4, 0x4000b
	v_cvt_pk_bf16_f32 v141, v5, v17
	v_cvt_pk_bf16_f32 v142, v13, v25
	v_cvt_pk_bf16_f32 v143, v21, v33
	ds_write_b128 v223, v[140:143] offset:128
	v_cvt_pk_bf16_f32 v140, v29, v53
	s_add_i32 s4, s3, s4
	v_cvt_pk_bf16_f32 v141, v69, v81
	v_cvt_pk_bf16_f32 v142, v89, v97
	v_cvt_pk_bf16_f32 v143, v109, v113
	ds_write_b128 v224, v[140:143] offset:128
	v_cvt_pk_bf16_f32 v140, v66, v10
	s_bfe_i32 s5, s4, 0x80000
	v_cvt_pk_bf16_f32 v141, v6, v18
	v_cvt_pk_bf16_f32 v142, v14, v26
	v_cvt_pk_bf16_f32 v143, v22, v34
	ds_write_b128 v223, v[140:143] offset:256
	v_cvt_pk_bf16_f32 v140, v30, v54
	s_and_b32 s4, s4, 0xf0
	v_cvt_pk_bf16_f32 v141, v70, v82
	v_cvt_pk_bf16_f32 v142, v90, v98
	v_cvt_pk_bf16_f32 v143, v110, v114
	ds_write_b128 v224, v[140:143] offset:256
	v_cvt_pk_bf16_f32 v140, v67, v11
	s_sub_i32 s3, s3, s4
	v_cvt_pk_bf16_f32 v141, v7, v19
	v_cvt_pk_bf16_f32 v142, v15, v27
	v_cvt_pk_bf16_f32 v143, v23, v35
	ds_write_b128 v223, v[140:143] offset:384
	v_cvt_pk_bf16_f32 v140, v31, v55
	s_sext_i32_i8 s4, s3
	s_ashr_i32 s3, s2, 31
	v_cvt_pk_bf16_f32 v141, v71, v83
	v_cvt_pk_bf16_f32 v142, v91, v99
	v_cvt_pk_bf16_f32 v143, v111, v115
	ds_write_b128 v224, v[140:143] offset:384
	s_lshl_b64 s[2:3], s[2:3], 19
	v_lshl_add_u32 v140, s4, 6, v222
	s_add_u32 s2, s22, s2
	v_ashrrev_i32_e32 v141, 31, v140
	s_sext_i32_i16 s5, s5
	s_addc_u32 s3, s23, s3
	v_lshlrev_b64 v[140:141], 9, v[140:141]
	v_lshl_add_u64 v[140:141], s[2:3], 0, v[140:141]
	s_lshl_b32 s2, s5, 2
	s_andn2_b32 s2, s2, 63
	s_ashr_i32 s3, s2, 31
	v_lshl_add_u64 v[140:141], s[2:3], 1, v[140:141]
	v_lshl_add_u64 v[144:145], v[140:141], 0, v[0:1]
	ds_read_b128 v[140:143], v135
	v_add_co_u32_e32 v146, vcc, s83, v144
	s_waitcnt lgkmcnt(0)
	global_store_dwordx4 v[144:145], v[140:143], off nt
	ds_read_b128 v[140:143], v137
	v_addc_co_u32_e32 v147, vcc, 0, v145, vcc
	s_waitcnt lgkmcnt(0)
	global_store_dwordx4 v[146:147], v[140:143], off offset:-4096 nt
	ds_read_b128 v[140:143], v136
	s_waitcnt lgkmcnt(0)
	global_store_dwordx4 v[146:147], v[140:143], off nt
	ds_read_b128 v[140:143], v138
	v_add_co_u32_e32 v146, vcc, 0x3000, v144
	s_nop 1
	v_addc_co_u32_e32 v147, vcc, 0, v145, vcc
	s_waitcnt lgkmcnt(0)
	global_store_dwordx4 v[146:147], v[140:143], off nt
	ds_read_b128 v[140:143], v135 offset:4096
	v_add_co_u32_e32 v146, vcc, s62, v144
	s_nop 1
	v_addc_co_u32_e32 v147, vcc, 0, v145, vcc
	s_waitcnt lgkmcnt(0)
	global_store_dwordx4 v[146:147], v[140:143], off nt
	ds_read_b128 v[140:143], v134
	v_add_co_u32_e32 v146, vcc, 0x5000, v144
	s_nop 1
	v_addc_co_u32_e32 v147, vcc, 0, v145, vcc
	s_waitcnt lgkmcnt(0)
	global_store_dwordx4 v[146:147], v[140:143], off nt
	ds_read_b128 v[140:143], v133
	v_add_co_u32_e32 v146, vcc, 0x6000, v144
	s_nop 1
	v_addc_co_u32_e32 v147, vcc, 0, v145, vcc
	s_waitcnt lgkmcnt(0)
	global_store_dwordx4 v[146:147], v[140:143], off nt
	ds_read_b128 v[140:143], v132
	v_add_co_u32_e32 v144, vcc, 0x7000, v144
	s_nop 1
	v_addc_co_u32_e32 v145, vcc, 0, v145, vcc
	s_waitcnt lgkmcnt(0)
	global_store_dwordx4 v[144:145], v[140:143], off nt
	s_andn2_b64 vcc, exec, s[0:1]
	s_cbranch_vccnz .LBB0_612
.LBB0_620:
	s_ashr_i32 s0, s7, 31
	s_lshr_b32 s0, s0, 26
	s_add_i32 s1, s7, s0
	s_ashr_i32 s0, s1, 6
	s_and_b32 s1, s1, 0xffc0
	v_cvt_pk_bf16_f32 v140, v92, v40
	s_sub_i32 s1, s7, s1
	v_cvt_pk_bf16_f32 v141, v36, v48
	v_cvt_pk_bf16_f32 v142, v44, v60
	v_cvt_pk_bf16_f32 v143, v56, v76
	ds_write_b128 v223, v[140:143]
	v_cvt_pk_bf16_f32 v140, v72, v84
	s_bfe_i32 s2, s1, 0x80000
	v_cvt_pk_bf16_f32 v141, v100, v104
	v_cvt_pk_bf16_f32 v142, v116, v120
	v_cvt_pk_bf16_f32 v143, v124, v128
	ds_write_b128 v224, v[140:143]
	v_cvt_pk_bf16_f32 v140, v93, v41
	s_bfe_u32 s2, s2, 0x4000b
	v_cvt_pk_bf16_f32 v141, v37, v49
	v_cvt_pk_bf16_f32 v142, v45, v61
	v_cvt_pk_bf16_f32 v143, v57, v77
	ds_write_b128 v223, v[140:143] offset:128
	v_cvt_pk_bf16_f32 v140, v73, v85
	s_add_i32 s2, s1, s2
	v_cvt_pk_bf16_f32 v141, v101, v105
	v_cvt_pk_bf16_f32 v142, v117, v121
	v_cvt_pk_bf16_f32 v143, v125, v129
	ds_write_b128 v224, v[140:143] offset:128
	v_cvt_pk_bf16_f32 v140, v94, v42
	s_bfe_i32 s3, s2, 0x80000
	v_cvt_pk_bf16_f32 v141, v38, v50
	v_cvt_pk_bf16_f32 v142, v46, v62
	v_cvt_pk_bf16_f32 v143, v58, v78
	ds_write_b128 v223, v[140:143] offset:256
	v_cvt_pk_bf16_f32 v140, v74, v86
	s_and_b32 s2, s2, 0xf0
	v_cvt_pk_bf16_f32 v141, v102, v106
	v_cvt_pk_bf16_f32 v142, v118, v122
	v_cvt_pk_bf16_f32 v143, v126, v130
	ds_write_b128 v224, v[140:143] offset:256
	v_cvt_pk_bf16_f32 v140, v95, v43
	s_sub_i32 s1, s1, s2
	v_cvt_pk_bf16_f32 v141, v39, v51
	v_cvt_pk_bf16_f32 v142, v47, v63
	v_cvt_pk_bf16_f32 v143, v59, v79
	ds_write_b128 v223, v[140:143] offset:384
	v_cvt_pk_bf16_f32 v140, v75, v87
	s_sext_i32_i8 s2, s1
	s_ashr_i32 s1, s0, 31
	v_cvt_pk_bf16_f32 v141, v103, v107
	v_cvt_pk_bf16_f32 v142, v119, v123
	v_cvt_pk_bf16_f32 v143, v127, v131
	ds_write_b128 v224, v[140:143] offset:384
	s_lshl_b64 s[0:1], s[0:1], 19
	v_lshl_add_u32 v140, s2, 6, v222
	s_add_u32 s0, s22, s0
	v_ashrrev_i32_e32 v141, 31, v140
	s_sext_i32_i16 s3, s3
	s_addc_u32 s1, s23, s1
	v_lshlrev_b64 v[140:141], 9, v[140:141]
	v_lshl_add_u64 v[140:141], s[0:1], 0, v[140:141]
	s_lshl_b32 s0, s3, 2
	s_andn2_b32 s0, s0, 63
	s_ashr_i32 s1, s0, 31
	v_lshl_add_u64 v[140:141], s[0:1], 1, v[140:141]
	v_mov_b32_e32 v1, v3
	v_lshl_add_u64 v[144:145], v[140:141], 0, v[0:1]
	ds_read_b128 v[140:143], v135
	v_add_co_u32_e32 v146, vcc, s83, v144
	s_waitcnt lgkmcnt(0)
	global_store_dwordx4 v[144:145], v[140:143], off nt
	ds_read_b128 v[140:143], v137
	v_addc_co_u32_e32 v147, vcc, 0, v145, vcc
	s_waitcnt lgkmcnt(0)
	global_store_dwordx4 v[146:147], v[140:143], off offset:-4096 nt
	ds_read_b128 v[140:143], v136
	ds_read_b128 v[136:139], v138
	s_waitcnt lgkmcnt(1)
	global_store_dwordx4 v[146:147], v[140:143], off nt
	s_nop 1
	v_add_co_u32_e32 v140, vcc, 0x3000, v144
	s_nop 1
	v_addc_co_u32_e32 v141, vcc, 0, v145, vcc
	s_waitcnt lgkmcnt(0)
	global_store_dwordx4 v[140:141], v[136:139], off nt
	ds_read_b128 v[136:139], v135 offset:4096
	v_add_co_u32_e32 v140, vcc, s62, v144
	s_nop 1
	v_addc_co_u32_e32 v141, vcc, 0, v145, vcc
	s_waitcnt lgkmcnt(0)
	global_store_dwordx4 v[140:141], v[136:139], off nt
	ds_read_b128 v[134:137], v134
	s_nop 0
	v_add_co_u32_e32 v138, vcc, 0x5000, v144
	s_nop 1
	v_addc_co_u32_e32 v139, vcc, 0, v145, vcc
	s_waitcnt lgkmcnt(0)
	global_store_dwordx4 v[138:139], v[134:137], off nt
	ds_read_b128 v[134:137], v133
	v_add_co_u32_e32 v138, vcc, 0x6000, v144
	s_nop 1
	v_addc_co_u32_e32 v139, vcc, 0, v145, vcc
	s_waitcnt lgkmcnt(0)
	global_store_dwordx4 v[138:139], v[134:137], off nt
	ds_read_b128 v[132:135], v132
	s_nop 0
	v_add_co_u32_e32 v136, vcc, 0x7000, v144
	s_nop 1
	v_addc_co_u32_e32 v137, vcc, 0, v145, vcc
	s_waitcnt lgkmcnt(0)
	global_store_dwordx4 v[136:137], v[132:135], off nt
	s_branch .LBB0_612

.LBB0_626:
	s_add_i32 s28, s38, s12
	s_cmpk_lt_i32 s28, 0x100
	s_cselect_b64 s[2:3], -1, 0
	s_ashr_i32 s0, s12, 31
	s_lshr_b32 s0, s0, 25
	s_add_i32 s0, s12, s0
	s_ashr_i32 s8, s0, 7
	s_and_b32 s0, s0, 0xff80
	s_sub_i32 s0, s12, s0
	s_bfe_i32 s1, s0, 0x80000
	s_bfe_u32 s1, s1, 0x2000d
	s_add_i32 s1, s0, s1
	s_bfe_i32 s4, s1, 0x80000
	s_and_b32 s1, s1, 0xfc
	s_sub_i32 s0, s0, s1
	s_sext_i32_i8 s0, s0
	s_ashr_i32 s9, s8, 31
	s_lshl_b32 s6, s0, 6
	s_lshl_b64 s[0:1], s[8:9], 21
	v_readlane_b32 s5, v252, 57
	s_sext_i32_i16 s4, s4
	s_add_u32 s0, s5, s0
	v_readlane_b32 s5, v252, 58
	s_addc_u32 s1, s5, s1
	s_lshl_b32 s4, s4, 4
	s_andn2_b32 s4, s4, 63
	v_add_u32_e32 v132, s4, v221
	v_ashrrev_i32_e32 v133, 31, v132
	v_lshlrev_b64 v[132:133], 10, v[132:133]
	s_ashr_i32 s7, s6, 31
	v_lshl_add_u64 v[132:133], s[0:1], 0, v[132:133]
	v_lshl_add_u64 v[132:133], s[6:7], 2, v[132:133]
	v_lshl_add_u64 v[180:181], v[132:133], 0, v[2:3]
	v_add_co_u32_e32 v148, vcc, 0x1000, v180
	global_load_dwordx4 v[136:139], v[180:181], off nt
	global_load_dwordx4 v[144:147], v[180:181], off offset:1024 nt
	global_load_dwordx4 v[132:135], v[180:181], off offset:2048 nt
	global_load_dwordx4 v[140:143], v[180:181], off offset:3072 nt
	v_addc_co_u32_e32 v149, vcc, 0, v181, vcc
	v_add_co_u32_e32 v160, vcc, 0x2000, v180
	global_load_dwordx4 v[164:167], v[148:149], off nt
	global_load_dwordx4 v[176:179], v[148:149], off offset:1024 nt
	global_load_dwordx4 v[152:155], v[148:149], off offset:2048 nt
	global_load_dwordx4 v[168:171], v[148:149], off offset:3072 nt
	v_addc_co_u32_e32 v161, vcc, 0, v181, vcc
	v_add_co_u32_e32 v188, vcc, 0x3000, v180
	global_load_dwordx4 v[156:159], v[160:161], off nt
	global_load_dwordx4 v[172:175], v[160:161], off offset:1024 nt
	global_load_dwordx4 v[148:151], v[160:161], off offset:2048 nt
	s_nop 0
	global_load_dwordx4 v[160:163], v[160:161], off offset:3072 nt
	v_addc_co_u32_e32 v189, vcc, 0, v181, vcc
	global_load_dwordx4 v[184:187], v[188:189], off nt
	global_load_dwordx4 v[192:195], v[188:189], off offset:1024 nt
	global_load_dwordx4 v[180:183], v[188:189], off offset:2048 nt
	s_nop 0
	global_load_dwordx4 v[188:191], v[188:189], off offset:3072 nt
	s_cmpk_gt_i32 s28, 0xff
	s_cbranch_scc1 .LBB0_628
	s_ashr_i32 s0, s28, 31
	s_lshr_b32 s0, s0, 25
	s_add_i32 s1, s28, s0
	s_and_b32 s0, s1, 0x80
	s_sub_i32 s0, s28, s0
	s_bfe_i32 s5, s0, 0x80000
	s_bfe_u32 s5, s5, 0x2000d
	s_add_i32 s5, s0, s5
	s_bfe_i32 s7, s5, 0x80000
	s_and_b32 s5, s5, 0xfc
	s_sub_i32 s0, s0, s5
	s_ashr_i32 s34, s1, 7
	s_sext_i32_i8 s0, s0
	s_ashr_i32 s35, s34, 31
	s_lshl_b32 s0, s0, 6
	s_lshl_b64 s[34:35], s[34:35], 21
	v_readlane_b32 s1, v252, 57
	s_sext_i32_i16 s7, s7
	s_add_u32 s34, s1, s34
	v_readlane_b32 s1, v252, 58
	s_addc_u32 s35, s1, s35
	s_lshl_b32 s1, s7, 4
	s_andn2_b32 s1, s1, 63
	v_add_u32_e32 v4, s1, v221
	v_ashrrev_i32_e32 v5, 31, v4
	v_lshlrev_b64 v[4:5], 10, v[4:5]
	v_lshl_add_u64 v[4:5], s[34:35], 0, v[4:5]
	s_ashr_i32 s1, s0, 31
	v_lshl_add_u64 v[4:5], s[0:1], 2, v[4:5]
	v_lshl_add_u64 v[52:53], v[4:5], 0, v[2:3]
	v_add_co_u32_e32 v20, vcc, 0x1000, v52
	global_load_dwordx4 v[16:19], v[52:53], off nt
	global_load_dwordx4 v[12:15], v[52:53], off offset:1024 nt
	global_load_dwordx4 v[8:11], v[52:53], off offset:2048 nt
	global_load_dwordx4 v[4:7], v[52:53], off offset:3072 nt
	v_addc_co_u32_e32 v21, vcc, 0, v53, vcc
	v_add_co_u32_e32 v36, vcc, 0x2000, v52
	global_load_dwordx4 v[32:35], v[20:21], off nt
	global_load_dwordx4 v[28:31], v[20:21], off offset:1024 nt
	global_load_dwordx4 v[24:27], v[20:21], off offset:2048 nt
	s_nop 0
	global_load_dwordx4 v[20:23], v[20:21], off offset:3072 nt
	v_addc_co_u32_e32 v37, vcc, 0, v53, vcc
	v_add_co_u32_e32 v52, vcc, 0x3000, v52
	global_load_dwordx4 v[48:51], v[36:37], off nt
	global_load_dwordx4 v[44:47], v[36:37], off offset:1024 nt
	global_load_dwordx4 v[40:43], v[36:37], off offset:2048 nt
	s_nop 0
	global_load_dwordx4 v[36:39], v[36:37], off offset:3072 nt
	v_addc_co_u32_e32 v53, vcc, 0, v53, vcc
	global_load_dwordx4 v[64:67], v[52:53], off nt
	global_load_dwordx4 v[60:63], v[52:53], off offset:1024 nt
	global_load_dwordx4 v[56:59], v[52:53], off offset:2048 nt
	s_nop 0
	global_load_dwordx4 v[52:55], v[52:53], off offset:3072 nt
.LBB0_628:
	s_add_i32 s7, s23, s12
	s_cmpk_lt_i32 s7, 0x100
	s_cselect_b64 s[0:1], -1, 0
	s_cmpk_gt_i32 s7, 0xff
	s_cbranch_scc1 .LBB0_630
	s_ashr_i32 s5, s7, 31
	s_lshr_b32 s5, s5, 25
	s_add_i32 s5, s7, s5
	s_and_b32 s14, s5, 0x80
	s_sub_i32 s14, s7, s14
	s_bfe_i32 s29, s14, 0x80000
	s_bfe_u32 s29, s29, 0x2000d
	s_add_i32 s29, s14, s29
	s_bfe_i32 s30, s29, 0x80000
	s_and_b32 s29, s29, 0xfc
	s_sub_i32 s14, s14, s29
	s_ashr_i32 s36, s5, 7
	s_sext_i32_i8 s14, s14
	s_ashr_i32 s37, s36, 31
	s_lshl_b32 s34, s14, 6
	s_lshl_b64 s[36:37], s[36:37], 21
	v_readlane_b32 s5, v252, 57
	s_sext_i32_i16 s30, s30
	s_add_u32 s36, s5, s36
	v_readlane_b32 s5, v252, 58
	s_addc_u32 s37, s5, s37
	s_lshl_b32 s5, s30, 4
	s_andn2_b32 s5, s5, 63
	v_add_u32_e32 v68, s5, v221
	v_ashrrev_i32_e32 v69, 31, v68
	v_lshlrev_b64 v[68:69], 10, v[68:69]
	v_lshl_add_u64 v[68:69], s[36:37], 0, v[68:69]
	s_ashr_i32 s35, s34, 31
	v_lshl_add_u64 v[68:69], s[34:35], 2, v[68:69]
	v_lshl_add_u64 v[116:117], v[68:69], 0, v[2:3]
	v_add_co_u32_e32 v84, vcc, 0x1000, v116
	global_load_dwordx4 v[80:83], v[116:117], off nt
	global_load_dwordx4 v[76:79], v[116:117], off offset:1024 nt
	global_load_dwordx4 v[72:75], v[116:117], off offset:2048 nt
	global_load_dwordx4 v[68:71], v[116:117], off offset:3072 nt
	v_addc_co_u32_e32 v85, vcc, 0, v117, vcc
	v_add_co_u32_e32 v100, vcc, 0x2000, v116
	global_load_dwordx4 v[96:99], v[84:85], off nt
	global_load_dwordx4 v[92:95], v[84:85], off offset:1024 nt
	global_load_dwordx4 v[88:91], v[84:85], off offset:2048 nt
	s_nop 0
	global_load_dwordx4 v[84:87], v[84:85], off offset:3072 nt
	v_addc_co_u32_e32 v101, vcc, 0, v117, vcc
	v_add_co_u32_e32 v116, vcc, 0x3000, v116
	global_load_dwordx4 v[112:115], v[100:101], off nt
	global_load_dwordx4 v[108:111], v[100:101], off offset:1024 nt
	global_load_dwordx4 v[104:107], v[100:101], off offset:2048 nt
	s_nop 0
	global_load_dwordx4 v[100:103], v[100:101], off offset:3072 nt
	v_addc_co_u32_e32 v117, vcc, 0, v117, vcc
	global_load_dwordx4 v[128:131], v[116:117], off nt
	global_load_dwordx4 v[124:127], v[116:117], off offset:1024 nt
	global_load_dwordx4 v[120:123], v[116:117], off offset:2048 nt
	s_nop 0
	global_load_dwordx4 v[116:119], v[116:117], off offset:3072 nt
.LBB0_630:
	s_waitcnt vmcnt(14)
	v_cvt_pk_bf16_f32 v240, v136, v144
	s_waitcnt vmcnt(12)
	v_cvt_pk_bf16_f32 v241, v132, v140
	s_waitcnt vmcnt(10)
	v_cvt_pk_bf16_f32 v242, v164, v176
	s_waitcnt vmcnt(8)
	v_cvt_pk_bf16_f32 v243, v152, v168
	ds_write_b128 v223, v[240:243]
	s_waitcnt vmcnt(6)
	v_cvt_pk_bf16_f32 v240, v156, v172
	s_waitcnt vmcnt(4)
	v_cvt_pk_bf16_f32 v241, v148, v160
	s_waitcnt vmcnt(2)
	v_cvt_pk_bf16_f32 v242, v184, v192
	s_waitcnt vmcnt(0)
	v_cvt_pk_bf16_f32 v243, v180, v188
	ds_write_b128 v224, v[240:243]
	v_cvt_pk_bf16_f32 v240, v137, v145
	v_cvt_pk_bf16_f32 v241, v133, v141
	v_cvt_pk_bf16_f32 v242, v165, v177
	v_cvt_pk_bf16_f32 v243, v153, v169
	ds_write_b128 v223, v[240:243] offset:128
	v_cvt_pk_bf16_f32 v240, v157, v173
	v_cvt_pk_bf16_f32 v241, v149, v161
	v_cvt_pk_bf16_f32 v242, v185, v193
	v_cvt_pk_bf16_f32 v243, v181, v189
	ds_write_b128 v224, v[240:243] offset:128
	v_cvt_pk_bf16_f32 v240, v138, v146
	v_cvt_pk_bf16_f32 v241, v134, v142
	v_cvt_pk_bf16_f32 v242, v166, v178
	v_cvt_pk_bf16_f32 v243, v154, v170
	ds_write_b128 v223, v[240:243] offset:256
	v_cvt_pk_bf16_f32 v240, v158, v174
	v_cvt_pk_bf16_f32 v241, v150, v162
	v_cvt_pk_bf16_f32 v242, v186, v194
	v_cvt_pk_bf16_f32 v243, v182, v190
	ds_write_b128 v224, v[240:243] offset:256
	v_cvt_pk_bf16_f32 v132, v139, v147
	v_cvt_pk_bf16_f32 v133, v135, v143
	v_cvt_pk_bf16_f32 v134, v167, v179
	v_cvt_pk_bf16_f32 v135, v155, v171
	s_lshl_b64 s[8:9], s[8:9], 19
	ds_write_b128 v223, v[132:135] offset:384
	v_cvt_pk_bf16_f32 v132, v159, v175
	v_cvt_pk_bf16_f32 v133, v151, v163
	v_cvt_pk_bf16_f32 v134, v187, v195
	v_cvt_pk_bf16_f32 v135, v183, v191
	ds_write_b128 v224, v[132:135] offset:384
	s_lshl_b64 s[8:9], s[8:9], 1
	v_add_u32_e32 v132, s6, v222
	v_add_u32_e32 v135, v225, v226
	s_add_u32 s8, s21, s8
	v_ashrrev_i32_e32 v133, 31, v132
	ds_read_b128 v[136:139], v135
	s_addc_u32 s9, s22, s9
	v_lshlrev_b64 v[132:133], 12, v[132:133]
	v_lshl_add_u64 v[132:133], s[8:9], 0, v[132:133]
	s_ashr_i32 s5, s4, 31
	v_lshl_add_u64 v[132:133], s[4:5], 1, v[132:133]
	v_mov_b32_e32 v1, v3
	v_lshl_add_u64 v[152:153], v[132:133], 0, v[0:1]
	s_waitcnt lgkmcnt(0)
	global_store_dwordx4 v[152:153], v[136:139], off nt
	v_add_co_u32_e32 v132, vcc, s88, v152
	s_nop 0
	v_add_u32_e32 v137, v227, v228
	ds_read_b128 v[144:147], v137
	v_add_u32_e32 v136, v229, v230
	ds_read_b128 v[148:151], v136
	v_addc_co_u32_e32 v133, vcc, 0, v153, vcc
	v_add_u32_e32 v138, v231, v232
	s_waitcnt lgkmcnt(1)
	global_store_dwordx4 v[132:133], v[144:147], off nt
	ds_read_b128 v[144:147], v138
	v_add_co_u32_e32 v132, vcc, s82, v152
	ds_read_b128 v[140:143], v135 offset:4096
	s_nop 0
	v_addc_co_u32_e32 v133, vcc, 0, v153, vcc
	s_mov_b32 s4, 0x18000
	s_waitcnt lgkmcnt(2)
	global_store_dwordx4 v[132:133], v[148:151], off nt
	v_add_co_u32_e32 v132, vcc, s4, v152
	v_add_u32_e32 v134, v233, v234
	s_nop 0
	v_addc_co_u32_e32 v133, vcc, 0, v153, vcc
	ds_read_b128 v[148:151], v134
	s_mov_b32 s4, 0x20000
	s_waitcnt lgkmcnt(2)
	global_store_dwordx4 v[132:133], v[144:147], off nt
	v_add_co_u32_e32 v132, vcc, s4, v152
	s_mov_b32 s4, 0x28000
	s_nop 0
	v_addc_co_u32_e32 v133, vcc, 0, v153, vcc
	s_waitcnt lgkmcnt(1)
	global_store_dwordx4 v[132:133], v[140:143], off nt
	v_add_co_u32_e32 v132, vcc, s4, v152
	s_nop 1
	v_addc_co_u32_e32 v133, vcc, 0, v153, vcc
	s_waitcnt lgkmcnt(0)
	global_store_dwordx4 v[132:133], v[148:151], off nt
	v_add_u32_e32 v133, v235, v236
	ds_read_b128 v[140:143], v133
	v_add_u32_e32 v132, v237, v238
	v_add_co_u32_e32 v148, vcc, 0x30000, v152
	ds_read_b128 v[144:147], v132
	s_nop 0
	v_addc_co_u32_e32 v149, vcc, 0, v153, vcc
	s_waitcnt lgkmcnt(1)
	global_store_dwordx4 v[148:149], v[140:143], off nt
	s_nop 1
	v_add_co_u32_e32 v140, vcc, 0x38000, v152
	s_nop 1
	v_addc_co_u32_e32 v141, vcc, 0, v153, vcc
	s_andn2_b64 vcc, exec, s[2:3]
	s_waitcnt lgkmcnt(0)
	global_store_dwordx4 v[140:141], v[144:147], off nt
	s_cbranch_vccz .LBB0_632
	s_andn2_b64 vcc, exec, s[0:1]
	s_cbranch_vccnz .LBB0_625
	s_branch .LBB0_633
.LBB0_632:
	s_ashr_i32 s2, s28, 31
	s_lshr_b32 s2, s2, 25
	s_add_i32 s3, s28, s2
	s_ashr_i32 s2, s3, 7
	s_and_b32 s3, s3, 0xff80
	v_cvt_pk_bf16_f32 v140, v16, v12
	s_sub_i32 s3, s28, s3
	v_cvt_pk_bf16_f32 v141, v8, v4
	v_cvt_pk_bf16_f32 v142, v32, v28
	v_cvt_pk_bf16_f32 v143, v24, v20
	ds_write_b128 v223, v[140:143]
	v_cvt_pk_bf16_f32 v140, v48, v44
	s_bfe_i32 s4, s3, 0x80000
	v_cvt_pk_bf16_f32 v141, v40, v36
	v_cvt_pk_bf16_f32 v142, v64, v60
	v_cvt_pk_bf16_f32 v143, v56, v52
	ds_write_b128 v224, v[140:143]
	v_cvt_pk_bf16_f32 v140, v17, v13
	s_bfe_u32 s4, s4, 0x2000d
	v_cvt_pk_bf16_f32 v141, v9, v5
	v_cvt_pk_bf16_f32 v142, v33, v29
	v_cvt_pk_bf16_f32 v143, v25, v21
	ds_write_b128 v223, v[140:143] offset:128
	v_cvt_pk_bf16_f32 v140, v49, v45
	s_add_i32 s4, s3, s4
	v_cvt_pk_bf16_f32 v141, v41, v37
	v_cvt_pk_bf16_f32 v142, v65, v61
	v_cvt_pk_bf16_f32 v143, v57, v53
	ds_write_b128 v224, v[140:143] offset:128
	v_cvt_pk_bf16_f32 v140, v18, v14
	s_bfe_i32 s5, s4, 0x80000
	v_cvt_pk_bf16_f32 v141, v10, v6
	v_cvt_pk_bf16_f32 v142, v34, v30
	v_cvt_pk_bf16_f32 v143, v26, v22
	ds_write_b128 v223, v[140:143] offset:256
	v_cvt_pk_bf16_f32 v140, v50, v46
	s_and_b32 s4, s4, 0xfc
	v_cvt_pk_bf16_f32 v141, v42, v38
	v_cvt_pk_bf16_f32 v142, v66, v62
	v_cvt_pk_bf16_f32 v143, v58, v54
	ds_write_b128 v224, v[140:143] offset:256
	v_cvt_pk_bf16_f32 v140, v19, v15
	s_sub_i32 s3, s3, s4
	v_cvt_pk_bf16_f32 v141, v11, v7
	v_cvt_pk_bf16_f32 v142, v35, v31
	v_cvt_pk_bf16_f32 v143, v27, v23
	ds_write_b128 v223, v[140:143] offset:384
	v_cvt_pk_bf16_f32 v140, v51, v47
	s_sext_i32_i8 s4, s3
	s_ashr_i32 s3, s2, 31
	v_cvt_pk_bf16_f32 v141, v43, v39
	v_cvt_pk_bf16_f32 v142, v67, v63
	v_cvt_pk_bf16_f32 v143, v59, v55
	ds_write_b128 v224, v[140:143] offset:384
	s_lshl_b64 s[2:3], s[2:3], 20
	v_lshl_add_u32 v140, s4, 6, v222
	s_add_u32 s2, s21, s2
	v_ashrrev_i32_e32 v141, 31, v140
	s_sext_i32_i16 s5, s5
	s_addc_u32 s3, s22, s3
	v_lshlrev_b64 v[140:141], 12, v[140:141]
	v_lshl_add_u64 v[140:141], s[2:3], 0, v[140:141]
	s_lshl_b32 s2, s5, 4
	s_andn2_b32 s2, s2, 63
	s_ashr_i32 s3, s2, 31
	v_lshl_add_u64 v[140:141], s[2:3], 1, v[140:141]
	v_lshl_add_u64 v[144:145], v[140:141], 0, v[0:1]
	ds_read_b128 v[140:143], v135
	v_add_co_u32_e32 v146, vcc, s88, v144
	s_mov_b32 s2, 0x18000
	s_nop 0
	v_addc_co_u32_e32 v147, vcc, 0, v145, vcc
	s_waitcnt lgkmcnt(0)
	global_store_dwordx4 v[144:145], v[140:143], off nt
	ds_read_b128 v[140:143], v137
	s_waitcnt lgkmcnt(0)
	global_store_dwordx4 v[146:147], v[140:143], off nt
	ds_read_b128 v[140:143], v136
	v_add_co_u32_e32 v146, vcc, s82, v144
	s_nop 1
	v_addc_co_u32_e32 v147, vcc, 0, v145, vcc
	s_waitcnt lgkmcnt(0)
	global_store_dwordx4 v[146:147], v[140:143], off nt
	ds_read_b128 v[140:143], v138
	v_add_co_u32_e32 v146, vcc, s2, v144
	s_mov_b32 s2, 0x20000
	s_nop 0
	v_addc_co_u32_e32 v147, vcc, 0, v145, vcc
	s_waitcnt lgkmcnt(0)
	global_store_dwordx4 v[146:147], v[140:143], off nt
	ds_read_b128 v[140:143], v135 offset:4096
	v_add_co_u32_e32 v146, vcc, s2, v144
	s_nop 1
	v_addc_co_u32_e32 v147, vcc, 0, v145, vcc
	s_waitcnt lgkmcnt(0)
	global_store_dwordx4 v[146:147], v[140:143], off nt
	ds_read_b128 v[140:143], v134
	v_add_co_u32_e32 v146, vcc, 0x28000, v144
	s_nop 1
	v_addc_co_u32_e32 v147, vcc, 0, v145, vcc
	s_waitcnt lgkmcnt(0)
	global_store_dwordx4 v[146:147], v[140:143], off nt
	ds_read_b128 v[140:143], v133
	v_add_co_u32_e32 v146, vcc, 0x30000, v144
	s_nop 1
	v_addc_co_u32_e32 v147, vcc, 0, v145, vcc
	s_waitcnt lgkmcnt(0)
	global_store_dwordx4 v[146:147], v[140:143], off nt
	ds_read_b128 v[140:143], v132
	v_add_co_u32_e32 v144, vcc, 0x38000, v144
	s_nop 1
	v_addc_co_u32_e32 v145, vcc, 0, v145, vcc
	s_waitcnt lgkmcnt(0)
	global_store_dwordx4 v[144:145], v[140:143], off nt
	s_andn2_b64 vcc, exec, s[0:1]
	s_cbranch_vccnz .LBB0_625
.LBB0_633:
	s_ashr_i32 s0, s7, 31
	s_lshr_b32 s0, s0, 25
	s_add_i32 s1, s7, s0
	s_ashr_i32 s0, s1, 7
	s_and_b32 s1, s1, 0xff80
	v_cvt_pk_bf16_f32 v140, v80, v76
	s_sub_i32 s1, s7, s1
	v_cvt_pk_bf16_f32 v141, v72, v68
	v_cvt_pk_bf16_f32 v142, v96, v92
	v_cvt_pk_bf16_f32 v143, v88, v84
	ds_write_b128 v223, v[140:143]
	v_cvt_pk_bf16_f32 v140, v112, v108
	s_bfe_i32 s2, s1, 0x80000
	v_cvt_pk_bf16_f32 v141, v104, v100
	v_cvt_pk_bf16_f32 v142, v128, v124
	v_cvt_pk_bf16_f32 v143, v120, v116
	ds_write_b128 v224, v[140:143]
	v_cvt_pk_bf16_f32 v140, v81, v77
	s_bfe_u32 s2, s2, 0x2000d
	v_cvt_pk_bf16_f32 v141, v73, v69
	v_cvt_pk_bf16_f32 v142, v97, v93
	v_cvt_pk_bf16_f32 v143, v89, v85
	ds_write_b128 v223, v[140:143] offset:128
	v_cvt_pk_bf16_f32 v140, v113, v109
	s_add_i32 s2, s1, s2
	v_cvt_pk_bf16_f32 v141, v105, v101
	v_cvt_pk_bf16_f32 v142, v129, v125
	v_cvt_pk_bf16_f32 v143, v121, v117
	ds_write_b128 v224, v[140:143] offset:128
	v_cvt_pk_bf16_f32 v140, v82, v78
	s_bfe_i32 s3, s2, 0x80000
	v_cvt_pk_bf16_f32 v141, v74, v70
	v_cvt_pk_bf16_f32 v142, v98, v94
	v_cvt_pk_bf16_f32 v143, v90, v86
	ds_write_b128 v223, v[140:143] offset:256
	v_cvt_pk_bf16_f32 v140, v114, v110
	s_and_b32 s2, s2, 0xfc
	v_cvt_pk_bf16_f32 v141, v106, v102
	v_cvt_pk_bf16_f32 v142, v130, v126
	v_cvt_pk_bf16_f32 v143, v122, v118
	ds_write_b128 v224, v[140:143] offset:256
	v_cvt_pk_bf16_f32 v140, v83, v79
	s_sub_i32 s1, s1, s2
	v_cvt_pk_bf16_f32 v141, v75, v71
	v_cvt_pk_bf16_f32 v142, v99, v95
	v_cvt_pk_bf16_f32 v143, v91, v87
	ds_write_b128 v223, v[140:143] offset:384
	v_cvt_pk_bf16_f32 v140, v115, v111
	s_sext_i32_i8 s2, s1
	s_ashr_i32 s1, s0, 31
	v_cvt_pk_bf16_f32 v141, v107, v103
	v_cvt_pk_bf16_f32 v142, v131, v127
	v_cvt_pk_bf16_f32 v143, v123, v119
	ds_write_b128 v224, v[140:143] offset:384
	s_lshl_b64 s[0:1], s[0:1], 20
	v_lshl_add_u32 v140, s2, 6, v222
	s_add_u32 s0, s21, s0
	v_ashrrev_i32_e32 v141, 31, v140
	s_sext_i32_i16 s3, s3
	s_addc_u32 s1, s22, s1
	v_lshlrev_b64 v[140:141], 12, v[140:141]
	v_lshl_add_u64 v[140:141], s[0:1], 0, v[140:141]
	s_lshl_b32 s0, s3, 4
	s_andn2_b32 s0, s0, 63
	s_ashr_i32 s1, s0, 31
	v_lshl_add_u64 v[140:141], s[0:1], 1, v[140:141]
	v_mov_b32_e32 v1, v3
	v_lshl_add_u64 v[144:145], v[140:141], 0, v[0:1]
	ds_read_b128 v[140:143], v135
	v_add_co_u32_e32 v146, vcc, s88, v144
	s_mov_b32 s0, 0x18000
	s_nop 0
	v_addc_co_u32_e32 v147, vcc, 0, v145, vcc
	s_waitcnt lgkmcnt(0)
	global_store_dwordx4 v[144:145], v[140:143], off nt
	ds_read_b128 v[140:143], v137
	s_waitcnt lgkmcnt(0)
	global_store_dwordx4 v[146:147], v[140:143], off nt
	ds_read_b128 v[140:143], v136
	v_add_co_u32_e32 v136, vcc, s82, v144
	s_nop 1
	v_addc_co_u32_e32 v137, vcc, 0, v145, vcc
	s_waitcnt lgkmcnt(0)
	global_store_dwordx4 v[136:137], v[140:143], off nt
	ds_read_b128 v[136:139], v138
	s_nop 0
	v_add_co_u32_e32 v140, vcc, s0, v144
	s_mov_b32 s0, 0x20000
	s_nop 0
	v_addc_co_u32_e32 v141, vcc, 0, v145, vcc
	s_waitcnt lgkmcnt(0)
	global_store_dwordx4 v[140:141], v[136:139], off nt
	ds_read_b128 v[136:139], v135 offset:4096
	v_add_co_u32_e32 v140, vcc, s0, v144
	s_nop 1
	v_addc_co_u32_e32 v141, vcc, 0, v145, vcc
	s_waitcnt lgkmcnt(0)
	global_store_dwordx4 v[140:141], v[136:139], off nt
	ds_read_b128 v[134:137], v134
	s_nop 0
	v_add_co_u32_e32 v138, vcc, 0x28000, v144
	s_nop 1
	v_addc_co_u32_e32 v139, vcc, 0, v145, vcc
	s_waitcnt lgkmcnt(0)
	global_store_dwordx4 v[138:139], v[134:137], off nt
	ds_read_b128 v[134:137], v133
	v_add_co_u32_e32 v138, vcc, 0x30000, v144
	s_nop 1
	v_addc_co_u32_e32 v139, vcc, 0, v145, vcc
	s_waitcnt lgkmcnt(0)
	global_store_dwordx4 v[138:139], v[134:137], off nt
	ds_read_b128 v[132:135], v132
	s_nop 0
	v_add_co_u32_e32 v136, vcc, 0x38000, v144
	s_nop 1
	v_addc_co_u32_e32 v137, vcc, 0, v145, vcc
	s_waitcnt lgkmcnt(0)
	global_store_dwordx4 v[136:137], v[132:135], off nt
	s_branch .LBB0_625

.LBB0_637:
	s_ashr_i32 s0, s8, 31
	s_lshr_b32 s0, s0, 28
	s_add_i32 s1, s8, s0
	s_ashr_i32 s0, s1, 4
	s_and_b32 s1, s1, 0xfff0
	s_sub_i32 s1, s8, s1
	s_bfe_i32 s2, s1, 0x80000
	s_bfe_u32 s2, s2, 0x2000d
	s_add_i32 s2, s1, s2
	s_bfe_i32 s3, s2, 0x80000
	s_and_b32 s2, s2, 0xfffc
	s_sext_i32_i16 s3, s3
	s_sub_i32 s1, s1, s2
	s_ashr_i32 s23, s3, 2
	s_bfe_i32 s3, s1, 0x80000
	s_sext_i32_i8 s1, s1
	s_lshl_b32 s2, s1, 6
	s_sext_i32_i16 s1, s3
	v_mov_b32_e32 v132, 0
	s_cmp_gt_i32 s1, 0
	v_mov_b32_e32 v133, 0
	v_mov_b32_e32 v134, 0
	v_mov_b32_e32 v135, 0
	v_mov_b32_e32 v136, 0
	v_mov_b32_e32 v137, 0
	v_mov_b32_e32 v138, 0
	v_mov_b32_e32 v139, 0
	v_mov_b32_e32 v140, 0
	v_mov_b32_e32 v141, 0
	v_mov_b32_e32 v142, 0
	v_mov_b32_e32 v143, 0
	v_mov_b32_e32 v144, 0
	v_mov_b32_e32 v145, 0
	v_mov_b32_e32 v146, 0
	v_mov_b32_e32 v147, 0
	v_mov_b32_e32 v148, 0
	v_mov_b32_e32 v149, 0
	v_mov_b32_e32 v150, 0
	v_mov_b32_e32 v151, 0
	v_mov_b32_e32 v152, 0
	v_mov_b32_e32 v153, 0
	v_mov_b32_e32 v154, 0
	v_mov_b32_e32 v155, 0
	v_mov_b32_e32 v156, 0
	v_mov_b32_e32 v157, 0
	v_mov_b32_e32 v158, 0
	v_mov_b32_e32 v159, 0
	v_mov_b32_e32 v160, 0
	v_mov_b32_e32 v161, 0
	v_mov_b32_e32 v162, 0
	v_mov_b32_e32 v163, 0
	v_mov_b32_e32 v164, 0
	v_mov_b32_e32 v165, 0
	v_mov_b32_e32 v166, 0
	v_mov_b32_e32 v167, 0
	v_mov_b32_e32 v168, 0
	v_mov_b32_e32 v169, 0
	v_mov_b32_e32 v170, 0
	v_mov_b32_e32 v171, 0
	v_mov_b32_e32 v172, 0
	v_mov_b32_e32 v173, 0
	v_mov_b32_e32 v174, 0
	v_mov_b32_e32 v175, 0
	v_mov_b32_e32 v176, 0
	v_mov_b32_e32 v177, 0
	v_mov_b32_e32 v178, 0
	v_mov_b32_e32 v179, 0
	v_mov_b32_e32 v180, 0
	v_mov_b32_e32 v181, 0
	v_mov_b32_e32 v182, 0
	v_mov_b32_e32 v183, 0
	v_mov_b32_e32 v184, 0
	v_mov_b32_e32 v185, 0
	v_mov_b32_e32 v186, 0
	v_mov_b32_e32 v187, 0
	v_mov_b32_e32 v188, 0
	v_mov_b32_e32 v189, 0
	v_mov_b32_e32 v190, 0
	v_mov_b32_e32 v191, 0
	v_mov_b32_e32 v192, 0
	v_mov_b32_e32 v193, 0
	v_mov_b32_e32 v194, 0
	v_mov_b32_e32 v195, 0
	s_cbranch_scc1 .LBB0_639
	s_ashr_i32 s1, s0, 31
	s_lshl_b64 s[4:5], s[0:1], 16
	v_readlane_b32 s1, v252, 59
	v_lshl_add_u32 v132, s23, 6, v221
	s_add_u32 s4, s1, s4
	v_readlane_b32 s1, v252, 60
	v_ashrrev_i32_e32 v133, 31, v132
	s_addc_u32 s5, s1, s5
	v_lshlrev_b64 v[132:133], 8, v[132:133]
	v_lshl_add_u64 v[132:133], s[4:5], 0, v[132:133]
	s_ashr_i32 s3, s2, 31
	v_lshl_add_u64 v[132:133], s[2:3], 2, v[132:133]
	v_lshl_add_u64 v[132:133], v[132:133], 0, v[2:3]
	global_load_dwordx4 v[192:195], v[132:133], off nt
	global_load_dwordx4 v[188:191], v[132:133], off offset:256 nt
	global_load_dwordx4 v[184:187], v[132:133], off offset:512 nt
	global_load_dwordx4 v[180:183], v[132:133], off offset:768 nt
	global_load_dwordx4 v[176:179], v[132:133], off offset:1024 nt
	global_load_dwordx4 v[172:175], v[132:133], off offset:1280 nt
	global_load_dwordx4 v[168:171], v[132:133], off offset:1536 nt
	global_load_dwordx4 v[164:167], v[132:133], off offset:1792 nt
	global_load_dwordx4 v[160:163], v[132:133], off offset:2048 nt
	global_load_dwordx4 v[156:159], v[132:133], off offset:2304 nt
	global_load_dwordx4 v[152:155], v[132:133], off offset:2560 nt
	global_load_dwordx4 v[148:151], v[132:133], off offset:2816 nt
	global_load_dwordx4 v[144:147], v[132:133], off offset:3072 nt
	global_load_dwordx4 v[140:143], v[132:133], off offset:3328 nt
	global_load_dwordx4 v[136:139], v[132:133], off offset:3584 nt
	s_nop 0
	global_load_dwordx4 v[132:135], v[132:133], off offset:3840 nt
.LBB0_639:
	s_add_i32 s3, s38, s8
	s_cmp_lt_i32 s3, 32
	s_cselect_b64 s[4:5], -1, 0
	s_cmp_gt_i32 s3, 31
	s_cbranch_scc1 .LBB0_642
	s_ashr_i32 s1, s3, 31
	s_lshr_b32 s1, s1, 28
	s_add_i32 s1, s3, s1
	s_and_b32 s6, s1, 0xfff0
	s_sub_i32 s7, s3, s6
	s_bfe_i32 s6, s7, 0x80000
	s_bfe_u32 s6, s6, 0x2000d
	s_add_i32 s6, s7, s6
	s_and_b32 s14, s6, 0xfc
	s_sub_i32 s7, s7, s14
	s_bfe_i32 s7, s7, 0x80000
	s_sext_i32_i16 s7, s7
	v_mov_b32_e32 v7, 0
	s_cmp_gt_i32 s7, 0
	v_mov_b32_e32 v6, 0
	v_mov_b32_e32 v5, 0
	v_mov_b32_e32 v4, 0
	v_mov_b32_e32 v11, 0
	v_mov_b32_e32 v10, 0
	v_mov_b32_e32 v9, 0
	v_mov_b32_e32 v8, 0
	v_mov_b32_e32 v15, 0
	v_mov_b32_e32 v14, 0
	v_mov_b32_e32 v13, 0
	v_mov_b32_e32 v12, 0
	v_mov_b32_e32 v19, 0
	v_mov_b32_e32 v18, 0
	v_mov_b32_e32 v17, 0
	v_mov_b32_e32 v16, 0
	v_mov_b32_e32 v23, 0
	v_mov_b32_e32 v22, 0
	v_mov_b32_e32 v21, 0
	v_mov_b32_e32 v20, 0
	v_mov_b32_e32 v27, 0
	v_mov_b32_e32 v26, 0
	v_mov_b32_e32 v25, 0
	v_mov_b32_e32 v24, 0
	v_mov_b32_e32 v31, 0
	v_mov_b32_e32 v30, 0
	v_mov_b32_e32 v29, 0
	v_mov_b32_e32 v28, 0
	v_mov_b32_e32 v35, 0
	v_mov_b32_e32 v34, 0
	v_mov_b32_e32 v33, 0
	v_mov_b32_e32 v32, 0
	v_mov_b32_e32 v39, 0
	v_mov_b32_e32 v38, 0
	v_mov_b32_e32 v37, 0
	v_mov_b32_e32 v36, 0
	v_mov_b32_e32 v43, 0
	v_mov_b32_e32 v42, 0
	v_mov_b32_e32 v41, 0
	v_mov_b32_e32 v40, 0
	v_mov_b32_e32 v47, 0
	v_mov_b32_e32 v46, 0
	v_mov_b32_e32 v45, 0
	v_mov_b32_e32 v44, 0
	v_mov_b32_e32 v51, 0
	v_mov_b32_e32 v50, 0
	v_mov_b32_e32 v49, 0
	v_mov_b32_e32 v48, 0
	v_mov_b32_e32 v55, 0
	v_mov_b32_e32 v54, 0
	v_mov_b32_e32 v53, 0
	v_mov_b32_e32 v52, 0
	v_mov_b32_e32 v59, 0
	v_mov_b32_e32 v58, 0
	v_mov_b32_e32 v57, 0
	v_mov_b32_e32 v56, 0
	v_mov_b32_e32 v63, 0
	v_mov_b32_e32 v62, 0
	v_mov_b32_e32 v61, 0
	v_mov_b32_e32 v60, 0
	v_mov_b32_e32 v67, 0
	v_mov_b32_e32 v66, 0
	v_mov_b32_e32 v65, 0
	v_mov_b32_e32 v64, 0
	s_cbranch_scc1 .LBB0_642
	s_bfe_i32 s6, s6, 0x80000
	s_sext_i32_i16 s6, s6
	s_lshr_b32 s14, s6, 2
	s_ashr_i32 s28, s1, 4
	s_lshl_b32 s6, s7, 6
	s_sext_i32_i8 s7, s14
	s_ashr_i32 s29, s28, 31
	s_lshl_b64 s[28:29], s[28:29], 16
	v_readlane_b32 s1, v252, 59
	v_lshl_add_u32 v4, s7, 6, v221
	s_add_u32 s28, s1, s28
	v_readlane_b32 s1, v252, 60
	v_ashrrev_i32_e32 v5, 31, v4
	s_addc_u32 s29, s1, s29
	v_lshlrev_b64 v[4:5], 8, v[4:5]
	v_lshl_add_u64 v[4:5], s[28:29], 0, v[4:5]
	s_ashr_i32 s7, s6, 31
	v_lshl_add_u64 v[4:5], s[6:7], 2, v[4:5]
	v_lshl_add_u64 v[64:65], v[4:5], 0, v[2:3]
	global_load_dwordx4 v[4:7], v[64:65], off nt
	global_load_dwordx4 v[8:11], v[64:65], off offset:256 nt
	global_load_dwordx4 v[12:15], v[64:65], off offset:512 nt
	global_load_dwordx4 v[16:19], v[64:65], off offset:768 nt
	global_load_dwordx4 v[20:23], v[64:65], off offset:1024 nt
	global_load_dwordx4 v[24:27], v[64:65], off offset:1280 nt
	global_load_dwordx4 v[28:31], v[64:65], off offset:1536 nt
	global_load_dwordx4 v[32:35], v[64:65], off offset:1792 nt
	global_load_dwordx4 v[36:39], v[64:65], off offset:2048 nt
	global_load_dwordx4 v[40:43], v[64:65], off offset:2304 nt
	global_load_dwordx4 v[44:47], v[64:65], off offset:2560 nt
	global_load_dwordx4 v[48:51], v[64:65], off offset:2816 nt
	global_load_dwordx4 v[52:55], v[64:65], off offset:3072 nt
	global_load_dwordx4 v[56:59], v[64:65], off offset:3328 nt
	global_load_dwordx4 v[60:63], v[64:65], off offset:3584 nt
	s_nop 0
	global_load_dwordx4 v[64:67], v[64:65], off offset:3840 nt
.LBB0_642:
	s_add_i32 s28, s22, s8
	s_cmp_lt_i32 s28, 32
	s_cselect_b64 s[6:7], -1, 0
	s_cmp_gt_i32 s28, 31
	s_cbranch_scc1 .LBB0_645
	s_ashr_i32 s1, s28, 31
	s_lshr_b32 s1, s1, 28
	s_add_i32 s1, s28, s1
	s_and_b32 s14, s1, 0xfff0
	s_sub_i32 s29, s28, s14
	s_bfe_i32 s14, s29, 0x80000
	s_bfe_u32 s14, s14, 0x2000d
	s_add_i32 s14, s29, s14
	s_and_b32 s30, s14, 0xfc
	s_sub_i32 s29, s29, s30
	s_bfe_i32 s29, s29, 0x80000
	s_sext_i32_i16 s29, s29
	v_mov_b32_e32 v71, 0
	s_cmp_gt_i32 s29, 0
	v_mov_b32_e32 v70, 0
	v_mov_b32_e32 v69, 0
	v_mov_b32_e32 v68, 0
	v_mov_b32_e32 v75, 0
	v_mov_b32_e32 v74, 0
	v_mov_b32_e32 v73, 0
	v_mov_b32_e32 v72, 0
	v_mov_b32_e32 v79, 0
	v_mov_b32_e32 v78, 0
	v_mov_b32_e32 v77, 0
	v_mov_b32_e32 v76, 0
	v_mov_b32_e32 v83, 0
	v_mov_b32_e32 v82, 0
	v_mov_b32_e32 v81, 0
	v_mov_b32_e32 v80, 0
	v_mov_b32_e32 v87, 0
	v_mov_b32_e32 v86, 0
	v_mov_b32_e32 v85, 0
	v_mov_b32_e32 v84, 0
	v_mov_b32_e32 v91, 0
	v_mov_b32_e32 v90, 0
	v_mov_b32_e32 v89, 0
	v_mov_b32_e32 v88, 0
	v_mov_b32_e32 v95, 0
	v_mov_b32_e32 v94, 0
	v_mov_b32_e32 v93, 0
	v_mov_b32_e32 v92, 0
	v_mov_b32_e32 v99, 0
	v_mov_b32_e32 v98, 0
	v_mov_b32_e32 v97, 0
	v_mov_b32_e32 v96, 0
	v_mov_b32_e32 v103, 0
	v_mov_b32_e32 v102, 0
	v_mov_b32_e32 v101, 0
	v_mov_b32_e32 v100, 0
	v_mov_b32_e32 v107, 0
	v_mov_b32_e32 v106, 0
	v_mov_b32_e32 v105, 0
	v_mov_b32_e32 v104, 0
	v_mov_b32_e32 v111, 0
	v_mov_b32_e32 v110, 0
	v_mov_b32_e32 v109, 0
	v_mov_b32_e32 v108, 0
	v_mov_b32_e32 v115, 0
	v_mov_b32_e32 v114, 0
	v_mov_b32_e32 v113, 0
	v_mov_b32_e32 v112, 0
	v_mov_b32_e32 v119, 0
	v_mov_b32_e32 v118, 0
	v_mov_b32_e32 v117, 0
	v_mov_b32_e32 v116, 0
	v_mov_b32_e32 v123, 0
	v_mov_b32_e32 v122, 0
	v_mov_b32_e32 v121, 0
	v_mov_b32_e32 v120, 0
	v_mov_b32_e32 v127, 0
	v_mov_b32_e32 v126, 0
	v_mov_b32_e32 v125, 0
	v_mov_b32_e32 v124, 0
	v_mov_b32_e32 v131, 0
	v_mov_b32_e32 v130, 0
	v_mov_b32_e32 v129, 0
	v_mov_b32_e32 v128, 0
	s_cbranch_scc1 .LBB0_645
	s_bfe_i32 s14, s14, 0x80000
	s_sext_i32_i16 s14, s14
	s_lshr_b32 s14, s14, 2
	s_ashr_i32 s40, s1, 4
	s_sext_i32_i8 s14, s14
	s_ashr_i32 s41, s40, 31
	s_lshl_b32 s36, s29, 6
	s_lshl_b64 s[40:41], s[40:41], 16
	v_readlane_b32 s1, v252, 59
	v_lshl_add_u32 v68, s14, 6, v221
	s_add_u32 s40, s1, s40
	v_readlane_b32 s1, v252, 60
	v_ashrrev_i32_e32 v69, 31, v68
	s_addc_u32 s41, s1, s41
	v_lshlrev_b64 v[68:69], 8, v[68:69]
	v_lshl_add_u64 v[68:69], s[40:41], 0, v[68:69]
	s_ashr_i32 s37, s36, 31
	v_lshl_add_u64 v[68:69], s[36:37], 2, v[68:69]
	v_lshl_add_u64 v[128:129], v[68:69], 0, v[2:3]
	global_load_dwordx4 v[68:71], v[128:129], off nt
	global_load_dwordx4 v[72:75], v[128:129], off offset:256 nt
	global_load_dwordx4 v[76:79], v[128:129], off offset:512 nt
	global_load_dwordx4 v[80:83], v[128:129], off offset:768 nt
	global_load_dwordx4 v[84:87], v[128:129], off offset:1024 nt
	global_load_dwordx4 v[88:91], v[128:129], off offset:1280 nt
	global_load_dwordx4 v[92:95], v[128:129], off offset:1536 nt
	global_load_dwordx4 v[96:99], v[128:129], off offset:1792 nt
	global_load_dwordx4 v[100:103], v[128:129], off offset:2048 nt
	global_load_dwordx4 v[104:107], v[128:129], off offset:2304 nt
	global_load_dwordx4 v[108:111], v[128:129], off offset:2560 nt
	global_load_dwordx4 v[112:115], v[128:129], off offset:2816 nt
	global_load_dwordx4 v[116:119], v[128:129], off offset:3072 nt
	global_load_dwordx4 v[120:123], v[128:129], off offset:3328 nt
	global_load_dwordx4 v[124:127], v[128:129], off offset:3584 nt
	s_nop 0
	global_load_dwordx4 v[128:131], v[128:129], off offset:3840 nt
.LBB0_645:
	s_waitcnt vmcnt(14)
	v_cvt_pk_bf16_f32 v240, v192, v188
	s_waitcnt vmcnt(12)
	v_cvt_pk_bf16_f32 v241, v184, v180
	s_waitcnt vmcnt(10)
	v_cvt_pk_bf16_f32 v242, v176, v172
	s_waitcnt vmcnt(8)
	v_cvt_pk_bf16_f32 v243, v168, v164
	ds_write_b128 v223, v[240:243]
	s_waitcnt vmcnt(6)
	v_cvt_pk_bf16_f32 v240, v160, v156
	s_waitcnt vmcnt(4)
	v_cvt_pk_bf16_f32 v241, v152, v148
	s_waitcnt vmcnt(2)
	v_cvt_pk_bf16_f32 v242, v144, v140
	s_waitcnt vmcnt(0)
	v_cvt_pk_bf16_f32 v243, v136, v132
	ds_write_b128 v224, v[240:243]
	v_cvt_pk_bf16_f32 v240, v193, v189
	v_cvt_pk_bf16_f32 v241, v185, v181
	v_cvt_pk_bf16_f32 v242, v177, v173
	v_cvt_pk_bf16_f32 v243, v169, v165
	ds_write_b128 v223, v[240:243] offset:128
	v_cvt_pk_bf16_f32 v240, v161, v157
	v_cvt_pk_bf16_f32 v241, v153, v149
	v_cvt_pk_bf16_f32 v242, v145, v141
	v_cvt_pk_bf16_f32 v243, v137, v133
	ds_write_b128 v224, v[240:243] offset:128
	v_cvt_pk_bf16_f32 v240, v194, v190
	v_cvt_pk_bf16_f32 v241, v186, v182
	v_cvt_pk_bf16_f32 v242, v178, v174
	v_cvt_pk_bf16_f32 v243, v170, v166
	ds_write_b128 v223, v[240:243] offset:256
	v_cvt_pk_bf16_f32 v240, v162, v158
	v_cvt_pk_bf16_f32 v241, v154, v150
	v_cvt_pk_bf16_f32 v242, v146, v142
	v_cvt_pk_bf16_f32 v243, v138, v134
	ds_write_b128 v224, v[240:243] offset:256
	v_cvt_pk_bf16_f32 v164, v195, v191
	v_cvt_pk_bf16_f32 v165, v187, v183
	v_cvt_pk_bf16_f32 v166, v179, v175
	v_cvt_pk_bf16_f32 v167, v171, v167
	ds_write_b128 v223, v[164:167] offset:384
	v_cvt_pk_bf16_f32 v132, v163, v159
	s_ashr_i32 s1, s0, 31
	v_cvt_pk_bf16_f32 v133, v155, v151
	v_cvt_pk_bf16_f32 v134, v147, v143
	v_cvt_pk_bf16_f32 v135, v139, v135
	ds_write_b128 v224, v[132:135] offset:384
	s_lshl_b64 s[0:1], s[0:1], 17
	v_add_u32_e32 v132, s2, v222
	s_add_u32 s0, s9, s0
	v_ashrrev_i32_e32 v133, 31, v132
	v_add_u32_e32 v135, v225, v226
	s_addc_u32 s1, s21, s1
	v_lshlrev_b64 v[132:133], 9, v[132:133]
	ds_read_b128 v[136:139], v135
	ds_read_b128 v[140:143], v135 offset:4096
	v_lshl_add_u64 v[132:133], s[0:1], 0, v[132:133]
	s_lshl_b32 s0, s23, 6
	s_ashr_i32 s1, s0, 31
	v_lshl_add_u64 v[132:133], s[0:1], 1, v[132:133]
	v_mov_b32_e32 v1, v3
	v_lshl_add_u64 v[152:153], v[132:133], 0, v[0:1]
	s_waitcnt lgkmcnt(1)
	global_store_dwordx4 v[152:153], v[136:139], off nt
	v_add_co_u32_e32 v132, vcc, s83, v152
	s_nop 0
	v_add_u32_e32 v137, v227, v228
	v_add_u32_e32 v136, v229, v230
	ds_read_b128 v[144:147], v137
	ds_read_b128 v[148:151], v136
	v_addc_co_u32_e32 v133, vcc, 0, v153, vcc
	s_waitcnt lgkmcnt(1)
	global_store_dwordx4 v[132:133], v[144:147], off offset:-4096 nt
	s_waitcnt lgkmcnt(0)
	global_store_dwordx4 v[132:133], v[148:151], off nt
	v_add_u32_e32 v138, v231, v232
	ds_read_b128 v[144:147], v138
	v_add_u32_e32 v134, v233, v234
	ds_read_b128 v[148:151], v134
	v_add_co_u32_e32 v132, vcc, s62, v152
	s_nop 1
	v_addc_co_u32_e32 v133, vcc, 0, v153, vcc
	s_waitcnt lgkmcnt(1)
	global_store_dwordx4 v[132:133], v[144:147], off offset:-4096 nt
	global_store_dwordx4 v[132:133], v[140:143], off nt
	v_add_co_u32_e32 v132, vcc, 0x5000, v152
	s_nop 1
	v_addc_co_u32_e32 v133, vcc, 0, v153, vcc
	s_waitcnt lgkmcnt(0)
	global_store_dwordx4 v[132:133], v[148:151], off nt
	v_add_u32_e32 v133, v235, v236
	ds_read_b128 v[140:143], v133
	v_add_u32_e32 v132, v237, v238
	v_add_co_u32_e32 v148, vcc, 0x6000, v152
	ds_read_b128 v[144:147], v132
	s_nop 0
	v_addc_co_u32_e32 v149, vcc, 0, v153, vcc
	s_waitcnt lgkmcnt(1)
	global_store_dwordx4 v[148:149], v[140:143], off nt
	s_nop 1
	v_add_co_u32_e32 v140, vcc, 0x7000, v152
	s_nop 1
	v_addc_co_u32_e32 v141, vcc, 0, v153, vcc
	s_andn2_b64 vcc, exec, s[4:5]
	s_waitcnt lgkmcnt(0)
	global_store_dwordx4 v[140:141], v[144:147], off nt
	s_cbranch_vccz .LBB0_647
	s_andn2_b64 vcc, exec, s[6:7]
	s_cbranch_vccnz .LBB0_636
	s_branch .LBB0_648
.LBB0_647:
	s_ashr_i32 s0, s3, 31
	s_lshr_b32 s0, s0, 28
	s_add_i32 s1, s3, s0
	s_ashr_i32 s0, s1, 4
	s_and_b32 s1, s1, 0xfff0
	v_cvt_pk_bf16_f32 v140, v4, v8
	s_sub_i32 s1, s3, s1
	v_cvt_pk_bf16_f32 v141, v12, v16
	v_cvt_pk_bf16_f32 v142, v20, v24
	v_cvt_pk_bf16_f32 v143, v28, v32
	ds_write_b128 v223, v[140:143]
	v_cvt_pk_bf16_f32 v140, v36, v40
	s_bfe_i32 s2, s1, 0x80000
	v_cvt_pk_bf16_f32 v141, v44, v48
	v_cvt_pk_bf16_f32 v142, v52, v56
	v_cvt_pk_bf16_f32 v143, v60, v64
	ds_write_b128 v224, v[140:143]
	v_cvt_pk_bf16_f32 v140, v5, v9
	s_bfe_u32 s2, s2, 0x2000d
	v_cvt_pk_bf16_f32 v141, v13, v17
	v_cvt_pk_bf16_f32 v142, v21, v25
	v_cvt_pk_bf16_f32 v143, v29, v33
	ds_write_b128 v223, v[140:143] offset:128
	v_cvt_pk_bf16_f32 v140, v37, v41
	s_add_i32 s2, s1, s2
	v_cvt_pk_bf16_f32 v141, v45, v49
	v_cvt_pk_bf16_f32 v142, v53, v57
	v_cvt_pk_bf16_f32 v143, v61, v65
	ds_write_b128 v224, v[140:143] offset:128
	v_cvt_pk_bf16_f32 v140, v6, v10
	s_bfe_i32 s3, s2, 0x80000
	s_and_b32 s2, s2, 0xfc
	v_cvt_pk_bf16_f32 v141, v14, v18
	v_cvt_pk_bf16_f32 v142, v22, v26
	v_cvt_pk_bf16_f32 v143, v30, v34
	ds_write_b128 v223, v[140:143] offset:256
	v_cvt_pk_bf16_f32 v140, v38, v42
	s_sub_i32 s1, s1, s2
	v_cvt_pk_bf16_f32 v141, v46, v50
	v_cvt_pk_bf16_f32 v142, v54, v58
	v_cvt_pk_bf16_f32 v143, v62, v66
	ds_write_b128 v224, v[140:143] offset:256
	v_cvt_pk_bf16_f32 v140, v7, v11
	v_cvt_pk_bf16_f32 v141, v15, v19
	v_cvt_pk_bf16_f32 v142, v23, v27
	v_cvt_pk_bf16_f32 v143, v31, v35
	ds_write_b128 v223, v[140:143] offset:384
	v_cvt_pk_bf16_f32 v140, v39, v43
	s_sext_i32_i8 s2, s1
	s_ashr_i32 s1, s0, 31
	v_cvt_pk_bf16_f32 v141, v47, v51
	v_cvt_pk_bf16_f32 v142, v55, v59
	v_cvt_pk_bf16_f32 v143, v63, v67
	ds_write_b128 v224, v[140:143] offset:384
	s_lshl_b64 s[0:1], s[0:1], 17
	v_lshl_add_u32 v140, s2, 6, v222
	s_add_u32 s0, s9, s0
	v_ashrrev_i32_e32 v141, 31, v140
	s_sext_i32_i16 s3, s3
	s_addc_u32 s1, s21, s1
	v_lshlrev_b64 v[140:141], 9, v[140:141]
	v_lshl_add_u64 v[140:141], s[0:1], 0, v[140:141]
	s_lshl_b32 s0, s3, 4
	s_andn2_b32 s0, s0, 63
	s_ashr_i32 s1, s0, 31
	v_lshl_add_u64 v[140:141], s[0:1], 1, v[140:141]
	v_lshl_add_u64 v[144:145], v[140:141], 0, v[0:1]
	ds_read_b128 v[140:143], v135
	v_add_co_u32_e32 v146, vcc, s83, v144
	s_waitcnt lgkmcnt(0)
	global_store_dwordx4 v[144:145], v[140:143], off nt
	ds_read_b128 v[140:143], v137
	v_addc_co_u32_e32 v147, vcc, 0, v145, vcc
	s_waitcnt lgkmcnt(0)
	global_store_dwordx4 v[146:147], v[140:143], off offset:-4096 nt
	ds_read_b128 v[140:143], v136
	s_waitcnt lgkmcnt(0)
	global_store_dwordx4 v[146:147], v[140:143], off nt
	ds_read_b128 v[140:143], v138
	v_add_co_u32_e32 v146, vcc, 0x3000, v144
	s_nop 1
	v_addc_co_u32_e32 v147, vcc, 0, v145, vcc
	s_waitcnt lgkmcnt(0)
	global_store_dwordx4 v[146:147], v[140:143], off nt
	ds_read_b128 v[140:143], v135 offset:4096
	v_add_co_u32_e32 v146, vcc, s62, v144
	s_nop 1
	v_addc_co_u32_e32 v147, vcc, 0, v145, vcc
	s_waitcnt lgkmcnt(0)
	global_store_dwordx4 v[146:147], v[140:143], off nt
	ds_read_b128 v[140:143], v134
	v_add_co_u32_e32 v146, vcc, 0x5000, v144
	s_nop 1
	v_addc_co_u32_e32 v147, vcc, 0, v145, vcc
	s_waitcnt lgkmcnt(0)
	global_store_dwordx4 v[146:147], v[140:143], off nt
	ds_read_b128 v[140:143], v133
	v_add_co_u32_e32 v146, vcc, 0x6000, v144
	s_nop 1
	v_addc_co_u32_e32 v147, vcc, 0, v145, vcc
	s_waitcnt lgkmcnt(0)
	global_store_dwordx4 v[146:147], v[140:143], off nt
	ds_read_b128 v[140:143], v132
	v_add_co_u32_e32 v144, vcc, 0x7000, v144
	s_nop 1
	v_addc_co_u32_e32 v145, vcc, 0, v145, vcc
	s_waitcnt lgkmcnt(0)
	global_store_dwordx4 v[144:145], v[140:143], off nt
	s_andn2_b64 vcc, exec, s[6:7]
	s_cbranch_vccnz .LBB0_636
.LBB0_648:
	s_ashr_i32 s0, s28, 31
	s_lshr_b32 s0, s0, 28
	s_add_i32 s1, s28, s0
	s_ashr_i32 s0, s1, 4
	s_and_b32 s1, s1, 0xfff0
	v_cvt_pk_bf16_f32 v140, v68, v72
	s_sub_i32 s1, s28, s1
	v_cvt_pk_bf16_f32 v141, v76, v80
	v_cvt_pk_bf16_f32 v142, v84, v88
	v_cvt_pk_bf16_f32 v143, v92, v96
	ds_write_b128 v223, v[140:143]
	v_cvt_pk_bf16_f32 v140, v100, v104
	s_bfe_i32 s2, s1, 0x80000
	v_cvt_pk_bf16_f32 v141, v108, v112
	v_cvt_pk_bf16_f32 v142, v116, v120
	v_cvt_pk_bf16_f32 v143, v124, v128
	ds_write_b128 v224, v[140:143]
	v_cvt_pk_bf16_f32 v140, v69, v73
	s_bfe_u32 s2, s2, 0x2000d
	v_cvt_pk_bf16_f32 v141, v77, v81
	v_cvt_pk_bf16_f32 v142, v85, v89
	v_cvt_pk_bf16_f32 v143, v93, v97
	ds_write_b128 v223, v[140:143] offset:128
	v_cvt_pk_bf16_f32 v140, v101, v105
	s_add_i32 s2, s1, s2
	v_cvt_pk_bf16_f32 v141, v109, v113
	v_cvt_pk_bf16_f32 v142, v117, v121
	v_cvt_pk_bf16_f32 v143, v125, v129
	ds_write_b128 v224, v[140:143] offset:128
	v_cvt_pk_bf16_f32 v140, v70, v74
	s_bfe_i32 s3, s2, 0x80000
	s_and_b32 s2, s2, 0xfc
	v_cvt_pk_bf16_f32 v141, v78, v82
	v_cvt_pk_bf16_f32 v142, v86, v90
	v_cvt_pk_bf16_f32 v143, v94, v98
	ds_write_b128 v223, v[140:143] offset:256
	v_cvt_pk_bf16_f32 v140, v102, v106
	s_sub_i32 s1, s1, s2
	v_cvt_pk_bf16_f32 v141, v110, v114
	v_cvt_pk_bf16_f32 v142, v118, v122
	v_cvt_pk_bf16_f32 v143, v126, v130
	ds_write_b128 v224, v[140:143] offset:256
	v_cvt_pk_bf16_f32 v140, v71, v75
	v_cvt_pk_bf16_f32 v141, v79, v83
	v_cvt_pk_bf16_f32 v142, v87, v91
	v_cvt_pk_bf16_f32 v143, v95, v99
	ds_write_b128 v223, v[140:143] offset:384
	v_cvt_pk_bf16_f32 v140, v103, v107
	s_sext_i32_i8 s2, s1
	s_ashr_i32 s1, s0, 31
	v_cvt_pk_bf16_f32 v141, v111, v115
	v_cvt_pk_bf16_f32 v142, v119, v123
	v_cvt_pk_bf16_f32 v143, v127, v131
	ds_write_b128 v224, v[140:143] offset:384
	s_lshl_b64 s[0:1], s[0:1], 17
	v_lshl_add_u32 v140, s2, 6, v222
	s_add_u32 s0, s9, s0
	v_ashrrev_i32_e32 v141, 31, v140
	s_sext_i32_i16 s3, s3
	s_addc_u32 s1, s21, s1
	v_lshlrev_b64 v[140:141], 9, v[140:141]
	v_lshl_add_u64 v[140:141], s[0:1], 0, v[140:141]
	s_lshl_b32 s0, s3, 4
	s_andn2_b32 s0, s0, 63
	s_ashr_i32 s1, s0, 31
	v_lshl_add_u64 v[140:141], s[0:1], 1, v[140:141]
	v_mov_b32_e32 v1, v3
	v_lshl_add_u64 v[144:145], v[140:141], 0, v[0:1]
	ds_read_b128 v[140:143], v135
	v_add_co_u32_e32 v146, vcc, s83, v144
	s_waitcnt lgkmcnt(0)
	global_store_dwordx4 v[144:145], v[140:143], off nt
	ds_read_b128 v[140:143], v137
	v_addc_co_u32_e32 v147, vcc, 0, v145, vcc
	s_waitcnt lgkmcnt(0)
	global_store_dwordx4 v[146:147], v[140:143], off offset:-4096 nt
	ds_read_b128 v[140:143], v136
	ds_read_b128 v[136:139], v138
	s_waitcnt lgkmcnt(1)
	global_store_dwordx4 v[146:147], v[140:143], off nt
	s_nop 1
	v_add_co_u32_e32 v140, vcc, 0x3000, v144
	s_nop 1
	v_addc_co_u32_e32 v141, vcc, 0, v145, vcc
	s_waitcnt lgkmcnt(0)
	global_store_dwordx4 v[140:141], v[136:139], off nt
	ds_read_b128 v[136:139], v135 offset:4096
	v_add_co_u32_e32 v140, vcc, s62, v144
	s_nop 1
	v_addc_co_u32_e32 v141, vcc, 0, v145, vcc
	s_waitcnt lgkmcnt(0)
	global_store_dwordx4 v[140:141], v[136:139], off nt
	ds_read_b128 v[134:137], v134
	s_nop 0
	v_add_co_u32_e32 v138, vcc, 0x5000, v144
	s_nop 1
	v_addc_co_u32_e32 v139, vcc, 0, v145, vcc
	s_waitcnt lgkmcnt(0)
	global_store_dwordx4 v[138:139], v[134:137], off nt
	ds_read_b128 v[134:137], v133
	v_add_co_u32_e32 v138, vcc, 0x6000, v144
	s_nop 1
	v_addc_co_u32_e32 v139, vcc, 0, v145, vcc
	s_waitcnt lgkmcnt(0)
	global_store_dwordx4 v[138:139], v[134:137], off nt
	ds_read_b128 v[132:135], v132
	s_nop 0
	v_add_co_u32_e32 v136, vcc, 0x7000, v144
	s_nop 1
	v_addc_co_u32_e32 v137, vcc, 0, v145, vcc
	s_waitcnt lgkmcnt(0)
	global_store_dwordx4 v[136:137], v[132:135], off nt
	s_branch .LBB0_636

.LBB0_652:
	s_add_i32 s29, s38, s21
	s_cmpk_lt_i32 s29, 0x180
	s_cselect_b64 s[2:3], -1, 0
	s_ashr_i32 s0, s21, 31
	s_lshr_b32 s0, s0, 25
	s_add_i32 s0, s21, s0
	s_ashr_i32 s4, s0, 7
	s_and_b32 s0, s0, 0xff80
	s_sub_i32 s0, s21, s0
	s_bfe_i32 s1, s0, 0x80000
	s_bfe_u32 s1, s1, 0x4000b
	s_add_i32 s1, s0, s1
	s_bfe_i32 s5, s1, 0x80000
	s_and_b32 s1, s1, 0xf0
	s_sub_i32 s0, s0, s1
	s_sext_i32_i16 s6, s5
	s_sext_i32_i8 s0, s0
	s_ashr_i32 s5, s4, 31
	s_lshl_b32 s8, s0, 6
	s_lshl_b64 s[0:1], s[4:5], 21
	v_readlane_b32 s7, v252, 61
	s_add_u32 s0, s7, s0
	v_readlane_b32 s7, v252, 62
	s_addc_u32 s1, s7, s1
	s_lshl_b32 s6, s6, 2
	s_andn2_b32 s6, s6, 63
	v_add_u32_e32 v132, s6, v221
	v_ashrrev_i32_e32 v133, 31, v132
	v_lshlrev_b64 v[132:133], 12, v[132:133]
	s_ashr_i32 s9, s8, 31
	v_lshl_add_u64 v[132:133], s[0:1], 0, v[132:133]
	v_lshl_add_u64 v[132:133], s[8:9], 2, v[132:133]
	v_lshl_add_u64 v[188:189], v[132:133], 0, v[2:3]
	v_add_co_u32_e32 v132, vcc, s83, v188
	s_cmpk_gt_i32 s29, 0x17f
	s_nop 0
	v_addc_co_u32_e32 v133, vcc, 0, v189, vcc
	v_add_co_u32_e32 v140, vcc, s62, v188
	global_load_dwordx4 v[136:139], v[132:133], off offset:-4096 nt
	s_nop 0
	global_load_dwordx4 v[132:135], v[132:133], off nt
	v_addc_co_u32_e32 v141, vcc, 0, v189, vcc
	v_add_co_u32_e32 v148, vcc, s77, v188
	global_load_dwordx4 v[144:147], v[140:141], off offset:-4096 nt
	s_nop 0
	global_load_dwordx4 v[140:143], v[140:141], off nt
	v_addc_co_u32_e32 v149, vcc, 0, v189, vcc
	v_add_co_u32_e32 v152, vcc, s88, v188
	global_load_dwordx4 v[156:159], v[148:149], off offset:-4096 nt
	s_nop 0
	global_load_dwordx4 v[148:151], v[148:149], off nt
	v_addc_co_u32_e32 v153, vcc, 0, v189, vcc
	v_add_co_u32_e32 v160, vcc, s72, v188
	global_load_dwordx4 v[164:167], v[152:153], off offset:-4096 nt
	s_nop 0
	global_load_dwordx4 v[152:155], v[152:153], off nt
	v_addc_co_u32_e32 v161, vcc, 0, v189, vcc
	v_add_co_u32_e32 v172, vcc, 0xb000, v188
	global_load_dwordx4 v[168:171], v[160:161], off offset:-4096 nt
	s_nop 0
	global_load_dwordx4 v[160:163], v[160:161], off nt
	v_addc_co_u32_e32 v173, vcc, 0, v189, vcc
	v_add_co_u32_e32 v176, vcc, s66, v188
	global_load_dwordx4 v[184:187], v[188:189], off nt
	s_nop 0
	global_load_dwordx4 v[172:175], v[172:173], off nt
	v_addc_co_u32_e32 v177, vcc, 0, v189, vcc
	v_add_co_u32_e32 v180, vcc, 0xd000, v188
	s_nop 1
	v_addc_co_u32_e32 v181, vcc, 0, v189, vcc
	v_add_co_u32_e32 v190, vcc, 0xe000, v188
	global_load_dwordx4 v[176:179], v[176:177], off nt
	s_nop 0
	global_load_dwordx4 v[180:183], v[180:181], off nt
	v_addc_co_u32_e32 v191, vcc, 0, v189, vcc
	v_add_co_u32_e32 v192, vcc, 0xf000, v188
	s_nop 1
	v_addc_co_u32_e32 v193, vcc, 0, v189, vcc
	global_load_dwordx4 v[188:191], v[190:191], off nt
	s_nop 0
	global_load_dwordx4 v[192:195], v[192:193], off nt
	s_cbranch_scc1 .LBB0_654
	s_ashr_i32 s0, s29, 31
	s_lshr_b32 s0, s0, 25
	s_add_i32 s1, s29, s0
	s_and_b32 s0, s1, 0x80
	s_sub_i32 s0, s29, s0
	s_bfe_i32 s7, s0, 0x80000
	s_bfe_u32 s7, s7, 0x4000b
	s_add_i32 s7, s0, s7
	s_bfe_i32 s9, s7, 0x80000
	s_and_b32 s7, s7, 0xf0
	s_sub_i32 s0, s0, s7
	s_ashr_i32 s36, s1, 7
	s_sext_i32_i8 s0, s0
	s_ashr_i32 s37, s36, 31
	s_lshl_b32 s0, s0, 6
	s_lshl_b64 s[36:37], s[36:37], 21
	v_readlane_b32 s1, v252, 61
	s_sext_i32_i16 s9, s9
	s_add_u32 s36, s1, s36
	v_readlane_b32 s1, v252, 62
	s_addc_u32 s37, s1, s37
	s_lshl_b32 s1, s9, 2
	s_andn2_b32 s1, s1, 63
	v_add_u32_e32 v4, s1, v221
	v_ashrrev_i32_e32 v5, 31, v4
	v_lshlrev_b64 v[4:5], 12, v[4:5]
	v_lshl_add_u64 v[4:5], s[36:37], 0, v[4:5]
	s_ashr_i32 s1, s0, 31
	v_lshl_add_u64 v[4:5], s[0:1], 2, v[4:5]
	v_lshl_add_u64 v[108:109], v[4:5], 0, v[2:3]
	v_add_co_u32_e32 v4, vcc, s83, v108
	s_nop 1
	v_addc_co_u32_e32 v5, vcc, 0, v109, vcc
	v_add_co_u32_e32 v12, vcc, s62, v108
	global_load_dwordx4 v[8:11], v[4:5], off offset:-4096 nt
	s_nop 0
	global_load_dwordx4 v[4:7], v[4:5], off nt
	v_addc_co_u32_e32 v13, vcc, 0, v109, vcc
	v_add_co_u32_e32 v20, vcc, s77, v108
	global_load_dwordx4 v[16:19], v[12:13], off offset:-4096 nt
	s_nop 0
	global_load_dwordx4 v[12:15], v[12:13], off nt
	v_addc_co_u32_e32 v21, vcc, 0, v109, vcc
	v_add_co_u32_e32 v28, vcc, s88, v108
	global_load_dwordx4 v[24:27], v[20:21], off offset:-4096 nt
	s_nop 0
	global_load_dwordx4 v[20:23], v[20:21], off nt
	v_addc_co_u32_e32 v29, vcc, 0, v109, vcc
	v_add_co_u32_e32 v52, vcc, 0x9000, v108
	global_load_dwordx4 v[32:35], v[28:29], off offset:-4096 nt
	s_nop 0
	global_load_dwordx4 v[28:31], v[28:29], off nt
	v_addc_co_u32_e32 v53, vcc, 0, v109, vcc
	v_add_co_u32_e32 v68, vcc, s72, v108
	global_load_dwordx4 v[64:67], v[108:109], off nt
	s_nop 0
	global_load_dwordx4 v[52:55], v[52:53], off nt
	v_addc_co_u32_e32 v69, vcc, 0, v109, vcc
	v_add_co_u32_e32 v80, vcc, 0xb000, v108
	s_nop 1
	v_addc_co_u32_e32 v81, vcc, 0, v109, vcc
	v_add_co_u32_e32 v88, vcc, 0xc000, v108
	global_load_dwordx4 v[68:71], v[68:69], off nt
	s_nop 0
	global_load_dwordx4 v[80:83], v[80:81], off nt
	v_addc_co_u32_e32 v89, vcc, 0, v109, vcc
	v_add_co_u32_e32 v96, vcc, 0xd000, v108
	s_nop 1
	v_addc_co_u32_e32 v97, vcc, 0, v109, vcc
	v_add_co_u32_e32 v110, vcc, 0xe000, v108
	global_load_dwordx4 v[88:91], v[88:89], off nt
	s_nop 0
	global_load_dwordx4 v[96:99], v[96:97], off nt
	v_addc_co_u32_e32 v111, vcc, 0, v109, vcc
	v_add_co_u32_e32 v112, vcc, 0xf000, v108
	s_nop 1
	v_addc_co_u32_e32 v113, vcc, 0, v109, vcc
	global_load_dwordx4 v[108:111], v[110:111], off nt
	s_nop 0
	global_load_dwordx4 v[112:115], v[112:113], off nt
.LBB0_654:
	s_add_i32 s9, s28, s21
	s_cmpk_lt_i32 s9, 0x180
	s_cselect_b64 s[0:1], -1, 0
	s_cmpk_gt_i32 s9, 0x17f
	s_cbranch_scc1 .LBB0_656
	s_ashr_i32 s7, s9, 31
	s_lshr_b32 s7, s7, 25
	s_add_i32 s7, s9, s7
	s_and_b32 s14, s7, 0x80
	s_sub_i32 s14, s9, s14
	s_bfe_i32 s30, s14, 0x80000
	s_bfe_u32 s30, s30, 0x4000b
	s_add_i32 s30, s14, s30
	s_bfe_i32 s35, s30, 0x80000
	s_and_b32 s30, s30, 0xf0
	s_sub_i32 s14, s14, s30
	s_ashr_i32 s40, s7, 7
	s_sext_i32_i8 s14, s14
	s_ashr_i32 s41, s40, 31
	s_lshl_b32 s36, s14, 6
	s_lshl_b64 s[40:41], s[40:41], 21
	v_readlane_b32 s7, v252, 61
	s_sext_i32_i16 s35, s35
	s_add_u32 s40, s7, s40
	v_readlane_b32 s7, v252, 62
	s_addc_u32 s41, s7, s41
	s_lshl_b32 s7, s35, 2
	s_andn2_b32 s7, s7, 63
	v_add_u32_e32 v36, s7, v221
	v_ashrrev_i32_e32 v37, 31, v36
	v_lshlrev_b64 v[36:37], 12, v[36:37]
	v_lshl_add_u64 v[36:37], s[40:41], 0, v[36:37]
	s_ashr_i32 s37, s36, 31
	v_lshl_add_u64 v[36:37], s[36:37], 2, v[36:37]
	v_lshl_add_u64 v[124:125], v[36:37], 0, v[2:3]
	v_add_co_u32_e32 v36, vcc, s83, v124
	s_nop 1
	v_addc_co_u32_e32 v37, vcc, 0, v125, vcc
	v_add_co_u32_e32 v44, vcc, s62, v124
	global_load_dwordx4 v[40:43], v[36:37], off offset:-4096 nt
	s_nop 0
	global_load_dwordx4 v[36:39], v[36:37], off nt
	v_addc_co_u32_e32 v45, vcc, 0, v125, vcc
	v_add_co_u32_e32 v56, vcc, s77, v124
	global_load_dwordx4 v[48:51], v[44:45], off offset:-4096 nt
	s_nop 0
	global_load_dwordx4 v[44:47], v[44:45], off nt
	v_addc_co_u32_e32 v57, vcc, 0, v125, vcc
	v_add_co_u32_e32 v72, vcc, s88, v124
	global_load_dwordx4 v[60:63], v[56:57], off offset:-4096 nt
	s_nop 0
	global_load_dwordx4 v[56:59], v[56:57], off nt
	v_addc_co_u32_e32 v73, vcc, 0, v125, vcc
	v_add_co_u32_e32 v84, vcc, 0x9000, v124
	global_load_dwordx4 v[76:79], v[72:73], off offset:-4096 nt
	s_nop 0
	global_load_dwordx4 v[72:75], v[72:73], off nt
	v_addc_co_u32_e32 v85, vcc, 0, v125, vcc
	v_add_co_u32_e32 v100, vcc, s72, v124
	global_load_dwordx4 v[92:95], v[124:125], off nt
	s_nop 0
	global_load_dwordx4 v[84:87], v[84:85], off nt
	v_addc_co_u32_e32 v101, vcc, 0, v125, vcc
	v_add_co_u32_e32 v104, vcc, 0xb000, v124
	s_nop 1
	v_addc_co_u32_e32 v105, vcc, 0, v125, vcc
	v_add_co_u32_e32 v116, vcc, 0xc000, v124
	global_load_dwordx4 v[100:103], v[100:101], off nt
	s_nop 0
	global_load_dwordx4 v[104:107], v[104:105], off nt
	v_addc_co_u32_e32 v117, vcc, 0, v125, vcc
	v_add_co_u32_e32 v120, vcc, 0xd000, v124
	s_nop 1
	v_addc_co_u32_e32 v121, vcc, 0, v125, vcc
	v_add_co_u32_e32 v126, vcc, 0xe000, v124
	global_load_dwordx4 v[116:119], v[116:117], off nt
	s_nop 0
	global_load_dwordx4 v[120:123], v[120:121], off nt
	v_addc_co_u32_e32 v127, vcc, 0, v125, vcc
	v_add_co_u32_e32 v128, vcc, 0xf000, v124
	s_nop 1
	v_addc_co_u32_e32 v129, vcc, 0, v125, vcc
	global_load_dwordx4 v[124:127], v[126:127], off nt
	s_nop 0
	global_load_dwordx4 v[128:131], v[128:129], off nt
.LBB0_656:
	s_waitcnt vmcnt(5)
	v_cvt_pk_bf16_f32 v240, v184, v136
	v_cvt_pk_bf16_f32 v241, v132, v144
	v_cvt_pk_bf16_f32 v242, v140, v156
	v_cvt_pk_bf16_f32 v243, v148, v164
	ds_write_b128 v223, v[240:243]
	v_cvt_pk_bf16_f32 v240, v152, v168
	s_waitcnt vmcnt(4)
	v_cvt_pk_bf16_f32 v241, v160, v172
	s_waitcnt vmcnt(2)
	v_cvt_pk_bf16_f32 v242, v176, v180
	s_waitcnt vmcnt(0)
	v_cvt_pk_bf16_f32 v243, v188, v192
	ds_write_b128 v224, v[240:243]
	v_cvt_pk_bf16_f32 v240, v185, v137
	v_cvt_pk_bf16_f32 v241, v133, v145
	v_cvt_pk_bf16_f32 v242, v141, v157
	v_cvt_pk_bf16_f32 v243, v149, v165
	ds_write_b128 v223, v[240:243] offset:128
	v_cvt_pk_bf16_f32 v240, v153, v169
	v_cvt_pk_bf16_f32 v241, v161, v173
	v_cvt_pk_bf16_f32 v242, v177, v181
	v_cvt_pk_bf16_f32 v243, v189, v193
	ds_write_b128 v224, v[240:243] offset:128
	v_cvt_pk_bf16_f32 v240, v186, v138
	v_cvt_pk_bf16_f32 v241, v134, v146
	v_cvt_pk_bf16_f32 v242, v142, v158
	v_cvt_pk_bf16_f32 v243, v150, v166
	ds_write_b128 v223, v[240:243] offset:256
	v_cvt_pk_bf16_f32 v240, v154, v170
	v_cvt_pk_bf16_f32 v241, v162, v174
	v_cvt_pk_bf16_f32 v242, v178, v182
	v_cvt_pk_bf16_f32 v243, v190, v194
	ds_write_b128 v224, v[240:243] offset:256
	v_cvt_pk_bf16_f32 v132, v187, v139
	v_cvt_pk_bf16_f32 v133, v135, v147
	v_cvt_pk_bf16_f32 v134, v143, v159
	v_cvt_pk_bf16_f32 v135, v151, v167
	ds_write_b128 v223, v[132:135] offset:384
	v_cvt_pk_bf16_f32 v132, v155, v171
	v_cvt_pk_bf16_f32 v133, v163, v175
	v_cvt_pk_bf16_f32 v134, v179, v183
	v_cvt_pk_bf16_f32 v135, v191, v195
	s_lshl_b64 s[4:5], s[4:5], 10
	ds_write_b128 v224, v[132:135] offset:384
	s_add_u32 s4, s22, s4
	v_add_u32_e32 v135, v225, v226
	s_addc_u32 s5, s23, s5
	ds_read_b128 v[136:139], v135
	v_add_u32_e32 v1, s8, v222
	v_mov_b64_e32 v[132:133], s[4:5]
	v_mad_i64_i32 v[132:133], s[4:5], v1, s16, v[132:133]
	s_ashr_i32 s7, s6, 31
	v_lshl_add_u64 v[132:133], s[6:7], 1, v[132:133]
	v_mov_b32_e32 v1, v3
	v_lshl_add_u64 v[152:153], v[132:133], 0, v[0:1]
	s_waitcnt lgkmcnt(0)
	global_store_dwordx4 v[152:153], v[136:139], off nt
	v_add_co_u32_e32 v132, vcc, s77, v152
	s_nop 0
	v_add_u32_e32 v137, v227, v228
	ds_read_b128 v[144:147], v137
	v_add_u32_e32 v136, v229, v230
	ds_read_b128 v[148:151], v136
	v_addc_co_u32_e32 v133, vcc, 0, v153, vcc
	v_add_u32_e32 v138, v231, v232
	s_waitcnt lgkmcnt(1)
	global_store_dwordx4 v[132:133], v[144:147], off nt
	ds_read_b128 v[144:147], v138
	v_add_co_u32_e32 v132, vcc, s66, v152
	ds_read_b128 v[140:143], v135 offset:4096
	s_nop 0
	v_addc_co_u32_e32 v133, vcc, 0, v153, vcc
	s_mov_b32 s4, 0x12000
	s_waitcnt lgkmcnt(2)
	global_store_dwordx4 v[132:133], v[148:151], off nt
	v_add_co_u32_e32 v132, vcc, s4, v152
	v_add_u32_e32 v134, v233, v234
	s_nop 0
	v_addc_co_u32_e32 v133, vcc, 0, v153, vcc
	ds_read_b128 v[148:151], v134
	s_mov_b32 s4, 0x18000
	s_waitcnt lgkmcnt(2)
	global_store_dwordx4 v[132:133], v[144:147], off nt
	v_add_co_u32_e32 v132, vcc, s4, v152
	s_mov_b32 s4, 0x1e000
	s_nop 0
	v_addc_co_u32_e32 v133, vcc, 0, v153, vcc
	s_waitcnt lgkmcnt(1)
	global_store_dwordx4 v[132:133], v[140:143], off nt
	v_add_co_u32_e32 v132, vcc, s4, v152
	s_nop 1
	v_addc_co_u32_e32 v133, vcc, 0, v153, vcc
	s_waitcnt lgkmcnt(0)
	global_store_dwordx4 v[132:133], v[148:151], off nt
	v_add_u32_e32 v133, v235, v236
	ds_read_b128 v[140:143], v133
	v_add_u32_e32 v132, v237, v238
	v_add_co_u32_e32 v148, vcc, 0x24000, v152
	ds_read_b128 v[144:147], v132
	s_nop 0
	v_addc_co_u32_e32 v149, vcc, 0, v153, vcc
	s_waitcnt lgkmcnt(1)
	global_store_dwordx4 v[148:149], v[140:143], off nt
	s_nop 1
	v_add_co_u32_e32 v140, vcc, 0x2a000, v152
	s_nop 1
	v_addc_co_u32_e32 v141, vcc, 0, v153, vcc
	s_andn2_b64 vcc, exec, s[2:3]
	s_waitcnt lgkmcnt(0)
	global_store_dwordx4 v[140:141], v[144:147], off nt
	s_cbranch_vccz .LBB0_658
	s_andn2_b64 vcc, exec, s[0:1]
	s_cbranch_vccnz .LBB0_651
	s_branch .LBB0_659
.LBB0_658:
	s_ashr_i32 s2, s29, 31
	s_lshr_b32 s2, s2, 25
	s_add_i32 s3, s29, s2
	s_ashr_i32 s2, s3, 7
	s_and_b32 s3, s3, 0xff80
	s_sub_i32 s3, s29, s3
	s_bfe_i32 s4, s3, 0x80000
	s_bfe_u32 s4, s4, 0x4000b
	v_cvt_pk_bf16_f32 v140, v64, v8
	v_cvt_pk_bf16_f32 v141, v4, v16
	s_add_i32 s4, s3, s4
	v_cvt_pk_bf16_f32 v142, v12, v24
	v_cvt_pk_bf16_f32 v143, v20, v32
	ds_write_b128 v223, v[140:143]
	v_cvt_pk_bf16_f32 v140, v28, v52
	v_cvt_pk_bf16_f32 v141, v68, v80
	s_bfe_i32 s5, s4, 0x80000
	v_cvt_pk_bf16_f32 v142, v88, v96
	v_cvt_pk_bf16_f32 v143, v108, v112
	ds_write_b128 v224, v[140:143]
	v_cvt_pk_bf16_f32 v140, v65, v9
	v_cvt_pk_bf16_f32 v141, v5, v17
	s_and_b32 s4, s4, 0xf0
	v_cvt_pk_bf16_f32 v142, v13, v25
	v_cvt_pk_bf16_f32 v143, v21, v33
	ds_write_b128 v223, v[140:143] offset:128
	v_cvt_pk_bf16_f32 v140, v29, v53
	v_cvt_pk_bf16_f32 v141, v69, v81
	s_sub_i32 s3, s3, s4
	v_cvt_pk_bf16_f32 v142, v89, v97
	v_cvt_pk_bf16_f32 v143, v109, v113
	ds_write_b128 v224, v[140:143] offset:128
	v_cvt_pk_bf16_f32 v140, v66, v10
	v_cvt_pk_bf16_f32 v141, v6, v18
	s_sext_i32_i8 s4, s3
	s_ashr_i32 s3, s2, 31
	v_cvt_pk_bf16_f32 v142, v14, v26
	v_cvt_pk_bf16_f32 v143, v22, v34
	ds_write_b128 v223, v[140:143] offset:256
	v_cvt_pk_bf16_f32 v140, v30, v54
	v_cvt_pk_bf16_f32 v141, v70, v82
	s_lshl_b64 s[2:3], s[2:3], 10
	v_cvt_pk_bf16_f32 v142, v90, v98
	v_cvt_pk_bf16_f32 v143, v110, v114
	ds_write_b128 v224, v[140:143] offset:256
	v_cvt_pk_bf16_f32 v140, v67, v11
	v_cvt_pk_bf16_f32 v141, v7, v19
	s_add_u32 s2, s22, s2
	v_cvt_pk_bf16_f32 v142, v15, v27
	v_cvt_pk_bf16_f32 v143, v23, v35
	ds_write_b128 v223, v[140:143] offset:384
	v_cvt_pk_bf16_f32 v140, v31, v55
	v_cvt_pk_bf16_f32 v141, v71, v83
	s_addc_u32 s3, s23, s3
	v_cvt_pk_bf16_f32 v142, v91, v99
	v_cvt_pk_bf16_f32 v143, v111, v115
	ds_write_b128 v224, v[140:143] offset:384
	v_lshl_add_u32 v139, s4, 6, v222
	v_mov_b64_e32 v[140:141], s[2:3]
	s_sext_i32_i16 s5, s5
	v_mad_i64_i32 v[140:141], s[2:3], v139, s16, v[140:141]
	s_lshl_b32 s2, s5, 2
	s_andn2_b32 s2, s2, 63
	s_ashr_i32 s3, s2, 31
	v_lshl_add_u64 v[140:141], s[2:3], 1, v[140:141]
	v_lshl_add_u64 v[144:145], v[140:141], 0, v[0:1]
	ds_read_b128 v[140:143], v135
	v_add_co_u32_e32 v146, vcc, s77, v144
	s_mov_b32 s2, 0x12000
	s_nop 0
	v_addc_co_u32_e32 v147, vcc, 0, v145, vcc
	s_waitcnt lgkmcnt(0)
	global_store_dwordx4 v[144:145], v[140:143], off nt
	ds_read_b128 v[140:143], v137
	s_waitcnt lgkmcnt(0)
	global_store_dwordx4 v[146:147], v[140:143], off nt
	ds_read_b128 v[140:143], v136
	v_add_co_u32_e32 v146, vcc, 0xc000, v144
	s_nop 1
	v_addc_co_u32_e32 v147, vcc, 0, v145, vcc
	s_waitcnt lgkmcnt(0)
	global_store_dwordx4 v[146:147], v[140:143], off nt
	ds_read_b128 v[140:143], v138
	v_add_co_u32_e32 v146, vcc, s2, v144
	s_mov_b32 s2, 0x18000
	s_nop 0
	v_addc_co_u32_e32 v147, vcc, 0, v145, vcc
	s_waitcnt lgkmcnt(0)
	global_store_dwordx4 v[146:147], v[140:143], off nt
	ds_read_b128 v[140:143], v135 offset:4096
	v_add_co_u32_e32 v146, vcc, s2, v144
	s_nop 1
	v_addc_co_u32_e32 v147, vcc, 0, v145, vcc
	s_waitcnt lgkmcnt(0)
	global_store_dwordx4 v[146:147], v[140:143], off nt
	ds_read_b128 v[140:143], v134
	v_add_co_u32_e32 v146, vcc, 0x1e000, v144
	s_nop 1
	v_addc_co_u32_e32 v147, vcc, 0, v145, vcc
	s_waitcnt lgkmcnt(0)
	global_store_dwordx4 v[146:147], v[140:143], off nt
	ds_read_b128 v[140:143], v133
	v_add_co_u32_e32 v146, vcc, 0x24000, v144
	s_nop 1
	v_addc_co_u32_e32 v147, vcc, 0, v145, vcc
	s_waitcnt lgkmcnt(0)
	global_store_dwordx4 v[146:147], v[140:143], off nt
	ds_read_b128 v[140:143], v132
	v_add_co_u32_e32 v144, vcc, 0x2a000, v144
	s_nop 1
	v_addc_co_u32_e32 v145, vcc, 0, v145, vcc
	s_waitcnt lgkmcnt(0)
	global_store_dwordx4 v[144:145], v[140:143], off nt
	s_andn2_b64 vcc, exec, s[0:1]
	s_cbranch_vccnz .LBB0_651
.LBB0_659:
	s_ashr_i32 s0, s9, 31
	s_lshr_b32 s0, s0, 25
	s_add_i32 s1, s9, s0
	s_ashr_i32 s0, s1, 7
	s_and_b32 s1, s1, 0xff80
	s_sub_i32 s1, s9, s1
	s_bfe_i32 s2, s1, 0x80000
	s_bfe_u32 s2, s2, 0x4000b
	v_cvt_pk_bf16_f32 v140, v92, v40
	v_cvt_pk_bf16_f32 v141, v36, v48
	s_add_i32 s2, s1, s2
	v_cvt_pk_bf16_f32 v142, v44, v60
	v_cvt_pk_bf16_f32 v143, v56, v76
	ds_write_b128 v223, v[140:143]
	v_cvt_pk_bf16_f32 v140, v72, v84
	v_cvt_pk_bf16_f32 v141, v100, v104
	s_bfe_i32 s3, s2, 0x80000
	v_cvt_pk_bf16_f32 v142, v116, v120
	v_cvt_pk_bf16_f32 v143, v124, v128
	ds_write_b128 v224, v[140:143]
	v_cvt_pk_bf16_f32 v140, v93, v41
	v_cvt_pk_bf16_f32 v141, v37, v49
	s_and_b32 s2, s2, 0xf0
	v_cvt_pk_bf16_f32 v142, v45, v61
	v_cvt_pk_bf16_f32 v143, v57, v77
	ds_write_b128 v223, v[140:143] offset:128
	v_cvt_pk_bf16_f32 v140, v73, v85
	v_cvt_pk_bf16_f32 v141, v101, v105
	s_sub_i32 s1, s1, s2
	v_cvt_pk_bf16_f32 v142, v117, v121
	v_cvt_pk_bf16_f32 v143, v125, v129
	ds_write_b128 v224, v[140:143] offset:128
	v_cvt_pk_bf16_f32 v140, v94, v42
	v_cvt_pk_bf16_f32 v141, v38, v50
	s_sext_i32_i8 s2, s1
	s_ashr_i32 s1, s0, 31
	v_cvt_pk_bf16_f32 v142, v46, v62
	v_cvt_pk_bf16_f32 v143, v58, v78
	ds_write_b128 v223, v[140:143] offset:256
	v_cvt_pk_bf16_f32 v140, v74, v86
	v_cvt_pk_bf16_f32 v141, v102, v106
	s_lshl_b64 s[0:1], s[0:1], 10
	v_cvt_pk_bf16_f32 v142, v118, v122
	v_cvt_pk_bf16_f32 v143, v126, v130
	ds_write_b128 v224, v[140:143] offset:256
	v_cvt_pk_bf16_f32 v140, v95, v43
	v_cvt_pk_bf16_f32 v141, v39, v51
	s_add_u32 s0, s22, s0
	v_cvt_pk_bf16_f32 v142, v47, v63
	v_cvt_pk_bf16_f32 v143, v59, v79
	ds_write_b128 v223, v[140:143] offset:384
	v_cvt_pk_bf16_f32 v140, v75, v87
	v_cvt_pk_bf16_f32 v141, v103, v107
	s_addc_u32 s1, s23, s1
	v_cvt_pk_bf16_f32 v142, v119, v123
	v_cvt_pk_bf16_f32 v143, v127, v131
	ds_write_b128 v224, v[140:143] offset:384
	v_lshl_add_u32 v1, s2, 6, v222
	v_mov_b64_e32 v[140:141], s[0:1]
	s_sext_i32_i16 s3, s3
	v_mad_i64_i32 v[140:141], s[0:1], v1, s16, v[140:141]
	s_lshl_b32 s0, s3, 2
	s_andn2_b32 s0, s0, 63
	s_ashr_i32 s1, s0, 31
	v_lshl_add_u64 v[140:141], s[0:1], 1, v[140:141]
	v_mov_b32_e32 v1, v3
	v_lshl_add_u64 v[144:145], v[140:141], 0, v[0:1]
	ds_read_b128 v[140:143], v135
	v_add_co_u32_e32 v146, vcc, s77, v144
	s_mov_b32 s0, 0x12000
	s_nop 0
	v_addc_co_u32_e32 v147, vcc, 0, v145, vcc
	s_waitcnt lgkmcnt(0)
	global_store_dwordx4 v[144:145], v[140:143], off nt
	ds_read_b128 v[140:143], v137
	s_waitcnt lgkmcnt(0)
	global_store_dwordx4 v[146:147], v[140:143], off nt
	ds_read_b128 v[140:143], v136
	v_add_co_u32_e32 v136, vcc, 0xc000, v144
	s_nop 1
	v_addc_co_u32_e32 v137, vcc, 0, v145, vcc
	s_waitcnt lgkmcnt(0)
	global_store_dwordx4 v[136:137], v[140:143], off nt
	ds_read_b128 v[136:139], v138
	s_nop 0
	v_add_co_u32_e32 v140, vcc, s0, v144
	s_mov_b32 s0, 0x18000
	s_nop 0
	v_addc_co_u32_e32 v141, vcc, 0, v145, vcc
	s_waitcnt lgkmcnt(0)
	global_store_dwordx4 v[140:141], v[136:139], off nt
	ds_read_b128 v[136:139], v135 offset:4096
	v_add_co_u32_e32 v140, vcc, s0, v144
	s_nop 1
	v_addc_co_u32_e32 v141, vcc, 0, v145, vcc
	s_waitcnt lgkmcnt(0)
	global_store_dwordx4 v[140:141], v[136:139], off nt
	ds_read_b128 v[134:137], v134
	s_nop 0
	v_add_co_u32_e32 v138, vcc, 0x1e000, v144
	s_nop 1
	v_addc_co_u32_e32 v139, vcc, 0, v145, vcc
	s_waitcnt lgkmcnt(0)
	global_store_dwordx4 v[138:139], v[134:137], off nt
	ds_read_b128 v[134:137], v133
	v_add_co_u32_e32 v138, vcc, 0x24000, v144
	s_nop 1
	v_addc_co_u32_e32 v139, vcc, 0, v145, vcc
	s_waitcnt lgkmcnt(0)
	global_store_dwordx4 v[138:139], v[134:137], off nt
	ds_read_b128 v[132:135], v132
	s_nop 0
	v_add_co_u32_e32 v136, vcc, 0x2a000, v144
	s_nop 1
	v_addc_co_u32_e32 v137, vcc, 0, v145, vcc
	s_waitcnt lgkmcnt(0)
	global_store_dwordx4 v[136:137], v[132:135], off nt
	s_branch .LBB0_651

.LBB0_663:
	s_add_i32 s21, s38, s8
	s_cmpk_lt_i32 s21, 0x100
	s_cselect_b64 s[2:3], -1, 0
	s_ashr_i32 s0, s8, 31
	s_lshr_b32 s0, s0, 24
	s_add_i32 s0, s8, s0
	s_and_b32 s0, s0, 0xff00
	s_sub_i32 s0, s8, s0
	s_sext_i32_i16 s1, s0
	s_bfe_u32 s1, s1, 0x4001b
	s_add_i32 s1, s0, s1
	s_sext_i32_i16 s4, s1
	s_and_b32 s1, s1, 0xfff0
	s_sub_i32 s0, s0, s1
	s_sext_i32_i16 s0, s0
	s_lshl_b32 s6, s0, 6
	s_lshl_b32 s0, s4, 2
	s_and_b32 s4, s0, 0xffffffc0
	v_add_u32_e32 v132, s4, v221
	v_ashrrev_i32_e32 v133, 31, v132
	v_readlane_b32 s0, v252, 63
	v_lshlrev_b64 v[132:133], 12, v[132:133]
	v_readlane_b32 s1, v253, 0
	s_ashr_i32 s7, s6, 31
	s_cmpk_gt_i32 s21, 0xff
	v_lshl_add_u64 v[132:133], s[0:1], 0, v[132:133]
	v_lshl_add_u64 v[132:133], s[6:7], 2, v[132:133]
	v_lshl_add_u64 v[188:189], v[132:133], 0, v[2:3]
	v_add_co_u32_e32 v132, vcc, s83, v188
	s_nop 1
	v_addc_co_u32_e32 v133, vcc, 0, v189, vcc
	v_add_co_u32_e32 v140, vcc, s62, v188
	global_load_dwordx4 v[136:139], v[132:133], off offset:-4096 nt
	s_nop 0
	global_load_dwordx4 v[132:135], v[132:133], off nt
	v_addc_co_u32_e32 v141, vcc, 0, v189, vcc
	v_add_co_u32_e32 v148, vcc, s77, v188
	global_load_dwordx4 v[144:147], v[140:141], off offset:-4096 nt
	s_nop 0
	global_load_dwordx4 v[140:143], v[140:141], off nt
	v_addc_co_u32_e32 v149, vcc, 0, v189, vcc
	v_add_co_u32_e32 v152, vcc, s88, v188
	global_load_dwordx4 v[156:159], v[148:149], off offset:-4096 nt
	s_nop 0
	global_load_dwordx4 v[148:151], v[148:149], off nt
	v_addc_co_u32_e32 v153, vcc, 0, v189, vcc
	v_add_co_u32_e32 v160, vcc, s72, v188
	global_load_dwordx4 v[164:167], v[152:153], off offset:-4096 nt
	s_nop 0
	global_load_dwordx4 v[152:155], v[152:153], off nt
	v_addc_co_u32_e32 v161, vcc, 0, v189, vcc
	v_add_co_u32_e32 v172, vcc, 0xb000, v188
	global_load_dwordx4 v[168:171], v[160:161], off offset:-4096 nt
	s_nop 0
	global_load_dwordx4 v[160:163], v[160:161], off nt
	v_addc_co_u32_e32 v173, vcc, 0, v189, vcc
	v_add_co_u32_e32 v176, vcc, s66, v188
	global_load_dwordx4 v[184:187], v[188:189], off nt
	s_nop 0
	global_load_dwordx4 v[172:175], v[172:173], off nt
	v_addc_co_u32_e32 v177, vcc, 0, v189, vcc
	v_add_co_u32_e32 v180, vcc, 0xd000, v188
	s_nop 1
	v_addc_co_u32_e32 v181, vcc, 0, v189, vcc
	v_add_co_u32_e32 v190, vcc, 0xe000, v188
	global_load_dwordx4 v[176:179], v[176:177], off nt
	s_nop 0
	global_load_dwordx4 v[180:183], v[180:181], off nt
	v_addc_co_u32_e32 v191, vcc, 0, v189, vcc
	v_add_co_u32_e32 v192, vcc, 0xf000, v188
	s_nop 1
	v_addc_co_u32_e32 v193, vcc, 0, v189, vcc
	global_load_dwordx4 v[188:191], v[190:191], off nt
	s_nop 0
	global_load_dwordx4 v[192:195], v[192:193], off nt
	s_cbranch_scc1 .LBB0_665
	s_ashr_i32 s0, s21, 31
	s_lshr_b32 s0, s0, 24
	s_add_i32 s0, s21, s0
	s_and_b32 s0, s0, 0xff00
	s_sub_i32 s0, s21, s0
	s_sext_i32_i16 s1, s0
	s_bfe_u32 s1, s1, 0x4001b
	s_add_i32 s1, s0, s1
	s_sext_i32_i16 s5, s1
	s_and_b32 s1, s1, 0xfff0
	s_sub_i32 s0, s0, s1
	s_lshl_b32 s1, s5, 2
	s_andn2_b32 s1, s1, 63
	v_add_u32_e32 v4, s1, v221
	s_sext_i32_i16 s0, s0
	v_ashrrev_i32_e32 v5, 31, v4
	v_readlane_b32 s22, v252, 63
	s_lshl_b32 s0, s0, 6
	v_lshlrev_b64 v[4:5], 12, v[4:5]
	v_readlane_b32 s23, v253, 0
	s_ashr_i32 s1, s0, 31
	s_nop 0
	v_lshl_add_u64 v[4:5], s[22:23], 0, v[4:5]
	v_lshl_add_u64 v[4:5], s[0:1], 2, v[4:5]
	v_lshl_add_u64 v[108:109], v[4:5], 0, v[2:3]
	v_add_co_u32_e32 v4, vcc, s83, v108
	s_nop 1
	v_addc_co_u32_e32 v5, vcc, 0, v109, vcc
	v_add_co_u32_e32 v12, vcc, s62, v108
	global_load_dwordx4 v[8:11], v[4:5], off offset:-4096 nt
	s_nop 0
	global_load_dwordx4 v[4:7], v[4:5], off nt
	v_addc_co_u32_e32 v13, vcc, 0, v109, vcc
	v_add_co_u32_e32 v20, vcc, s77, v108
	global_load_dwordx4 v[16:19], v[12:13], off offset:-4096 nt
	s_nop 0
	global_load_dwordx4 v[12:15], v[12:13], off nt
	v_addc_co_u32_e32 v21, vcc, 0, v109, vcc
	v_add_co_u32_e32 v28, vcc, s88, v108
	global_load_dwordx4 v[24:27], v[20:21], off offset:-4096 nt
	s_nop 0
	global_load_dwordx4 v[20:23], v[20:21], off nt
	v_addc_co_u32_e32 v29, vcc, 0, v109, vcc
	v_add_co_u32_e32 v52, vcc, 0x9000, v108
	global_load_dwordx4 v[32:35], v[28:29], off offset:-4096 nt
	s_nop 0
	global_load_dwordx4 v[28:31], v[28:29], off nt
	v_addc_co_u32_e32 v53, vcc, 0, v109, vcc
	v_add_co_u32_e32 v68, vcc, s72, v108
	global_load_dwordx4 v[64:67], v[108:109], off nt
	s_nop 0
	global_load_dwordx4 v[52:55], v[52:53], off nt
	v_addc_co_u32_e32 v69, vcc, 0, v109, vcc
	v_add_co_u32_e32 v80, vcc, 0xb000, v108
	s_nop 1
	v_addc_co_u32_e32 v81, vcc, 0, v109, vcc
	v_add_co_u32_e32 v88, vcc, 0xc000, v108
	global_load_dwordx4 v[68:71], v[68:69], off nt
	s_nop 0
	global_load_dwordx4 v[80:83], v[80:81], off nt
	v_addc_co_u32_e32 v89, vcc, 0, v109, vcc
	v_add_co_u32_e32 v96, vcc, 0xd000, v108
	s_nop 1
	v_addc_co_u32_e32 v97, vcc, 0, v109, vcc
	v_add_co_u32_e32 v110, vcc, 0xe000, v108
	global_load_dwordx4 v[88:91], v[88:89], off nt
	s_nop 0
	global_load_dwordx4 v[96:99], v[96:97], off nt
	v_addc_co_u32_e32 v111, vcc, 0, v109, vcc
	v_add_co_u32_e32 v112, vcc, 0xf000, v108
	s_nop 1
	v_addc_co_u32_e32 v113, vcc, 0, v109, vcc
	global_load_dwordx4 v[108:111], v[110:111], off nt
	s_nop 0
	global_load_dwordx4 v[112:115], v[112:113], off nt
.LBB0_665:
	s_add_i32 s7, s9, s8
	s_cmpk_lt_i32 s7, 0x100
	s_cselect_b64 s[0:1], -1, 0
	s_cmpk_gt_i32 s7, 0xff
	s_cbranch_scc1 .LBB0_667
	s_ashr_i32 s5, s7, 31
	s_lshr_b32 s5, s5, 24
	s_add_i32 s5, s7, s5
	s_and_b32 s5, s5, 0xff00
	s_sub_i32 s5, s7, s5
	s_sext_i32_i16 s14, s5
	s_bfe_u32 s14, s14, 0x4001b
	s_add_i32 s14, s5, s14
	s_sext_i32_i16 s23, s14
	s_and_b32 s14, s14, 0xfff0
	s_sub_i32 s5, s5, s14
	s_sext_i32_i16 s5, s5
	s_lshl_b32 s22, s5, 6
	s_lshl_b32 s5, s23, 2
	s_andn2_b32 s5, s5, 63
	v_add_u32_e32 v36, s5, v221
	v_ashrrev_i32_e32 v37, 31, v36
	v_readlane_b32 s36, v252, 63
	v_lshlrev_b64 v[36:37], 12, v[36:37]
	v_readlane_b32 s37, v253, 0
	s_ashr_i32 s23, s22, 31
	s_nop 0
	v_lshl_add_u64 v[36:37], s[36:37], 0, v[36:37]
	v_lshl_add_u64 v[36:37], s[22:23], 2, v[36:37]
	v_lshl_add_u64 v[124:125], v[36:37], 0, v[2:3]
	v_add_co_u32_e32 v36, vcc, s83, v124
	s_nop 1
	v_addc_co_u32_e32 v37, vcc, 0, v125, vcc
	v_add_co_u32_e32 v44, vcc, s62, v124
	global_load_dwordx4 v[40:43], v[36:37], off offset:-4096 nt
	s_nop 0
	global_load_dwordx4 v[36:39], v[36:37], off nt
	v_addc_co_u32_e32 v45, vcc, 0, v125, vcc
	v_add_co_u32_e32 v56, vcc, s77, v124
	global_load_dwordx4 v[48:51], v[44:45], off offset:-4096 nt
	s_nop 0
	global_load_dwordx4 v[44:47], v[44:45], off nt
	v_addc_co_u32_e32 v57, vcc, 0, v125, vcc
	v_add_co_u32_e32 v72, vcc, s88, v124
	global_load_dwordx4 v[60:63], v[56:57], off offset:-4096 nt
	s_nop 0
	global_load_dwordx4 v[56:59], v[56:57], off nt
	v_addc_co_u32_e32 v73, vcc, 0, v125, vcc
	v_add_co_u32_e32 v84, vcc, 0x9000, v124
	global_load_dwordx4 v[76:79], v[72:73], off offset:-4096 nt
	s_nop 0
	global_load_dwordx4 v[72:75], v[72:73], off nt
	v_addc_co_u32_e32 v85, vcc, 0, v125, vcc
	v_add_co_u32_e32 v100, vcc, s72, v124
	global_load_dwordx4 v[92:95], v[124:125], off nt
	s_nop 0
	global_load_dwordx4 v[84:87], v[84:85], off nt
	v_addc_co_u32_e32 v101, vcc, 0, v125, vcc
	v_add_co_u32_e32 v104, vcc, 0xb000, v124
	s_nop 1
	v_addc_co_u32_e32 v105, vcc, 0, v125, vcc
	v_add_co_u32_e32 v116, vcc, 0xc000, v124
	global_load_dwordx4 v[100:103], v[100:101], off nt
	s_nop 0
	global_load_dwordx4 v[104:107], v[104:105], off nt
	v_addc_co_u32_e32 v117, vcc, 0, v125, vcc
	v_add_co_u32_e32 v120, vcc, 0xd000, v124
	s_nop 1
	v_addc_co_u32_e32 v121, vcc, 0, v125, vcc
	v_add_co_u32_e32 v126, vcc, 0xe000, v124
	global_load_dwordx4 v[116:119], v[116:117], off nt
	s_nop 0
	global_load_dwordx4 v[120:123], v[120:121], off nt
	v_addc_co_u32_e32 v127, vcc, 0, v125, vcc
	v_add_co_u32_e32 v128, vcc, 0xf000, v124
	s_nop 1
	v_addc_co_u32_e32 v129, vcc, 0, v125, vcc
	global_load_dwordx4 v[124:127], v[126:127], off nt
	s_nop 0
	global_load_dwordx4 v[128:131], v[128:129], off nt
.LBB0_667:
	s_waitcnt vmcnt(5)
	v_cvt_pk_bf16_f32 v240, v184, v136
	v_cvt_pk_bf16_f32 v241, v132, v144
	v_cvt_pk_bf16_f32 v242, v140, v156
	v_cvt_pk_bf16_f32 v243, v148, v164
	ds_write_b128 v223, v[240:243]
	v_cvt_pk_bf16_f32 v240, v152, v168
	s_waitcnt vmcnt(4)
	v_cvt_pk_bf16_f32 v241, v160, v172
	s_waitcnt vmcnt(2)
	v_cvt_pk_bf16_f32 v242, v176, v180
	s_waitcnt vmcnt(0)
	v_cvt_pk_bf16_f32 v243, v188, v192
	ds_write_b128 v224, v[240:243]
	v_cvt_pk_bf16_f32 v240, v185, v137
	v_cvt_pk_bf16_f32 v241, v133, v145
	v_cvt_pk_bf16_f32 v242, v141, v157
	v_cvt_pk_bf16_f32 v243, v149, v165
	ds_write_b128 v223, v[240:243] offset:128
	v_cvt_pk_bf16_f32 v240, v153, v169
	v_cvt_pk_bf16_f32 v241, v161, v173
	v_cvt_pk_bf16_f32 v242, v177, v181
	v_cvt_pk_bf16_f32 v243, v189, v193
	ds_write_b128 v224, v[240:243] offset:128
	v_cvt_pk_bf16_f32 v240, v186, v138
	v_cvt_pk_bf16_f32 v241, v134, v146
	v_cvt_pk_bf16_f32 v242, v142, v158
	v_cvt_pk_bf16_f32 v243, v150, v166
	ds_write_b128 v223, v[240:243] offset:256
	v_cvt_pk_bf16_f32 v240, v154, v170
	v_cvt_pk_bf16_f32 v241, v162, v174
	v_cvt_pk_bf16_f32 v242, v178, v182
	v_cvt_pk_bf16_f32 v243, v190, v194
	ds_write_b128 v224, v[240:243] offset:256
	v_cvt_pk_bf16_f32 v132, v187, v139
	v_cvt_pk_bf16_f32 v133, v135, v147
	v_cvt_pk_bf16_f32 v134, v143, v159
	v_cvt_pk_bf16_f32 v135, v151, v167
	ds_write_b128 v223, v[132:135] offset:384
	v_cvt_pk_bf16_f32 v132, v155, v171
	v_cvt_pk_bf16_f32 v133, v163, v175
	v_cvt_pk_bf16_f32 v134, v179, v183
	v_cvt_pk_bf16_f32 v135, v191, v195
	ds_write_b128 v224, v[132:135] offset:384
	v_add_u32_e32 v132, s6, v222
	v_add_u32_e32 v135, v225, v226
	v_ashrrev_i32_e32 v133, 31, v132
	ds_read_b128 v[136:139], v135
	v_lshlrev_b64 v[132:133], 11, v[132:133]
	v_lshl_add_u64 v[132:133], s[28:29], 0, v[132:133]
	s_ashr_i32 s5, s4, 31
	v_lshl_add_u64 v[132:133], s[4:5], 1, v[132:133]
	v_mov_b32_e32 v1, v3
	v_lshl_add_u64 v[152:153], v[132:133], 0, v[0:1]
	s_waitcnt lgkmcnt(0)
	global_store_dwordx4 v[152:153], v[136:139], off nt
	v_add_co_u32_e32 v132, vcc, s62, v152
	s_nop 0
	v_add_u32_e32 v137, v227, v228
	ds_read_b128 v[144:147], v137
	v_add_u32_e32 v136, v229, v230
	ds_read_b128 v[148:151], v136
	v_addc_co_u32_e32 v133, vcc, 0, v153, vcc
	v_add_u32_e32 v138, v231, v232
	s_waitcnt lgkmcnt(1)
	global_store_dwordx4 v[132:133], v[144:147], off nt
	ds_read_b128 v[144:147], v138
	v_add_co_u32_e32 v132, vcc, s88, v152
	ds_read_b128 v[140:143], v135 offset:4096
	s_nop 0
	v_addc_co_u32_e32 v133, vcc, 0, v153, vcc
	s_waitcnt lgkmcnt(2)
	global_store_dwordx4 v[132:133], v[148:151], off nt
	v_add_co_u32_e32 v132, vcc, s66, v152
	v_add_u32_e32 v134, v233, v234
	s_nop 0
	v_addc_co_u32_e32 v133, vcc, 0, v153, vcc
	ds_read_b128 v[148:151], v134
	s_waitcnt lgkmcnt(2)
	global_store_dwordx4 v[132:133], v[144:147], off nt
	v_add_co_u32_e32 v132, vcc, s82, v152
	s_mov_b32 s4, 0x14000
	s_nop 0
	v_addc_co_u32_e32 v133, vcc, 0, v153, vcc
	s_waitcnt lgkmcnt(1)
	global_store_dwordx4 v[132:133], v[140:143], off nt
	v_add_co_u32_e32 v132, vcc, s4, v152
	s_nop 1
	v_addc_co_u32_e32 v133, vcc, 0, v153, vcc
	s_waitcnt lgkmcnt(0)
	global_store_dwordx4 v[132:133], v[148:151], off nt
	v_add_u32_e32 v133, v235, v236
	ds_read_b128 v[140:143], v133
	v_add_u32_e32 v132, v237, v238
	v_add_co_u32_e32 v148, vcc, 0x18000, v152
	ds_read_b128 v[144:147], v132
	s_nop 0
	v_addc_co_u32_e32 v149, vcc, 0, v153, vcc
	s_waitcnt lgkmcnt(1)
	global_store_dwordx4 v[148:149], v[140:143], off nt
	s_nop 1
	v_add_co_u32_e32 v140, vcc, 0x1c000, v152
	s_nop 1
	v_addc_co_u32_e32 v141, vcc, 0, v153, vcc
	s_andn2_b64 vcc, exec, s[2:3]
	s_waitcnt lgkmcnt(0)
	global_store_dwordx4 v[140:141], v[144:147], off nt
	s_cbranch_vccz .LBB0_669
	s_andn2_b64 vcc, exec, s[0:1]
	s_cbranch_vccnz .LBB0_662
	s_branch .LBB0_670
.LBB0_669:
	s_ashr_i32 s2, s21, 31
	s_lshr_b32 s2, s2, 24
	s_add_i32 s2, s21, s2
	s_and_b32 s2, s2, 0xff00
	v_cvt_pk_bf16_f32 v140, v64, v8
	s_sub_i32 s2, s21, s2
	v_cvt_pk_bf16_f32 v141, v4, v16
	v_cvt_pk_bf16_f32 v142, v12, v24
	v_cvt_pk_bf16_f32 v143, v20, v32
	ds_write_b128 v223, v[140:143]
	v_cvt_pk_bf16_f32 v140, v28, v52
	s_sext_i32_i16 s3, s2
	v_cvt_pk_bf16_f32 v141, v68, v80
	v_cvt_pk_bf16_f32 v142, v88, v96
	v_cvt_pk_bf16_f32 v143, v108, v112
	ds_write_b128 v224, v[140:143]
	v_cvt_pk_bf16_f32 v140, v65, v9
	s_bfe_u32 s3, s3, 0x4001b
	v_cvt_pk_bf16_f32 v141, v5, v17
	v_cvt_pk_bf16_f32 v142, v13, v25
	v_cvt_pk_bf16_f32 v143, v21, v33
	ds_write_b128 v223, v[140:143] offset:128
	v_cvt_pk_bf16_f32 v140, v29, v53
	s_add_i32 s3, s2, s3
	v_cvt_pk_bf16_f32 v141, v69, v81
	v_cvt_pk_bf16_f32 v142, v89, v97
	v_cvt_pk_bf16_f32 v143, v109, v113
	ds_write_b128 v224, v[140:143] offset:128
	v_cvt_pk_bf16_f32 v140, v66, v10
	s_sext_i32_i16 s4, s3
	v_cvt_pk_bf16_f32 v141, v6, v18
	v_cvt_pk_bf16_f32 v142, v14, v26
	v_cvt_pk_bf16_f32 v143, v22, v34
	ds_write_b128 v223, v[140:143] offset:256
	v_cvt_pk_bf16_f32 v140, v30, v54
	s_and_b32 s3, s3, 0xfff0
	v_cvt_pk_bf16_f32 v141, v70, v82
	v_cvt_pk_bf16_f32 v142, v90, v98
	v_cvt_pk_bf16_f32 v143, v110, v114
	ds_write_b128 v224, v[140:143] offset:256
	v_cvt_pk_bf16_f32 v140, v67, v11
	s_sub_i32 s2, s2, s3
	v_cvt_pk_bf16_f32 v141, v7, v19
	v_cvt_pk_bf16_f32 v142, v15, v27
	v_cvt_pk_bf16_f32 v143, v23, v35
	ds_write_b128 v223, v[140:143] offset:384
	v_cvt_pk_bf16_f32 v140, v31, v55
	s_sext_i32_i16 s2, s2
	v_cvt_pk_bf16_f32 v141, v71, v83
	v_cvt_pk_bf16_f32 v142, v91, v99
	v_cvt_pk_bf16_f32 v143, v111, v115
	ds_write_b128 v224, v[140:143] offset:384
	v_lshl_add_u32 v140, s2, 6, v222
	v_ashrrev_i32_e32 v141, 31, v140
	s_lshl_b32 s2, s4, 2
	v_lshlrev_b64 v[140:141], 11, v[140:141]
	s_andn2_b32 s2, s2, 63
	v_lshl_add_u64 v[140:141], s[28:29], 0, v[140:141]
	s_ashr_i32 s3, s2, 31
	v_lshl_add_u64 v[140:141], s[2:3], 1, v[140:141]
	v_lshl_add_u64 v[144:145], v[140:141], 0, v[0:1]
	ds_read_b128 v[140:143], v135
	v_add_co_u32_e32 v146, vcc, s62, v144
	s_waitcnt lgkmcnt(0)
	global_store_dwordx4 v[144:145], v[140:143], off nt
	ds_read_b128 v[140:143], v137
	v_addc_co_u32_e32 v147, vcc, 0, v145, vcc
	s_waitcnt lgkmcnt(0)
	global_store_dwordx4 v[146:147], v[140:143], off nt
	ds_read_b128 v[140:143], v136
	v_add_co_u32_e32 v146, vcc, 0x8000, v144
	s_nop 1
	v_addc_co_u32_e32 v147, vcc, 0, v145, vcc
	s_waitcnt lgkmcnt(0)
	global_store_dwordx4 v[146:147], v[140:143], off nt
	ds_read_b128 v[140:143], v138
	v_add_co_u32_e32 v146, vcc, 0xc000, v144
	s_nop 1
	v_addc_co_u32_e32 v147, vcc, 0, v145, vcc
	s_waitcnt lgkmcnt(0)
	global_store_dwordx4 v[146:147], v[140:143], off nt
	ds_read_b128 v[140:143], v135 offset:4096
	v_add_co_u32_e32 v146, vcc, s82, v144
	s_nop 1
	v_addc_co_u32_e32 v147, vcc, 0, v145, vcc
	s_waitcnt lgkmcnt(0)
	global_store_dwordx4 v[146:147], v[140:143], off nt
	ds_read_b128 v[140:143], v134
	v_add_co_u32_e32 v146, vcc, 0x14000, v144
	s_nop 1
	v_addc_co_u32_e32 v147, vcc, 0, v145, vcc
	s_waitcnt lgkmcnt(0)
	global_store_dwordx4 v[146:147], v[140:143], off nt
	ds_read_b128 v[140:143], v133
	v_add_co_u32_e32 v146, vcc, 0x18000, v144
	s_nop 1
	v_addc_co_u32_e32 v147, vcc, 0, v145, vcc
	s_waitcnt lgkmcnt(0)
	global_store_dwordx4 v[146:147], v[140:143], off nt
	ds_read_b128 v[140:143], v132
	v_add_co_u32_e32 v144, vcc, 0x1c000, v144
	s_nop 1
	v_addc_co_u32_e32 v145, vcc, 0, v145, vcc
	s_waitcnt lgkmcnt(0)
	global_store_dwordx4 v[144:145], v[140:143], off nt
	s_andn2_b64 vcc, exec, s[0:1]
	s_cbranch_vccnz .LBB0_662
.LBB0_670:
	s_ashr_i32 s0, s7, 31
	s_lshr_b32 s0, s0, 24
	s_add_i32 s0, s7, s0
	s_and_b32 s0, s0, 0xff00
	v_cvt_pk_bf16_f32 v140, v92, v40
	s_sub_i32 s0, s7, s0
	v_cvt_pk_bf16_f32 v141, v36, v48
	v_cvt_pk_bf16_f32 v142, v44, v60
	v_cvt_pk_bf16_f32 v143, v56, v76
	ds_write_b128 v223, v[140:143]
	v_cvt_pk_bf16_f32 v140, v72, v84
	s_sext_i32_i16 s1, s0
	v_cvt_pk_bf16_f32 v141, v100, v104
	v_cvt_pk_bf16_f32 v142, v116, v120
	v_cvt_pk_bf16_f32 v143, v124, v128
	ds_write_b128 v224, v[140:143]
	v_cvt_pk_bf16_f32 v140, v93, v41
	s_bfe_u32 s1, s1, 0x4001b
	v_cvt_pk_bf16_f32 v141, v37, v49
	v_cvt_pk_bf16_f32 v142, v45, v61
	v_cvt_pk_bf16_f32 v143, v57, v77
	ds_write_b128 v223, v[140:143] offset:128
	v_cvt_pk_bf16_f32 v140, v73, v85
	s_add_i32 s1, s0, s1
	v_cvt_pk_bf16_f32 v141, v101, v105
	v_cvt_pk_bf16_f32 v142, v117, v121
	v_cvt_pk_bf16_f32 v143, v125, v129
	ds_write_b128 v224, v[140:143] offset:128
	v_cvt_pk_bf16_f32 v140, v94, v42
	s_sext_i32_i16 s2, s1
	v_cvt_pk_bf16_f32 v141, v38, v50
	v_cvt_pk_bf16_f32 v142, v46, v62
	v_cvt_pk_bf16_f32 v143, v58, v78
	ds_write_b128 v223, v[140:143] offset:256
	v_cvt_pk_bf16_f32 v140, v74, v86
	s_and_b32 s1, s1, 0xfff0
	v_cvt_pk_bf16_f32 v141, v102, v106
	v_cvt_pk_bf16_f32 v142, v118, v122
	v_cvt_pk_bf16_f32 v143, v126, v130
	ds_write_b128 v224, v[140:143] offset:256
	v_cvt_pk_bf16_f32 v140, v95, v43
	s_sub_i32 s0, s0, s1
	v_cvt_pk_bf16_f32 v141, v39, v51
	v_cvt_pk_bf16_f32 v142, v47, v63
	v_cvt_pk_bf16_f32 v143, v59, v79
	ds_write_b128 v223, v[140:143] offset:384
	v_cvt_pk_bf16_f32 v140, v75, v87
	s_sext_i32_i16 s0, s0
	v_cvt_pk_bf16_f32 v141, v103, v107
	v_cvt_pk_bf16_f32 v142, v119, v123
	v_cvt_pk_bf16_f32 v143, v127, v131
	ds_write_b128 v224, v[140:143] offset:384
	v_lshl_add_u32 v140, s0, 6, v222
	v_ashrrev_i32_e32 v141, 31, v140
	s_lshl_b32 s0, s2, 2
	v_lshlrev_b64 v[140:141], 11, v[140:141]
	s_andn2_b32 s0, s0, 63
	v_lshl_add_u64 v[140:141], s[28:29], 0, v[140:141]
	s_ashr_i32 s1, s0, 31
	v_lshl_add_u64 v[140:141], s[0:1], 1, v[140:141]
	v_mov_b32_e32 v1, v3
	v_lshl_add_u64 v[144:145], v[140:141], 0, v[0:1]
	ds_read_b128 v[140:143], v135
	v_add_co_u32_e32 v146, vcc, s62, v144
	s_waitcnt lgkmcnt(0)
	global_store_dwordx4 v[144:145], v[140:143], off nt
	ds_read_b128 v[140:143], v137
	v_addc_co_u32_e32 v147, vcc, 0, v145, vcc
	s_waitcnt lgkmcnt(0)
	global_store_dwordx4 v[146:147], v[140:143], off nt
	ds_read_b128 v[140:143], v136
	v_add_co_u32_e32 v136, vcc, 0x8000, v144
	s_nop 1
	v_addc_co_u32_e32 v137, vcc, 0, v145, vcc
	s_waitcnt lgkmcnt(0)
	global_store_dwordx4 v[136:137], v[140:143], off nt
	ds_read_b128 v[136:139], v138
	s_nop 0
	v_add_co_u32_e32 v140, vcc, 0xc000, v144
	s_nop 1
	v_addc_co_u32_e32 v141, vcc, 0, v145, vcc
	s_waitcnt lgkmcnt(0)
	global_store_dwordx4 v[140:141], v[136:139], off nt
	ds_read_b128 v[136:139], v135 offset:4096
	v_add_co_u32_e32 v140, vcc, s82, v144
	s_nop 1
	v_addc_co_u32_e32 v141, vcc, 0, v145, vcc
	s_waitcnt lgkmcnt(0)
	global_store_dwordx4 v[140:141], v[136:139], off nt
	ds_read_b128 v[134:137], v134
	s_nop 0
	v_add_co_u32_e32 v138, vcc, 0x14000, v144
	s_nop 1
	v_addc_co_u32_e32 v139, vcc, 0, v145, vcc
	s_waitcnt lgkmcnt(0)
	global_store_dwordx4 v[138:139], v[134:137], off nt
	ds_read_b128 v[134:137], v133
	v_add_co_u32_e32 v138, vcc, 0x18000, v144
	s_nop 1
	v_addc_co_u32_e32 v139, vcc, 0, v145, vcc
	s_waitcnt lgkmcnt(0)
	global_store_dwordx4 v[138:139], v[134:137], off nt
	ds_read_b128 v[132:135], v132
	s_nop 0
	v_add_co_u32_e32 v136, vcc, 0x1c000, v144
	s_nop 1
	v_addc_co_u32_e32 v137, vcc, 0, v145, vcc
	s_waitcnt lgkmcnt(0)
	global_store_dwordx4 v[136:137], v[132:135], off nt
	s_branch .LBB0_662

.LBB0_674:
	s_add_i32 s21, s38, s8
	s_cmpk_lt_i32 s21, 0x80
	s_cselect_b64 s[2:3], -1, 0
	s_ashr_i32 s0, s8, 31
	s_lshr_b32 s0, s0, 25
	s_add_i32 s0, s8, s0
	s_and_b32 s0, s0, 0xff80
	s_sub_i32 s0, s8, s0
	s_bfe_i32 s1, s0, 0x80000
	s_bfe_u32 s1, s1, 0x3000c
	s_add_i32 s1, s0, s1
	s_bfe_i32 s4, s1, 0x80000
	s_and_b32 s1, s1, 0xf8
	s_sub_i32 s0, s0, s1
	s_sext_i32_i16 s4, s4
	s_sext_i32_i8 s0, s0
	s_lshl_b32 s6, s0, 6
	s_lshl_b32 s0, s4, 3
	s_and_b32 s4, s0, 0xffffffc0
	v_add_u32_e32 v132, s4, v221
	v_ashrrev_i32_e32 v133, 31, v132
	v_readlane_b32 s0, v253, 1
	v_lshlrev_b64 v[132:133], 11, v[132:133]
	v_readlane_b32 s1, v253, 2
	s_ashr_i32 s7, s6, 31
	s_cmpk_gt_i32 s21, 0x7f
	v_lshl_add_u64 v[132:133], s[0:1], 0, v[132:133]
	v_lshl_add_u64 v[132:133], s[6:7], 2, v[132:133]
	v_lshl_add_u64 v[180:181], v[132:133], 0, v[2:3]
	s_movk_i32 s0, 0x1000
	v_add_co_u32_e32 v148, vcc, s0, v180
	global_load_dwordx4 v[132:135], v[180:181], off nt
	global_load_dwordx4 v[136:139], v[180:181], off offset:2048 nt
	v_addc_co_u32_e32 v149, vcc, 0, v181, vcc
	v_add_co_u32_e32 v188, vcc, s83, v180
	s_nop 1
	v_addc_co_u32_e32 v189, vcc, 0, v181, vcc
	v_add_co_u32_e32 v152, vcc, 0x3000, v180
	global_load_dwordx4 v[140:143], v[188:189], off nt
	global_load_dwordx4 v[144:147], v[188:189], off offset:2048 nt
	v_addc_co_u32_e32 v153, vcc, 0, v181, vcc
	v_add_co_u32_e32 v164, vcc, s62, v180
	global_load_dwordx4 v[156:159], v[148:149], off offset:2048 nt
	s_nop 0
	global_load_dwordx4 v[148:151], v[152:153], off nt
	v_addc_co_u32_e32 v165, vcc, 0, v181, vcc
	v_add_co_u32_e32 v172, vcc, 0x5000, v180
	global_load_dwordx4 v[160:163], v[152:153], off offset:2048 nt
	s_nop 0
	global_load_dwordx4 v[152:155], v[164:165], off nt
	v_addc_co_u32_e32 v173, vcc, 0, v181, vcc
	v_add_co_u32_e32 v182, vcc, 0x6000, v180
	global_load_dwordx4 v[164:167], v[164:165], off offset:2048 nt
	s_nop 0
	global_load_dwordx4 v[168:171], v[172:173], off nt
	v_addc_co_u32_e32 v183, vcc, 0, v181, vcc
	v_add_co_u32_e32 v190, vcc, 0x7000, v180
	global_load_dwordx4 v[172:175], v[172:173], off offset:2048 nt
	s_nop 0
	global_load_dwordx4 v[176:179], v[182:183], off nt
	v_addc_co_u32_e32 v191, vcc, 0, v181, vcc
	global_load_dwordx4 v[180:183], v[182:183], off offset:2048 nt
	s_nop 0
	global_load_dwordx4 v[184:187], v[190:191], off nt
	global_load_dwordx4 v[192:195], v[188:189], off offset:-4096 nt
	s_nop 0
	global_load_dwordx4 v[188:191], v[190:191], off offset:2048 nt
	s_cbranch_scc1 .LBB0_676
	s_ashr_i32 s0, s21, 31
	s_lshr_b32 s0, s0, 25
	s_add_i32 s0, s21, s0
	s_and_b32 s0, s0, 0xff80
	s_sub_i32 s0, s21, s0
	s_bfe_i32 s1, s0, 0x80000
	s_bfe_u32 s1, s1, 0x3000c
	s_add_i32 s1, s0, s1
	s_bfe_i32 s5, s1, 0x80000
	s_sext_i32_i16 s5, s5
	s_and_b32 s1, s1, 0xf8
	s_sub_i32 s0, s0, s1
	s_lshl_b32 s1, s5, 3
	s_andn2_b32 s1, s1, 63
	v_add_u32_e32 v4, s1, v221
	s_sext_i32_i8 s0, s0
	v_ashrrev_i32_e32 v5, 31, v4
	v_readlane_b32 s22, v253, 1
	s_lshl_b32 s0, s0, 6
	v_lshlrev_b64 v[4:5], 11, v[4:5]
	v_readlane_b32 s23, v253, 2
	s_ashr_i32 s1, s0, 31
	s_nop 0
	v_lshl_add_u64 v[4:5], s[22:23], 0, v[4:5]
	v_lshl_add_u64 v[4:5], s[0:1], 2, v[4:5]
	v_lshl_add_u64 v[84:85], v[4:5], 0, v[2:3]
	s_movk_i32 s0, 0x1000
	v_add_co_u32_e32 v28, vcc, s0, v84
	global_load_dwordx4 v[8:11], v[84:85], off nt
	global_load_dwordx4 v[4:7], v[84:85], off offset:2048 nt
	v_addc_co_u32_e32 v29, vcc, 0, v85, vcc
	v_add_co_u32_e32 v92, vcc, s83, v84
	s_nop 1
	v_addc_co_u32_e32 v93, vcc, 0, v85, vcc
	v_add_co_u32_e32 v36, vcc, 0x3000, v84
	global_load_dwordx4 v[16:19], v[92:93], off nt
	global_load_dwordx4 v[12:15], v[92:93], off offset:2048 nt
	v_addc_co_u32_e32 v37, vcc, 0, v85, vcc
	v_add_co_u32_e32 v52, vcc, s62, v84
	global_load_dwordx4 v[32:35], v[28:29], off offset:2048 nt
	s_nop 0
	global_load_dwordx4 v[28:31], v[36:37], off nt
	v_addc_co_u32_e32 v53, vcc, 0, v85, vcc
	v_add_co_u32_e32 v68, vcc, 0x5000, v84
	global_load_dwordx4 v[36:39], v[36:37], off offset:2048 nt
	s_nop 0
	global_load_dwordx4 v[40:43], v[52:53], off nt
	v_addc_co_u32_e32 v69, vcc, 0, v85, vcc
	v_add_co_u32_e32 v86, vcc, 0x6000, v84
	global_load_dwordx4 v[52:55], v[52:53], off offset:2048 nt
	s_nop 0
	global_load_dwordx4 v[56:59], v[68:69], off nt
	v_addc_co_u32_e32 v87, vcc, 0, v85, vcc
	v_add_co_u32_e32 v94, vcc, 0x7000, v84
	global_load_dwordx4 v[68:71], v[68:69], off offset:2048 nt
	s_nop 0
	global_load_dwordx4 v[72:75], v[86:87], off nt
	v_addc_co_u32_e32 v95, vcc, 0, v85, vcc
	global_load_dwordx4 v[84:87], v[86:87], off offset:2048 nt
	s_nop 0
	global_load_dwordx4 v[88:91], v[94:95], off nt
	global_load_dwordx4 v[112:115], v[92:93], off offset:-4096 nt
	s_nop 0
	global_load_dwordx4 v[92:95], v[94:95], off offset:2048 nt
.LBB0_676:
	s_add_i32 s7, s9, s8
	s_cmpk_lt_i32 s7, 0x80
	s_cselect_b64 s[0:1], -1, 0
	s_cmpk_gt_i32 s7, 0x7f
	s_cbranch_scc1 .LBB0_678
	s_ashr_i32 s5, s7, 31
	s_lshr_b32 s5, s5, 25
	s_add_i32 s5, s7, s5
	s_and_b32 s5, s5, 0xff80
	s_sub_i32 s5, s7, s5
	s_bfe_i32 s14, s5, 0x80000
	s_bfe_u32 s14, s14, 0x3000c
	s_add_i32 s14, s5, s14
	s_bfe_i32 s22, s14, 0x80000
	s_and_b32 s14, s14, 0xf8
	s_sub_i32 s5, s5, s14
	s_sext_i32_i16 s23, s22
	s_sext_i32_i8 s5, s5
	s_lshl_b32 s22, s5, 6
	s_lshl_b32 s5, s23, 3
	s_andn2_b32 s5, s5, 63
	v_add_u32_e32 v20, s5, v221
	v_ashrrev_i32_e32 v21, 31, v20
	v_readlane_b32 s36, v253, 1
	v_lshlrev_b64 v[20:21], 11, v[20:21]
	v_readlane_b32 s37, v253, 2
	s_ashr_i32 s23, s22, 31
	s_movk_i32 s5, 0x1000
	v_lshl_add_u64 v[20:21], s[36:37], 0, v[20:21]
	v_lshl_add_u64 v[20:21], s[22:23], 2, v[20:21]
	v_lshl_add_u64 v[116:117], v[20:21], 0, v[2:3]
	v_add_co_u32_e32 v60, vcc, s5, v116
	global_load_dwordx4 v[24:27], v[116:117], off nt
	global_load_dwordx4 v[20:23], v[116:117], off offset:2048 nt
	v_addc_co_u32_e32 v61, vcc, 0, v117, vcc
	v_add_co_u32_e32 v124, vcc, s83, v116
	s_nop 1
	v_addc_co_u32_e32 v125, vcc, 0, v117, vcc
	v_add_co_u32_e32 v76, vcc, 0x3000, v116
	global_load_dwordx4 v[48:51], v[124:125], off nt
	global_load_dwordx4 v[44:47], v[124:125], off offset:2048 nt
	v_addc_co_u32_e32 v77, vcc, 0, v117, vcc
	v_add_co_u32_e32 v96, vcc, s62, v116
	global_load_dwordx4 v[64:67], v[60:61], off offset:2048 nt
	s_nop 0
	global_load_dwordx4 v[60:63], v[76:77], off nt
	v_addc_co_u32_e32 v97, vcc, 0, v117, vcc
	v_add_co_u32_e32 v104, vcc, 0x5000, v116
	global_load_dwordx4 v[76:79], v[76:77], off offset:2048 nt
	s_nop 0
	global_load_dwordx4 v[80:83], v[96:97], off nt
	v_addc_co_u32_e32 v105, vcc, 0, v117, vcc
	v_add_co_u32_e32 v118, vcc, 0x6000, v116
	global_load_dwordx4 v[96:99], v[96:97], off offset:2048 nt
	s_nop 0
	global_load_dwordx4 v[100:103], v[104:105], off nt
	v_addc_co_u32_e32 v119, vcc, 0, v117, vcc
	v_add_co_u32_e32 v126, vcc, 0x7000, v116
	global_load_dwordx4 v[104:107], v[104:105], off offset:2048 nt
	s_nop 0
	global_load_dwordx4 v[108:111], v[118:119], off nt
	v_addc_co_u32_e32 v127, vcc, 0, v117, vcc
	global_load_dwordx4 v[116:119], v[118:119], off offset:2048 nt
	s_nop 0
	global_load_dwordx4 v[120:123], v[126:127], off nt
	global_load_dwordx4 v[128:131], v[124:125], off offset:-4096 nt
	s_nop 0
	global_load_dwordx4 v[124:127], v[126:127], off offset:2048 nt
.LBB0_678:
	s_waitcnt vmcnt(14)
	v_cvt_pk_bf16_f32 v240, v132, v136
	s_waitcnt vmcnt(1)
	v_cvt_pk_bf16_f32 v241, v192, v156
	v_cvt_pk_bf16_f32 v242, v140, v144
	v_cvt_pk_bf16_f32 v243, v148, v160
	ds_write_b128 v223, v[240:243]
	v_cvt_pk_bf16_f32 v240, v152, v164
	v_cvt_pk_bf16_f32 v241, v168, v172
	v_cvt_pk_bf16_f32 v242, v176, v180
	s_waitcnt vmcnt(0)
	v_cvt_pk_bf16_f32 v243, v184, v188
	ds_write_b128 v224, v[240:243]
	v_cvt_pk_bf16_f32 v240, v133, v137
	v_cvt_pk_bf16_f32 v241, v193, v157
	v_cvt_pk_bf16_f32 v242, v141, v145
	v_cvt_pk_bf16_f32 v243, v149, v161
	ds_write_b128 v223, v[240:243] offset:128
	v_cvt_pk_bf16_f32 v240, v153, v165
	v_cvt_pk_bf16_f32 v241, v169, v173
	v_cvt_pk_bf16_f32 v242, v177, v181
	v_cvt_pk_bf16_f32 v243, v185, v189
	ds_write_b128 v224, v[240:243] offset:128
	v_cvt_pk_bf16_f32 v240, v134, v138
	v_cvt_pk_bf16_f32 v241, v194, v158
	v_cvt_pk_bf16_f32 v242, v142, v146
	v_cvt_pk_bf16_f32 v243, v150, v162
	ds_write_b128 v223, v[240:243] offset:256
	v_cvt_pk_bf16_f32 v240, v154, v166
	v_cvt_pk_bf16_f32 v241, v170, v174
	v_cvt_pk_bf16_f32 v242, v178, v182
	v_cvt_pk_bf16_f32 v243, v186, v190
	ds_write_b128 v224, v[240:243] offset:256
	v_cvt_pk_bf16_f32 v132, v135, v139
	v_cvt_pk_bf16_f32 v133, v195, v159
	v_cvt_pk_bf16_f32 v134, v143, v147
	v_cvt_pk_bf16_f32 v135, v151, v163
	ds_write_b128 v223, v[132:135] offset:384
	v_cvt_pk_bf16_f32 v132, v155, v167
	v_cvt_pk_bf16_f32 v133, v171, v175
	v_cvt_pk_bf16_f32 v134, v179, v183
	v_cvt_pk_bf16_f32 v135, v187, v191
	ds_write_b128 v224, v[132:135] offset:384
	v_add_u32_e32 v132, s6, v222
	v_add_u32_e32 v135, v225, v226
	v_ashrrev_i32_e32 v133, 31, v132
	ds_read_b128 v[136:139], v135
	v_lshlrev_b64 v[132:133], 11, v[132:133]
	v_lshl_add_u64 v[132:133], s[28:29], 0, v[132:133]
	s_ashr_i32 s5, s4, 31
	v_lshl_add_u64 v[132:133], s[4:5], 1, v[132:133]
	v_mov_b32_e32 v1, v3
	v_lshl_add_u64 v[152:153], v[132:133], 0, v[0:1]
	s_waitcnt lgkmcnt(0)
	global_store_dwordx4 v[152:153], v[136:139], off nt
	v_add_co_u32_e32 v132, vcc, s62, v152
	s_nop 0
	v_add_u32_e32 v137, v227, v228
	ds_read_b128 v[144:147], v137
	v_add_u32_e32 v136, v229, v230
	ds_read_b128 v[148:151], v136
	v_addc_co_u32_e32 v133, vcc, 0, v153, vcc
	v_add_u32_e32 v138, v231, v232
	s_waitcnt lgkmcnt(1)
	global_store_dwordx4 v[132:133], v[144:147], off nt
	ds_read_b128 v[144:147], v138
	v_add_co_u32_e32 v132, vcc, s88, v152
	ds_read_b128 v[140:143], v135 offset:4096
	s_nop 0
	v_addc_co_u32_e32 v133, vcc, 0, v153, vcc
	s_waitcnt lgkmcnt(2)
	global_store_dwordx4 v[132:133], v[148:151], off nt
	v_add_co_u32_e32 v132, vcc, s66, v152
	v_add_u32_e32 v134, v233, v234
	s_nop 0
	v_addc_co_u32_e32 v133, vcc, 0, v153, vcc
	ds_read_b128 v[148:151], v134
	s_waitcnt lgkmcnt(2)
	global_store_dwordx4 v[132:133], v[144:147], off nt
	v_add_co_u32_e32 v132, vcc, s82, v152
	s_mov_b32 s4, 0x14000
	s_nop 0
	v_addc_co_u32_e32 v133, vcc, 0, v153, vcc
	s_waitcnt lgkmcnt(1)
	global_store_dwordx4 v[132:133], v[140:143], off nt
	v_add_co_u32_e32 v132, vcc, s4, v152
	s_nop 1
	v_addc_co_u32_e32 v133, vcc, 0, v153, vcc
	s_waitcnt lgkmcnt(0)
	global_store_dwordx4 v[132:133], v[148:151], off nt
	v_add_u32_e32 v133, v235, v236
	ds_read_b128 v[140:143], v133
	v_add_u32_e32 v132, v237, v238
	v_add_co_u32_e32 v148, vcc, 0x18000, v152
	ds_read_b128 v[144:147], v132
	s_nop 0
	v_addc_co_u32_e32 v149, vcc, 0, v153, vcc
	s_waitcnt lgkmcnt(1)
	global_store_dwordx4 v[148:149], v[140:143], off nt
	s_nop 1
	v_add_co_u32_e32 v140, vcc, 0x1c000, v152
	s_nop 1
	v_addc_co_u32_e32 v141, vcc, 0, v153, vcc
	s_andn2_b64 vcc, exec, s[2:3]
	s_waitcnt lgkmcnt(0)
	global_store_dwordx4 v[140:141], v[144:147], off nt
	s_cbranch_vccz .LBB0_680
	s_andn2_b64 vcc, exec, s[0:1]
	s_cbranch_vccnz .LBB0_673
	s_branch .LBB0_681
.LBB0_680:
	s_ashr_i32 s2, s21, 31
	s_lshr_b32 s2, s2, 25
	s_add_i32 s2, s21, s2
	s_and_b32 s2, s2, 0xff80
	v_cvt_pk_bf16_f32 v140, v8, v4
	s_sub_i32 s2, s21, s2
	v_cvt_pk_bf16_f32 v141, v112, v32
	v_cvt_pk_bf16_f32 v142, v16, v12
	v_cvt_pk_bf16_f32 v143, v28, v36
	ds_write_b128 v223, v[140:143]
	v_cvt_pk_bf16_f32 v140, v40, v52
	s_bfe_i32 s3, s2, 0x80000
	v_cvt_pk_bf16_f32 v141, v56, v68
	v_cvt_pk_bf16_f32 v142, v72, v84
	v_cvt_pk_bf16_f32 v143, v88, v92
	ds_write_b128 v224, v[140:143]
	v_cvt_pk_bf16_f32 v140, v9, v5
	s_bfe_u32 s3, s3, 0x3000c
	v_cvt_pk_bf16_f32 v141, v113, v33
	v_cvt_pk_bf16_f32 v142, v17, v13
	v_cvt_pk_bf16_f32 v143, v29, v37
	ds_write_b128 v223, v[140:143] offset:128
	v_cvt_pk_bf16_f32 v140, v41, v53
	s_add_i32 s3, s2, s3
	v_cvt_pk_bf16_f32 v141, v57, v69
	v_cvt_pk_bf16_f32 v142, v73, v85
	v_cvt_pk_bf16_f32 v143, v89, v93
	ds_write_b128 v224, v[140:143] offset:128
	v_cvt_pk_bf16_f32 v140, v10, v6
	s_bfe_i32 s4, s3, 0x80000
	v_cvt_pk_bf16_f32 v141, v114, v34
	v_cvt_pk_bf16_f32 v142, v18, v14
	v_cvt_pk_bf16_f32 v143, v30, v38
	ds_write_b128 v223, v[140:143] offset:256
	v_cvt_pk_bf16_f32 v140, v42, v54
	s_and_b32 s3, s3, 0xf8
	v_cvt_pk_bf16_f32 v141, v58, v70
	v_cvt_pk_bf16_f32 v142, v74, v86
	v_cvt_pk_bf16_f32 v143, v90, v94
	ds_write_b128 v224, v[140:143] offset:256
	v_cvt_pk_bf16_f32 v140, v11, v7
	s_sub_i32 s2, s2, s3
	v_cvt_pk_bf16_f32 v141, v115, v35
	v_cvt_pk_bf16_f32 v142, v19, v15
	v_cvt_pk_bf16_f32 v143, v31, v39
	ds_write_b128 v223, v[140:143] offset:384
	v_cvt_pk_bf16_f32 v140, v43, v55
	s_sext_i32_i8 s2, s2
	s_sext_i32_i16 s4, s4
	v_cvt_pk_bf16_f32 v141, v59, v71
	v_cvt_pk_bf16_f32 v142, v75, v87
	v_cvt_pk_bf16_f32 v143, v91, v95
	ds_write_b128 v224, v[140:143] offset:384
	v_lshl_add_u32 v140, s2, 6, v222
	v_ashrrev_i32_e32 v141, 31, v140
	s_lshl_b32 s2, s4, 3
	v_lshlrev_b64 v[140:141], 11, v[140:141]
	s_andn2_b32 s2, s2, 63
	v_lshl_add_u64 v[140:141], s[28:29], 0, v[140:141]
	s_ashr_i32 s3, s2, 31
	v_lshl_add_u64 v[140:141], s[2:3], 1, v[140:141]
	v_lshl_add_u64 v[144:145], v[140:141], 0, v[0:1]
	ds_read_b128 v[140:143], v135
	v_add_co_u32_e32 v146, vcc, s62, v144
	s_waitcnt lgkmcnt(0)
	global_store_dwordx4 v[144:145], v[140:143], off nt
	ds_read_b128 v[140:143], v137
	v_addc_co_u32_e32 v147, vcc, 0, v145, vcc
	s_waitcnt lgkmcnt(0)
	global_store_dwordx4 v[146:147], v[140:143], off nt
	ds_read_b128 v[140:143], v136
	v_add_co_u32_e32 v146, vcc, 0x8000, v144
	s_nop 1
	v_addc_co_u32_e32 v147, vcc, 0, v145, vcc
	s_waitcnt lgkmcnt(0)
	global_store_dwordx4 v[146:147], v[140:143], off nt
	ds_read_b128 v[140:143], v138
	v_add_co_u32_e32 v146, vcc, 0xc000, v144
	s_nop 1
	v_addc_co_u32_e32 v147, vcc, 0, v145, vcc
	s_waitcnt lgkmcnt(0)
	global_store_dwordx4 v[146:147], v[140:143], off nt
	ds_read_b128 v[140:143], v135 offset:4096
	v_add_co_u32_e32 v146, vcc, s82, v144
	s_nop 1
	v_addc_co_u32_e32 v147, vcc, 0, v145, vcc
	s_waitcnt lgkmcnt(0)
	global_store_dwordx4 v[146:147], v[140:143], off nt
	ds_read_b128 v[140:143], v134
	v_add_co_u32_e32 v146, vcc, 0x14000, v144
	s_nop 1
	v_addc_co_u32_e32 v147, vcc, 0, v145, vcc
	s_waitcnt lgkmcnt(0)
	global_store_dwordx4 v[146:147], v[140:143], off nt
	ds_read_b128 v[140:143], v133
	v_add_co_u32_e32 v146, vcc, 0x18000, v144
	s_nop 1
	v_addc_co_u32_e32 v147, vcc, 0, v145, vcc
	s_waitcnt lgkmcnt(0)
	global_store_dwordx4 v[146:147], v[140:143], off nt
	ds_read_b128 v[140:143], v132
	v_add_co_u32_e32 v144, vcc, 0x1c000, v144
	s_nop 1
	v_addc_co_u32_e32 v145, vcc, 0, v145, vcc
	s_waitcnt lgkmcnt(0)
	global_store_dwordx4 v[144:145], v[140:143], off nt
	s_andn2_b64 vcc, exec, s[0:1]
	s_cbranch_vccnz .LBB0_673
.LBB0_681:
	s_ashr_i32 s0, s7, 31
	s_lshr_b32 s0, s0, 25
	s_add_i32 s0, s7, s0
	s_and_b32 s0, s0, 0xff80
	v_cvt_pk_bf16_f32 v140, v24, v20
	s_sub_i32 s0, s7, s0
	v_cvt_pk_bf16_f32 v141, v128, v64
	v_cvt_pk_bf16_f32 v142, v48, v44
	v_cvt_pk_bf16_f32 v143, v60, v76
	ds_write_b128 v223, v[140:143]
	v_cvt_pk_bf16_f32 v140, v80, v96
	s_bfe_i32 s1, s0, 0x80000
	v_cvt_pk_bf16_f32 v141, v100, v104
	v_cvt_pk_bf16_f32 v142, v108, v116
	v_cvt_pk_bf16_f32 v143, v120, v124
	ds_write_b128 v224, v[140:143]
	v_cvt_pk_bf16_f32 v140, v25, v21
	s_bfe_u32 s1, s1, 0x3000c
	v_cvt_pk_bf16_f32 v141, v129, v65
	v_cvt_pk_bf16_f32 v142, v49, v45
	v_cvt_pk_bf16_f32 v143, v61, v77
	ds_write_b128 v223, v[140:143] offset:128
	v_cvt_pk_bf16_f32 v140, v81, v97
	s_add_i32 s1, s0, s1
	v_cvt_pk_bf16_f32 v141, v101, v105
	v_cvt_pk_bf16_f32 v142, v109, v117
	v_cvt_pk_bf16_f32 v143, v121, v125
	ds_write_b128 v224, v[140:143] offset:128
	v_cvt_pk_bf16_f32 v140, v26, v22
	s_bfe_i32 s2, s1, 0x80000
	v_cvt_pk_bf16_f32 v141, v130, v66
	v_cvt_pk_bf16_f32 v142, v50, v46
	v_cvt_pk_bf16_f32 v143, v62, v78
	ds_write_b128 v223, v[140:143] offset:256
	v_cvt_pk_bf16_f32 v140, v82, v98
	s_and_b32 s1, s1, 0xf8
	v_cvt_pk_bf16_f32 v141, v102, v106
	v_cvt_pk_bf16_f32 v142, v110, v118
	v_cvt_pk_bf16_f32 v143, v122, v126
	ds_write_b128 v224, v[140:143] offset:256
	v_cvt_pk_bf16_f32 v140, v27, v23
	s_sub_i32 s0, s0, s1
	v_cvt_pk_bf16_f32 v141, v131, v67
	v_cvt_pk_bf16_f32 v142, v51, v47
	v_cvt_pk_bf16_f32 v143, v63, v79
	ds_write_b128 v223, v[140:143] offset:384
	v_cvt_pk_bf16_f32 v140, v83, v99
	s_sext_i32_i8 s0, s0
	s_sext_i32_i16 s2, s2
	v_cvt_pk_bf16_f32 v141, v103, v107
	v_cvt_pk_bf16_f32 v142, v111, v119
	v_cvt_pk_bf16_f32 v143, v123, v127
	ds_write_b128 v224, v[140:143] offset:384
	v_lshl_add_u32 v140, s0, 6, v222
	v_ashrrev_i32_e32 v141, 31, v140
	s_lshl_b32 s0, s2, 3
	v_lshlrev_b64 v[140:141], 11, v[140:141]
	s_andn2_b32 s0, s0, 63
	v_lshl_add_u64 v[140:141], s[28:29], 0, v[140:141]
	s_ashr_i32 s1, s0, 31
	v_lshl_add_u64 v[140:141], s[0:1], 1, v[140:141]
	v_mov_b32_e32 v1, v3
	v_lshl_add_u64 v[144:145], v[140:141], 0, v[0:1]
	ds_read_b128 v[140:143], v135
	v_add_co_u32_e32 v146, vcc, s62, v144
	s_waitcnt lgkmcnt(0)
	global_store_dwordx4 v[144:145], v[140:143], off nt
	ds_read_b128 v[140:143], v137
	v_addc_co_u32_e32 v147, vcc, 0, v145, vcc
	s_waitcnt lgkmcnt(0)
	global_store_dwordx4 v[146:147], v[140:143], off nt
	ds_read_b128 v[140:143], v136
	v_add_co_u32_e32 v136, vcc, 0x8000, v144
	s_nop 1
	v_addc_co_u32_e32 v137, vcc, 0, v145, vcc
	s_waitcnt lgkmcnt(0)
	global_store_dwordx4 v[136:137], v[140:143], off nt
	ds_read_b128 v[136:139], v138
	s_nop 0
	v_add_co_u32_e32 v140, vcc, 0xc000, v144
	s_nop 1
	v_addc_co_u32_e32 v141, vcc, 0, v145, vcc
	s_waitcnt lgkmcnt(0)
	global_store_dwordx4 v[140:141], v[136:139], off nt
	ds_read_b128 v[136:139], v135 offset:4096
	v_add_co_u32_e32 v140, vcc, s82, v144
	s_nop 1
	v_addc_co_u32_e32 v141, vcc, 0, v145, vcc
	s_waitcnt lgkmcnt(0)
	global_store_dwordx4 v[140:141], v[136:139], off nt
	ds_read_b128 v[134:137], v134
	s_nop 0
	v_add_co_u32_e32 v138, vcc, 0x14000, v144
	s_nop 1
	v_addc_co_u32_e32 v139, vcc, 0, v145, vcc
	s_waitcnt lgkmcnt(0)
	global_store_dwordx4 v[138:139], v[134:137], off nt
	ds_read_b128 v[134:137], v133
	v_add_co_u32_e32 v138, vcc, 0x18000, v144
	s_nop 1
	v_addc_co_u32_e32 v139, vcc, 0, v145, vcc
	s_waitcnt lgkmcnt(0)
	global_store_dwordx4 v[138:139], v[134:137], off nt
	ds_read_b128 v[132:135], v132
	s_nop 0
	v_add_co_u32_e32 v136, vcc, 0x1c000, v144
	s_nop 1
	v_addc_co_u32_e32 v137, vcc, 0, v145, vcc
	s_waitcnt lgkmcnt(0)
	global_store_dwordx4 v[136:137], v[132:135], off nt
	s_branch .LBB0_673

.LBB0_685:
	s_add_i32 s21, s38, s8
	s_cmpk_lt_i32 s21, 0x100
	s_cselect_b64 s[2:3], -1, 0
	s_ashr_i32 s0, s8, 31
	s_lshr_b32 s0, s0, 24
	s_add_i32 s0, s8, s0
	s_and_b32 s0, s0, 0xff00
	s_sub_i32 s0, s8, s0
	s_sext_i32_i16 s1, s0
	s_bfe_u32 s1, s1, 0x4001b
	s_add_i32 s1, s0, s1
	s_sext_i32_i16 s4, s1
	s_and_b32 s1, s1, 0xfff0
	s_sub_i32 s0, s0, s1
	s_sext_i32_i16 s0, s0
	s_lshl_b32 s6, s0, 6
	s_lshl_b32 s0, s4, 2
	s_and_b32 s4, s0, 0xffffffc0
	v_add_u32_e32 v132, s4, v221
	v_ashrrev_i32_e32 v133, 31, v132
	v_readlane_b32 s0, v253, 3
	v_lshlrev_b64 v[132:133], 12, v[132:133]
	v_readlane_b32 s1, v253, 4
	s_ashr_i32 s7, s6, 31
	s_cmpk_gt_i32 s21, 0xff
	v_lshl_add_u64 v[132:133], s[0:1], 0, v[132:133]
	v_lshl_add_u64 v[132:133], s[6:7], 2, v[132:133]
	v_lshl_add_u64 v[188:189], v[132:133], 0, v[2:3]
	v_add_co_u32_e32 v132, vcc, s83, v188
	s_nop 1
	v_addc_co_u32_e32 v133, vcc, 0, v189, vcc
	v_add_co_u32_e32 v140, vcc, s62, v188
	global_load_dwordx4 v[136:139], v[132:133], off offset:-4096 nt
	s_nop 0
	global_load_dwordx4 v[132:135], v[132:133], off nt
	v_addc_co_u32_e32 v141, vcc, 0, v189, vcc
	v_add_co_u32_e32 v148, vcc, s77, v188
	global_load_dwordx4 v[144:147], v[140:141], off offset:-4096 nt
	s_nop 0
	global_load_dwordx4 v[140:143], v[140:141], off nt
	v_addc_co_u32_e32 v149, vcc, 0, v189, vcc
	v_add_co_u32_e32 v152, vcc, s88, v188
	global_load_dwordx4 v[156:159], v[148:149], off offset:-4096 nt
	s_nop 0
	global_load_dwordx4 v[148:151], v[148:149], off nt
	v_addc_co_u32_e32 v153, vcc, 0, v189, vcc
	v_add_co_u32_e32 v160, vcc, s72, v188
	global_load_dwordx4 v[164:167], v[152:153], off offset:-4096 nt
	s_nop 0
	global_load_dwordx4 v[152:155], v[152:153], off nt
	v_addc_co_u32_e32 v161, vcc, 0, v189, vcc
	v_add_co_u32_e32 v172, vcc, 0xb000, v188
	global_load_dwordx4 v[168:171], v[160:161], off offset:-4096 nt
	s_nop 0
	global_load_dwordx4 v[160:163], v[160:161], off nt
	v_addc_co_u32_e32 v173, vcc, 0, v189, vcc
	v_add_co_u32_e32 v176, vcc, s66, v188
	global_load_dwordx4 v[184:187], v[188:189], off nt
	s_nop 0
	global_load_dwordx4 v[172:175], v[172:173], off nt
	v_addc_co_u32_e32 v177, vcc, 0, v189, vcc
	v_add_co_u32_e32 v180, vcc, 0xd000, v188
	s_nop 1
	v_addc_co_u32_e32 v181, vcc, 0, v189, vcc
	v_add_co_u32_e32 v190, vcc, 0xe000, v188
	global_load_dwordx4 v[176:179], v[176:177], off nt
	s_nop 0
	global_load_dwordx4 v[180:183], v[180:181], off nt
	v_addc_co_u32_e32 v191, vcc, 0, v189, vcc
	v_add_co_u32_e32 v192, vcc, 0xf000, v188
	s_nop 1
	v_addc_co_u32_e32 v193, vcc, 0, v189, vcc
	global_load_dwordx4 v[188:191], v[190:191], off nt
	s_nop 0
	global_load_dwordx4 v[192:195], v[192:193], off nt
	s_cbranch_scc1 .LBB0_687
	s_ashr_i32 s0, s21, 31
	s_lshr_b32 s0, s0, 24
	s_add_i32 s0, s21, s0
	s_and_b32 s0, s0, 0xff00
	s_sub_i32 s0, s21, s0
	s_sext_i32_i16 s1, s0
	s_bfe_u32 s1, s1, 0x4001b
	s_add_i32 s1, s0, s1
	s_sext_i32_i16 s5, s1
	s_and_b32 s1, s1, 0xfff0
	s_sub_i32 s0, s0, s1
	s_lshl_b32 s1, s5, 2
	s_andn2_b32 s1, s1, 63
	v_add_u32_e32 v4, s1, v221
	s_sext_i32_i16 s0, s0
	v_ashrrev_i32_e32 v5, 31, v4
	v_readlane_b32 s22, v253, 3
	s_lshl_b32 s0, s0, 6
	v_lshlrev_b64 v[4:5], 12, v[4:5]
	v_readlane_b32 s23, v253, 4
	s_ashr_i32 s1, s0, 31
	s_nop 0
	v_lshl_add_u64 v[4:5], s[22:23], 0, v[4:5]
	v_lshl_add_u64 v[4:5], s[0:1], 2, v[4:5]
	v_lshl_add_u64 v[108:109], v[4:5], 0, v[2:3]
	v_add_co_u32_e32 v4, vcc, s83, v108
	s_nop 1
	v_addc_co_u32_e32 v5, vcc, 0, v109, vcc
	v_add_co_u32_e32 v12, vcc, s62, v108
	global_load_dwordx4 v[8:11], v[4:5], off offset:-4096 nt
	s_nop 0
	global_load_dwordx4 v[4:7], v[4:5], off nt
	v_addc_co_u32_e32 v13, vcc, 0, v109, vcc
	v_add_co_u32_e32 v20, vcc, s77, v108
	global_load_dwordx4 v[16:19], v[12:13], off offset:-4096 nt
	s_nop 0
	global_load_dwordx4 v[12:15], v[12:13], off nt
	v_addc_co_u32_e32 v21, vcc, 0, v109, vcc
	v_add_co_u32_e32 v28, vcc, s88, v108
	global_load_dwordx4 v[24:27], v[20:21], off offset:-4096 nt
	s_nop 0
	global_load_dwordx4 v[20:23], v[20:21], off nt
	v_addc_co_u32_e32 v29, vcc, 0, v109, vcc
	v_add_co_u32_e32 v52, vcc, 0x9000, v108
	global_load_dwordx4 v[32:35], v[28:29], off offset:-4096 nt
	s_nop 0
	global_load_dwordx4 v[28:31], v[28:29], off nt
	v_addc_co_u32_e32 v53, vcc, 0, v109, vcc
	v_add_co_u32_e32 v68, vcc, s72, v108
	global_load_dwordx4 v[64:67], v[108:109], off nt
	s_nop 0
	global_load_dwordx4 v[52:55], v[52:53], off nt
	v_addc_co_u32_e32 v69, vcc, 0, v109, vcc
	v_add_co_u32_e32 v80, vcc, 0xb000, v108
	s_nop 1
	v_addc_co_u32_e32 v81, vcc, 0, v109, vcc
	v_add_co_u32_e32 v88, vcc, 0xc000, v108
	global_load_dwordx4 v[68:71], v[68:69], off nt
	s_nop 0
	global_load_dwordx4 v[80:83], v[80:81], off nt
	v_addc_co_u32_e32 v89, vcc, 0, v109, vcc
	v_add_co_u32_e32 v96, vcc, 0xd000, v108
	s_nop 1
	v_addc_co_u32_e32 v97, vcc, 0, v109, vcc
	v_add_co_u32_e32 v110, vcc, 0xe000, v108
	global_load_dwordx4 v[88:91], v[88:89], off nt
	s_nop 0
	global_load_dwordx4 v[96:99], v[96:97], off nt
	v_addc_co_u32_e32 v111, vcc, 0, v109, vcc
	v_add_co_u32_e32 v112, vcc, 0xf000, v108
	s_nop 1
	v_addc_co_u32_e32 v113, vcc, 0, v109, vcc
	global_load_dwordx4 v[108:111], v[110:111], off nt
	s_nop 0
	global_load_dwordx4 v[112:115], v[112:113], off nt
.LBB0_687:
	s_add_i32 s7, s9, s8
	s_cmpk_lt_i32 s7, 0x100
	s_cselect_b64 s[0:1], -1, 0
	s_cmpk_gt_i32 s7, 0xff
	s_cbranch_scc1 .LBB0_689
	s_ashr_i32 s5, s7, 31
	s_lshr_b32 s5, s5, 24
	s_add_i32 s5, s7, s5
	s_and_b32 s5, s5, 0xff00
	s_sub_i32 s5, s7, s5
	s_sext_i32_i16 s14, s5
	s_bfe_u32 s14, s14, 0x4001b
	s_add_i32 s14, s5, s14
	s_sext_i32_i16 s23, s14
	s_and_b32 s14, s14, 0xfff0
	s_sub_i32 s5, s5, s14
	s_sext_i32_i16 s5, s5
	s_lshl_b32 s22, s5, 6
	s_lshl_b32 s5, s23, 2
	s_andn2_b32 s5, s5, 63
	v_add_u32_e32 v36, s5, v221
	v_ashrrev_i32_e32 v37, 31, v36
	v_readlane_b32 s36, v253, 3
	v_lshlrev_b64 v[36:37], 12, v[36:37]
	v_readlane_b32 s37, v253, 4
	s_ashr_i32 s23, s22, 31
	s_nop 0
	v_lshl_add_u64 v[36:37], s[36:37], 0, v[36:37]
	v_lshl_add_u64 v[36:37], s[22:23], 2, v[36:37]
	v_lshl_add_u64 v[124:125], v[36:37], 0, v[2:3]
	v_add_co_u32_e32 v36, vcc, s83, v124
	s_nop 1
	v_addc_co_u32_e32 v37, vcc, 0, v125, vcc
	v_add_co_u32_e32 v44, vcc, s62, v124
	global_load_dwordx4 v[40:43], v[36:37], off offset:-4096 nt
	s_nop 0
	global_load_dwordx4 v[36:39], v[36:37], off nt
	v_addc_co_u32_e32 v45, vcc, 0, v125, vcc
	v_add_co_u32_e32 v56, vcc, s77, v124
	global_load_dwordx4 v[48:51], v[44:45], off offset:-4096 nt
	s_nop 0
	global_load_dwordx4 v[44:47], v[44:45], off nt
	v_addc_co_u32_e32 v57, vcc, 0, v125, vcc
	v_add_co_u32_e32 v72, vcc, s88, v124
	global_load_dwordx4 v[60:63], v[56:57], off offset:-4096 nt
	s_nop 0
	global_load_dwordx4 v[56:59], v[56:57], off nt
	v_addc_co_u32_e32 v73, vcc, 0, v125, vcc
	v_add_co_u32_e32 v84, vcc, 0x9000, v124
	global_load_dwordx4 v[76:79], v[72:73], off offset:-4096 nt
	s_nop 0
	global_load_dwordx4 v[72:75], v[72:73], off nt
	v_addc_co_u32_e32 v85, vcc, 0, v125, vcc
	v_add_co_u32_e32 v100, vcc, s72, v124
	global_load_dwordx4 v[92:95], v[124:125], off nt
	s_nop 0
	global_load_dwordx4 v[84:87], v[84:85], off nt
	v_addc_co_u32_e32 v101, vcc, 0, v125, vcc
	v_add_co_u32_e32 v104, vcc, 0xb000, v124
	s_nop 1
	v_addc_co_u32_e32 v105, vcc, 0, v125, vcc
	v_add_co_u32_e32 v116, vcc, 0xc000, v124
	global_load_dwordx4 v[100:103], v[100:101], off nt
	s_nop 0
	global_load_dwordx4 v[104:107], v[104:105], off nt
	v_addc_co_u32_e32 v117, vcc, 0, v125, vcc
	v_add_co_u32_e32 v120, vcc, 0xd000, v124
	s_nop 1
	v_addc_co_u32_e32 v121, vcc, 0, v125, vcc
	v_add_co_u32_e32 v126, vcc, 0xe000, v124
	global_load_dwordx4 v[116:119], v[116:117], off nt
	s_nop 0
	global_load_dwordx4 v[120:123], v[120:121], off nt
	v_addc_co_u32_e32 v127, vcc, 0, v125, vcc
	v_add_co_u32_e32 v128, vcc, 0xf000, v124
	s_nop 1
	v_addc_co_u32_e32 v129, vcc, 0, v125, vcc
	global_load_dwordx4 v[124:127], v[126:127], off nt
	s_nop 0
	global_load_dwordx4 v[128:131], v[128:129], off nt

.LBB0_696:
	s_add_i32 s21, s38, s8
	s_cmpk_lt_i32 s21, 0x80
	s_cselect_b64 s[2:3], -1, 0
	s_ashr_i32 s0, s8, 31
	s_lshr_b32 s0, s0, 25
	s_add_i32 s0, s8, s0
	s_and_b32 s0, s0, 0xff80
	s_sub_i32 s0, s8, s0
	s_bfe_i32 s1, s0, 0x80000
	s_bfe_u32 s1, s1, 0x4000b
	s_add_i32 s1, s0, s1
	s_bfe_i32 s4, s1, 0x80000
	s_and_b32 s1, s1, 0xf0
	s_sub_i32 s0, s0, s1
	s_sext_i32_i16 s4, s4
	s_sext_i32_i8 s0, s0
	s_lshl_b32 s6, s0, 6
	s_lshl_b32 s0, s4, 2
	s_and_b32 s4, s0, 0xffffffc0
	v_add_u32_e32 v132, s4, v221
	v_ashrrev_i32_e32 v133, 31, v132
	v_readlane_b32 s0, v253, 5
	v_lshlrev_b64 v[132:133], 12, v[132:133]
	v_readlane_b32 s1, v253, 6
	s_ashr_i32 s7, s6, 31
	s_cmpk_gt_i32 s21, 0x7f
	v_lshl_add_u64 v[132:133], s[0:1], 0, v[132:133]
	v_lshl_add_u64 v[132:133], s[6:7], 2, v[132:133]
	v_lshl_add_u64 v[188:189], v[132:133], 0, v[2:3]
	v_add_co_u32_e32 v132, vcc, s83, v188
	s_nop 1
	v_addc_co_u32_e32 v133, vcc, 0, v189, vcc
	v_add_co_u32_e32 v140, vcc, s62, v188
	global_load_dwordx4 v[136:139], v[132:133], off offset:-4096 nt
	s_nop 0
	global_load_dwordx4 v[132:135], v[132:133], off nt
	v_addc_co_u32_e32 v141, vcc, 0, v189, vcc
	v_add_co_u32_e32 v148, vcc, s77, v188
	global_load_dwordx4 v[144:147], v[140:141], off offset:-4096 nt
	s_nop 0
	global_load_dwordx4 v[140:143], v[140:141], off nt
	v_addc_co_u32_e32 v149, vcc, 0, v189, vcc
	v_add_co_u32_e32 v152, vcc, s88, v188
	global_load_dwordx4 v[156:159], v[148:149], off offset:-4096 nt
	s_nop 0
	global_load_dwordx4 v[148:151], v[148:149], off nt
	v_addc_co_u32_e32 v153, vcc, 0, v189, vcc
	v_add_co_u32_e32 v160, vcc, s72, v188
	global_load_dwordx4 v[164:167], v[152:153], off offset:-4096 nt
	s_nop 0
	global_load_dwordx4 v[152:155], v[152:153], off nt
	v_addc_co_u32_e32 v161, vcc, 0, v189, vcc
	v_add_co_u32_e32 v172, vcc, 0xb000, v188
	global_load_dwordx4 v[168:171], v[160:161], off offset:-4096 nt
	s_nop 0
	global_load_dwordx4 v[160:163], v[160:161], off nt
	v_addc_co_u32_e32 v173, vcc, 0, v189, vcc
	v_add_co_u32_e32 v176, vcc, s66, v188
	global_load_dwordx4 v[184:187], v[188:189], off nt
	s_nop 0
	global_load_dwordx4 v[172:175], v[172:173], off nt
	v_addc_co_u32_e32 v177, vcc, 0, v189, vcc
	v_add_co_u32_e32 v180, vcc, 0xd000, v188
	s_nop 1
	v_addc_co_u32_e32 v181, vcc, 0, v189, vcc
	v_add_co_u32_e32 v190, vcc, 0xe000, v188
	global_load_dwordx4 v[176:179], v[176:177], off nt
	s_nop 0
	global_load_dwordx4 v[180:183], v[180:181], off nt
	v_addc_co_u32_e32 v191, vcc, 0, v189, vcc
	v_add_co_u32_e32 v192, vcc, 0xf000, v188
	s_nop 1
	v_addc_co_u32_e32 v193, vcc, 0, v189, vcc
	global_load_dwordx4 v[188:191], v[190:191], off nt
	s_nop 0
	global_load_dwordx4 v[192:195], v[192:193], off nt
	s_cbranch_scc1 .LBB0_698
	s_ashr_i32 s0, s21, 31
	s_lshr_b32 s0, s0, 25
	s_add_i32 s0, s21, s0
	s_and_b32 s0, s0, 0xff80
	s_sub_i32 s0, s21, s0
	s_bfe_i32 s1, s0, 0x80000
	s_bfe_u32 s1, s1, 0x4000b
	s_add_i32 s1, s0, s1
	s_bfe_i32 s5, s1, 0x80000
	s_sext_i32_i16 s5, s5
	s_and_b32 s1, s1, 0xf0
	s_sub_i32 s0, s0, s1
	s_lshl_b32 s1, s5, 2
	s_andn2_b32 s1, s1, 63
	v_add_u32_e32 v4, s1, v221
	s_sext_i32_i8 s0, s0
	v_ashrrev_i32_e32 v5, 31, v4
	v_readlane_b32 s22, v253, 5
	s_lshl_b32 s0, s0, 6
	v_lshlrev_b64 v[4:5], 12, v[4:5]
	v_readlane_b32 s23, v253, 6
	s_ashr_i32 s1, s0, 31
	s_nop 0
	v_lshl_add_u64 v[4:5], s[22:23], 0, v[4:5]
	v_lshl_add_u64 v[4:5], s[0:1], 2, v[4:5]
	v_lshl_add_u64 v[108:109], v[4:5], 0, v[2:3]
	v_add_co_u32_e32 v4, vcc, s83, v108
	s_nop 1
	v_addc_co_u32_e32 v5, vcc, 0, v109, vcc
	v_add_co_u32_e32 v12, vcc, s62, v108
	global_load_dwordx4 v[8:11], v[4:5], off offset:-4096 nt
	s_nop 0
	global_load_dwordx4 v[4:7], v[4:5], off nt
	v_addc_co_u32_e32 v13, vcc, 0, v109, vcc
	v_add_co_u32_e32 v20, vcc, s77, v108
	global_load_dwordx4 v[16:19], v[12:13], off offset:-4096 nt
	s_nop 0
	global_load_dwordx4 v[12:15], v[12:13], off nt
	v_addc_co_u32_e32 v21, vcc, 0, v109, vcc
	v_add_co_u32_e32 v28, vcc, s88, v108
	global_load_dwordx4 v[24:27], v[20:21], off offset:-4096 nt
	s_nop 0
	global_load_dwordx4 v[20:23], v[20:21], off nt
	v_addc_co_u32_e32 v29, vcc, 0, v109, vcc
	v_add_co_u32_e32 v52, vcc, 0x9000, v108
	global_load_dwordx4 v[32:35], v[28:29], off offset:-4096 nt
	s_nop 0
	global_load_dwordx4 v[28:31], v[28:29], off nt
	v_addc_co_u32_e32 v53, vcc, 0, v109, vcc
	v_add_co_u32_e32 v68, vcc, s72, v108
	global_load_dwordx4 v[64:67], v[108:109], off nt
	s_nop 0
	global_load_dwordx4 v[52:55], v[52:53], off nt
	v_addc_co_u32_e32 v69, vcc, 0, v109, vcc
	v_add_co_u32_e32 v80, vcc, 0xb000, v108
	s_nop 1
	v_addc_co_u32_e32 v81, vcc, 0, v109, vcc
	v_add_co_u32_e32 v88, vcc, 0xc000, v108
	global_load_dwordx4 v[68:71], v[68:69], off nt
	s_nop 0
	global_load_dwordx4 v[80:83], v[80:81], off nt
	v_addc_co_u32_e32 v89, vcc, 0, v109, vcc
	v_add_co_u32_e32 v96, vcc, 0xd000, v108
	s_nop 1
	v_addc_co_u32_e32 v97, vcc, 0, v109, vcc
	v_add_co_u32_e32 v110, vcc, 0xe000, v108
	global_load_dwordx4 v[88:91], v[88:89], off nt
	s_nop 0
	global_load_dwordx4 v[96:99], v[96:97], off nt
	v_addc_co_u32_e32 v111, vcc, 0, v109, vcc
	v_add_co_u32_e32 v112, vcc, 0xf000, v108
	s_nop 1
	v_addc_co_u32_e32 v113, vcc, 0, v109, vcc
	global_load_dwordx4 v[108:111], v[110:111], off nt
	s_nop 0
	global_load_dwordx4 v[112:115], v[112:113], off nt
.LBB0_698:
	s_add_i32 s7, s9, s8
	s_cmpk_lt_i32 s7, 0x80
	s_cselect_b64 s[0:1], -1, 0
	s_cmpk_gt_i32 s7, 0x7f
	s_cbranch_scc1 .LBB0_700
	s_ashr_i32 s5, s7, 31
	s_lshr_b32 s5, s5, 25
	s_add_i32 s5, s7, s5
	s_and_b32 s5, s5, 0xff80
	s_sub_i32 s5, s7, s5
	s_bfe_i32 s14, s5, 0x80000
	s_bfe_u32 s14, s14, 0x4000b
	s_add_i32 s14, s5, s14
	s_bfe_i32 s22, s14, 0x80000
	s_and_b32 s14, s14, 0xf0
	s_sub_i32 s5, s5, s14
	s_sext_i32_i16 s23, s22
	s_sext_i32_i8 s5, s5
	s_lshl_b32 s22, s5, 6
	s_lshl_b32 s5, s23, 2
	s_andn2_b32 s5, s5, 63
	v_add_u32_e32 v36, s5, v221
	v_ashrrev_i32_e32 v37, 31, v36
	v_readlane_b32 s36, v253, 5
	v_lshlrev_b64 v[36:37], 12, v[36:37]
	v_readlane_b32 s37, v253, 6
	s_ashr_i32 s23, s22, 31
	s_nop 0
	v_lshl_add_u64 v[36:37], s[36:37], 0, v[36:37]
	v_lshl_add_u64 v[36:37], s[22:23], 2, v[36:37]
	v_lshl_add_u64 v[124:125], v[36:37], 0, v[2:3]
	v_add_co_u32_e32 v36, vcc, s83, v124
	s_nop 1
	v_addc_co_u32_e32 v37, vcc, 0, v125, vcc
	v_add_co_u32_e32 v44, vcc, s62, v124
	global_load_dwordx4 v[40:43], v[36:37], off offset:-4096 nt
	s_nop 0
	global_load_dwordx4 v[36:39], v[36:37], off nt
	v_addc_co_u32_e32 v45, vcc, 0, v125, vcc
	v_add_co_u32_e32 v56, vcc, s77, v124
	global_load_dwordx4 v[48:51], v[44:45], off offset:-4096 nt
	s_nop 0
	global_load_dwordx4 v[44:47], v[44:45], off nt
	v_addc_co_u32_e32 v57, vcc, 0, v125, vcc
	v_add_co_u32_e32 v72, vcc, s88, v124
	global_load_dwordx4 v[60:63], v[56:57], off offset:-4096 nt
	s_nop 0
	global_load_dwordx4 v[56:59], v[56:57], off nt
	v_addc_co_u32_e32 v73, vcc, 0, v125, vcc
	v_add_co_u32_e32 v84, vcc, 0x9000, v124
	global_load_dwordx4 v[76:79], v[72:73], off offset:-4096 nt
	s_nop 0
	global_load_dwordx4 v[72:75], v[72:73], off nt
	v_addc_co_u32_e32 v85, vcc, 0, v125, vcc
	v_add_co_u32_e32 v100, vcc, s72, v124
	global_load_dwordx4 v[92:95], v[124:125], off nt
	s_nop 0
	global_load_dwordx4 v[84:87], v[84:85], off nt
	v_addc_co_u32_e32 v101, vcc, 0, v125, vcc
	v_add_co_u32_e32 v104, vcc, 0xb000, v124
	s_nop 1
	v_addc_co_u32_e32 v105, vcc, 0, v125, vcc
	v_add_co_u32_e32 v116, vcc, 0xc000, v124
	global_load_dwordx4 v[100:103], v[100:101], off nt
	s_nop 0
	global_load_dwordx4 v[104:107], v[104:105], off nt
	v_addc_co_u32_e32 v117, vcc, 0, v125, vcc
	v_add_co_u32_e32 v120, vcc, 0xd000, v124
	s_nop 1
	v_addc_co_u32_e32 v121, vcc, 0, v125, vcc
	v_add_co_u32_e32 v126, vcc, 0xe000, v124
	global_load_dwordx4 v[116:119], v[116:117], off nt
	s_nop 0
	global_load_dwordx4 v[120:123], v[120:121], off nt
	v_addc_co_u32_e32 v127, vcc, 0, v125, vcc
	v_add_co_u32_e32 v128, vcc, 0xf000, v124
	s_nop 1
	v_addc_co_u32_e32 v129, vcc, 0, v125, vcc
	global_load_dwordx4 v[124:127], v[126:127], off nt
	s_nop 0
	global_load_dwordx4 v[128:131], v[128:129], off nt
.LBB0_700:
	s_waitcnt vmcnt(5)
	v_cvt_pk_bf16_f32 v240, v184, v136
	v_cvt_pk_bf16_f32 v241, v132, v144
	v_cvt_pk_bf16_f32 v242, v140, v156
	v_cvt_pk_bf16_f32 v243, v148, v164
	ds_write_b128 v223, v[240:243]
	v_cvt_pk_bf16_f32 v240, v152, v168
	s_waitcnt vmcnt(4)
	v_cvt_pk_bf16_f32 v241, v160, v172
	s_waitcnt vmcnt(2)
	v_cvt_pk_bf16_f32 v242, v176, v180
	s_waitcnt vmcnt(0)
	v_cvt_pk_bf16_f32 v243, v188, v192
	ds_write_b128 v224, v[240:243]
	v_cvt_pk_bf16_f32 v240, v185, v137
	v_cvt_pk_bf16_f32 v241, v133, v145
	v_cvt_pk_bf16_f32 v242, v141, v157
	v_cvt_pk_bf16_f32 v243, v149, v165
	ds_write_b128 v223, v[240:243] offset:128
	v_cvt_pk_bf16_f32 v240, v153, v169
	v_cvt_pk_bf16_f32 v241, v161, v173
	v_cvt_pk_bf16_f32 v242, v177, v181
	v_cvt_pk_bf16_f32 v243, v189, v193
	ds_write_b128 v224, v[240:243] offset:128
	v_cvt_pk_bf16_f32 v240, v186, v138
	v_cvt_pk_bf16_f32 v241, v134, v146
	v_cvt_pk_bf16_f32 v242, v142, v158
	v_cvt_pk_bf16_f32 v243, v150, v166
	ds_write_b128 v223, v[240:243] offset:256
	v_cvt_pk_bf16_f32 v240, v154, v170
	v_cvt_pk_bf16_f32 v241, v162, v174
	v_cvt_pk_bf16_f32 v242, v178, v182
	v_cvt_pk_bf16_f32 v243, v190, v194
	ds_write_b128 v224, v[240:243] offset:256
	v_cvt_pk_bf16_f32 v132, v187, v139
	v_cvt_pk_bf16_f32 v133, v135, v147
	v_cvt_pk_bf16_f32 v134, v143, v159
	v_cvt_pk_bf16_f32 v135, v151, v167
	ds_write_b128 v223, v[132:135] offset:384
	v_cvt_pk_bf16_f32 v132, v155, v171
	v_cvt_pk_bf16_f32 v133, v163, v175
	v_cvt_pk_bf16_f32 v134, v179, v183
	v_cvt_pk_bf16_f32 v135, v191, v195
	ds_write_b128 v224, v[132:135] offset:384
	v_add_u32_e32 v132, s6, v222
	v_add_u32_e32 v135, v225, v226
	v_ashrrev_i32_e32 v133, 31, v132
	ds_read_b128 v[136:139], v135
	v_lshlrev_b64 v[132:133], 10, v[132:133]
	v_lshl_add_u64 v[132:133], s[28:29], 0, v[132:133]
	s_ashr_i32 s5, s4, 31
	v_lshl_add_u64 v[132:133], s[4:5], 1, v[132:133]
	v_mov_b32_e32 v1, v3
	v_lshl_add_u64 v[152:153], v[132:133], 0, v[0:1]
	s_waitcnt lgkmcnt(0)
	global_store_dwordx4 v[152:153], v[136:139], off nt
	v_add_co_u32_e32 v132, vcc, s83, v152
	s_nop 0
	v_add_u32_e32 v136, v227, v228
	ds_read_b128 v[144:147], v136
	v_add_u32_e32 v137, v229, v230
	ds_read_b128 v[148:151], v137
	v_addc_co_u32_e32 v133, vcc, 0, v153, vcc
	v_add_u32_e32 v138, v231, v232
	s_waitcnt lgkmcnt(1)
	global_store_dwordx4 v[132:133], v[144:147], off nt
	ds_read_b128 v[144:147], v138
	v_add_co_u32_e32 v132, vcc, s62, v152
	ds_read_b128 v[140:143], v135 offset:4096
	s_nop 0
	v_addc_co_u32_e32 v133, vcc, 0, v153, vcc
	s_waitcnt lgkmcnt(2)
	global_store_dwordx4 v[132:133], v[148:151], off nt
	v_add_co_u32_e32 v132, vcc, s77, v152
	v_add_u32_e32 v134, v233, v234
	s_nop 0
	v_addc_co_u32_e32 v133, vcc, 0, v153, vcc
	ds_read_b128 v[148:151], v134
	s_waitcnt lgkmcnt(2)
	global_store_dwordx4 v[132:133], v[144:147], off nt
	v_add_co_u32_e32 v132, vcc, s88, v152
	s_nop 1
	v_addc_co_u32_e32 v133, vcc, 0, v153, vcc
	s_waitcnt lgkmcnt(1)
	global_store_dwordx4 v[132:133], v[140:143], off nt
	v_add_co_u32_e32 v132, vcc, s72, v152
	s_nop 1
	v_addc_co_u32_e32 v133, vcc, 0, v153, vcc
	s_waitcnt lgkmcnt(0)
	global_store_dwordx4 v[132:133], v[148:151], off nt
	v_add_u32_e32 v133, v235, v236
	ds_read_b128 v[140:143], v133
	v_add_u32_e32 v132, v237, v238
	v_add_co_u32_e32 v148, vcc, 0xc000, v152
	ds_read_b128 v[144:147], v132
	s_nop 0
	v_addc_co_u32_e32 v149, vcc, 0, v153, vcc
	s_waitcnt lgkmcnt(1)
	global_store_dwordx4 v[148:149], v[140:143], off nt
	s_nop 1
	v_add_co_u32_e32 v140, vcc, 0xe000, v152
	s_nop 1
	v_addc_co_u32_e32 v141, vcc, 0, v153, vcc
	s_andn2_b64 vcc, exec, s[2:3]
	s_waitcnt lgkmcnt(0)
	global_store_dwordx4 v[140:141], v[144:147], off nt
	s_cbranch_vccz .LBB0_702
	s_andn2_b64 vcc, exec, s[0:1]
	s_cbranch_vccnz .LBB0_695
	s_branch .LBB0_703
.LBB0_702:
	s_ashr_i32 s2, s21, 31
	s_lshr_b32 s2, s2, 25
	s_add_i32 s2, s21, s2
	s_and_b32 s2, s2, 0xff80
	v_cvt_pk_bf16_f32 v140, v64, v8
	s_sub_i32 s2, s21, s2
	v_cvt_pk_bf16_f32 v141, v4, v16
	v_cvt_pk_bf16_f32 v142, v12, v24
	v_cvt_pk_bf16_f32 v143, v20, v32
	ds_write_b128 v223, v[140:143]
	v_cvt_pk_bf16_f32 v140, v28, v52
	s_bfe_i32 s3, s2, 0x80000
	v_cvt_pk_bf16_f32 v141, v68, v80
	v_cvt_pk_bf16_f32 v142, v88, v96
	v_cvt_pk_bf16_f32 v143, v108, v112
	ds_write_b128 v224, v[140:143]
	v_cvt_pk_bf16_f32 v140, v65, v9
	s_bfe_u32 s3, s3, 0x4000b
	v_cvt_pk_bf16_f32 v141, v5, v17
	v_cvt_pk_bf16_f32 v142, v13, v25
	v_cvt_pk_bf16_f32 v143, v21, v33
	ds_write_b128 v223, v[140:143] offset:128
	v_cvt_pk_bf16_f32 v140, v29, v53
	s_add_i32 s3, s2, s3
	v_cvt_pk_bf16_f32 v141, v69, v81
	v_cvt_pk_bf16_f32 v142, v89, v97
	v_cvt_pk_bf16_f32 v143, v109, v113
	ds_write_b128 v224, v[140:143] offset:128
	v_cvt_pk_bf16_f32 v140, v66, v10
	s_bfe_i32 s4, s3, 0x80000
	v_cvt_pk_bf16_f32 v141, v6, v18
	v_cvt_pk_bf16_f32 v142, v14, v26
	v_cvt_pk_bf16_f32 v143, v22, v34
	ds_write_b128 v223, v[140:143] offset:256
	v_cvt_pk_bf16_f32 v140, v30, v54
	s_and_b32 s3, s3, 0xf0
	v_cvt_pk_bf16_f32 v141, v70, v82
	v_cvt_pk_bf16_f32 v142, v90, v98
	v_cvt_pk_bf16_f32 v143, v110, v114
	ds_write_b128 v224, v[140:143] offset:256
	v_cvt_pk_bf16_f32 v140, v67, v11
	s_sub_i32 s2, s2, s3
	v_cvt_pk_bf16_f32 v141, v7, v19
	v_cvt_pk_bf16_f32 v142, v15, v27
	v_cvt_pk_bf16_f32 v143, v23, v35
	ds_write_b128 v223, v[140:143] offset:384
	v_cvt_pk_bf16_f32 v140, v31, v55
	s_sext_i32_i8 s2, s2
	s_sext_i32_i16 s4, s4
	v_cvt_pk_bf16_f32 v141, v71, v83
	v_cvt_pk_bf16_f32 v142, v91, v99
	v_cvt_pk_bf16_f32 v143, v111, v115
	ds_write_b128 v224, v[140:143] offset:384
	v_lshl_add_u32 v140, s2, 6, v222
	v_ashrrev_i32_e32 v141, 31, v140
	s_lshl_b32 s2, s4, 2
	v_lshlrev_b64 v[140:141], 10, v[140:141]
	s_andn2_b32 s2, s2, 63
	v_lshl_add_u64 v[140:141], s[28:29], 0, v[140:141]
	s_ashr_i32 s3, s2, 31
	v_lshl_add_u64 v[140:141], s[2:3], 1, v[140:141]
	v_lshl_add_u64 v[144:145], v[140:141], 0, v[0:1]
	ds_read_b128 v[140:143], v135
	v_add_co_u32_e32 v146, vcc, s83, v144
	s_waitcnt lgkmcnt(0)
	global_store_dwordx4 v[144:145], v[140:143], off nt
	ds_read_b128 v[140:143], v136
	v_addc_co_u32_e32 v147, vcc, 0, v145, vcc
	s_waitcnt lgkmcnt(0)
	global_store_dwordx4 v[146:147], v[140:143], off nt
	ds_read_b128 v[140:143], v137
	v_add_co_u32_e32 v146, vcc, s62, v144
	s_nop 1
	v_addc_co_u32_e32 v147, vcc, 0, v145, vcc
	s_waitcnt lgkmcnt(0)
	global_store_dwordx4 v[146:147], v[140:143], off nt
	ds_read_b128 v[140:143], v138
	v_add_co_u32_e32 v146, vcc, s77, v144
	s_nop 1
	v_addc_co_u32_e32 v147, vcc, 0, v145, vcc
	s_waitcnt lgkmcnt(0)
	global_store_dwordx4 v[146:147], v[140:143], off nt
	ds_read_b128 v[140:143], v135 offset:4096
	v_add_co_u32_e32 v146, vcc, s88, v144
	s_nop 1
	v_addc_co_u32_e32 v147, vcc, 0, v145, vcc
	s_waitcnt lgkmcnt(0)
	global_store_dwordx4 v[146:147], v[140:143], off nt
	ds_read_b128 v[140:143], v134
	v_add_co_u32_e32 v146, vcc, 0xa000, v144
	s_nop 1
	v_addc_co_u32_e32 v147, vcc, 0, v145, vcc
	s_waitcnt lgkmcnt(0)
	global_store_dwordx4 v[146:147], v[140:143], off nt
	ds_read_b128 v[140:143], v133
	v_add_co_u32_e32 v146, vcc, 0xc000, v144
	s_nop 1
	v_addc_co_u32_e32 v147, vcc, 0, v145, vcc
	s_waitcnt lgkmcnt(0)
	global_store_dwordx4 v[146:147], v[140:143], off nt
	ds_read_b128 v[140:143], v132
	v_add_co_u32_e32 v144, vcc, 0xe000, v144
	s_nop 1
	v_addc_co_u32_e32 v145, vcc, 0, v145, vcc
	s_waitcnt lgkmcnt(0)
	global_store_dwordx4 v[144:145], v[140:143], off nt
	s_andn2_b64 vcc, exec, s[0:1]
	s_cbranch_vccnz .LBB0_695
.LBB0_703:
	s_ashr_i32 s0, s7, 31
	s_lshr_b32 s0, s0, 25
	s_add_i32 s0, s7, s0
	s_and_b32 s0, s0, 0xff80
	v_cvt_pk_bf16_f32 v140, v92, v40
	s_sub_i32 s0, s7, s0
	v_cvt_pk_bf16_f32 v141, v36, v48
	v_cvt_pk_bf16_f32 v142, v44, v60
	v_cvt_pk_bf16_f32 v143, v56, v76
	ds_write_b128 v223, v[140:143]
	v_cvt_pk_bf16_f32 v140, v72, v84
	s_bfe_i32 s1, s0, 0x80000
	v_cvt_pk_bf16_f32 v141, v100, v104
	v_cvt_pk_bf16_f32 v142, v116, v120
	v_cvt_pk_bf16_f32 v143, v124, v128
	ds_write_b128 v224, v[140:143]
	v_cvt_pk_bf16_f32 v140, v93, v41
	s_bfe_u32 s1, s1, 0x4000b
	v_cvt_pk_bf16_f32 v141, v37, v49
	v_cvt_pk_bf16_f32 v142, v45, v61
	v_cvt_pk_bf16_f32 v143, v57, v77
	ds_write_b128 v223, v[140:143] offset:128
	v_cvt_pk_bf16_f32 v140, v73, v85
	s_add_i32 s1, s0, s1
	v_cvt_pk_bf16_f32 v141, v101, v105
	v_cvt_pk_bf16_f32 v142, v117, v121
	v_cvt_pk_bf16_f32 v143, v125, v129
	ds_write_b128 v224, v[140:143] offset:128
	v_cvt_pk_bf16_f32 v140, v94, v42
	s_bfe_i32 s2, s1, 0x80000
	v_cvt_pk_bf16_f32 v141, v38, v50
	v_cvt_pk_bf16_f32 v142, v46, v62
	v_cvt_pk_bf16_f32 v143, v58, v78
	ds_write_b128 v223, v[140:143] offset:256
	v_cvt_pk_bf16_f32 v140, v74, v86
	s_and_b32 s1, s1, 0xf0
	v_cvt_pk_bf16_f32 v141, v102, v106
	v_cvt_pk_bf16_f32 v142, v118, v122
	v_cvt_pk_bf16_f32 v143, v126, v130
	ds_write_b128 v224, v[140:143] offset:256
	v_cvt_pk_bf16_f32 v140, v95, v43
	s_sub_i32 s0, s0, s1
	v_cvt_pk_bf16_f32 v141, v39, v51
	v_cvt_pk_bf16_f32 v142, v47, v63
	v_cvt_pk_bf16_f32 v143, v59, v79
	ds_write_b128 v223, v[140:143] offset:384
	v_cvt_pk_bf16_f32 v140, v75, v87
	s_sext_i32_i8 s0, s0
	s_sext_i32_i16 s2, s2
	v_cvt_pk_bf16_f32 v141, v103, v107
	v_cvt_pk_bf16_f32 v142, v119, v123
	v_cvt_pk_bf16_f32 v143, v127, v131
	ds_write_b128 v224, v[140:143] offset:384
	v_lshl_add_u32 v140, s0, 6, v222
	v_ashrrev_i32_e32 v141, 31, v140
	s_lshl_b32 s0, s2, 2
	v_lshlrev_b64 v[140:141], 10, v[140:141]
	s_andn2_b32 s0, s0, 63
	v_lshl_add_u64 v[140:141], s[28:29], 0, v[140:141]
	s_ashr_i32 s1, s0, 31
	v_lshl_add_u64 v[140:141], s[0:1], 1, v[140:141]
	v_mov_b32_e32 v1, v3
	v_lshl_add_u64 v[144:145], v[140:141], 0, v[0:1]
	ds_read_b128 v[140:143], v135
	v_add_co_u32_e32 v146, vcc, s83, v144
	s_waitcnt lgkmcnt(0)
	global_store_dwordx4 v[144:145], v[140:143], off nt
	ds_read_b128 v[140:143], v136
	v_addc_co_u32_e32 v147, vcc, 0, v145, vcc
	v_add_co_u32_e32 v136, vcc, s62, v144
	s_waitcnt lgkmcnt(0)
	global_store_dwordx4 v[146:147], v[140:143], off nt
	ds_read_b128 v[140:143], v137
	v_addc_co_u32_e32 v137, vcc, 0, v145, vcc
	s_waitcnt lgkmcnt(0)
	global_store_dwordx4 v[136:137], v[140:143], off nt
	ds_read_b128 v[136:139], v138
	s_nop 0
	v_add_co_u32_e32 v140, vcc, s77, v144
	s_nop 1
	v_addc_co_u32_e32 v141, vcc, 0, v145, vcc
	s_waitcnt lgkmcnt(0)
	global_store_dwordx4 v[140:141], v[136:139], off nt
	ds_read_b128 v[136:139], v135 offset:4096
	v_add_co_u32_e32 v140, vcc, s88, v144
	s_nop 1
	v_addc_co_u32_e32 v141, vcc, 0, v145, vcc
	s_waitcnt lgkmcnt(0)
	global_store_dwordx4 v[140:141], v[136:139], off nt
	ds_read_b128 v[134:137], v134
	s_nop 0
	v_add_co_u32_e32 v138, vcc, 0xa000, v144
	s_nop 1
	v_addc_co_u32_e32 v139, vcc, 0, v145, vcc
	s_waitcnt lgkmcnt(0)
	global_store_dwordx4 v[138:139], v[134:137], off nt
	ds_read_b128 v[134:137], v133
	v_add_co_u32_e32 v138, vcc, 0xc000, v144
	s_nop 1
	v_addc_co_u32_e32 v139, vcc, 0, v145, vcc
	s_waitcnt lgkmcnt(0)
	global_store_dwordx4 v[138:139], v[134:137], off nt
	ds_read_b128 v[132:135], v132
	s_nop 0
	v_add_co_u32_e32 v136, vcc, 0xe000, v144
	s_nop 1
	v_addc_co_u32_e32 v137, vcc, 0, v145, vcc
	s_waitcnt lgkmcnt(0)
	global_store_dwordx4 v[136:137], v[132:135], off nt
	s_branch .LBB0_695

.LBB0_707:
	s_add_i32 s23, s38, s21
	s_cmp_lt_i32 s23, 64
	s_cselect_b64 s[4:5], -1, 0
	s_ashr_i32 s2, s21, 31
	s_lshr_b32 s2, s2, 26
	s_add_i32 s2, s21, s2
	s_and_b32 s2, s2, 0xffc0
	s_sub_i32 s2, s21, s2
	s_bfe_i32 s3, s2, 0x80000
	s_bfe_u32 s3, s3, 0x2000d
	s_add_i32 s3, s2, s3
	s_bfe_i32 s6, s3, 0x80000
	s_and_b32 s3, s3, 0xfc
	s_sub_i32 s2, s2, s3
	s_sext_i32_i16 s6, s6
	s_sext_i32_i8 s2, s2
	s_lshl_b32 s8, s2, 6
	s_lshl_b32 s2, s6, 4
	s_and_b32 s6, s2, 0xffffffc0
	v_add_u32_e32 v132, s6, v221
	v_ashrrev_i32_e32 v133, 31, v132
	v_readlane_b32 s2, v253, 7
	v_lshlrev_b64 v[132:133], 10, v[132:133]
	v_readlane_b32 s3, v253, 8
	s_ashr_i32 s9, s8, 31
	s_cmp_gt_i32 s23, 63
	v_lshl_add_u64 v[132:133], s[2:3], 0, v[132:133]
	v_lshl_add_u64 v[132:133], s[8:9], 2, v[132:133]
	v_lshl_add_u64 v[180:181], v[132:133], 0, v[2:3]
	v_add_co_u32_e32 v148, vcc, 0x1000, v180
	global_load_dwordx4 v[136:139], v[180:181], off nt
	global_load_dwordx4 v[144:147], v[180:181], off offset:1024 nt
	global_load_dwordx4 v[132:135], v[180:181], off offset:2048 nt
	global_load_dwordx4 v[140:143], v[180:181], off offset:3072 nt
	v_addc_co_u32_e32 v149, vcc, 0, v181, vcc
	v_add_co_u32_e32 v160, vcc, 0x2000, v180
	global_load_dwordx4 v[164:167], v[148:149], off nt
	global_load_dwordx4 v[176:179], v[148:149], off offset:1024 nt
	global_load_dwordx4 v[152:155], v[148:149], off offset:2048 nt
	global_load_dwordx4 v[168:171], v[148:149], off offset:3072 nt
	v_addc_co_u32_e32 v161, vcc, 0, v181, vcc
	v_add_co_u32_e32 v188, vcc, 0x3000, v180
	global_load_dwordx4 v[156:159], v[160:161], off nt
	global_load_dwordx4 v[172:175], v[160:161], off offset:1024 nt
	global_load_dwordx4 v[148:151], v[160:161], off offset:2048 nt
	s_nop 0
	global_load_dwordx4 v[160:163], v[160:161], off offset:3072 nt
	v_addc_co_u32_e32 v189, vcc, 0, v181, vcc
	global_load_dwordx4 v[184:187], v[188:189], off nt
	global_load_dwordx4 v[192:195], v[188:189], off offset:1024 nt
	global_load_dwordx4 v[180:183], v[188:189], off offset:2048 nt
	s_nop 0
	global_load_dwordx4 v[188:191], v[188:189], off offset:3072 nt
	s_cbranch_scc1 .LBB0_709
	s_ashr_i32 s2, s23, 31
	s_lshr_b32 s2, s2, 26
	s_add_i32 s2, s23, s2
	s_and_b32 s2, s2, 0xffc0
	s_sub_i32 s2, s23, s2
	s_bfe_i32 s3, s2, 0x80000
	s_bfe_u32 s3, s3, 0x2000d
	s_add_i32 s3, s2, s3
	s_bfe_i32 s7, s3, 0x80000
	s_sext_i32_i16 s7, s7
	s_and_b32 s3, s3, 0xfc
	s_sub_i32 s2, s2, s3
	s_lshl_b32 s3, s7, 4
	s_andn2_b32 s3, s3, 63
	v_add_u32_e32 v4, s3, v221
	s_sext_i32_i8 s2, s2
	v_ashrrev_i32_e32 v5, 31, v4
	v_readlane_b32 s28, v253, 7
	s_lshl_b32 s2, s2, 6
	v_lshlrev_b64 v[4:5], 10, v[4:5]
	v_readlane_b32 s29, v253, 8
	s_ashr_i32 s3, s2, 31
	s_nop 0
	v_lshl_add_u64 v[4:5], s[28:29], 0, v[4:5]
	v_lshl_add_u64 v[4:5], s[2:3], 2, v[4:5]
	v_lshl_add_u64 v[52:53], v[4:5], 0, v[2:3]
	v_add_co_u32_e32 v20, vcc, 0x1000, v52
	global_load_dwordx4 v[16:19], v[52:53], off nt
	global_load_dwordx4 v[12:15], v[52:53], off offset:1024 nt
	global_load_dwordx4 v[8:11], v[52:53], off offset:2048 nt
	global_load_dwordx4 v[4:7], v[52:53], off offset:3072 nt
	v_addc_co_u32_e32 v21, vcc, 0, v53, vcc
	v_add_co_u32_e32 v36, vcc, 0x2000, v52
	global_load_dwordx4 v[32:35], v[20:21], off nt
	global_load_dwordx4 v[28:31], v[20:21], off offset:1024 nt
	global_load_dwordx4 v[24:27], v[20:21], off offset:2048 nt
	s_nop 0
	global_load_dwordx4 v[20:23], v[20:21], off offset:3072 nt
	v_addc_co_u32_e32 v37, vcc, 0, v53, vcc
	v_add_co_u32_e32 v52, vcc, 0x3000, v52
	global_load_dwordx4 v[48:51], v[36:37], off nt
	global_load_dwordx4 v[44:47], v[36:37], off offset:1024 nt
	global_load_dwordx4 v[40:43], v[36:37], off offset:2048 nt
	s_nop 0
	global_load_dwordx4 v[36:39], v[36:37], off offset:3072 nt
	v_addc_co_u32_e32 v53, vcc, 0, v53, vcc
	global_load_dwordx4 v[64:67], v[52:53], off nt
	global_load_dwordx4 v[60:63], v[52:53], off offset:1024 nt
	global_load_dwordx4 v[56:59], v[52:53], off offset:2048 nt
	s_nop 0
	global_load_dwordx4 v[52:55], v[52:53], off offset:3072 nt
.LBB0_709:
	s_add_i32 s9, s22, s21
	s_cmp_lt_i32 s9, 64
	s_cselect_b64 s[2:3], -1, 0
	s_cmp_gt_i32 s9, 63
	s_cbranch_scc1 .LBB0_711
	s_ashr_i32 s7, s9, 31
	s_lshr_b32 s7, s7, 26
	s_add_i32 s7, s9, s7
	s_and_b32 s7, s7, 0xffc0
	s_sub_i32 s7, s9, s7
	s_bfe_i32 s14, s7, 0x80000
	s_bfe_u32 s14, s14, 0x2000d
	s_add_i32 s14, s7, s14
	s_bfe_i32 s28, s14, 0x80000
	s_and_b32 s14, s14, 0xfc
	s_sub_i32 s7, s7, s14
	s_sext_i32_i16 s29, s28
	s_sext_i32_i8 s7, s7
	s_lshl_b32 s28, s7, 6
	s_lshl_b32 s7, s29, 4
	s_andn2_b32 s7, s7, 63
	v_add_u32_e32 v68, s7, v221
	v_ashrrev_i32_e32 v69, 31, v68
	v_readlane_b32 s36, v253, 7
	v_lshlrev_b64 v[68:69], 10, v[68:69]
	v_readlane_b32 s37, v253, 8
	s_ashr_i32 s29, s28, 31
	s_nop 0
	v_lshl_add_u64 v[68:69], s[36:37], 0, v[68:69]
	v_lshl_add_u64 v[68:69], s[28:29], 2, v[68:69]
	v_lshl_add_u64 v[116:117], v[68:69], 0, v[2:3]
	v_add_co_u32_e32 v84, vcc, 0x1000, v116
	global_load_dwordx4 v[80:83], v[116:117], off nt
	global_load_dwordx4 v[76:79], v[116:117], off offset:1024 nt
	global_load_dwordx4 v[72:75], v[116:117], off offset:2048 nt
	global_load_dwordx4 v[68:71], v[116:117], off offset:3072 nt
	v_addc_co_u32_e32 v85, vcc, 0, v117, vcc
	v_add_co_u32_e32 v100, vcc, 0x2000, v116
	global_load_dwordx4 v[96:99], v[84:85], off nt
	global_load_dwordx4 v[92:95], v[84:85], off offset:1024 nt
	global_load_dwordx4 v[88:91], v[84:85], off offset:2048 nt
	s_nop 0
	global_load_dwordx4 v[84:87], v[84:85], off offset:3072 nt
	v_addc_co_u32_e32 v101, vcc, 0, v117, vcc
	v_add_co_u32_e32 v116, vcc, 0x3000, v116
	global_load_dwordx4 v[112:115], v[100:101], off nt
	global_load_dwordx4 v[108:111], v[100:101], off offset:1024 nt
	global_load_dwordx4 v[104:107], v[100:101], off offset:2048 nt
	s_nop 0
	global_load_dwordx4 v[100:103], v[100:101], off offset:3072 nt
	v_addc_co_u32_e32 v117, vcc, 0, v117, vcc
	global_load_dwordx4 v[128:131], v[116:117], off nt
	global_load_dwordx4 v[124:127], v[116:117], off offset:1024 nt
	global_load_dwordx4 v[120:123], v[116:117], off offset:2048 nt
	s_nop 0
	global_load_dwordx4 v[116:119], v[116:117], off offset:3072 nt
.LBB0_711:
	s_waitcnt vmcnt(14)
	v_cvt_pk_bf16_f32 v240, v136, v144
	s_waitcnt vmcnt(12)
	v_cvt_pk_bf16_f32 v241, v132, v140
	s_waitcnt vmcnt(10)
	v_cvt_pk_bf16_f32 v242, v164, v176
	s_waitcnt vmcnt(8)
	v_cvt_pk_bf16_f32 v243, v152, v168
	ds_write_b128 v223, v[240:243]
	s_waitcnt vmcnt(6)
	v_cvt_pk_bf16_f32 v240, v156, v172
	s_waitcnt vmcnt(4)
	v_cvt_pk_bf16_f32 v241, v148, v160
	s_waitcnt vmcnt(2)
	v_cvt_pk_bf16_f32 v242, v184, v192
	s_waitcnt vmcnt(0)
	v_cvt_pk_bf16_f32 v243, v180, v188
	ds_write_b128 v224, v[240:243]
	v_cvt_pk_bf16_f32 v240, v137, v145
	v_cvt_pk_bf16_f32 v241, v133, v141
	v_cvt_pk_bf16_f32 v242, v165, v177
	v_cvt_pk_bf16_f32 v243, v153, v169
	ds_write_b128 v223, v[240:243] offset:128
	v_cvt_pk_bf16_f32 v240, v157, v173
	v_cvt_pk_bf16_f32 v241, v149, v161
	v_cvt_pk_bf16_f32 v242, v185, v193
	v_cvt_pk_bf16_f32 v243, v181, v189
	ds_write_b128 v224, v[240:243] offset:128
	v_cvt_pk_bf16_f32 v240, v138, v146
	v_cvt_pk_bf16_f32 v241, v134, v142
	v_cvt_pk_bf16_f32 v242, v166, v178
	v_cvt_pk_bf16_f32 v243, v154, v170
	ds_write_b128 v223, v[240:243] offset:256
	v_cvt_pk_bf16_f32 v240, v158, v174
	v_cvt_pk_bf16_f32 v241, v150, v162
	v_cvt_pk_bf16_f32 v242, v186, v194
	v_cvt_pk_bf16_f32 v243, v182, v190
	ds_write_b128 v224, v[240:243] offset:256
	v_cvt_pk_bf16_f32 v132, v139, v147
	v_cvt_pk_bf16_f32 v133, v135, v143
	v_cvt_pk_bf16_f32 v134, v167, v179
	v_cvt_pk_bf16_f32 v135, v155, v171
	ds_write_b128 v223, v[132:135] offset:384
	v_cvt_pk_bf16_f32 v132, v159, v175
	v_cvt_pk_bf16_f32 v133, v151, v163
	v_cvt_pk_bf16_f32 v134, v187, v195
	v_cvt_pk_bf16_f32 v135, v183, v191
	ds_write_b128 v224, v[132:135] offset:384
	v_add_u32_e32 v132, s8, v222
	v_add_u32_e32 v135, v225, v226
	v_ashrrev_i32_e32 v133, 31, v132
	ds_read_b128 v[136:139], v135
	v_lshlrev_b64 v[132:133], 11, v[132:133]
	v_lshl_add_u64 v[132:133], s[0:1], 0, v[132:133]
	s_ashr_i32 s7, s6, 31
	v_lshl_add_u64 v[132:133], s[6:7], 1, v[132:133]
	v_mov_b32_e32 v1, v3
	v_lshl_add_u64 v[152:153], v[132:133], 0, v[0:1]
	s_waitcnt lgkmcnt(0)
	global_store_dwordx4 v[152:153], v[136:139], off nt
	v_add_co_u32_e32 v132, vcc, s62, v152
	s_nop 0
	v_add_u32_e32 v137, v227, v228
	ds_read_b128 v[144:147], v137
	v_add_u32_e32 v136, v229, v230
	ds_read_b128 v[148:151], v136
	v_addc_co_u32_e32 v133, vcc, 0, v153, vcc
	v_add_u32_e32 v138, v231, v232
	s_waitcnt lgkmcnt(1)
	global_store_dwordx4 v[132:133], v[144:147], off nt
	ds_read_b128 v[144:147], v138
	v_add_co_u32_e32 v132, vcc, s88, v152
	ds_read_b128 v[140:143], v135 offset:4096
	s_nop 0
	v_addc_co_u32_e32 v133, vcc, 0, v153, vcc
	s_waitcnt lgkmcnt(2)
	global_store_dwordx4 v[132:133], v[148:151], off nt
	v_add_co_u32_e32 v132, vcc, s66, v152
	v_add_u32_e32 v134, v233, v234
	s_nop 0
	v_addc_co_u32_e32 v133, vcc, 0, v153, vcc
	ds_read_b128 v[148:151], v134
	s_waitcnt lgkmcnt(2)
	global_store_dwordx4 v[132:133], v[144:147], off nt
	v_add_co_u32_e32 v132, vcc, s82, v152
	s_mov_b32 s6, 0x14000
	s_nop 0
	v_addc_co_u32_e32 v133, vcc, 0, v153, vcc
	s_waitcnt lgkmcnt(1)
	global_store_dwordx4 v[132:133], v[140:143], off nt
	v_add_co_u32_e32 v132, vcc, s6, v152
	s_nop 1
	v_addc_co_u32_e32 v133, vcc, 0, v153, vcc
	s_waitcnt lgkmcnt(0)
	global_store_dwordx4 v[132:133], v[148:151], off nt
	v_add_u32_e32 v133, v235, v236
	ds_read_b128 v[140:143], v133
	v_add_u32_e32 v132, v237, v238
	v_add_co_u32_e32 v148, vcc, 0x18000, v152
	ds_read_b128 v[144:147], v132
	s_nop 0
	v_addc_co_u32_e32 v149, vcc, 0, v153, vcc
	s_waitcnt lgkmcnt(1)
	global_store_dwordx4 v[148:149], v[140:143], off nt
	s_nop 1
	v_add_co_u32_e32 v140, vcc, 0x1c000, v152
	s_nop 1
	v_addc_co_u32_e32 v141, vcc, 0, v153, vcc
	s_andn2_b64 vcc, exec, s[4:5]
	s_waitcnt lgkmcnt(0)
	global_store_dwordx4 v[140:141], v[144:147], off nt
	s_cbranch_vccz .LBB0_713
	s_andn2_b64 vcc, exec, s[2:3]
	s_cbranch_vccnz .LBB0_706
	s_branch .LBB0_714
.LBB0_713:
	s_ashr_i32 s4, s23, 31
	s_lshr_b32 s4, s4, 26
	s_add_i32 s4, s23, s4
	s_and_b32 s4, s4, 0xffc0
	v_cvt_pk_bf16_f32 v140, v16, v12
	s_sub_i32 s4, s23, s4
	v_cvt_pk_bf16_f32 v141, v8, v4
	v_cvt_pk_bf16_f32 v142, v32, v28
	v_cvt_pk_bf16_f32 v143, v24, v20
	ds_write_b128 v223, v[140:143]
	v_cvt_pk_bf16_f32 v140, v48, v44
	s_bfe_i32 s5, s4, 0x80000
	v_cvt_pk_bf16_f32 v141, v40, v36
	v_cvt_pk_bf16_f32 v142, v64, v60
	v_cvt_pk_bf16_f32 v143, v56, v52
	ds_write_b128 v224, v[140:143]
	v_cvt_pk_bf16_f32 v140, v17, v13
	s_bfe_u32 s5, s5, 0x2000d
	v_cvt_pk_bf16_f32 v141, v9, v5
	v_cvt_pk_bf16_f32 v142, v33, v29
	v_cvt_pk_bf16_f32 v143, v25, v21
	ds_write_b128 v223, v[140:143] offset:128
	v_cvt_pk_bf16_f32 v140, v49, v45
	s_add_i32 s5, s4, s5
	v_cvt_pk_bf16_f32 v141, v41, v37
	v_cvt_pk_bf16_f32 v142, v65, v61
	v_cvt_pk_bf16_f32 v143, v57, v53
	ds_write_b128 v224, v[140:143] offset:128
	v_cvt_pk_bf16_f32 v140, v18, v14
	s_bfe_i32 s6, s5, 0x80000
	v_cvt_pk_bf16_f32 v141, v10, v6
	v_cvt_pk_bf16_f32 v142, v34, v30
	v_cvt_pk_bf16_f32 v143, v26, v22
	ds_write_b128 v223, v[140:143] offset:256
	v_cvt_pk_bf16_f32 v140, v50, v46
	s_and_b32 s5, s5, 0xfc
	v_cvt_pk_bf16_f32 v141, v42, v38
	v_cvt_pk_bf16_f32 v142, v66, v62
	v_cvt_pk_bf16_f32 v143, v58, v54
	ds_write_b128 v224, v[140:143] offset:256
	v_cvt_pk_bf16_f32 v140, v19, v15
	s_sub_i32 s4, s4, s5
	v_cvt_pk_bf16_f32 v141, v11, v7
	v_cvt_pk_bf16_f32 v142, v35, v31
	v_cvt_pk_bf16_f32 v143, v27, v23
	ds_write_b128 v223, v[140:143] offset:384
	v_cvt_pk_bf16_f32 v140, v51, v47
	s_sext_i32_i8 s4, s4
	s_sext_i32_i16 s6, s6
	v_cvt_pk_bf16_f32 v141, v43, v39
	v_cvt_pk_bf16_f32 v142, v67, v63
	v_cvt_pk_bf16_f32 v143, v59, v55
	ds_write_b128 v224, v[140:143] offset:384
	v_lshl_add_u32 v140, s4, 6, v222
	v_ashrrev_i32_e32 v141, 31, v140
	s_lshl_b32 s4, s6, 4
	v_lshlrev_b64 v[140:141], 11, v[140:141]
	s_andn2_b32 s4, s4, 63
	v_lshl_add_u64 v[140:141], s[0:1], 0, v[140:141]
	s_ashr_i32 s5, s4, 31
	v_lshl_add_u64 v[140:141], s[4:5], 1, v[140:141]
	v_lshl_add_u64 v[144:145], v[140:141], 0, v[0:1]
	ds_read_b128 v[140:143], v135
	v_add_co_u32_e32 v146, vcc, s62, v144
	s_waitcnt lgkmcnt(0)
	global_store_dwordx4 v[144:145], v[140:143], off nt
	ds_read_b128 v[140:143], v137
	v_addc_co_u32_e32 v147, vcc, 0, v145, vcc
	s_waitcnt lgkmcnt(0)
	global_store_dwordx4 v[146:147], v[140:143], off nt
	ds_read_b128 v[140:143], v136
	v_add_co_u32_e32 v146, vcc, 0x8000, v144
	s_nop 1
	v_addc_co_u32_e32 v147, vcc, 0, v145, vcc
	s_waitcnt lgkmcnt(0)
	global_store_dwordx4 v[146:147], v[140:143], off nt
	ds_read_b128 v[140:143], v138
	v_add_co_u32_e32 v146, vcc, 0xc000, v144
	s_nop 1
	v_addc_co_u32_e32 v147, vcc, 0, v145, vcc
	s_waitcnt lgkmcnt(0)
	global_store_dwordx4 v[146:147], v[140:143], off nt
	ds_read_b128 v[140:143], v135 offset:4096
	v_add_co_u32_e32 v146, vcc, s82, v144
	s_nop 1
	v_addc_co_u32_e32 v147, vcc, 0, v145, vcc
	s_waitcnt lgkmcnt(0)
	global_store_dwordx4 v[146:147], v[140:143], off nt
	ds_read_b128 v[140:143], v134
	v_add_co_u32_e32 v146, vcc, 0x14000, v144
	s_nop 1
	v_addc_co_u32_e32 v147, vcc, 0, v145, vcc
	s_waitcnt lgkmcnt(0)
	global_store_dwordx4 v[146:147], v[140:143], off nt
	ds_read_b128 v[140:143], v133
	v_add_co_u32_e32 v146, vcc, 0x18000, v144
	s_nop 1
	v_addc_co_u32_e32 v147, vcc, 0, v145, vcc
	s_waitcnt lgkmcnt(0)
	global_store_dwordx4 v[146:147], v[140:143], off nt
	ds_read_b128 v[140:143], v132
	v_add_co_u32_e32 v144, vcc, 0x1c000, v144
	s_nop 1
	v_addc_co_u32_e32 v145, vcc, 0, v145, vcc
	s_waitcnt lgkmcnt(0)
	global_store_dwordx4 v[144:145], v[140:143], off nt
	s_andn2_b64 vcc, exec, s[2:3]
	s_cbranch_vccnz .LBB0_706
.LBB0_714:
	s_ashr_i32 s2, s9, 31
	s_lshr_b32 s2, s2, 26
	s_add_i32 s2, s9, s2
	s_and_b32 s2, s2, 0xffc0
	v_cvt_pk_bf16_f32 v140, v80, v76
	s_sub_i32 s2, s9, s2
	v_cvt_pk_bf16_f32 v141, v72, v68
	v_cvt_pk_bf16_f32 v142, v96, v92
	v_cvt_pk_bf16_f32 v143, v88, v84
	ds_write_b128 v223, v[140:143]
	v_cvt_pk_bf16_f32 v140, v112, v108
	s_bfe_i32 s3, s2, 0x80000
	v_cvt_pk_bf16_f32 v141, v104, v100
	v_cvt_pk_bf16_f32 v142, v128, v124
	v_cvt_pk_bf16_f32 v143, v120, v116
	ds_write_b128 v224, v[140:143]
	v_cvt_pk_bf16_f32 v140, v81, v77
	s_bfe_u32 s3, s3, 0x2000d
	v_cvt_pk_bf16_f32 v141, v73, v69
	v_cvt_pk_bf16_f32 v142, v97, v93
	v_cvt_pk_bf16_f32 v143, v89, v85
	ds_write_b128 v223, v[140:143] offset:128
	v_cvt_pk_bf16_f32 v140, v113, v109
	s_add_i32 s3, s2, s3
	v_cvt_pk_bf16_f32 v141, v105, v101
	v_cvt_pk_bf16_f32 v142, v129, v125
	v_cvt_pk_bf16_f32 v143, v121, v117
	ds_write_b128 v224, v[140:143] offset:128
	v_cvt_pk_bf16_f32 v140, v82, v78
	s_bfe_i32 s4, s3, 0x80000
	v_cvt_pk_bf16_f32 v141, v74, v70
	v_cvt_pk_bf16_f32 v142, v98, v94
	v_cvt_pk_bf16_f32 v143, v90, v86
	ds_write_b128 v223, v[140:143] offset:256
	v_cvt_pk_bf16_f32 v140, v114, v110
	s_and_b32 s3, s3, 0xfc
	v_cvt_pk_bf16_f32 v141, v106, v102
	v_cvt_pk_bf16_f32 v142, v130, v126
	v_cvt_pk_bf16_f32 v143, v122, v118
	ds_write_b128 v224, v[140:143] offset:256
	v_cvt_pk_bf16_f32 v140, v83, v79
	s_sub_i32 s2, s2, s3
	v_cvt_pk_bf16_f32 v141, v75, v71
	v_cvt_pk_bf16_f32 v142, v99, v95
	v_cvt_pk_bf16_f32 v143, v91, v87
	ds_write_b128 v223, v[140:143] offset:384
	v_cvt_pk_bf16_f32 v140, v115, v111
	s_sext_i32_i8 s2, s2
	s_sext_i32_i16 s4, s4
	v_cvt_pk_bf16_f32 v141, v107, v103
	v_cvt_pk_bf16_f32 v142, v131, v127
	v_cvt_pk_bf16_f32 v143, v123, v119
	ds_write_b128 v224, v[140:143] offset:384
	v_lshl_add_u32 v140, s2, 6, v222
	v_ashrrev_i32_e32 v141, 31, v140
	s_lshl_b32 s2, s4, 4
	v_lshlrev_b64 v[140:141], 11, v[140:141]
	s_andn2_b32 s2, s2, 63
	v_lshl_add_u64 v[140:141], s[0:1], 0, v[140:141]
	s_ashr_i32 s3, s2, 31
	v_lshl_add_u64 v[140:141], s[2:3], 1, v[140:141]
	v_mov_b32_e32 v1, v3
	v_lshl_add_u64 v[144:145], v[140:141], 0, v[0:1]
	ds_read_b128 v[140:143], v135
	v_add_co_u32_e32 v146, vcc, s62, v144
	s_waitcnt lgkmcnt(0)
	global_store_dwordx4 v[144:145], v[140:143], off nt
	ds_read_b128 v[140:143], v137
	v_addc_co_u32_e32 v147, vcc, 0, v145, vcc
	s_waitcnt lgkmcnt(0)
	global_store_dwordx4 v[146:147], v[140:143], off nt
	ds_read_b128 v[140:143], v136
	v_add_co_u32_e32 v136, vcc, 0x8000, v144
	s_nop 1
	v_addc_co_u32_e32 v137, vcc, 0, v145, vcc
	s_waitcnt lgkmcnt(0)
	global_store_dwordx4 v[136:137], v[140:143], off nt
	ds_read_b128 v[136:139], v138
	s_nop 0
	v_add_co_u32_e32 v140, vcc, 0xc000, v144
	s_nop 1
	v_addc_co_u32_e32 v141, vcc, 0, v145, vcc
	s_waitcnt lgkmcnt(0)
	global_store_dwordx4 v[140:141], v[136:139], off nt
	ds_read_b128 v[136:139], v135 offset:4096
	v_add_co_u32_e32 v140, vcc, s82, v144
	s_nop 1
	v_addc_co_u32_e32 v141, vcc, 0, v145, vcc
	s_waitcnt lgkmcnt(0)
	global_store_dwordx4 v[140:141], v[136:139], off nt
	ds_read_b128 v[134:137], v134
	s_nop 0
	v_add_co_u32_e32 v138, vcc, 0x14000, v144
	s_nop 1
	v_addc_co_u32_e32 v139, vcc, 0, v145, vcc
	s_waitcnt lgkmcnt(0)
	global_store_dwordx4 v[138:139], v[134:137], off nt
	ds_read_b128 v[134:137], v133
	v_add_co_u32_e32 v138, vcc, 0x18000, v144
	s_nop 1
	v_addc_co_u32_e32 v139, vcc, 0, v145, vcc
	s_waitcnt lgkmcnt(0)
	global_store_dwordx4 v[138:139], v[134:137], off nt
	ds_read_b128 v[132:135], v132
	s_nop 0
	v_add_co_u32_e32 v136, vcc, 0x1c000, v144
	s_nop 1
	v_addc_co_u32_e32 v137, vcc, 0, v145, vcc
	s_waitcnt lgkmcnt(0)
	global_store_dwordx4 v[136:137], v[132:135], off nt
	s_branch .LBB0_706

.LBB0_718:
	s_add_i32 s9, s38, s6
	s_cmpk_lt_i32 s9, 0x80
	s_cselect_b64 s[2:3], -1, 0
	s_ashr_i32 s0, s6, 31
	s_lshr_b32 s0, s0, 25
	s_add_i32 s0, s6, s0
	s_and_b32 s0, s0, 0xff80
	s_sub_i32 s0, s6, s0
	s_bfe_i32 s1, s0, 0x80000
	s_bfe_u32 s1, s1, 0x3000c
	s_add_i32 s1, s0, s1
	s_bfe_i32 s4, s1, 0x80000
	s_and_b32 s1, s1, 0xf8
	s_sub_i32 s0, s0, s1
	s_sext_i32_i8 s0, s0
	s_lshl_b32 s5, s0, 6
	s_lshl_b32 s0, s0, 5
	s_and_b32 s1, s5, 0xc0
	s_and_b32 s0, s0, 0xffffff80
	s_or_b32 s8, s0, s1
	s_add_i32 s0, s1, s0
	s_addk_i32 s0, 0x80
	s_sext_i32_i16 s4, s4
	s_cmpk_lt_u32 s1, 0x80
	s_cselect_b32 s0, s8, s0
	s_lshl_b32 s1, s4, 3
	s_and_b32 s4, s1, 0xffffffc0
	v_add_u32_e32 v132, s4, v221
	v_ashrrev_i32_e32 v133, 31, v132
	v_readlane_b32 s22, v253, 9
	v_lshlrev_b64 v[132:133], 11, v[132:133]
	v_readlane_b32 s23, v253, 10
	s_ashr_i32 s1, s0, 31
	s_cmpk_gt_i32 s9, 0x7f
	v_lshl_add_u64 v[132:133], s[22:23], 0, v[132:133]
	v_lshl_add_u64 v[132:133], s[0:1], 2, v[132:133]
	v_lshl_add_u64 v[180:181], v[132:133], 0, v[2:3]
	s_movk_i32 s0, 0x1000
	v_add_co_u32_e32 v148, vcc, s0, v180
	global_load_dwordx4 v[132:135], v[180:181], off nt
	global_load_dwordx4 v[136:139], v[180:181], off offset:2048 nt
	v_addc_co_u32_e32 v149, vcc, 0, v181, vcc
	v_add_co_u32_e32 v188, vcc, s83, v180
	s_nop 1
	v_addc_co_u32_e32 v189, vcc, 0, v181, vcc
	v_add_co_u32_e32 v152, vcc, 0x3000, v180
	global_load_dwordx4 v[140:143], v[188:189], off nt
	global_load_dwordx4 v[144:147], v[188:189], off offset:2048 nt
	v_addc_co_u32_e32 v153, vcc, 0, v181, vcc
	v_add_co_u32_e32 v164, vcc, s62, v180
	global_load_dwordx4 v[156:159], v[148:149], off offset:2048 nt
	s_nop 0
	global_load_dwordx4 v[148:151], v[152:153], off nt
	v_addc_co_u32_e32 v165, vcc, 0, v181, vcc
	v_add_co_u32_e32 v172, vcc, 0x5000, v180
	global_load_dwordx4 v[160:163], v[152:153], off offset:2048 nt
	s_nop 0
	global_load_dwordx4 v[152:155], v[164:165], off nt
	v_addc_co_u32_e32 v173, vcc, 0, v181, vcc
	v_add_co_u32_e32 v182, vcc, 0x6000, v180
	global_load_dwordx4 v[164:167], v[164:165], off offset:2048 nt
	s_nop 0
	global_load_dwordx4 v[168:171], v[172:173], off nt
	v_addc_co_u32_e32 v183, vcc, 0, v181, vcc
	v_add_co_u32_e32 v190, vcc, 0x7000, v180
	global_load_dwordx4 v[172:175], v[172:173], off offset:2048 nt
	s_nop 0
	global_load_dwordx4 v[176:179], v[182:183], off nt
	v_addc_co_u32_e32 v191, vcc, 0, v181, vcc
	global_load_dwordx4 v[180:183], v[182:183], off offset:2048 nt
	s_nop 0
	global_load_dwordx4 v[184:187], v[190:191], off nt
	global_load_dwordx4 v[192:195], v[188:189], off offset:-4096 nt
	s_nop 0
	global_load_dwordx4 v[188:191], v[190:191], off offset:2048 nt
	s_cbranch_scc1 .LBB0_720
	s_ashr_i32 s0, s9, 31
	s_lshr_b32 s0, s0, 25
	s_add_i32 s0, s9, s0
	s_and_b32 s0, s0, 0xff80
	s_sub_i32 s0, s9, s0
	s_bfe_i32 s1, s0, 0x80000
	s_bfe_u32 s1, s1, 0x3000c
	s_add_i32 s1, s0, s1
	s_bfe_i32 s8, s1, 0x80000
	s_and_b32 s1, s1, 0xf8
	s_sub_i32 s0, s0, s1
	s_sext_i32_i8 s1, s0
	s_lshl_b32 s0, s0, 6
	s_lshl_b32 s1, s1, 5
	s_and_b32 s0, s0, 0xc0
	s_and_b32 s1, s1, 0xffffff80
	s_or_b32 s14, s1, s0
	s_add_i32 s1, s0, s1
	s_addk_i32 s1, 0x80
	s_sext_i32_i16 s8, s8
	s_cmpk_lt_u32 s0, 0x80
	s_cselect_b32 s0, s14, s1
	s_lshl_b32 s1, s8, 3
	s_andn2_b32 s1, s1, 63
	v_add_u32_e32 v4, s1, v221
	v_ashrrev_i32_e32 v5, 31, v4
	v_readlane_b32 s22, v253, 9
	v_lshlrev_b64 v[4:5], 11, v[4:5]
	v_readlane_b32 s23, v253, 10
	s_ashr_i32 s1, s0, 31
	s_nop 0
	v_lshl_add_u64 v[4:5], s[22:23], 0, v[4:5]
	v_lshl_add_u64 v[4:5], s[0:1], 2, v[4:5]
	v_lshl_add_u64 v[84:85], v[4:5], 0, v[2:3]
	s_movk_i32 s0, 0x1000
	v_add_co_u32_e32 v28, vcc, s0, v84
	global_load_dwordx4 v[8:11], v[84:85], off nt
	global_load_dwordx4 v[4:7], v[84:85], off offset:2048 nt
	v_addc_co_u32_e32 v29, vcc, 0, v85, vcc
	v_add_co_u32_e32 v92, vcc, s83, v84
	s_nop 1
	v_addc_co_u32_e32 v93, vcc, 0, v85, vcc
	v_add_co_u32_e32 v36, vcc, 0x3000, v84
	global_load_dwordx4 v[16:19], v[92:93], off nt
	global_load_dwordx4 v[12:15], v[92:93], off offset:2048 nt
	v_addc_co_u32_e32 v37, vcc, 0, v85, vcc
	v_add_co_u32_e32 v52, vcc, s62, v84
	global_load_dwordx4 v[32:35], v[28:29], off offset:2048 nt
	s_nop 0
	global_load_dwordx4 v[28:31], v[36:37], off nt
	v_addc_co_u32_e32 v53, vcc, 0, v85, vcc
	v_add_co_u32_e32 v68, vcc, 0x5000, v84
	global_load_dwordx4 v[36:39], v[36:37], off offset:2048 nt
	s_nop 0
	global_load_dwordx4 v[40:43], v[52:53], off nt
	v_addc_co_u32_e32 v69, vcc, 0, v85, vcc
	v_add_co_u32_e32 v86, vcc, 0x6000, v84
	global_load_dwordx4 v[52:55], v[52:53], off offset:2048 nt
	s_nop 0
	global_load_dwordx4 v[56:59], v[68:69], off nt
	v_addc_co_u32_e32 v87, vcc, 0, v85, vcc
	v_add_co_u32_e32 v94, vcc, 0x7000, v84
	global_load_dwordx4 v[68:71], v[68:69], off offset:2048 nt
	s_nop 0
	global_load_dwordx4 v[72:75], v[86:87], off nt
	v_addc_co_u32_e32 v95, vcc, 0, v85, vcc
	global_load_dwordx4 v[84:87], v[86:87], off offset:2048 nt
	s_nop 0
	global_load_dwordx4 v[88:91], v[94:95], off nt
	global_load_dwordx4 v[112:115], v[92:93], off offset:-4096 nt
	s_nop 0
	global_load_dwordx4 v[92:95], v[94:95], off offset:2048 nt
.LBB0_720:
	s_add_i32 s8, s7, s6
	s_cmpk_lt_i32 s8, 0x80
	s_cselect_b64 s[0:1], -1, 0
	s_cmpk_gt_i32 s8, 0x7f
	s_cbranch_scc1 .LBB0_722
	s_ashr_i32 s14, s8, 31
	s_lshr_b32 s14, s14, 25
	s_add_i32 s14, s8, s14
	s_and_b32 s14, s14, 0xff80
	s_sub_i32 s14, s8, s14
	s_bfe_i32 s21, s14, 0x80000
	s_bfe_u32 s21, s21, 0x3000c
	s_add_i32 s21, s14, s21
	s_bfe_i32 s22, s21, 0x80000
	s_and_b32 s21, s21, 0xf8
	s_sub_i32 s14, s14, s21
	s_sext_i32_i8 s21, s14
	s_lshl_b32 s14, s14, 6
	s_lshl_b32 s21, s21, 5
	s_and_b32 s14, s14, 0xc0
	s_and_b32 s21, s21, 0xffffff80
	s_sext_i32_i16 s23, s22
	s_or_b32 s22, s21, s14
	s_add_i32 s21, s14, s21
	s_addk_i32 s21, 0x80
	s_cmpk_lt_u32 s14, 0x80
	s_cselect_b32 s22, s22, s21
	s_lshl_b32 s14, s23, 3
	s_andn2_b32 s14, s14, 63
	v_add_u32_e32 v20, s14, v221
	v_ashrrev_i32_e32 v21, 31, v20
	v_readlane_b32 s36, v253, 9
	v_lshlrev_b64 v[20:21], 11, v[20:21]
	v_readlane_b32 s37, v253, 10
	s_ashr_i32 s23, s22, 31
	s_movk_i32 s14, 0x1000
	v_lshl_add_u64 v[20:21], s[36:37], 0, v[20:21]
	v_lshl_add_u64 v[20:21], s[22:23], 2, v[20:21]
	v_lshl_add_u64 v[116:117], v[20:21], 0, v[2:3]
	v_add_co_u32_e32 v60, vcc, s14, v116
	global_load_dwordx4 v[24:27], v[116:117], off nt
	global_load_dwordx4 v[20:23], v[116:117], off offset:2048 nt
	v_addc_co_u32_e32 v61, vcc, 0, v117, vcc
	v_add_co_u32_e32 v124, vcc, s83, v116
	s_nop 1
	v_addc_co_u32_e32 v125, vcc, 0, v117, vcc
	v_add_co_u32_e32 v76, vcc, 0x3000, v116
	global_load_dwordx4 v[48:51], v[124:125], off nt
	global_load_dwordx4 v[44:47], v[124:125], off offset:2048 nt
	v_addc_co_u32_e32 v77, vcc, 0, v117, vcc
	v_add_co_u32_e32 v96, vcc, s62, v116
	global_load_dwordx4 v[64:67], v[60:61], off offset:2048 nt
	s_nop 0
	global_load_dwordx4 v[60:63], v[76:77], off nt
	v_addc_co_u32_e32 v97, vcc, 0, v117, vcc
	v_add_co_u32_e32 v104, vcc, 0x5000, v116
	global_load_dwordx4 v[76:79], v[76:77], off offset:2048 nt
	s_nop 0
	global_load_dwordx4 v[80:83], v[96:97], off nt
	v_addc_co_u32_e32 v105, vcc, 0, v117, vcc
	v_add_co_u32_e32 v118, vcc, 0x6000, v116
	global_load_dwordx4 v[96:99], v[96:97], off offset:2048 nt
	s_nop 0
	global_load_dwordx4 v[100:103], v[104:105], off nt
	v_addc_co_u32_e32 v119, vcc, 0, v117, vcc
	v_add_co_u32_e32 v126, vcc, 0x7000, v116
	global_load_dwordx4 v[104:107], v[104:105], off offset:2048 nt
	s_nop 0
	global_load_dwordx4 v[108:111], v[118:119], off nt
	v_addc_co_u32_e32 v127, vcc, 0, v117, vcc
	global_load_dwordx4 v[116:119], v[118:119], off offset:2048 nt
	s_nop 0
	global_load_dwordx4 v[120:123], v[126:127], off nt
	global_load_dwordx4 v[128:131], v[124:125], off offset:-4096 nt
	s_nop 0
	global_load_dwordx4 v[124:127], v[126:127], off offset:2048 nt
.LBB0_722:
	s_waitcnt vmcnt(14)
	v_cvt_pk_bf16_f32 v240, v132, v136
	s_waitcnt vmcnt(1)
	v_cvt_pk_bf16_f32 v241, v192, v156
	v_cvt_pk_bf16_f32 v242, v140, v144
	v_cvt_pk_bf16_f32 v243, v148, v160
	ds_write_b128 v223, v[240:243]
	v_cvt_pk_bf16_f32 v240, v152, v164
	v_cvt_pk_bf16_f32 v241, v168, v172
	v_cvt_pk_bf16_f32 v242, v176, v180
	s_waitcnt vmcnt(0)
	v_cvt_pk_bf16_f32 v243, v184, v188
	ds_write_b128 v224, v[240:243]
	v_cvt_pk_bf16_f32 v240, v133, v137
	v_cvt_pk_bf16_f32 v241, v193, v157
	v_cvt_pk_bf16_f32 v242, v141, v145
	v_cvt_pk_bf16_f32 v243, v149, v161
	ds_write_b128 v223, v[240:243] offset:128
	v_cvt_pk_bf16_f32 v240, v153, v165
	v_cvt_pk_bf16_f32 v241, v169, v173
	v_cvt_pk_bf16_f32 v242, v177, v181
	v_cvt_pk_bf16_f32 v243, v185, v189
	ds_write_b128 v224, v[240:243] offset:128
	v_cvt_pk_bf16_f32 v240, v134, v138
	v_cvt_pk_bf16_f32 v241, v194, v158
	v_cvt_pk_bf16_f32 v242, v142, v146
	v_cvt_pk_bf16_f32 v243, v150, v162
	ds_write_b128 v223, v[240:243] offset:256
	v_cvt_pk_bf16_f32 v240, v154, v166
	v_cvt_pk_bf16_f32 v241, v170, v174
	v_cvt_pk_bf16_f32 v242, v178, v182
	v_cvt_pk_bf16_f32 v243, v186, v190
	ds_write_b128 v224, v[240:243] offset:256
	v_cvt_pk_bf16_f32 v132, v135, v139
	v_cvt_pk_bf16_f32 v133, v195, v159
	v_cvt_pk_bf16_f32 v134, v143, v147
	v_cvt_pk_bf16_f32 v135, v151, v163
	ds_write_b128 v223, v[132:135] offset:384
	v_cvt_pk_bf16_f32 v132, v155, v167
	v_cvt_pk_bf16_f32 v133, v171, v175
	v_cvt_pk_bf16_f32 v134, v179, v183
	v_cvt_pk_bf16_f32 v135, v187, v191
	ds_write_b128 v224, v[132:135] offset:384
	v_add_u32_e32 v132, s5, v222
	v_add_u32_e32 v135, v225, v226
	v_ashrrev_i32_e32 v133, 31, v132
	ds_read_b128 v[136:139], v135
	v_lshlrev_b64 v[132:133], 11, v[132:133]
	v_lshl_add_u64 v[132:133], s[28:29], 0, v[132:133]
	s_ashr_i32 s5, s4, 31
	v_lshl_add_u64 v[132:133], s[4:5], 1, v[132:133]
	v_mov_b32_e32 v1, v3
	v_lshl_add_u64 v[152:153], v[132:133], 0, v[0:1]
	s_waitcnt lgkmcnt(0)
	global_store_dwordx4 v[152:153], v[136:139], off nt
	v_add_co_u32_e32 v132, vcc, s62, v152
	s_nop 0
	v_add_u32_e32 v137, v227, v228
	ds_read_b128 v[144:147], v137
	v_add_u32_e32 v136, v229, v230
	ds_read_b128 v[148:151], v136
	v_addc_co_u32_e32 v133, vcc, 0, v153, vcc
	v_add_u32_e32 v138, v231, v232
	s_waitcnt lgkmcnt(1)
	global_store_dwordx4 v[132:133], v[144:147], off nt
	ds_read_b128 v[144:147], v138
	v_add_co_u32_e32 v132, vcc, s88, v152
	ds_read_b128 v[140:143], v135 offset:4096
	s_nop 0
	v_addc_co_u32_e32 v133, vcc, 0, v153, vcc
	s_waitcnt lgkmcnt(2)
	global_store_dwordx4 v[132:133], v[148:151], off nt
	v_add_co_u32_e32 v132, vcc, s66, v152
	v_add_u32_e32 v134, v233, v234
	s_nop 0
	v_addc_co_u32_e32 v133, vcc, 0, v153, vcc
	ds_read_b128 v[148:151], v134
	s_waitcnt lgkmcnt(2)
	global_store_dwordx4 v[132:133], v[144:147], off nt
	v_add_co_u32_e32 v132, vcc, s82, v152
	s_mov_b32 s4, 0x14000
	s_nop 0
	v_addc_co_u32_e32 v133, vcc, 0, v153, vcc
	s_waitcnt lgkmcnt(1)
	global_store_dwordx4 v[132:133], v[140:143], off nt
	v_add_co_u32_e32 v132, vcc, s4, v152
	s_nop 1
	v_addc_co_u32_e32 v133, vcc, 0, v153, vcc
	s_waitcnt lgkmcnt(0)
	global_store_dwordx4 v[132:133], v[148:151], off nt
	v_add_u32_e32 v133, v235, v236
	ds_read_b128 v[140:143], v133
	v_add_u32_e32 v132, v237, v238
	v_add_co_u32_e32 v148, vcc, 0x18000, v152
	ds_read_b128 v[144:147], v132
	s_nop 0
	v_addc_co_u32_e32 v149, vcc, 0, v153, vcc
	s_waitcnt lgkmcnt(1)
	global_store_dwordx4 v[148:149], v[140:143], off nt
	s_nop 1
	v_add_co_u32_e32 v140, vcc, 0x1c000, v152
	s_nop 1
	v_addc_co_u32_e32 v141, vcc, 0, v153, vcc
	s_andn2_b64 vcc, exec, s[2:3]
	s_waitcnt lgkmcnt(0)
	global_store_dwordx4 v[140:141], v[144:147], off nt
	s_cbranch_vccz .LBB0_724
	s_andn2_b64 vcc, exec, s[0:1]
	s_cbranch_vccnz .LBB0_717
	s_branch .LBB0_725
.LBB0_724:
	s_ashr_i32 s2, s9, 31
	s_lshr_b32 s2, s2, 25
	s_add_i32 s2, s9, s2
	s_and_b32 s2, s2, 0xff80
	v_cvt_pk_bf16_f32 v140, v8, v4
	s_sub_i32 s2, s9, s2
	v_cvt_pk_bf16_f32 v141, v112, v32
	v_cvt_pk_bf16_f32 v142, v16, v12
	v_cvt_pk_bf16_f32 v143, v28, v36
	ds_write_b128 v223, v[140:143]
	v_cvt_pk_bf16_f32 v140, v40, v52
	s_bfe_i32 s3, s2, 0x80000
	v_cvt_pk_bf16_f32 v141, v56, v68
	v_cvt_pk_bf16_f32 v142, v72, v84
	v_cvt_pk_bf16_f32 v143, v88, v92
	ds_write_b128 v224, v[140:143]
	v_cvt_pk_bf16_f32 v140, v9, v5
	s_bfe_u32 s3, s3, 0x3000c
	v_cvt_pk_bf16_f32 v141, v113, v33
	v_cvt_pk_bf16_f32 v142, v17, v13
	v_cvt_pk_bf16_f32 v143, v29, v37
	ds_write_b128 v223, v[140:143] offset:128
	v_cvt_pk_bf16_f32 v140, v41, v53
	s_add_i32 s3, s2, s3
	v_cvt_pk_bf16_f32 v141, v57, v69
	v_cvt_pk_bf16_f32 v142, v73, v85
	v_cvt_pk_bf16_f32 v143, v89, v93
	ds_write_b128 v224, v[140:143] offset:128
	v_cvt_pk_bf16_f32 v140, v10, v6
	s_bfe_i32 s4, s3, 0x80000
	s_and_b32 s3, s3, 0xf8
	v_cvt_pk_bf16_f32 v141, v114, v34
	v_cvt_pk_bf16_f32 v142, v18, v14
	v_cvt_pk_bf16_f32 v143, v30, v38
	ds_write_b128 v223, v[140:143] offset:256
	v_cvt_pk_bf16_f32 v140, v42, v54
	s_sub_i32 s2, s2, s3
	v_cvt_pk_bf16_f32 v141, v58, v70
	v_cvt_pk_bf16_f32 v142, v74, v86
	v_cvt_pk_bf16_f32 v143, v90, v94
	ds_write_b128 v224, v[140:143] offset:256
	v_cvt_pk_bf16_f32 v140, v11, v7
	v_cvt_pk_bf16_f32 v141, v115, v35
	v_cvt_pk_bf16_f32 v142, v19, v15
	v_cvt_pk_bf16_f32 v143, v31, v39
	ds_write_b128 v223, v[140:143] offset:384
	v_cvt_pk_bf16_f32 v140, v43, v55
	s_sext_i32_i8 s2, s2
	s_sext_i32_i16 s4, s4
	v_cvt_pk_bf16_f32 v141, v59, v71
	v_cvt_pk_bf16_f32 v142, v75, v87
	v_cvt_pk_bf16_f32 v143, v91, v95
	ds_write_b128 v224, v[140:143] offset:384
	v_lshl_add_u32 v140, s2, 6, v222
	v_ashrrev_i32_e32 v141, 31, v140
	s_lshl_b32 s2, s4, 3
	v_lshlrev_b64 v[140:141], 11, v[140:141]
	s_andn2_b32 s2, s2, 63
	v_lshl_add_u64 v[140:141], s[28:29], 0, v[140:141]
	s_ashr_i32 s3, s2, 31
	v_lshl_add_u64 v[140:141], s[2:3], 1, v[140:141]
	v_lshl_add_u64 v[144:145], v[140:141], 0, v[0:1]
	ds_read_b128 v[140:143], v135
	v_add_co_u32_e32 v146, vcc, s62, v144
	s_waitcnt lgkmcnt(0)
	global_store_dwordx4 v[144:145], v[140:143], off nt
	ds_read_b128 v[140:143], v137
	v_addc_co_u32_e32 v147, vcc, 0, v145, vcc
	s_waitcnt lgkmcnt(0)
	global_store_dwordx4 v[146:147], v[140:143], off nt
	ds_read_b128 v[140:143], v136
	v_add_co_u32_e32 v146, vcc, 0x8000, v144
	s_nop 1
	v_addc_co_u32_e32 v147, vcc, 0, v145, vcc
	s_waitcnt lgkmcnt(0)
	global_store_dwordx4 v[146:147], v[140:143], off nt
	ds_read_b128 v[140:143], v138
	v_add_co_u32_e32 v146, vcc, 0xc000, v144
	s_nop 1
	v_addc_co_u32_e32 v147, vcc, 0, v145, vcc
	s_waitcnt lgkmcnt(0)
	global_store_dwordx4 v[146:147], v[140:143], off nt
	ds_read_b128 v[140:143], v135 offset:4096
	v_add_co_u32_e32 v146, vcc, s82, v144
	s_nop 1
	v_addc_co_u32_e32 v147, vcc, 0, v145, vcc
	s_waitcnt lgkmcnt(0)
	global_store_dwordx4 v[146:147], v[140:143], off nt
	ds_read_b128 v[140:143], v134
	v_add_co_u32_e32 v146, vcc, 0x14000, v144
	s_nop 1
	v_addc_co_u32_e32 v147, vcc, 0, v145, vcc
	s_waitcnt lgkmcnt(0)
	global_store_dwordx4 v[146:147], v[140:143], off nt
	ds_read_b128 v[140:143], v133
	v_add_co_u32_e32 v146, vcc, 0x18000, v144
	s_nop 1
	v_addc_co_u32_e32 v147, vcc, 0, v145, vcc
	s_waitcnt lgkmcnt(0)
	global_store_dwordx4 v[146:147], v[140:143], off nt
	ds_read_b128 v[140:143], v132
	v_add_co_u32_e32 v144, vcc, 0x1c000, v144
	s_nop 1
	v_addc_co_u32_e32 v145, vcc, 0, v145, vcc
	s_waitcnt lgkmcnt(0)
	global_store_dwordx4 v[144:145], v[140:143], off nt
	s_andn2_b64 vcc, exec, s[0:1]
	s_cbranch_vccnz .LBB0_717
.LBB0_725:
	s_ashr_i32 s0, s8, 31
	s_lshr_b32 s0, s0, 25
	s_add_i32 s0, s8, s0
	s_and_b32 s0, s0, 0xff80
	v_cvt_pk_bf16_f32 v140, v24, v20
	s_sub_i32 s0, s8, s0
	v_cvt_pk_bf16_f32 v141, v128, v64
	v_cvt_pk_bf16_f32 v142, v48, v44
	v_cvt_pk_bf16_f32 v143, v60, v76
	ds_write_b128 v223, v[140:143]
	v_cvt_pk_bf16_f32 v140, v80, v96
	s_bfe_i32 s1, s0, 0x80000
	v_cvt_pk_bf16_f32 v141, v100, v104
	v_cvt_pk_bf16_f32 v142, v108, v116
	v_cvt_pk_bf16_f32 v143, v120, v124
	ds_write_b128 v224, v[140:143]
	v_cvt_pk_bf16_f32 v140, v25, v21
	s_bfe_u32 s1, s1, 0x3000c
	v_cvt_pk_bf16_f32 v141, v129, v65
	v_cvt_pk_bf16_f32 v142, v49, v45
	v_cvt_pk_bf16_f32 v143, v61, v77
	ds_write_b128 v223, v[140:143] offset:128
	v_cvt_pk_bf16_f32 v140, v81, v97
	s_add_i32 s1, s0, s1
	v_cvt_pk_bf16_f32 v141, v101, v105
	v_cvt_pk_bf16_f32 v142, v109, v117
	v_cvt_pk_bf16_f32 v143, v121, v125
	ds_write_b128 v224, v[140:143] offset:128
	v_cvt_pk_bf16_f32 v140, v26, v22
	s_bfe_i32 s2, s1, 0x80000
	s_and_b32 s1, s1, 0xf8
	v_cvt_pk_bf16_f32 v141, v130, v66
	v_cvt_pk_bf16_f32 v142, v50, v46
	v_cvt_pk_bf16_f32 v143, v62, v78
	ds_write_b128 v223, v[140:143] offset:256
	v_cvt_pk_bf16_f32 v140, v82, v98
	s_sub_i32 s0, s0, s1
	v_cvt_pk_bf16_f32 v141, v102, v106
	v_cvt_pk_bf16_f32 v142, v110, v118
	v_cvt_pk_bf16_f32 v143, v122, v126
	ds_write_b128 v224, v[140:143] offset:256
	v_cvt_pk_bf16_f32 v140, v27, v23
	v_cvt_pk_bf16_f32 v141, v131, v67
	v_cvt_pk_bf16_f32 v142, v51, v47
	v_cvt_pk_bf16_f32 v143, v63, v79
	ds_write_b128 v223, v[140:143] offset:384
	v_cvt_pk_bf16_f32 v140, v83, v99
	s_sext_i32_i8 s0, s0
	s_sext_i32_i16 s2, s2
	v_cvt_pk_bf16_f32 v141, v103, v107
	v_cvt_pk_bf16_f32 v142, v111, v119
	v_cvt_pk_bf16_f32 v143, v123, v127
	ds_write_b128 v224, v[140:143] offset:384
	v_lshl_add_u32 v140, s0, 6, v222
	v_ashrrev_i32_e32 v141, 31, v140
	s_lshl_b32 s0, s2, 3
	v_lshlrev_b64 v[140:141], 11, v[140:141]
	s_andn2_b32 s0, s0, 63
	v_lshl_add_u64 v[140:141], s[28:29], 0, v[140:141]
	s_ashr_i32 s1, s0, 31
	v_lshl_add_u64 v[140:141], s[0:1], 1, v[140:141]
	v_mov_b32_e32 v1, v3
	v_lshl_add_u64 v[144:145], v[140:141], 0, v[0:1]
	ds_read_b128 v[140:143], v135
	v_add_co_u32_e32 v146, vcc, s62, v144
	s_waitcnt lgkmcnt(0)
	global_store_dwordx4 v[144:145], v[140:143], off nt
	ds_read_b128 v[140:143], v137
	v_addc_co_u32_e32 v147, vcc, 0, v145, vcc
	s_waitcnt lgkmcnt(0)
	global_store_dwordx4 v[146:147], v[140:143], off nt
	ds_read_b128 v[140:143], v136
	v_add_co_u32_e32 v136, vcc, 0x8000, v144
	s_nop 1
	v_addc_co_u32_e32 v137, vcc, 0, v145, vcc
	s_waitcnt lgkmcnt(0)
	global_store_dwordx4 v[136:137], v[140:143], off nt
	ds_read_b128 v[136:139], v138
	s_nop 0
	v_add_co_u32_e32 v140, vcc, 0xc000, v144
	s_nop 1
	v_addc_co_u32_e32 v141, vcc, 0, v145, vcc
	s_waitcnt lgkmcnt(0)
	global_store_dwordx4 v[140:141], v[136:139], off nt
	ds_read_b128 v[136:139], v135 offset:4096
	v_add_co_u32_e32 v140, vcc, s82, v144
	s_nop 1
	v_addc_co_u32_e32 v141, vcc, 0, v145, vcc
	s_waitcnt lgkmcnt(0)
	global_store_dwordx4 v[140:141], v[136:139], off nt
	ds_read_b128 v[134:137], v134
	s_nop 0
	v_add_co_u32_e32 v138, vcc, 0x14000, v144
	s_nop 1
	v_addc_co_u32_e32 v139, vcc, 0, v145, vcc
	s_waitcnt lgkmcnt(0)
	global_store_dwordx4 v[138:139], v[134:137], off nt
	ds_read_b128 v[134:137], v133
	v_add_co_u32_e32 v138, vcc, 0x18000, v144
	s_nop 1
	v_addc_co_u32_e32 v139, vcc, 0, v145, vcc
	s_waitcnt lgkmcnt(0)
	global_store_dwordx4 v[138:139], v[134:137], off nt
	ds_read_b128 v[132:135], v132
	s_nop 0
	v_add_co_u32_e32 v136, vcc, 0x1c000, v144
	s_nop 1
	v_addc_co_u32_e32 v137, vcc, 0, v145, vcc
	s_waitcnt lgkmcnt(0)
	global_store_dwordx4 v[136:137], v[132:135], off nt
	s_branch .LBB0_717

.LBB0_729:
	s_add_i32 s21, s38, s8
	s_cmp_lt_i32 s21, 64
	s_cselect_b64 s[2:3], -1, 0
	s_ashr_i32 s0, s8, 31
	s_lshr_b32 s0, s0, 26
	s_add_i32 s0, s8, s0
	s_and_b32 s0, s0, 0xffc0
	s_sub_i32 s0, s8, s0
	s_bfe_i32 s1, s0, 0x80000
	s_bfe_u32 s1, s1, 0x4000b
	s_add_i32 s1, s0, s1
	s_bfe_i32 s4, s1, 0x80000
	s_and_b32 s1, s1, 0xf0
	s_sub_i32 s0, s0, s1
	s_sext_i32_i16 s4, s4
	s_sext_i32_i8 s0, s0
	s_lshl_b32 s6, s0, 6
	s_lshl_b32 s0, s4, 2
	s_and_b32 s4, s0, 0xffffffc0
	v_add_u32_e32 v132, s4, v221
	v_ashrrev_i32_e32 v133, 31, v132
	v_readlane_b32 s0, v253, 11
	v_lshlrev_b64 v[132:133], 12, v[132:133]
	v_readlane_b32 s1, v253, 12
	s_ashr_i32 s7, s6, 31
	s_cmp_gt_i32 s21, 63
	v_lshl_add_u64 v[132:133], s[0:1], 0, v[132:133]
	v_lshl_add_u64 v[132:133], s[6:7], 2, v[132:133]
	v_lshl_add_u64 v[188:189], v[132:133], 0, v[2:3]
	v_add_co_u32_e32 v132, vcc, s83, v188
	s_nop 1
	v_addc_co_u32_e32 v133, vcc, 0, v189, vcc
	v_add_co_u32_e32 v140, vcc, s62, v188
	global_load_dwordx4 v[136:139], v[132:133], off offset:-4096 nt
	s_nop 0
	global_load_dwordx4 v[132:135], v[132:133], off nt
	v_addc_co_u32_e32 v141, vcc, 0, v189, vcc
	v_add_co_u32_e32 v148, vcc, s77, v188
	global_load_dwordx4 v[144:147], v[140:141], off offset:-4096 nt
	s_nop 0
	global_load_dwordx4 v[140:143], v[140:141], off nt
	v_addc_co_u32_e32 v149, vcc, 0, v189, vcc
	v_add_co_u32_e32 v152, vcc, s88, v188
	global_load_dwordx4 v[156:159], v[148:149], off offset:-4096 nt
	s_nop 0
	global_load_dwordx4 v[148:151], v[148:149], off nt
	v_addc_co_u32_e32 v153, vcc, 0, v189, vcc
	v_add_co_u32_e32 v160, vcc, s72, v188
	global_load_dwordx4 v[164:167], v[152:153], off offset:-4096 nt
	s_nop 0
	global_load_dwordx4 v[152:155], v[152:153], off nt
	v_addc_co_u32_e32 v161, vcc, 0, v189, vcc
	v_add_co_u32_e32 v172, vcc, 0xb000, v188
	global_load_dwordx4 v[168:171], v[160:161], off offset:-4096 nt
	s_nop 0
	global_load_dwordx4 v[160:163], v[160:161], off nt
	v_addc_co_u32_e32 v173, vcc, 0, v189, vcc
	v_add_co_u32_e32 v176, vcc, s66, v188
	global_load_dwordx4 v[184:187], v[188:189], off nt
	s_nop 0
	global_load_dwordx4 v[172:175], v[172:173], off nt
	v_addc_co_u32_e32 v177, vcc, 0, v189, vcc
	v_add_co_u32_e32 v180, vcc, 0xd000, v188
	s_nop 1
	v_addc_co_u32_e32 v181, vcc, 0, v189, vcc
	v_add_co_u32_e32 v190, vcc, 0xe000, v188
	global_load_dwordx4 v[176:179], v[176:177], off nt
	s_nop 0
	global_load_dwordx4 v[180:183], v[180:181], off nt
	v_addc_co_u32_e32 v191, vcc, 0, v189, vcc
	v_add_co_u32_e32 v192, vcc, 0xf000, v188
	s_nop 1
	v_addc_co_u32_e32 v193, vcc, 0, v189, vcc
	global_load_dwordx4 v[188:191], v[190:191], off nt
	s_nop 0
	global_load_dwordx4 v[192:195], v[192:193], off nt
	s_cbranch_scc1 .LBB0_731
	s_ashr_i32 s0, s21, 31
	s_lshr_b32 s0, s0, 26
	s_add_i32 s0, s21, s0
	s_and_b32 s0, s0, 0xffc0
	s_sub_i32 s0, s21, s0
	s_bfe_i32 s1, s0, 0x80000
	s_bfe_u32 s1, s1, 0x4000b
	s_add_i32 s1, s0, s1
	s_bfe_i32 s5, s1, 0x80000
	s_sext_i32_i16 s5, s5
	s_and_b32 s1, s1, 0xf0
	s_sub_i32 s0, s0, s1
	s_lshl_b32 s1, s5, 2
	s_andn2_b32 s1, s1, 63
	v_add_u32_e32 v4, s1, v221
	s_sext_i32_i8 s0, s0
	v_ashrrev_i32_e32 v5, 31, v4
	v_readlane_b32 s22, v253, 11
	s_lshl_b32 s0, s0, 6
	v_lshlrev_b64 v[4:5], 12, v[4:5]
	v_readlane_b32 s23, v253, 12
	s_ashr_i32 s1, s0, 31
	s_nop 0
	v_lshl_add_u64 v[4:5], s[22:23], 0, v[4:5]
	v_lshl_add_u64 v[4:5], s[0:1], 2, v[4:5]
	v_lshl_add_u64 v[108:109], v[4:5], 0, v[2:3]
	v_add_co_u32_e32 v4, vcc, s83, v108
	s_nop 1
	v_addc_co_u32_e32 v5, vcc, 0, v109, vcc
	v_add_co_u32_e32 v12, vcc, s62, v108
	global_load_dwordx4 v[8:11], v[4:5], off offset:-4096 nt
	s_nop 0
	global_load_dwordx4 v[4:7], v[4:5], off nt
	v_addc_co_u32_e32 v13, vcc, 0, v109, vcc
	v_add_co_u32_e32 v20, vcc, s77, v108
	global_load_dwordx4 v[16:19], v[12:13], off offset:-4096 nt
	s_nop 0
	global_load_dwordx4 v[12:15], v[12:13], off nt
	v_addc_co_u32_e32 v21, vcc, 0, v109, vcc
	v_add_co_u32_e32 v28, vcc, s88, v108
	global_load_dwordx4 v[24:27], v[20:21], off offset:-4096 nt
	s_nop 0
	global_load_dwordx4 v[20:23], v[20:21], off nt
	v_addc_co_u32_e32 v29, vcc, 0, v109, vcc
	v_add_co_u32_e32 v52, vcc, 0x9000, v108
	global_load_dwordx4 v[32:35], v[28:29], off offset:-4096 nt
	s_nop 0
	global_load_dwordx4 v[28:31], v[28:29], off nt
	v_addc_co_u32_e32 v53, vcc, 0, v109, vcc
	v_add_co_u32_e32 v68, vcc, s72, v108
	global_load_dwordx4 v[64:67], v[108:109], off nt
	s_nop 0
	global_load_dwordx4 v[52:55], v[52:53], off nt
	v_addc_co_u32_e32 v69, vcc, 0, v109, vcc
	v_add_co_u32_e32 v80, vcc, 0xb000, v108
	s_nop 1
	v_addc_co_u32_e32 v81, vcc, 0, v109, vcc
	v_add_co_u32_e32 v88, vcc, 0xc000, v108
	global_load_dwordx4 v[68:71], v[68:69], off nt
	s_nop 0
	global_load_dwordx4 v[80:83], v[80:81], off nt
	v_addc_co_u32_e32 v89, vcc, 0, v109, vcc
	v_add_co_u32_e32 v96, vcc, 0xd000, v108
	s_nop 1
	v_addc_co_u32_e32 v97, vcc, 0, v109, vcc
	v_add_co_u32_e32 v110, vcc, 0xe000, v108
	global_load_dwordx4 v[88:91], v[88:89], off nt
	s_nop 0
	global_load_dwordx4 v[96:99], v[96:97], off nt
	v_addc_co_u32_e32 v111, vcc, 0, v109, vcc
	v_add_co_u32_e32 v112, vcc, 0xf000, v108
	s_nop 1
	v_addc_co_u32_e32 v113, vcc, 0, v109, vcc
	global_load_dwordx4 v[108:111], v[110:111], off nt
	s_nop 0
	global_load_dwordx4 v[112:115], v[112:113], off nt
.LBB0_731:
	s_add_i32 s7, s9, s8
	s_cmp_lt_i32 s7, 64
	s_cselect_b64 s[0:1], -1, 0
	s_cmp_gt_i32 s7, 63
	s_cbranch_scc1 .LBB0_733
	s_ashr_i32 s5, s7, 31
	s_lshr_b32 s5, s5, 26
	s_add_i32 s5, s7, s5
	s_and_b32 s5, s5, 0xffc0
	s_sub_i32 s5, s7, s5
	s_bfe_i32 s14, s5, 0x80000
	s_bfe_u32 s14, s14, 0x4000b
	s_add_i32 s14, s5, s14
	s_bfe_i32 s22, s14, 0x80000
	s_and_b32 s14, s14, 0xf0
	s_sub_i32 s5, s5, s14
	s_sext_i32_i16 s23, s22
	s_sext_i32_i8 s5, s5
	s_lshl_b32 s22, s5, 6
	s_lshl_b32 s5, s23, 2
	s_andn2_b32 s5, s5, 63
	v_add_u32_e32 v36, s5, v221
	v_ashrrev_i32_e32 v37, 31, v36
	v_readlane_b32 s36, v253, 11
	v_lshlrev_b64 v[36:37], 12, v[36:37]
	v_readlane_b32 s37, v253, 12
	s_ashr_i32 s23, s22, 31
	s_nop 0
	v_lshl_add_u64 v[36:37], s[36:37], 0, v[36:37]
	v_lshl_add_u64 v[36:37], s[22:23], 2, v[36:37]
	v_lshl_add_u64 v[124:125], v[36:37], 0, v[2:3]
	v_add_co_u32_e32 v36, vcc, s83, v124
	s_nop 1
	v_addc_co_u32_e32 v37, vcc, 0, v125, vcc
	v_add_co_u32_e32 v44, vcc, s62, v124
	global_load_dwordx4 v[40:43], v[36:37], off offset:-4096 nt
	s_nop 0
	global_load_dwordx4 v[36:39], v[36:37], off nt
	v_addc_co_u32_e32 v45, vcc, 0, v125, vcc
	v_add_co_u32_e32 v56, vcc, s77, v124
	global_load_dwordx4 v[48:51], v[44:45], off offset:-4096 nt
	s_nop 0
	global_load_dwordx4 v[44:47], v[44:45], off nt
	v_addc_co_u32_e32 v57, vcc, 0, v125, vcc
	v_add_co_u32_e32 v72, vcc, s88, v124
	global_load_dwordx4 v[60:63], v[56:57], off offset:-4096 nt
	s_nop 0
	global_load_dwordx4 v[56:59], v[56:57], off nt
	v_addc_co_u32_e32 v73, vcc, 0, v125, vcc
	v_add_co_u32_e32 v84, vcc, 0x9000, v124
	global_load_dwordx4 v[76:79], v[72:73], off offset:-4096 nt
	s_nop 0
	global_load_dwordx4 v[72:75], v[72:73], off nt
	v_addc_co_u32_e32 v85, vcc, 0, v125, vcc
	v_add_co_u32_e32 v100, vcc, s72, v124
	global_load_dwordx4 v[92:95], v[124:125], off nt
	s_nop 0
	global_load_dwordx4 v[84:87], v[84:85], off nt
	v_addc_co_u32_e32 v101, vcc, 0, v125, vcc
	v_add_co_u32_e32 v104, vcc, 0xb000, v124
	s_nop 1
	v_addc_co_u32_e32 v105, vcc, 0, v125, vcc
	v_add_co_u32_e32 v116, vcc, 0xc000, v124
	global_load_dwordx4 v[100:103], v[100:101], off nt
	s_nop 0
	global_load_dwordx4 v[104:107], v[104:105], off nt
	v_addc_co_u32_e32 v117, vcc, 0, v125, vcc
	v_add_co_u32_e32 v120, vcc, 0xd000, v124
	s_nop 1
	v_addc_co_u32_e32 v121, vcc, 0, v125, vcc
	v_add_co_u32_e32 v126, vcc, 0xe000, v124
	global_load_dwordx4 v[116:119], v[116:117], off nt
	s_nop 0
	global_load_dwordx4 v[120:123], v[120:121], off nt
	v_addc_co_u32_e32 v127, vcc, 0, v125, vcc
	v_add_co_u32_e32 v128, vcc, 0xf000, v124
	s_nop 1
	v_addc_co_u32_e32 v129, vcc, 0, v125, vcc
	global_load_dwordx4 v[124:127], v[126:127], off nt
	s_nop 0
	global_load_dwordx4 v[128:131], v[128:129], off nt
.LBB0_733:
	s_waitcnt vmcnt(5)
	v_cvt_pk_bf16_f32 v240, v184, v136
	v_cvt_pk_bf16_f32 v241, v132, v144
	v_cvt_pk_bf16_f32 v242, v140, v156
	v_cvt_pk_bf16_f32 v243, v148, v164
	ds_write_b128 v223, v[240:243]
	v_cvt_pk_bf16_f32 v240, v152, v168
	s_waitcnt vmcnt(4)
	v_cvt_pk_bf16_f32 v241, v160, v172
	s_waitcnt vmcnt(2)
	v_cvt_pk_bf16_f32 v242, v176, v180
	s_waitcnt vmcnt(0)
	v_cvt_pk_bf16_f32 v243, v188, v192
	ds_write_b128 v224, v[240:243]
	v_cvt_pk_bf16_f32 v240, v185, v137
	v_cvt_pk_bf16_f32 v241, v133, v145
	v_cvt_pk_bf16_f32 v242, v141, v157
	v_cvt_pk_bf16_f32 v243, v149, v165
	ds_write_b128 v223, v[240:243] offset:128
	v_cvt_pk_bf16_f32 v240, v153, v169
	v_cvt_pk_bf16_f32 v241, v161, v173
	v_cvt_pk_bf16_f32 v242, v177, v181
	v_cvt_pk_bf16_f32 v243, v189, v193
	ds_write_b128 v224, v[240:243] offset:128
	v_cvt_pk_bf16_f32 v240, v186, v138
	v_cvt_pk_bf16_f32 v241, v134, v146
	v_cvt_pk_bf16_f32 v242, v142, v158
	v_cvt_pk_bf16_f32 v243, v150, v166
	ds_write_b128 v223, v[240:243] offset:256
	v_cvt_pk_bf16_f32 v240, v154, v170
	v_cvt_pk_bf16_f32 v241, v162, v174
	v_cvt_pk_bf16_f32 v242, v178, v182
	v_cvt_pk_bf16_f32 v243, v190, v194
	ds_write_b128 v224, v[240:243] offset:256
	v_cvt_pk_bf16_f32 v132, v187, v139
	v_cvt_pk_bf16_f32 v133, v135, v147
	v_cvt_pk_bf16_f32 v134, v143, v159
	v_cvt_pk_bf16_f32 v135, v151, v167
	ds_write_b128 v223, v[132:135] offset:384
	v_cvt_pk_bf16_f32 v132, v155, v171
	v_cvt_pk_bf16_f32 v133, v163, v175
	v_cvt_pk_bf16_f32 v134, v179, v183
	v_cvt_pk_bf16_f32 v135, v191, v195
	ds_write_b128 v224, v[132:135] offset:384
	v_add_u32_e32 v132, s6, v222
	v_add_u32_e32 v135, v225, v226
	v_ashrrev_i32_e32 v133, 31, v132
	ds_read_b128 v[136:139], v135
	ds_read_b128 v[140:143], v135 offset:4096
	v_lshlrev_b64 v[132:133], 9, v[132:133]
	v_lshl_add_u64 v[132:133], s[28:29], 0, v[132:133]
	s_ashr_i32 s5, s4, 31
	v_lshl_add_u64 v[132:133], s[4:5], 1, v[132:133]
	v_mov_b32_e32 v1, v3
	v_lshl_add_u64 v[152:153], v[132:133], 0, v[0:1]
	s_waitcnt lgkmcnt(1)
	global_store_dwordx4 v[152:153], v[136:139], off nt
	v_add_co_u32_e32 v132, vcc, s83, v152
	s_nop 0
	v_add_u32_e32 v137, v227, v228
	v_add_u32_e32 v136, v229, v230
	ds_read_b128 v[144:147], v137
	ds_read_b128 v[148:151], v136
	v_addc_co_u32_e32 v133, vcc, 0, v153, vcc
	s_waitcnt lgkmcnt(1)
	global_store_dwordx4 v[132:133], v[144:147], off offset:-4096 nt
	s_waitcnt lgkmcnt(0)
	global_store_dwordx4 v[132:133], v[148:151], off nt
	v_add_u32_e32 v138, v231, v232
	ds_read_b128 v[144:147], v138
	v_add_u32_e32 v134, v233, v234
	ds_read_b128 v[148:151], v134
	v_add_co_u32_e32 v132, vcc, s62, v152
	s_nop 1
	v_addc_co_u32_e32 v133, vcc, 0, v153, vcc
	s_waitcnt lgkmcnt(1)
	global_store_dwordx4 v[132:133], v[144:147], off offset:-4096 nt
	global_store_dwordx4 v[132:133], v[140:143], off nt
	v_add_co_u32_e32 v132, vcc, 0x5000, v152
	s_nop 1
	v_addc_co_u32_e32 v133, vcc, 0, v153, vcc
	s_waitcnt lgkmcnt(0)
	global_store_dwordx4 v[132:133], v[148:151], off nt
	v_add_u32_e32 v133, v235, v236
	ds_read_b128 v[140:143], v133
	v_add_u32_e32 v132, v237, v238
	v_add_co_u32_e32 v148, vcc, 0x6000, v152
	ds_read_b128 v[144:147], v132
	s_nop 0
	v_addc_co_u32_e32 v149, vcc, 0, v153, vcc
	s_waitcnt lgkmcnt(1)
	global_store_dwordx4 v[148:149], v[140:143], off nt
	s_nop 1
	v_add_co_u32_e32 v140, vcc, 0x7000, v152
	s_nop 1
	v_addc_co_u32_e32 v141, vcc, 0, v153, vcc
	s_andn2_b64 vcc, exec, s[2:3]
	s_waitcnt lgkmcnt(0)
	global_store_dwordx4 v[140:141], v[144:147], off nt
	s_cbranch_vccz .LBB0_735
	s_andn2_b64 vcc, exec, s[0:1]
	s_cbranch_vccnz .LBB0_728
	s_branch .LBB0_736
.LBB0_735:
	s_ashr_i32 s2, s21, 31
	s_lshr_b32 s2, s2, 26
	s_add_i32 s2, s21, s2
	s_and_b32 s2, s2, 0xffc0
	v_cvt_pk_bf16_f32 v140, v64, v8
	s_sub_i32 s2, s21, s2
	v_cvt_pk_bf16_f32 v141, v4, v16
	v_cvt_pk_bf16_f32 v142, v12, v24
	v_cvt_pk_bf16_f32 v143, v20, v32
	ds_write_b128 v223, v[140:143]
	v_cvt_pk_bf16_f32 v140, v28, v52
	s_bfe_i32 s3, s2, 0x80000
	v_cvt_pk_bf16_f32 v141, v68, v80
	v_cvt_pk_bf16_f32 v142, v88, v96
	v_cvt_pk_bf16_f32 v143, v108, v112
	ds_write_b128 v224, v[140:143]
	v_cvt_pk_bf16_f32 v140, v65, v9
	s_bfe_u32 s3, s3, 0x4000b
	v_cvt_pk_bf16_f32 v141, v5, v17
	v_cvt_pk_bf16_f32 v142, v13, v25
	v_cvt_pk_bf16_f32 v143, v21, v33
	ds_write_b128 v223, v[140:143] offset:128
	v_cvt_pk_bf16_f32 v140, v29, v53
	s_add_i32 s3, s2, s3
	v_cvt_pk_bf16_f32 v141, v69, v81
	v_cvt_pk_bf16_f32 v142, v89, v97
	v_cvt_pk_bf16_f32 v143, v109, v113
	ds_write_b128 v224, v[140:143] offset:128
	v_cvt_pk_bf16_f32 v140, v66, v10
	s_bfe_i32 s4, s3, 0x80000
	v_cvt_pk_bf16_f32 v141, v6, v18
	v_cvt_pk_bf16_f32 v142, v14, v26
	v_cvt_pk_bf16_f32 v143, v22, v34
	ds_write_b128 v223, v[140:143] offset:256
	v_cvt_pk_bf16_f32 v140, v30, v54
	s_and_b32 s3, s3, 0xf0
	v_cvt_pk_bf16_f32 v141, v70, v82
	v_cvt_pk_bf16_f32 v142, v90, v98
	v_cvt_pk_bf16_f32 v143, v110, v114
	ds_write_b128 v224, v[140:143] offset:256
	v_cvt_pk_bf16_f32 v140, v67, v11
	s_sub_i32 s2, s2, s3
	v_cvt_pk_bf16_f32 v141, v7, v19
	v_cvt_pk_bf16_f32 v142, v15, v27
	v_cvt_pk_bf16_f32 v143, v23, v35
	ds_write_b128 v223, v[140:143] offset:384
	v_cvt_pk_bf16_f32 v140, v31, v55
	s_sext_i32_i8 s2, s2
	s_sext_i32_i16 s4, s4
	v_cvt_pk_bf16_f32 v141, v71, v83
	v_cvt_pk_bf16_f32 v142, v91, v99
	v_cvt_pk_bf16_f32 v143, v111, v115
	ds_write_b128 v224, v[140:143] offset:384
	v_lshl_add_u32 v140, s2, 6, v222
	v_ashrrev_i32_e32 v141, 31, v140
	s_lshl_b32 s2, s4, 2
	v_lshlrev_b64 v[140:141], 9, v[140:141]
	s_andn2_b32 s2, s2, 63
	v_lshl_add_u64 v[140:141], s[28:29], 0, v[140:141]
	s_ashr_i32 s3, s2, 31
	v_lshl_add_u64 v[140:141], s[2:3], 1, v[140:141]
	v_lshl_add_u64 v[144:145], v[140:141], 0, v[0:1]
	ds_read_b128 v[140:143], v135
	v_add_co_u32_e32 v146, vcc, s83, v144
	s_waitcnt lgkmcnt(0)
	global_store_dwordx4 v[144:145], v[140:143], off nt
	ds_read_b128 v[140:143], v137
	v_addc_co_u32_e32 v147, vcc, 0, v145, vcc
	s_waitcnt lgkmcnt(0)
	global_store_dwordx4 v[146:147], v[140:143], off offset:-4096 nt
	ds_read_b128 v[140:143], v136
	s_waitcnt lgkmcnt(0)
	global_store_dwordx4 v[146:147], v[140:143], off nt
	ds_read_b128 v[140:143], v138
	v_add_co_u32_e32 v146, vcc, 0x3000, v144
	s_nop 1
	v_addc_co_u32_e32 v147, vcc, 0, v145, vcc
	s_waitcnt lgkmcnt(0)
	global_store_dwordx4 v[146:147], v[140:143], off nt
	ds_read_b128 v[140:143], v135 offset:4096
	v_add_co_u32_e32 v146, vcc, s62, v144
	s_nop 1
	v_addc_co_u32_e32 v147, vcc, 0, v145, vcc
	s_waitcnt lgkmcnt(0)
	global_store_dwordx4 v[146:147], v[140:143], off nt
	ds_read_b128 v[140:143], v134
	v_add_co_u32_e32 v146, vcc, 0x5000, v144
	s_nop 1
	v_addc_co_u32_e32 v147, vcc, 0, v145, vcc
	s_waitcnt lgkmcnt(0)
	global_store_dwordx4 v[146:147], v[140:143], off nt
	ds_read_b128 v[140:143], v133
	v_add_co_u32_e32 v146, vcc, 0x6000, v144
	s_nop 1
	v_addc_co_u32_e32 v147, vcc, 0, v145, vcc
	s_waitcnt lgkmcnt(0)
	global_store_dwordx4 v[146:147], v[140:143], off nt
	ds_read_b128 v[140:143], v132
	v_add_co_u32_e32 v144, vcc, 0x7000, v144
	s_nop 1
	v_addc_co_u32_e32 v145, vcc, 0, v145, vcc
	s_waitcnt lgkmcnt(0)
	global_store_dwordx4 v[144:145], v[140:143], off nt
	s_andn2_b64 vcc, exec, s[0:1]
	s_cbranch_vccnz .LBB0_728
.LBB0_736:
	s_ashr_i32 s0, s7, 31
	s_lshr_b32 s0, s0, 26
	s_add_i32 s0, s7, s0
	s_and_b32 s0, s0, 0xffc0
	v_cvt_pk_bf16_f32 v140, v92, v40
	s_sub_i32 s0, s7, s0
	v_cvt_pk_bf16_f32 v141, v36, v48
	v_cvt_pk_bf16_f32 v142, v44, v60
	v_cvt_pk_bf16_f32 v143, v56, v76
	ds_write_b128 v223, v[140:143]
	v_cvt_pk_bf16_f32 v140, v72, v84
	s_bfe_i32 s1, s0, 0x80000
	v_cvt_pk_bf16_f32 v141, v100, v104
	v_cvt_pk_bf16_f32 v142, v116, v120
	v_cvt_pk_bf16_f32 v143, v124, v128
	ds_write_b128 v224, v[140:143]
	v_cvt_pk_bf16_f32 v140, v93, v41
	s_bfe_u32 s1, s1, 0x4000b
	v_cvt_pk_bf16_f32 v141, v37, v49
	v_cvt_pk_bf16_f32 v142, v45, v61
	v_cvt_pk_bf16_f32 v143, v57, v77
	ds_write_b128 v223, v[140:143] offset:128
	v_cvt_pk_bf16_f32 v140, v73, v85
	s_add_i32 s1, s0, s1
	v_cvt_pk_bf16_f32 v141, v101, v105
	v_cvt_pk_bf16_f32 v142, v117, v121
	v_cvt_pk_bf16_f32 v143, v125, v129
	ds_write_b128 v224, v[140:143] offset:128
	v_cvt_pk_bf16_f32 v140, v94, v42
	s_bfe_i32 s2, s1, 0x80000
	v_cvt_pk_bf16_f32 v141, v38, v50
	v_cvt_pk_bf16_f32 v142, v46, v62
	v_cvt_pk_bf16_f32 v143, v58, v78
	ds_write_b128 v223, v[140:143] offset:256
	v_cvt_pk_bf16_f32 v140, v74, v86
	s_and_b32 s1, s1, 0xf0
	v_cvt_pk_bf16_f32 v141, v102, v106
	v_cvt_pk_bf16_f32 v142, v118, v122
	v_cvt_pk_bf16_f32 v143, v126, v130
	ds_write_b128 v224, v[140:143] offset:256
	v_cvt_pk_bf16_f32 v140, v95, v43
	s_sub_i32 s0, s0, s1
	v_cvt_pk_bf16_f32 v141, v39, v51
	v_cvt_pk_bf16_f32 v142, v47, v63
	v_cvt_pk_bf16_f32 v143, v59, v79
	ds_write_b128 v223, v[140:143] offset:384
	v_cvt_pk_bf16_f32 v140, v75, v87
	s_sext_i32_i8 s0, s0
	s_sext_i32_i16 s2, s2
	v_cvt_pk_bf16_f32 v141, v103, v107
	v_cvt_pk_bf16_f32 v142, v119, v123
	v_cvt_pk_bf16_f32 v143, v127, v131
	ds_write_b128 v224, v[140:143] offset:384
	v_lshl_add_u32 v140, s0, 6, v222
	v_ashrrev_i32_e32 v141, 31, v140
	s_lshl_b32 s0, s2, 2
	v_lshlrev_b64 v[140:141], 9, v[140:141]
	s_andn2_b32 s0, s0, 63
	v_lshl_add_u64 v[140:141], s[28:29], 0, v[140:141]
	s_ashr_i32 s1, s0, 31
	v_lshl_add_u64 v[140:141], s[0:1], 1, v[140:141]
	v_mov_b32_e32 v1, v3
	v_lshl_add_u64 v[144:145], v[140:141], 0, v[0:1]
	ds_read_b128 v[140:143], v135
	v_add_co_u32_e32 v146, vcc, s83, v144
	s_waitcnt lgkmcnt(0)
	global_store_dwordx4 v[144:145], v[140:143], off nt
	ds_read_b128 v[140:143], v137
	v_addc_co_u32_e32 v147, vcc, 0, v145, vcc
	s_waitcnt lgkmcnt(0)
	global_store_dwordx4 v[146:147], v[140:143], off offset:-4096 nt
	ds_read_b128 v[140:143], v136
	ds_read_b128 v[136:139], v138
	s_waitcnt lgkmcnt(1)
	global_store_dwordx4 v[146:147], v[140:143], off nt
	s_nop 1
	v_add_co_u32_e32 v140, vcc, 0x3000, v144
	s_nop 1
	v_addc_co_u32_e32 v141, vcc, 0, v145, vcc
	s_waitcnt lgkmcnt(0)
	global_store_dwordx4 v[140:141], v[136:139], off nt
	ds_read_b128 v[136:139], v135 offset:4096
	v_add_co_u32_e32 v140, vcc, s62, v144
	s_nop 1
	v_addc_co_u32_e32 v141, vcc, 0, v145, vcc
	s_waitcnt lgkmcnt(0)
	global_store_dwordx4 v[140:141], v[136:139], off nt
	ds_read_b128 v[134:137], v134
	s_nop 0
	v_add_co_u32_e32 v138, vcc, 0x5000, v144
	s_nop 1
	v_addc_co_u32_e32 v139, vcc, 0, v145, vcc
	s_waitcnt lgkmcnt(0)
	global_store_dwordx4 v[138:139], v[134:137], off nt
	ds_read_b128 v[134:137], v133
	v_add_co_u32_e32 v138, vcc, 0x6000, v144
	s_nop 1
	v_addc_co_u32_e32 v139, vcc, 0, v145, vcc
	s_waitcnt lgkmcnt(0)
	global_store_dwordx4 v[138:139], v[134:137], off nt
	ds_read_b128 v[132:135], v132
	s_nop 0
	v_add_co_u32_e32 v136, vcc, 0x7000, v144
	s_nop 1
	v_addc_co_u32_e32 v137, vcc, 0, v145, vcc
	s_waitcnt lgkmcnt(0)
	global_store_dwordx4 v[136:137], v[132:135], off nt
	s_branch .LBB0_728

.LBB0_761:
	s_sext_i32_i16 s21, s3
	v_mov_b32_e32 v188, 0
	v_mov_b32_e32 v189, 0
	v_mov_b32_e32 v190, 0
	v_mov_b32_e32 v191, 0
	v_mov_b32_e32 v192, 0
	v_mov_b32_e32 v193, 0
	v_mov_b32_e32 v194, 0
	v_mov_b32_e32 v195, 0
	v_mov_b32_e32 v180, 0
	v_mov_b32_e32 v181, 0
	v_mov_b32_e32 v182, 0
	v_mov_b32_e32 v183, 0
	v_mov_b32_e32 v184, 0
	v_mov_b32_e32 v185, 0
	v_mov_b32_e32 v186, 0
	v_mov_b32_e32 v187, 0
	v_mov_b32_e32 v172, 0
	v_mov_b32_e32 v173, 0
	v_mov_b32_e32 v174, 0
	v_mov_b32_e32 v175, 0
	v_mov_b32_e32 v176, 0
	v_mov_b32_e32 v177, 0
	v_mov_b32_e32 v178, 0
	v_mov_b32_e32 v179, 0
	v_mov_b32_e32 v164, 0
	v_mov_b32_e32 v165, 0
	v_mov_b32_e32 v166, 0
	v_mov_b32_e32 v167, 0
	v_mov_b32_e32 v168, 0
	v_mov_b32_e32 v169, 0
	v_mov_b32_e32 v170, 0
	v_mov_b32_e32 v171, 0
	v_mov_b32_e32 v156, 0
	v_mov_b32_e32 v157, 0
	v_mov_b32_e32 v158, 0
	v_mov_b32_e32 v159, 0
	v_mov_b32_e32 v160, 0
	v_mov_b32_e32 v161, 0
	v_mov_b32_e32 v162, 0
	v_mov_b32_e32 v163, 0
	v_mov_b32_e32 v148, 0
	v_mov_b32_e32 v149, 0
	v_mov_b32_e32 v150, 0
	v_mov_b32_e32 v151, 0
	v_mov_b32_e32 v152, 0
	v_mov_b32_e32 v153, 0
	v_mov_b32_e32 v154, 0
	v_mov_b32_e32 v155, 0
	v_mov_b32_e32 v140, 0
	v_mov_b32_e32 v141, 0
	v_mov_b32_e32 v142, 0
	v_mov_b32_e32 v143, 0
	v_mov_b32_e32 v144, 0
	v_mov_b32_e32 v145, 0
	v_mov_b32_e32 v146, 0
	v_mov_b32_e32 v147, 0
	v_mov_b32_e32 v132, 0
	v_mov_b32_e32 v133, 0
	v_mov_b32_e32 v134, 0
	v_mov_b32_e32 v135, 0
	v_mov_b32_e32 v136, 0
	v_mov_b32_e32 v137, 0
	v_mov_b32_e32 v138, 0
	v_mov_b32_e32 v139, 0
	s_and_saveexec_b64 s[0:1], s[4:5]
	s_cbranch_execz .LBB0_763
	v_readlane_b32 s4, v253, 13
	v_readlane_b32 s5, v253, 14
	v_lshl_add_u32 v1, s21, 6, v221
	s_movk_i32 s3, 0x7460
	v_mov_b64_e32 v[132:133], s[4:5]
	v_mad_i64_i32 v[132:133], s[4:5], v1, s3, v[132:133]
	s_ashr_i32 s3, s2, 31
	v_lshl_add_u64 v[132:133], s[2:3], 2, v[132:133]
	v_lshl_add_u64 v[188:189], v[132:133], 0, v[2:3]
	v_add_co_u32_e32 v132, vcc, 0x7000, v188
	s_mov_b32 s2, 0xe000
	s_nop 0
	v_addc_co_u32_e32 v133, vcc, 0, v189, vcc
	v_add_co_u32_e32 v140, vcc, s2, v188
	s_mov_b32 s2, 0x24000
	s_nop 0
	v_addc_co_u32_e32 v141, vcc, 0, v189, vcc
	v_add_co_u32_e32 v142, vcc, 0x15000, v188
	global_load_dwordx4 v[136:139], v[188:189], off nt
	s_nop 0
	global_load_dwordx4 v[132:135], v[132:133], off offset:1120 nt
	v_addc_co_u32_e32 v143, vcc, 0, v189, vcc
	v_add_co_u32_e32 v148, vcc, 0x1d000, v188
	global_load_dwordx4 v[144:147], v[140:141], off offset:2240 nt
	s_nop 0
	global_load_dwordx4 v[140:143], v[142:143], off offset:3360 nt
	v_addc_co_u32_e32 v149, vcc, 0, v189, vcc
	v_add_co_u32_e32 v150, vcc, s2, v188
	s_nop 1
	v_addc_co_u32_e32 v151, vcc, 0, v189, vcc
	v_add_co_u32_e32 v156, vcc, 0x2b000, v188
	global_load_dwordx4 v[152:155], v[148:149], off offset:384 nt
	s_nop 0
	global_load_dwordx4 v[148:151], v[150:151], off offset:1504 nt
	v_addc_co_u32_e32 v157, vcc, 0, v189, vcc
	v_add_co_u32_e32 v158, vcc, 0x32000, v188
	s_nop 1
	v_addc_co_u32_e32 v159, vcc, 0, v189, vcc
	v_add_co_u32_e32 v164, vcc, 0x3a000, v188
	global_load_dwordx4 v[160:163], v[156:157], off offset:2624 nt
	s_nop 0
	global_load_dwordx4 v[156:159], v[158:159], off offset:3744 nt
	v_addc_co_u32_e32 v165, vcc, 0, v189, vcc
	v_add_co_u32_e32 v166, vcc, 0x41000, v188
	s_nop 1
	v_addc_co_u32_e32 v167, vcc, 0, v189, vcc
	v_add_co_u32_e32 v172, vcc, 0x48000, v188
	global_load_dwordx4 v[168:171], v[164:165], off offset:768 nt
	s_nop 0
	global_load_dwordx4 v[164:167], v[166:167], off offset:1888 nt
	v_addc_co_u32_e32 v173, vcc, 0, v189, vcc
	v_add_co_u32_e32 v174, vcc, 0x50000, v188
	s_nop 1
	v_addc_co_u32_e32 v175, vcc, 0, v189, vcc
	v_add_co_u32_e32 v180, vcc, 0x57000, v188
	global_load_dwordx4 v[176:179], v[172:173], off offset:3008 nt
	s_nop 0
	global_load_dwordx4 v[172:175], v[174:175], off offset:32 nt
	v_addc_co_u32_e32 v181, vcc, 0, v189, vcc
	v_add_co_u32_e32 v182, vcc, 0x5e000, v188
	s_nop 1
	v_addc_co_u32_e32 v183, vcc, 0, v189, vcc
	v_add_co_u32_e32 v190, vcc, 0x65000, v188
	global_load_dwordx4 v[184:187], v[180:181], off offset:1152 nt
	s_nop 0
	global_load_dwordx4 v[180:183], v[182:183], off offset:2272 nt
	v_addc_co_u32_e32 v191, vcc, 0, v189, vcc
	v_add_co_u32_e32 v188, vcc, 0x6d000, v188
	s_nop 1
	v_addc_co_u32_e32 v189, vcc, 0, v189, vcc
	global_load_dwordx4 v[192:195], v[190:191], off offset:3392 nt
	s_nop 0
	global_load_dwordx4 v[188:191], v[188:189], off offset:416 nt

.LBB0_786:
	v_mov_b32_e32 v7, 0
	v_mov_b32_e32 v6, 0
	v_mov_b32_e32 v5, 0
	v_mov_b32_e32 v4, 0
	v_mov_b32_e32 v11, 0
	v_mov_b32_e32 v10, 0
	v_mov_b32_e32 v9, 0
	v_mov_b32_e32 v8, 0
	v_mov_b32_e32 v15, 0
	v_mov_b32_e32 v14, 0
	v_mov_b32_e32 v13, 0
	v_mov_b32_e32 v12, 0
	v_mov_b32_e32 v19, 0
	v_mov_b32_e32 v18, 0
	v_mov_b32_e32 v17, 0
	v_mov_b32_e32 v16, 0
	v_mov_b32_e32 v23, 0
	v_mov_b32_e32 v22, 0
	v_mov_b32_e32 v21, 0
	v_mov_b32_e32 v20, 0
	v_mov_b32_e32 v27, 0
	v_mov_b32_e32 v26, 0
	v_mov_b32_e32 v25, 0
	v_mov_b32_e32 v24, 0
	v_mov_b32_e32 v31, 0
	v_mov_b32_e32 v30, 0
	v_mov_b32_e32 v29, 0
	v_mov_b32_e32 v28, 0
	v_mov_b32_e32 v35, 0
	v_mov_b32_e32 v34, 0
	v_mov_b32_e32 v33, 0
	v_mov_b32_e32 v32, 0
	v_mov_b32_e32 v39, 0
	v_mov_b32_e32 v38, 0
	v_mov_b32_e32 v37, 0
	v_mov_b32_e32 v36, 0
	v_mov_b32_e32 v47, 0
	v_mov_b32_e32 v46, 0
	v_mov_b32_e32 v45, 0
	v_mov_b32_e32 v44, 0
	v_mov_b32_e32 v55, 0
	v_mov_b32_e32 v54, 0
	v_mov_b32_e32 v53, 0
	v_mov_b32_e32 v52, 0
	v_mov_b32_e32 v59, 0
	v_mov_b32_e32 v58, 0
	v_mov_b32_e32 v57, 0
	v_mov_b32_e32 v56, 0
	v_mov_b32_e32 v71, 0
	v_mov_b32_e32 v70, 0
	v_mov_b32_e32 v69, 0
	v_mov_b32_e32 v68, 0
	v_mov_b32_e32 v75, 0
	v_mov_b32_e32 v74, 0
	v_mov_b32_e32 v73, 0
	v_mov_b32_e32 v72, 0
	v_mov_b32_e32 v87, 0
	v_mov_b32_e32 v86, 0
	v_mov_b32_e32 v85, 0
	v_mov_b32_e32 v84, 0
	v_mov_b32_e32 v91, 0
	v_mov_b32_e32 v90, 0
	v_mov_b32_e32 v89, 0
	v_mov_b32_e32 v88, 0
	s_and_saveexec_b64 s[0:1], s[4:5]
	s_cbranch_execz .LBB0_788
	v_readlane_b32 s4, v253, 13
	s_sext_i32_i16 s3, s3
	v_readlane_b32 s5, v253, 14
	v_lshl_add_u32 v1, s3, 6, v221
	s_movk_i32 s3, 0x7460
	v_mov_b64_e32 v[4:5], s[4:5]
	v_mad_i64_i32 v[4:5], s[4:5], v1, s3, v[4:5]
	s_ashr_i32 s3, s2, 31
	v_lshl_add_u64 v[4:5], s[2:3], 2, v[4:5]
	v_lshl_add_u64 v[84:85], v[4:5], 0, v[2:3]
	v_add_co_u32_e32 v8, vcc, 0x7000, v84
	s_mov_b32 s2, 0xe000
	s_nop 0
	v_addc_co_u32_e32 v9, vcc, 0, v85, vcc
	v_add_co_u32_e32 v12, vcc, s2, v84
	s_mov_b32 s2, 0x24000
	s_nop 0
	v_addc_co_u32_e32 v13, vcc, 0, v85, vcc
	v_add_co_u32_e32 v16, vcc, 0x15000, v84
	global_load_dwordx4 v[4:7], v[84:85], off nt
	s_nop 0
	global_load_dwordx4 v[8:11], v[8:9], off offset:1120 nt
	v_addc_co_u32_e32 v17, vcc, 0, v85, vcc
	v_add_co_u32_e32 v20, vcc, 0x1d000, v84
	global_load_dwordx4 v[12:15], v[12:13], off offset:2240 nt
	s_nop 0
	global_load_dwordx4 v[16:19], v[16:17], off offset:3360 nt
	v_addc_co_u32_e32 v21, vcc, 0, v85, vcc
	v_add_co_u32_e32 v24, vcc, s2, v84
	s_nop 1
	v_addc_co_u32_e32 v25, vcc, 0, v85, vcc
	v_add_co_u32_e32 v28, vcc, 0x2b000, v84
	global_load_dwordx4 v[20:23], v[20:21], off offset:384 nt
	s_nop 0
	global_load_dwordx4 v[24:27], v[24:25], off offset:1504 nt
	v_addc_co_u32_e32 v29, vcc, 0, v85, vcc
	v_add_co_u32_e32 v32, vcc, 0x32000, v84
	s_nop 1
	v_addc_co_u32_e32 v33, vcc, 0, v85, vcc
	v_add_co_u32_e32 v36, vcc, 0x3a000, v84
	global_load_dwordx4 v[28:31], v[28:29], off offset:2624 nt
	s_nop 0
	global_load_dwordx4 v[32:35], v[32:33], off offset:3744 nt
	v_addc_co_u32_e32 v37, vcc, 0, v85, vcc
	v_add_co_u32_e32 v44, vcc, 0x41000, v84
	s_nop 1
	v_addc_co_u32_e32 v45, vcc, 0, v85, vcc
	v_add_co_u32_e32 v52, vcc, 0x48000, v84
	global_load_dwordx4 v[36:39], v[36:37], off offset:768 nt
	s_nop 0
	global_load_dwordx4 v[44:47], v[44:45], off offset:1888 nt
	v_addc_co_u32_e32 v53, vcc, 0, v85, vcc
	v_add_co_u32_e32 v56, vcc, 0x50000, v84
	s_nop 1
	v_addc_co_u32_e32 v57, vcc, 0, v85, vcc
	v_add_co_u32_e32 v68, vcc, 0x57000, v84
	global_load_dwordx4 v[52:55], v[52:53], off offset:3008 nt
	s_nop 0
	global_load_dwordx4 v[56:59], v[56:57], off offset:32 nt
	v_addc_co_u32_e32 v69, vcc, 0, v85, vcc
	v_add_co_u32_e32 v72, vcc, 0x5e000, v84
	s_nop 1
	v_addc_co_u32_e32 v73, vcc, 0, v85, vcc
	v_add_co_u32_e32 v86, vcc, 0x65000, v84
	global_load_dwordx4 v[68:71], v[68:69], off offset:1152 nt
	s_nop 0
	global_load_dwordx4 v[72:75], v[72:73], off offset:2272 nt
	v_addc_co_u32_e32 v87, vcc, 0, v85, vcc
	v_add_co_u32_e32 v88, vcc, 0x6d000, v84
	s_nop 1
	v_addc_co_u32_e32 v89, vcc, 0, v85, vcc
	global_load_dwordx4 v[84:87], v[86:87], off offset:3392 nt
	s_nop 0
	global_load_dwordx4 v[88:91], v[88:89], off offset:416 nt

.LBB0_812:
	v_mov_b32_e32 v43, 0
	v_mov_b32_e32 v42, 0
	v_mov_b32_e32 v41, 0
	v_mov_b32_e32 v40, 0
	v_mov_b32_e32 v51, 0
	v_mov_b32_e32 v50, 0
	v_mov_b32_e32 v49, 0
	v_mov_b32_e32 v48, 0
	v_mov_b32_e32 v63, 0
	v_mov_b32_e32 v62, 0
	v_mov_b32_e32 v61, 0
	v_mov_b32_e32 v60, 0
	v_mov_b32_e32 v67, 0
	v_mov_b32_e32 v66, 0
	v_mov_b32_e32 v65, 0
	v_mov_b32_e32 v64, 0
	v_mov_b32_e32 v79, 0
	v_mov_b32_e32 v78, 0
	v_mov_b32_e32 v77, 0
	v_mov_b32_e32 v76, 0
	v_mov_b32_e32 v83, 0
	v_mov_b32_e32 v82, 0
	v_mov_b32_e32 v81, 0
	v_mov_b32_e32 v80, 0
	v_mov_b32_e32 v95, 0
	v_mov_b32_e32 v94, 0
	v_mov_b32_e32 v93, 0
	v_mov_b32_e32 v92, 0
	v_mov_b32_e32 v99, 0
	v_mov_b32_e32 v98, 0
	v_mov_b32_e32 v97, 0
	v_mov_b32_e32 v96, 0
	v_mov_b32_e32 v103, 0
	v_mov_b32_e32 v102, 0
	v_mov_b32_e32 v101, 0
	v_mov_b32_e32 v100, 0
	v_mov_b32_e32 v107, 0
	v_mov_b32_e32 v106, 0
	v_mov_b32_e32 v105, 0
	v_mov_b32_e32 v104, 0
	v_mov_b32_e32 v111, 0
	v_mov_b32_e32 v110, 0
	v_mov_b32_e32 v109, 0
	v_mov_b32_e32 v108, 0
	v_mov_b32_e32 v115, 0
	v_mov_b32_e32 v114, 0
	v_mov_b32_e32 v113, 0
	v_mov_b32_e32 v112, 0
	v_mov_b32_e32 v119, 0
	v_mov_b32_e32 v118, 0
	v_mov_b32_e32 v117, 0
	v_mov_b32_e32 v116, 0
	v_mov_b32_e32 v123, 0
	v_mov_b32_e32 v122, 0
	v_mov_b32_e32 v121, 0
	v_mov_b32_e32 v120, 0
	v_mov_b32_e32 v127, 0
	v_mov_b32_e32 v126, 0
	v_mov_b32_e32 v125, 0
	v_mov_b32_e32 v124, 0
	v_mov_b32_e32 v131, 0
	v_mov_b32_e32 v130, 0
	v_mov_b32_e32 v129, 0
	v_mov_b32_e32 v128, 0
	s_and_saveexec_b64 s[2:3], s[6:7]
	s_cbranch_execz .LBB0_814
	v_readlane_b32 s6, v253, 13
	s_sext_i32_i16 s5, s5
	v_readlane_b32 s7, v253, 14
	v_lshl_add_u32 v1, s5, 6, v221
	s_movk_i32 s5, 0x7460
	v_mov_b64_e32 v[40:41], s[6:7]
	v_mad_i64_i32 v[40:41], s[6:7], v1, s5, v[40:41]
	s_ashr_i32 s5, s4, 31
	v_lshl_add_u64 v[40:41], s[4:5], 2, v[40:41]
	v_lshl_add_u64 v[124:125], v[40:41], 0, v[2:3]
	v_add_co_u32_e32 v48, vcc, 0x7000, v124
	s_mov_b32 s4, 0xe000
	s_nop 0
	v_addc_co_u32_e32 v49, vcc, 0, v125, vcc
	v_add_co_u32_e32 v60, vcc, s4, v124
	s_mov_b32 s4, 0x24000
	s_nop 0
	v_addc_co_u32_e32 v61, vcc, 0, v125, vcc
	v_add_co_u32_e32 v64, vcc, 0x15000, v124
	global_load_dwordx4 v[40:43], v[124:125], off nt
	s_nop 0
	global_load_dwordx4 v[48:51], v[48:49], off offset:1120 nt
	v_addc_co_u32_e32 v65, vcc, 0, v125, vcc
	v_add_co_u32_e32 v76, vcc, 0x1d000, v124
	global_load_dwordx4 v[60:63], v[60:61], off offset:2240 nt
	s_nop 0
	global_load_dwordx4 v[64:67], v[64:65], off offset:3360 nt
	v_addc_co_u32_e32 v77, vcc, 0, v125, vcc
	v_add_co_u32_e32 v80, vcc, s4, v124
	s_nop 1
	v_addc_co_u32_e32 v81, vcc, 0, v125, vcc
	v_add_co_u32_e32 v92, vcc, 0x2b000, v124
	global_load_dwordx4 v[76:79], v[76:77], off offset:384 nt
	s_nop 0
	global_load_dwordx4 v[80:83], v[80:81], off offset:1504 nt
	v_addc_co_u32_e32 v93, vcc, 0, v125, vcc
	v_add_co_u32_e32 v96, vcc, 0x32000, v124
	s_nop 1
	v_addc_co_u32_e32 v97, vcc, 0, v125, vcc
	v_add_co_u32_e32 v100, vcc, 0x3a000, v124
	global_load_dwordx4 v[92:95], v[92:93], off offset:2624 nt
	s_nop 0
	global_load_dwordx4 v[96:99], v[96:97], off offset:3744 nt
	v_addc_co_u32_e32 v101, vcc, 0, v125, vcc
	v_add_co_u32_e32 v104, vcc, 0x41000, v124
	s_nop 1
	v_addc_co_u32_e32 v105, vcc, 0, v125, vcc
	v_add_co_u32_e32 v108, vcc, 0x48000, v124
	global_load_dwordx4 v[100:103], v[100:101], off offset:768 nt
	s_nop 0
	global_load_dwordx4 v[104:107], v[104:105], off offset:1888 nt
	v_addc_co_u32_e32 v109, vcc, 0, v125, vcc
	v_add_co_u32_e32 v112, vcc, 0x50000, v124
	s_nop 1
	v_addc_co_u32_e32 v113, vcc, 0, v125, vcc
	v_add_co_u32_e32 v116, vcc, 0x57000, v124
	global_load_dwordx4 v[108:111], v[108:109], off offset:3008 nt
	s_nop 0
	global_load_dwordx4 v[112:115], v[112:113], off offset:32 nt
	v_addc_co_u32_e32 v117, vcc, 0, v125, vcc
	v_add_co_u32_e32 v120, vcc, 0x5e000, v124
	s_nop 1
	v_addc_co_u32_e32 v121, vcc, 0, v125, vcc
	v_add_co_u32_e32 v126, vcc, 0x65000, v124
	global_load_dwordx4 v[116:119], v[116:117], off offset:1152 nt
	s_nop 0
	global_load_dwordx4 v[120:123], v[120:121], off offset:2272 nt
	v_addc_co_u32_e32 v127, vcc, 0, v125, vcc
	v_add_co_u32_e32 v128, vcc, 0x6d000, v124
	s_nop 1
	v_addc_co_u32_e32 v129, vcc, 0, v125, vcc
	global_load_dwordx4 v[124:127], v[126:127], off offset:3392 nt
	s_nop 0
	global_load_dwordx4 v[128:131], v[128:129], off offset:416 nt

.LBB0_815:
	s_waitcnt vmcnt(14)
	v_cvt_pk_bf16_f32 v240, v136, v132
	s_waitcnt vmcnt(12)
	v_cvt_pk_bf16_f32 v241, v144, v140
	s_waitcnt vmcnt(10)
	v_cvt_pk_bf16_f32 v242, v152, v148
	s_waitcnt vmcnt(8)
	v_cvt_pk_bf16_f32 v243, v160, v156
	ds_write_b128 v223, v[240:243]
	s_waitcnt vmcnt(6)
	v_cvt_pk_bf16_f32 v240, v168, v164
	s_waitcnt vmcnt(4)
	v_cvt_pk_bf16_f32 v241, v176, v172
	s_waitcnt vmcnt(2)
	v_cvt_pk_bf16_f32 v242, v184, v180
	s_waitcnt vmcnt(0)
	v_cvt_pk_bf16_f32 v243, v192, v188
	ds_write_b128 v224, v[240:243]
	v_cvt_pk_bf16_f32 v240, v137, v133
	v_cvt_pk_bf16_f32 v241, v145, v141
	v_cvt_pk_bf16_f32 v242, v153, v149
	v_cvt_pk_bf16_f32 v243, v161, v157
	ds_write_b128 v223, v[240:243] offset:128
	v_cvt_pk_bf16_f32 v240, v169, v165
	v_cvt_pk_bf16_f32 v241, v177, v173
	v_cvt_pk_bf16_f32 v242, v185, v181
	v_cvt_pk_bf16_f32 v243, v193, v189
	ds_write_b128 v224, v[240:243] offset:128
	v_cvt_pk_bf16_f32 v240, v138, v134
	v_cvt_pk_bf16_f32 v241, v146, v142
	v_cvt_pk_bf16_f32 v242, v154, v150
	v_cvt_pk_bf16_f32 v243, v162, v158
	ds_write_b128 v223, v[240:243] offset:256
	v_cvt_pk_bf16_f32 v240, v170, v166
	v_cvt_pk_bf16_f32 v241, v178, v174
	v_cvt_pk_bf16_f32 v242, v186, v182
	v_cvt_pk_bf16_f32 v243, v194, v190
	ds_write_b128 v224, v[240:243] offset:256
	v_cvt_pk_bf16_f32 v132, v139, v135
	v_cvt_pk_bf16_f32 v133, v147, v143
	v_cvt_pk_bf16_f32 v134, v155, v151
	v_cvt_pk_bf16_f32 v135, v163, v159
	ds_write_b128 v223, v[132:135] offset:384
	v_cvt_pk_bf16_f32 v132, v171, v167
	v_cvt_pk_bf16_f32 v133, v179, v175
	v_cvt_pk_bf16_f32 v134, v187, v183
	v_cvt_pk_bf16_f32 v135, v195, v191
	ds_write_b128 v224, v[132:135] offset:384
	v_add_u32_e32 v132, s12, v222
	v_add_u32_e32 v135, v225, v226
	v_ashrrev_i32_e32 v133, 31, v132
	ds_read_b128 v[136:139], v135
	v_lshlrev_b64 v[132:133], 11, v[132:133]
	s_lshl_b32 s2, s21, 6
	v_lshl_add_u64 v[132:133], s[28:29], 0, v[132:133]
	s_ashr_i32 s3, s2, 31
	v_lshl_add_u64 v[132:133], s[2:3], 1, v[132:133]
	v_mov_b32_e32 v1, v3
	v_lshl_add_u64 v[152:153], v[132:133], 0, v[0:1]
	s_waitcnt lgkmcnt(0)
	global_store_dwordx4 v[152:153], v[136:139], off nt
	v_add_co_u32_e32 v132, vcc, s62, v152
	s_nop 0
	v_add_u32_e32 v137, v227, v228
	ds_read_b128 v[144:147], v137
	v_add_u32_e32 v136, v229, v230
	ds_read_b128 v[148:151], v136
	v_addc_co_u32_e32 v133, vcc, 0, v153, vcc
	v_add_u32_e32 v138, v231, v232
	s_waitcnt lgkmcnt(1)
	global_store_dwordx4 v[132:133], v[144:147], off nt
	ds_read_b128 v[144:147], v138
	v_add_co_u32_e32 v132, vcc, s88, v152
	ds_read_b128 v[140:143], v135 offset:4096
	s_nop 0
	v_addc_co_u32_e32 v133, vcc, 0, v153, vcc
	s_waitcnt lgkmcnt(2)
	global_store_dwordx4 v[132:133], v[148:151], off nt
	v_add_co_u32_e32 v132, vcc, s66, v152
	v_add_u32_e32 v134, v233, v234
	s_nop 0
	v_addc_co_u32_e32 v133, vcc, 0, v153, vcc
	ds_read_b128 v[148:151], v134
	s_waitcnt lgkmcnt(2)
	global_store_dwordx4 v[132:133], v[144:147], off nt
	v_add_co_u32_e32 v132, vcc, s82, v152
	s_mov_b32 s2, 0x14000
	s_nop 0
	v_addc_co_u32_e32 v133, vcc, 0, v153, vcc
	s_waitcnt lgkmcnt(1)
	global_store_dwordx4 v[132:133], v[140:143], off nt
	v_add_co_u32_e32 v132, vcc, s2, v152
	s_nop 1
	v_addc_co_u32_e32 v133, vcc, 0, v153, vcc
	s_waitcnt lgkmcnt(0)
	global_store_dwordx4 v[132:133], v[148:151], off nt
	v_add_u32_e32 v133, v235, v236
	ds_read_b128 v[140:143], v133
	v_add_u32_e32 v132, v237, v238
	v_add_co_u32_e32 v148, vcc, 0x18000, v152
	ds_read_b128 v[144:147], v132
	s_nop 0
	v_addc_co_u32_e32 v149, vcc, 0, v153, vcc
	s_waitcnt lgkmcnt(1)
	global_store_dwordx4 v[148:149], v[140:143], off nt
	s_nop 1
	v_add_co_u32_e32 v140, vcc, 0x1c000, v152
	s_nop 1
	v_addc_co_u32_e32 v141, vcc, 0, v153, vcc
	s_andn2_b64 vcc, exec, s[36:37]
	s_waitcnt lgkmcnt(0)
	global_store_dwordx4 v[140:141], v[144:147], off nt
	s_cbranch_vccz .LBB0_817
	s_andn2_b64 vcc, exec, s[0:1]
	s_cbranch_vccnz .LBB0_739
	s_branch .LBB0_818
.LBB0_817:
	s_add_i32 s23, s23, s22
	s_lshr_b32 s2, s23, 31
	s_ashr_i32 s3, s23, 10
	s_add_i32 s2, s3, s2
	s_mulk_i32 s2, 0x780
	s_sub_i32 s2, s22, s2
	s_sext_i32_i16 s3, s2
	s_mulk_i32 s3, 0x8889
	s_lshr_b32 s3, s3, 16
	v_cvt_pk_bf16_f32 v140, v4, v8
	s_add_i32 s3, s3, s2
	v_cvt_pk_bf16_f32 v141, v12, v16
	v_cvt_pk_bf16_f32 v142, v20, v24
	v_cvt_pk_bf16_f32 v143, v28, v32
	ds_write_b128 v223, v[140:143]
	v_cvt_pk_bf16_f32 v140, v36, v44
	s_sext_i32_i16 s4, s3
	v_cvt_pk_bf16_f32 v141, v52, v56
	v_cvt_pk_bf16_f32 v142, v68, v72
	v_cvt_pk_bf16_f32 v143, v84, v88
	ds_write_b128 v224, v[140:143]
	v_cvt_pk_bf16_f32 v140, v5, v9
	s_ashr_i32 s4, s4, 6
	s_bfe_u32 s3, s3, 0x1000f
	v_cvt_pk_bf16_f32 v141, v13, v17
	v_cvt_pk_bf16_f32 v142, v21, v25
	v_cvt_pk_bf16_f32 v143, v29, v33
	ds_write_b128 v223, v[140:143] offset:128
	v_cvt_pk_bf16_f32 v140, v37, v45
	s_add_i32 s3, s4, s3
	v_cvt_pk_bf16_f32 v141, v53, v57
	v_cvt_pk_bf16_f32 v142, v69, v73
	v_cvt_pk_bf16_f32 v143, v85, v89
	ds_write_b128 v224, v[140:143] offset:128
	v_cvt_pk_bf16_f32 v140, v6, v10
	s_mul_i32 s4, s3, 0x78
	v_cvt_pk_bf16_f32 v141, v14, v18
	v_cvt_pk_bf16_f32 v142, v22, v26
	v_cvt_pk_bf16_f32 v143, v30, v34
	ds_write_b128 v223, v[140:143] offset:256
	v_cvt_pk_bf16_f32 v140, v38, v46
	s_sub_i32 s2, s2, s4
	v_cvt_pk_bf16_f32 v141, v54, v58
	v_cvt_pk_bf16_f32 v142, v70, v74
	v_cvt_pk_bf16_f32 v143, v86, v90
	ds_write_b128 v224, v[140:143] offset:256
	v_cvt_pk_bf16_f32 v140, v7, v11
	v_cvt_pk_bf16_f32 v141, v15, v19
	v_cvt_pk_bf16_f32 v142, v23, v27
	v_cvt_pk_bf16_f32 v143, v31, v35
	ds_write_b128 v223, v[140:143] offset:384
	v_cvt_pk_bf16_f32 v140, v39, v47
	s_sext_i32_i16 s2, s2
	v_cvt_pk_bf16_f32 v141, v55, v59
	v_cvt_pk_bf16_f32 v142, v71, v75
	v_cvt_pk_bf16_f32 v143, v87, v91
	ds_write_b128 v224, v[140:143] offset:384
	v_lshl_add_u32 v140, s2, 6, v222
	s_sext_i32_i16 s3, s3
	v_ashrrev_i32_e32 v141, 31, v140
	v_lshlrev_b64 v[140:141], 11, v[140:141]
	s_lshl_b32 s2, s3, 6
	v_lshl_add_u64 v[140:141], s[28:29], 0, v[140:141]
	s_ashr_i32 s3, s2, 31
	v_lshl_add_u64 v[140:141], s[2:3], 1, v[140:141]
	v_lshl_add_u64 v[144:145], v[140:141], 0, v[0:1]
	ds_read_b128 v[140:143], v135
	v_add_co_u32_e32 v146, vcc, s62, v144
	s_waitcnt lgkmcnt(0)
	global_store_dwordx4 v[144:145], v[140:143], off nt
	ds_read_b128 v[140:143], v137
	v_addc_co_u32_e32 v147, vcc, 0, v145, vcc
	s_waitcnt lgkmcnt(0)
	global_store_dwordx4 v[146:147], v[140:143], off nt
	ds_read_b128 v[140:143], v136
	v_add_co_u32_e32 v146, vcc, 0x8000, v144
	s_nop 1
	v_addc_co_u32_e32 v147, vcc, 0, v145, vcc
	s_waitcnt lgkmcnt(0)
	global_store_dwordx4 v[146:147], v[140:143], off nt
	ds_read_b128 v[140:143], v138
	v_add_co_u32_e32 v146, vcc, 0xc000, v144
	s_nop 1
	v_addc_co_u32_e32 v147, vcc, 0, v145, vcc
	s_waitcnt lgkmcnt(0)
	global_store_dwordx4 v[146:147], v[140:143], off nt
	ds_read_b128 v[140:143], v135 offset:4096
	v_add_co_u32_e32 v146, vcc, s82, v144
	s_nop 1
	v_addc_co_u32_e32 v147, vcc, 0, v145, vcc
	s_waitcnt lgkmcnt(0)
	global_store_dwordx4 v[146:147], v[140:143], off nt
	ds_read_b128 v[140:143], v134
	v_add_co_u32_e32 v146, vcc, 0x14000, v144
	s_nop 1
	v_addc_co_u32_e32 v147, vcc, 0, v145, vcc
	s_waitcnt lgkmcnt(0)
	global_store_dwordx4 v[146:147], v[140:143], off nt
	ds_read_b128 v[140:143], v133
	v_add_co_u32_e32 v146, vcc, 0x18000, v144
	s_nop 1
	v_addc_co_u32_e32 v147, vcc, 0, v145, vcc
	s_waitcnt lgkmcnt(0)
	global_store_dwordx4 v[146:147], v[140:143], off nt
	ds_read_b128 v[140:143], v132
	v_add_co_u32_e32 v144, vcc, 0x1c000, v144
	s_nop 1
	v_addc_co_u32_e32 v145, vcc, 0, v145, vcc
	s_waitcnt lgkmcnt(0)
	global_store_dwordx4 v[144:145], v[140:143], off nt
	s_andn2_b64 vcc, exec, s[0:1]
	s_cbranch_vccnz .LBB0_739
.LBB0_818:
	s_add_i32 s31, s31, s30
	s_lshr_b32 s0, s31, 31
	s_ashr_i32 s1, s31, 10
	s_add_i32 s0, s1, s0
	s_mulk_i32 s0, 0x780
	s_sub_i32 s0, s30, s0
	s_sext_i32_i16 s1, s0
	s_mulk_i32 s1, 0x8889
	s_lshr_b32 s1, s1, 16
	v_cvt_pk_bf16_f32 v140, v40, v48
	s_add_i32 s1, s1, s0
	v_cvt_pk_bf16_f32 v141, v60, v64
	v_cvt_pk_bf16_f32 v142, v76, v80
	v_cvt_pk_bf16_f32 v143, v92, v96
	ds_write_b128 v223, v[140:143]
	v_cvt_pk_bf16_f32 v140, v100, v104
	s_sext_i32_i16 s2, s1
	v_cvt_pk_bf16_f32 v141, v108, v112
	v_cvt_pk_bf16_f32 v142, v116, v120
	v_cvt_pk_bf16_f32 v143, v124, v128
	ds_write_b128 v224, v[140:143]
	v_cvt_pk_bf16_f32 v140, v41, v49
	s_ashr_i32 s2, s2, 6
	s_bfe_u32 s1, s1, 0x1000f
	v_cvt_pk_bf16_f32 v141, v61, v65
	v_cvt_pk_bf16_f32 v142, v77, v81
	v_cvt_pk_bf16_f32 v143, v93, v97
	ds_write_b128 v223, v[140:143] offset:128
	v_cvt_pk_bf16_f32 v140, v101, v105
	s_add_i32 s1, s2, s1
	v_cvt_pk_bf16_f32 v141, v109, v113
	v_cvt_pk_bf16_f32 v142, v117, v121
	v_cvt_pk_bf16_f32 v143, v125, v129
	ds_write_b128 v224, v[140:143] offset:128
	v_cvt_pk_bf16_f32 v140, v42, v50
	s_mul_i32 s2, s1, 0x78
	v_cvt_pk_bf16_f32 v141, v62, v66
	v_cvt_pk_bf16_f32 v142, v78, v82
	v_cvt_pk_bf16_f32 v143, v94, v98
	ds_write_b128 v223, v[140:143] offset:256
	v_cvt_pk_bf16_f32 v140, v102, v106
	s_sub_i32 s0, s0, s2
	v_cvt_pk_bf16_f32 v141, v110, v114
	v_cvt_pk_bf16_f32 v142, v118, v122
	v_cvt_pk_bf16_f32 v143, v126, v130
	ds_write_b128 v224, v[140:143] offset:256
	v_cvt_pk_bf16_f32 v140, v43, v51
	v_cvt_pk_bf16_f32 v141, v63, v67
	v_cvt_pk_bf16_f32 v142, v79, v83
	v_cvt_pk_bf16_f32 v143, v95, v99
	ds_write_b128 v223, v[140:143] offset:384
	v_cvt_pk_bf16_f32 v140, v103, v107
	s_sext_i32_i16 s0, s0
	v_cvt_pk_bf16_f32 v141, v111, v115
	v_cvt_pk_bf16_f32 v142, v119, v123
	v_cvt_pk_bf16_f32 v143, v127, v131
	ds_write_b128 v224, v[140:143] offset:384
	v_lshl_add_u32 v140, s0, 6, v222
	s_sext_i32_i16 s1, s1
	v_ashrrev_i32_e32 v141, 31, v140
	v_lshlrev_b64 v[140:141], 11, v[140:141]
	s_lshl_b32 s0, s1, 6
	v_lshl_add_u64 v[140:141], s[28:29], 0, v[140:141]
	s_ashr_i32 s1, s0, 31
	v_lshl_add_u64 v[140:141], s[0:1], 1, v[140:141]
	v_mov_b32_e32 v1, v3
	v_lshl_add_u64 v[144:145], v[140:141], 0, v[0:1]
	ds_read_b128 v[140:143], v135
	v_add_co_u32_e32 v146, vcc, s62, v144
	s_waitcnt lgkmcnt(0)
	global_store_dwordx4 v[144:145], v[140:143], off nt
	ds_read_b128 v[140:143], v137
	v_addc_co_u32_e32 v147, vcc, 0, v145, vcc
	s_waitcnt lgkmcnt(0)
	global_store_dwordx4 v[146:147], v[140:143], off nt
	ds_read_b128 v[140:143], v136
	v_add_co_u32_e32 v136, vcc, 0x8000, v144
	s_nop 1
	v_addc_co_u32_e32 v137, vcc, 0, v145, vcc
	s_waitcnt lgkmcnt(0)
	global_store_dwordx4 v[136:137], v[140:143], off nt
	ds_read_b128 v[136:139], v138
	s_nop 0
	v_add_co_u32_e32 v140, vcc, 0xc000, v144
	s_nop 1
	v_addc_co_u32_e32 v141, vcc, 0, v145, vcc
	s_waitcnt lgkmcnt(0)
	global_store_dwordx4 v[140:141], v[136:139], off nt
	ds_read_b128 v[136:139], v135 offset:4096
	v_add_co_u32_e32 v140, vcc, s82, v144
	s_nop 1
	v_addc_co_u32_e32 v141, vcc, 0, v145, vcc
	s_waitcnt lgkmcnt(0)
	global_store_dwordx4 v[140:141], v[136:139], off nt
	ds_read_b128 v[134:137], v134
	s_nop 0
	v_add_co_u32_e32 v138, vcc, 0x14000, v144
	s_nop 1
	v_addc_co_u32_e32 v139, vcc, 0, v145, vcc
	s_waitcnt lgkmcnt(0)
	global_store_dwordx4 v[138:139], v[134:137], off nt
	ds_read_b128 v[134:137], v133
	v_add_co_u32_e32 v138, vcc, 0x18000, v144
	s_nop 1
	v_addc_co_u32_e32 v139, vcc, 0, v145, vcc
	s_waitcnt lgkmcnt(0)
	global_store_dwordx4 v[138:139], v[134:137], off nt
	ds_read_b128 v[132:135], v132
	s_nop 0
	v_add_co_u32_e32 v136, vcc, 0x1c000, v144
	s_nop 1
	v_addc_co_u32_e32 v137, vcc, 0, v145, vcc
	s_waitcnt lgkmcnt(0)
	global_store_dwordx4 v[136:137], v[132:135], off nt
	s_branch .LBB0_739

.LBB0_2220:
	s_lshl_b32 s4, s0, 3
	s_add_i32 s8, s4, s90
	s_lshl_b32 s0, s0, 7
	s_and_b32 s4, s4, 0xf8
	s_and_b32 s0, s0, 0xfffff000
	s_add_i32 s4, s4, s90
	s_add_i32 s9, s4, s0
	s_add_i32 s13, s0, 0x1000
	s_cmpk_eq_i32 s1, 0x100
	s_cselect_b64 s[4:5], -1, 0
	v_readlane_b32 s20, v252, 52
	s_and_b64 s[6:7], s[4:5], exec
	v_readlane_b32 s22, v252, 54
	v_readlane_b32 s23, v252, 55
	s_cselect_b32 s0, s9, s8
	s_cselect_b32 s13, s13, 0x8000
	s_mov_b64 s[2:3], s[22:23]
	s_cmp_ge_i32 s0, s13
	v_readlane_b32 s21, v252, 53
	s_cbranch_scc1 .LBB0_2227
	s_lshl_b32 s1, s1, 3
	v_readlane_b32 s8, v254, 43
	s_add_u32 s6, s2, 0x3b982000
	v_readlane_b32 s9, v254, 44
	s_addc_u32 s7, s3, 0
	s_lshl_b32 s8, s8, 10
	s_mov_b32 s9, s11
	v_readlane_b32 s36, v252, 20
	s_lshl_b64 s[8:9], s[8:9], 2
	v_readlane_b32 s38, v252, 22
	v_readlane_b32 s39, v252, 23
	s_add_u32 s14, s38, s8
	v_readlane_b32 s40, v252, 24
	s_addc_u32 s15, s39, s9
	v_readlane_b32 s41, v252, 25
	s_add_u32 s8, s40, s8
	s_addc_u32 s9, s41, s9
	v_ashrrev_i32_e32 v5, 31, v4
	v_lshlrev_b64 v[38:39], 3, v[4:5]
	s_cmp_lg_u64 s[2:3], 0
	v_lshlrev_b64 v[0:1], 4, v[4:5]
	v_lshl_add_u64 v[6:7], s[2:3], 0, v[38:39]
	s_cselect_b64 s[2:3], -1, 0
	s_and_b64 s[4:5], s[4:5], exec
	v_lshl_add_u64 v[32:33], s[8:9], 0, v[0:1]
	s_mov_b64 s[8:9], 0x6f1c8000
	s_cselect_b32 s4, 0x100, s1
	s_ashr_i32 s1, s0, 31
	v_lshl_add_u64 v[28:29], s[14:15], 0, v[0:1]
	v_lshl_add_u64 v[0:1], s[6:7], 0, v[38:39]
	v_lshl_add_u64 v[36:37], v[6:7], 0, s[8:9]
	s_lshl_b64 s[8:9], s[0:1], 11
	v_lshlrev_b32_e32 v4, 2, v4
	v_lshl_add_u64 v[40:41], v[0:1], 0, s[8:9]
	v_xor_b32_e32 v2, 4, v4
	v_xor_b32_e32 v72, 8, v4
	v_xor_b32_e32 v73, 16, v4
	v_xor_b32_e32 v74, 32, v4
	v_xor_b32_e32 v75, 64, v4
	v_xor_b32_e32 v76, 0x80, v4
	global_load_dwordx4 v[4:7], v[28:29], off
	global_load_dwordx4 v[8:11], v[32:33], off
	global_load_dwordx4 v[12:15], v[28:29], off offset:1024
	global_load_dwordx4 v[16:19], v[32:33], off offset:1024
	global_load_dwordx4 v[20:23], v[28:29], off offset:2048
	global_load_dwordx4 v[24:27], v[32:33], off offset:2048
	s_nop 0
	global_load_dwordx4 v[28:31], v[28:29], off offset:3072
	s_nop 0
	global_load_dwordx4 v[32:35], v[32:33], off offset:3072
	v_lshl_add_u64 v[42:43], v[36:37], 0, s[8:9]
	global_load_dwordx2 v[66:67], v[40:41], off nt
	global_load_dwordx2 v[70:71], v[42:43], off nt
	global_load_dwordx2 v[60:61], v[40:41], off offset:512 nt
	global_load_dwordx2 v[68:69], v[42:43], off offset:512 nt
	global_load_dwordx2 v[58:59], v[40:41], off offset:1024 nt
	global_load_dwordx2 v[64:65], v[42:43], off offset:1024 nt
	global_load_dwordx2 v[56:57], v[40:41], off offset:1536 nt
	global_load_dwordx2 v[62:63], v[42:43], off offset:1536 nt
	s_add_u32 s6, s6, s8
	s_addc_u32 s7, s7, s9
	s_ashr_i32 s5, s4, 31
	v_lshl_add_u64 v[38:39], s[6:7], 0, v[38:39]
	s_lshl_b64 s[6:7], s[4:5], 11
	v_readlane_b32 s37, v252, 21
	v_readlane_b32 s42, v252, 26
	v_readlane_b32 s43, v252, 27
	v_readlane_b32 s44, v252, 28
	v_readlane_b32 s45, v252, 29
	v_readlane_b32 s46, v252, 30
	v_readlane_b32 s47, v252, 31
	v_readlane_b32 s48, v252, 32
	v_readlane_b32 s49, v252, 33
	v_readlane_b32 s50, v252, 34
	v_readlane_b32 s51, v252, 35
	s_branch .LBB0_2223

.LBB0_2223:
	s_add_i32 s0, s0, s4
	s_cmp_ge_i32 s0, s13
	s_cselect_b64 s[8:9], -1, 0
	s_and_b64 vcc, exec, s[8:9]
	s_waitcnt vmcnt(0)
	v_mov_b32_e32 v40, v70
	v_mov_b32_e32 v41, v71
	v_mov_b32_e32 v42, v68
	v_mov_b32_e32 v43, v69
	v_mov_b32_e32 v44, v64
	v_mov_b32_e32 v45, v65
	v_mov_b32_e32 v46, v62
	v_mov_b32_e32 v47, v63
	v_mov_b32_e32 v48, v66
	v_mov_b32_e32 v49, v67
	v_mov_b32_e32 v50, v60
	v_mov_b32_e32 v51, v61
	v_mov_b32_e32 v52, v58
	v_mov_b32_e32 v53, v59
	v_mov_b32_e32 v54, v56
	v_mov_b32_e32 v55, v57
	s_cbranch_vccnz .LBB0_2225
	s_ashr_i32 s1, s0, 31
	s_lshl_b64 s[14:15], s[0:1], 11
	v_lshl_add_u64 v[40:41], v[0:1], 0, s[14:15]
	v_lshl_add_u64 v[46:47], v[36:37], 0, s[14:15]
	global_load_dwordx2 v[48:49], v[40:41], off nt
	global_load_dwordx2 v[50:51], v[40:41], off offset:512 nt
	global_load_dwordx2 v[52:53], v[40:41], off offset:1024 nt
	global_load_dwordx2 v[54:55], v[40:41], off offset:1536 nt
	s_nop 0
	global_load_dwordx2 v[40:41], v[46:47], off nt
	global_load_dwordx2 v[42:43], v[46:47], off offset:512 nt
	global_load_dwordx2 v[44:45], v[46:47], off offset:1024 nt
	s_nop 0
	global_load_dwordx2 v[46:47], v[46:47], off offset:1536 nt

.LBB0_2576:
	s_lshl_b32 s4, s0, 3
	s_add_i32 s8, s4, s90
	s_lshl_b32 s0, s0, 7
	s_and_b32 s4, s4, 0xf8
	s_and_b32 s0, s0, 0xfffff000
	s_add_i32 s4, s4, s90
	s_add_i32 s9, s4, s0
	s_add_i32 s13, s0, 0x1000
	s_cmpk_eq_i32 s1, 0x100
	s_cselect_b64 s[4:5], -1, 0
	v_readlane_b32 s20, v252, 52
	s_and_b64 s[6:7], s[4:5], exec
	v_readlane_b32 s22, v252, 54
	v_readlane_b32 s23, v252, 55
	s_cselect_b32 s0, s9, s8
	s_cselect_b32 s13, s13, 0x8000
	s_mov_b64 s[2:3], s[22:23]
	s_cmp_ge_i32 s0, s13
	v_readlane_b32 s21, v252, 53
	s_cbranch_scc1 .LBB0_2583
	s_lshl_b32 s1, s1, 3
	v_readlane_b32 s8, v254, 43
	s_add_u32 s6, s2, 0x3b982000
	v_readlane_b32 s9, v254, 44
	s_addc_u32 s7, s3, 0
	s_lshl_b32 s8, s8, 10
	s_mov_b32 s9, s11
	v_readlane_b32 s36, v252, 20
	s_lshl_b64 s[8:9], s[8:9], 2
	v_readlane_b32 s48, v252, 32
	v_readlane_b32 s49, v252, 33
	s_add_u32 s14, s48, s8
	v_readlane_b32 s50, v252, 34
	s_addc_u32 s15, s49, s9
	v_readlane_b32 s51, v252, 35
	s_add_u32 s8, s50, s8
	s_addc_u32 s9, s51, s9
	v_ashrrev_i32_e32 v5, 31, v4
	v_lshlrev_b64 v[38:39], 3, v[4:5]
	s_cmp_lg_u64 s[2:3], 0
	v_lshlrev_b64 v[0:1], 4, v[4:5]
	v_lshl_add_u64 v[6:7], s[2:3], 0, v[38:39]
	s_cselect_b64 s[2:3], -1, 0
	s_and_b64 s[4:5], s[4:5], exec
	v_lshl_add_u64 v[32:33], s[8:9], 0, v[0:1]
	s_mov_b64 s[8:9], 0x6f1c8000
	s_cselect_b32 s4, 0x100, s1
	s_ashr_i32 s1, s0, 31
	v_lshl_add_u64 v[28:29], s[14:15], 0, v[0:1]
	v_lshl_add_u64 v[0:1], s[6:7], 0, v[38:39]
	v_lshl_add_u64 v[36:37], v[6:7], 0, s[8:9]
	s_lshl_b64 s[8:9], s[0:1], 11
	v_lshlrev_b32_e32 v4, 2, v4
	v_lshl_add_u64 v[40:41], v[0:1], 0, s[8:9]
	v_xor_b32_e32 v2, 4, v4
	v_xor_b32_e32 v72, 8, v4
	v_xor_b32_e32 v73, 16, v4
	v_xor_b32_e32 v74, 32, v4
	v_xor_b32_e32 v75, 64, v4
	v_xor_b32_e32 v76, 0x80, v4
	global_load_dwordx4 v[4:7], v[28:29], off
	global_load_dwordx4 v[8:11], v[32:33], off
	global_load_dwordx4 v[12:15], v[28:29], off offset:1024
	global_load_dwordx4 v[16:19], v[32:33], off offset:1024
	global_load_dwordx4 v[20:23], v[28:29], off offset:2048
	global_load_dwordx4 v[24:27], v[32:33], off offset:2048
	s_nop 0
	global_load_dwordx4 v[28:31], v[28:29], off offset:3072
	s_nop 0
	global_load_dwordx4 v[32:35], v[32:33], off offset:3072
	v_lshl_add_u64 v[42:43], v[36:37], 0, s[8:9]
	global_load_dwordx2 v[66:67], v[40:41], off nt
	global_load_dwordx2 v[70:71], v[42:43], off nt
	global_load_dwordx2 v[60:61], v[40:41], off offset:512 nt
	global_load_dwordx2 v[68:69], v[42:43], off offset:512 nt
	global_load_dwordx2 v[58:59], v[40:41], off offset:1024 nt
	global_load_dwordx2 v[64:65], v[42:43], off offset:1024 nt
	global_load_dwordx2 v[56:57], v[40:41], off offset:1536 nt
	global_load_dwordx2 v[62:63], v[42:43], off offset:1536 nt
	s_add_u32 s6, s6, s8
	s_addc_u32 s7, s7, s9
	s_ashr_i32 s5, s4, 31
	v_lshl_add_u64 v[38:39], s[6:7], 0, v[38:39]
	s_lshl_b64 s[6:7], s[4:5], 11
	v_readlane_b32 s37, v252, 21
	v_readlane_b32 s38, v252, 22
	v_readlane_b32 s39, v252, 23
	v_readlane_b32 s40, v252, 24
	v_readlane_b32 s41, v252, 25
	v_readlane_b32 s42, v252, 26
	v_readlane_b32 s43, v252, 27
	v_readlane_b32 s44, v252, 28
	v_readlane_b32 s45, v252, 29
	v_readlane_b32 s46, v252, 30
	v_readlane_b32 s47, v252, 31
	s_branch .LBB0_2579

.LBB0_3193:
	s_lshl_b32 s2, s1, 3
	s_add_i32 s8, s2, s90
	s_lshl_b32 s1, s1, 7
	s_and_b32 s2, s2, 0xf8
	s_and_b32 s1, s1, 0xfffff000
	s_add_i32 s2, s2, s90
	v_readlane_b32 s4, v252, 52
	s_add_i32 s9, s2, s1
	s_addk_i32 s1, 0x1000
	v_readlane_b32 s5, v252, 53
	s_cmpk_eq_i32 s0, 0x100
	s_cselect_b64 s[4:5], -1, 0
	s_and_b64 s[2:3], s[4:5], exec
	s_cselect_b32 s28, s9, s8
	s_cselect_b32 s13, s1, 0x8000
	v_readlane_b32 s6, v252, 54
	v_readlane_b32 s7, v252, 55
	s_cmp_ge_i32 s28, s13
	s_cbranch_scc1 .LBB0_3214
	v_readlane_b32 s52, v254, 55
	s_lshl_b32 s14, s0, 3
	v_readlane_b32 s53, v254, 56
	s_and_b64 s[0:1], s[52:53], exec
	v_readlane_b32 s0, v252, 52
	v_readlane_b32 s1, v252, 53
	s_cselect_b32 s1, s1, 0
	s_cselect_b32 s0, s0, 0
	s_add_u32 s8, s6, 0x3b982000
	s_addc_u32 s9, s7, 0
	v_readlane_b32 s2, v252, 54
	v_readlane_b32 s3, v252, 55
	s_add_u32 s15, s6, 0x7b0c8000
	s_addc_u32 s20, s7, 0
	v_readlane_b32 s2, v254, 43
	s_add_u32 s21, s6, 0x7aec8000
	v_readlane_b32 s3, v254, 44
	s_addc_u32 s22, s7, 0
	s_lshl_b32 s2, s2, 10
	s_mov_b32 s3, s11
	v_readlane_b32 s36, v252, 36
	s_lshl_b64 s[2:3], s[2:3], 2
	v_readlane_b32 s48, v252, 48
	v_readlane_b32 s49, v252, 49
	s_add_u32 s30, s48, s2
	v_readlane_b32 s50, v252, 50
	s_addc_u32 s31, s49, s3
	v_readlane_b32 s51, v252, 51
	s_add_u32 s34, s50, s2
	s_addc_u32 s35, s51, s3
	s_and_b64 s[2:3], s[52:53], exec
	v_ashrrev_i32_e32 v5, 31, v4
	s_cselect_b32 s3, 0, s9
	s_cselect_b32 s2, 0, s8
	v_lshlrev_b64 v[16:17], 3, v[4:5]
	s_cmp_lg_u64 s[0:1], 0
	v_readlane_b32 s38, v252, 38
	v_readlane_b32 s39, v252, 39
	v_lshl_add_u64 v[24:25], s[8:9], 0, v[16:17]
	s_cselect_b64 s[8:9], -1, 0
	s_cmp_lg_u64 s[2:3], 0
	v_readlane_b32 s40, v252, 40
	v_lshl_add_u64 v[6:7], s[6:7], 0, v[16:17]
	s_mov_b64 s[6:7], 0x7b309500
	s_cselect_b64 s[38:39], -1, 0
	s_and_b64 s[4:5], s[4:5], exec
	v_lshl_add_u64 v[0:1], v[6:7], 0, s[6:7]
	s_mov_b64 s[6:7], 0x6f1c8000
	s_cselect_b32 s40, 0x100, s14
	s_ashr_i32 s29, s28, 31
	v_lshl_add_u64 v[26:27], v[6:7], 0, s[6:7]
	v_lshlrev_b64 v[18:19], 4, v[4:5]
	s_lshl_b64 s[4:5], s[28:29], 11
	s_lshl_b64 s[6:7], s[28:29], 5
	v_lshl_add_u64 v[28:29], s[30:31], 0, v[18:19]
	s_add_u32 s30, s15, s6
	v_lshlrev_b32_e32 v6, 2, v4
	v_lshl_add_u64 v[4:5], v[24:25], 0, s[4:5]
	s_addc_u32 s31, s20, s7
	v_xor_b32_e32 v2, 4, v6
	v_xor_b32_e32 v192, 8, v6
	v_xor_b32_e32 v193, 16, v6
	v_xor_b32_e32 v194, 32, v6
	v_xor_b32_e32 v195, 64, v6
	v_xor_b32_e32 v221, 0x80, v6
	v_lshl_add_u64 v[6:7], v[26:27], 0, s[4:5]
	global_load_dwordx2 v[72:73], v[4:5], off nt
	global_load_dwordx2 v[80:81], v[6:7], off nt
	global_load_dwordx2 v[54:55], v[4:5], off offset:512 nt
	global_load_dwordx2 v[58:59], v[6:7], off offset:512 nt
	global_load_dwordx2 v[46:47], v[4:5], off offset:1024 nt
	global_load_dwordx2 v[50:51], v[6:7], off offset:1024 nt
	global_load_dwordx2 v[42:43], v[4:5], off offset:1536 nt
	global_load_dwordx2 v[44:45], v[6:7], off offset:1536 nt
	global_load_dwordx4 v[12:15], v3, s[30:31] offset:16
	global_load_dwordx4 v[20:23], v3, s[30:31]
	s_add_u32 s6, s21, s6
	s_addc_u32 s7, s22, s7
	v_readlane_b32 s41, v252, 41
	s_add_u32 s2, s2, s4
	v_readlane_b32 s42, v252, 42
	v_readlane_b32 s43, v252, 43
	s_addc_u32 s3, s3, s5
	s_ashr_i32 s41, s40, 31
	s_lshl_b64 s[42:43], s[40:41], 11
	v_readlane_b32 s44, v252, 44
	v_readlane_b32 s45, v252, 45
	v_lshl_add_u64 v[30:31], s[34:35], 0, v[18:19]
	v_readlane_b32 s37, v252, 37
	v_readlane_b32 s46, v252, 46
	v_readlane_b32 s47, v252, 47
	s_waitcnt vmcnt(0)
	v_mov_b64_e32 v[60:61], v[72:73]
	v_mov_b64_e32 v[68:69], v[80:81]
	v_mov_b64_e32 v[62:63], v[54:55]
	v_mov_b64_e32 v[70:71], v[58:59]
	v_mov_b64_e32 v[64:65], v[46:47]
	v_mov_b64_e32 v[74:75], v[50:51]
	v_mov_b64_e32 v[66:67], v[42:43]
	v_mov_b64_e32 v[76:77], v[44:45]
	v_ashrrev_i32_e32 v5, 31, v20
	v_mov_b32_e32 v4, v20
	v_ashrrev_i32_e32 v7, 31, v21
	v_mov_b32_e32 v6, v21
	v_lshlrev_b64 v[20:21], 11, v[6:7]
	v_lshlrev_b64 v[4:5], 11, v[4:5]
	v_lshl_add_u64 v[4:5], v[0:1], 0, v[4:5]
	v_lshl_add_u64 v[20:21], v[0:1], 0, v[20:21]
	global_load_dwordx2 v[92:93], v[4:5], off nt
	global_load_dwordx2 v[90:91], v[4:5], off offset:512 nt
	global_load_dwordx2 v[86:87], v[4:5], off offset:1024 nt
	global_load_dwordx2 v[84:85], v[4:5], off offset:1536 nt
	s_nop 0
	global_load_dwordx4 v[4:7], v3, s[6:7] offset:16
	global_load_dwordx4 v[8:11], v3, s[6:7]
	global_load_dwordx2 v[106:107], v[20:21], off nt
	global_load_dwordx2 v[88:89], v[20:21], off offset:512 nt
	global_load_dwordx2 v[48:49], v[20:21], off offset:1024 nt
	global_load_dwordx2 v[36:37], v[20:21], off offset:1536 nt
	v_ashrrev_i32_e32 v21, 31, v22
	v_mov_b32_e32 v20, v22
	v_ashrrev_i32_e32 v33, 31, v23
	v_mov_b32_e32 v32, v23
	v_lshlrev_b64 v[20:21], 11, v[20:21]
	v_lshlrev_b64 v[22:23], 11, v[32:33]
	v_lshl_add_u64 v[20:21], v[0:1], 0, v[20:21]
	global_load_dwordx2 v[126:127], v[20:21], off nt
	global_load_dwordx2 v[102:103], v[20:21], off offset:512 nt
	global_load_dwordx2 v[82:83], v[20:21], off offset:1024 nt
	global_load_dwordx2 v[40:41], v[20:21], off offset:1536 nt
	v_lshl_add_u64 v[20:21], v[0:1], 0, v[22:23]
	global_load_dwordx2 v[122:123], v[20:21], off nt
	global_load_dwordx2 v[100:101], v[20:21], off offset:512 nt
	global_load_dwordx2 v[78:79], v[20:21], off offset:1024 nt
	global_load_dwordx2 v[38:39], v[20:21], off offset:1536 nt
	v_ashrrev_i32_e32 v21, 31, v12
	v_mov_b32_e32 v20, v12
	v_ashrrev_i32_e32 v23, 31, v13
	v_mov_b32_e32 v22, v13
	v_lshlrev_b64 v[12:13], 11, v[22:23]
	v_lshlrev_b64 v[20:21], 11, v[20:21]
	v_lshl_add_u64 v[20:21], v[0:1], 0, v[20:21]
	v_lshl_add_u64 v[12:13], v[0:1], 0, v[12:13]
	global_load_dwordx2 v[130:131], v[20:21], off nt
	global_load_dwordx2 v[118:119], v[20:21], off offset:512 nt
	global_load_dwordx2 v[96:97], v[20:21], off offset:1024 nt
	global_load_dwordx2 v[56:57], v[20:21], off offset:1536 nt
	global_load_dwordx2 v[128:129], v[12:13], off nt
	global_load_dwordx2 v[116:117], v[12:13], off offset:512 nt
	global_load_dwordx2 v[94:95], v[12:13], off offset:1024 nt
	global_load_dwordx2 v[52:53], v[12:13], off offset:1536 nt
	v_ashrrev_i32_e32 v13, 31, v14
	v_mov_b32_e32 v12, v14
	v_ashrrev_i32_e32 v21, 31, v15
	v_mov_b32_e32 v20, v15
	v_lshlrev_b64 v[12:13], 11, v[12:13]
	v_lshlrev_b64 v[14:15], 11, v[20:21]
	v_lshl_add_u64 v[12:13], v[0:1], 0, v[12:13]
	global_load_dwordx2 v[160:161], v[12:13], off nt
	global_load_dwordx2 v[132:133], v[12:13], off offset:512 nt
	global_load_dwordx2 v[120:121], v[12:13], off offset:1024 nt
	global_load_dwordx2 v[98:99], v[12:13], off offset:1536 nt
	v_lshl_add_u64 v[12:13], v[0:1], 0, v[14:15]
	global_load_dwordx2 v[162:163], v[12:13], off nt
	global_load_dwordx2 v[142:143], v[12:13], off offset:512 nt
	global_load_dwordx2 v[124:125], v[12:13], off offset:1024 nt
	global_load_dwordx2 v[104:105], v[12:13], off offset:1536 nt
	v_lshl_add_u64 v[32:33], s[2:3], 0, v[16:17]
	s_lshl_b64 s[2:3], s[28:29], 12
	s_add_u32 s0, s0, s2
	s_addc_u32 s1, s1, s3
	v_lshl_add_u64 v[12:13], s[0:1], 0, v[18:19]
	s_mov_b64 s[0:1], 0xc00
	v_lshl_add_u64 v[34:35], v[12:13], 0, s[0:1]
	s_lshl_b64 s[44:45], s[40:41], 12
	s_waitcnt vmcnt(33)
	v_mov_b64_e32 v[114:115], v[92:93]
	s_waitcnt vmcnt(32)
	v_mov_b64_e32 v[112:113], v[90:91]
	s_waitcnt vmcnt(31)
	v_mov_b64_e32 v[110:111], v[86:87]
	s_waitcnt vmcnt(27)
	v_mov_b64_e32 v[140:141], v[106:107]
	v_mov_b64_e32 v[14:15], v[6:7]
	v_mov_b64_e32 v[12:13], v[4:5]
	v_mov_b64_e32 v[18:19], v[10:11]
	v_mov_b64_e32 v[16:17], v[8:9]
	s_waitcnt vmcnt(24)
	v_mov_b64_e32 v[134:135], v[36:37]
	v_mov_b64_e32 v[136:137], v[48:49]
	v_mov_b64_e32 v[138:139], v[88:89]
	s_waitcnt vmcnt(23)
	v_mov_b64_e32 v[150:151], v[126:127]
	s_waitcnt vmcnt(22)
	v_mov_b64_e32 v[148:149], v[102:103]
	s_waitcnt vmcnt(19)
	v_mov_b64_e32 v[158:159], v[122:123]
	s_waitcnt vmcnt(18)
	v_mov_b64_e32 v[156:157], v[100:101]
	s_waitcnt vmcnt(17)
	v_mov_b64_e32 v[154:155], v[78:79]
	s_waitcnt vmcnt(16)
	v_mov_b64_e32 v[152:153], v[38:39]
	v_mov_b64_e32 v[144:145], v[40:41]
	v_mov_b64_e32 v[146:147], v[82:83]
	v_mov_b64_e32 v[108:109], v[84:85]
	s_waitcnt vmcnt(15)
	v_mov_b64_e32 v[168:169], v[130:131]
	s_waitcnt vmcnt(11)
	v_mov_b64_e32 v[176:177], v[128:129]
	s_waitcnt vmcnt(10)
	v_mov_b64_e32 v[174:175], v[116:117]
	s_waitcnt vmcnt(9)
	v_mov_b64_e32 v[172:173], v[94:95]
	s_waitcnt vmcnt(8)
	v_mov_b64_e32 v[170:171], v[52:53]
	v_mov_b64_e32 v[20:21], v[56:57]
	v_mov_b64_e32 v[164:165], v[96:97]
	v_mov_b64_e32 v[166:167], v[118:119]
	s_waitcnt vmcnt(7)
	v_mov_b64_e32 v[182:183], v[160:161]
	s_waitcnt vmcnt(6)
	v_mov_b64_e32 v[180:181], v[132:133]
	s_waitcnt vmcnt(3)
	v_mov_b64_e32 v[190:191], v[162:163]
	s_waitcnt vmcnt(2)
	v_mov_b64_e32 v[188:189], v[142:143]
	s_waitcnt vmcnt(1)
	v_mov_b64_e32 v[186:187], v[124:125]
	s_waitcnt vmcnt(0)
	v_mov_b64_e32 v[184:185], v[104:105]
	v_mov_b64_e32 v[22:23], v[98:99]
	v_mov_b64_e32 v[178:179], v[120:121]
	s_branch .LBB0_3196

.LBB0_3196:
	s_add_i32 s28, s28, s40
	s_cmp_ge_i32 s28, s13
	s_cselect_b64 s[46:47], -1, 0
	v_mov_b32_e32 v226, 0x3f80
	v_mov_b32_e32 v225, 0x3f803f80
	v_mov_b32_e32 v224, 0x4000
	v_mov_b32_e32 v223, 0x2000
	v_mov_b32_e32 v222, 0x1000
	v_mov_b32_e32 v220, 0x800
	s_and_b64 vcc, exec, s[46:47]
	s_cbranch_vccnz .LBB0_3198
	s_ashr_i32 s29, s28, 31
	s_lshl_b64 s[0:1], s[28:29], 11
	v_lshl_add_u64 v[12:13], v[24:25], 0, s[0:1]
	v_lshl_add_u64 v[14:15], v[26:27], 0, s[0:1]
	s_lshl_b64 s[0:1], s[28:29], 5
	s_add_u32 s2, s15, s0
	s_addc_u32 s3, s20, s1
	global_load_dwordx2 v[60:61], v[12:13], off nt
	global_load_dwordx2 v[68:69], v[14:15], off nt
	global_load_dwordx2 v[62:63], v[12:13], off offset:512 nt
	global_load_dwordx2 v[70:71], v[14:15], off offset:512 nt
	global_load_dwordx2 v[64:65], v[12:13], off offset:1024 nt
	global_load_dwordx2 v[74:75], v[14:15], off offset:1024 nt
	global_load_dwordx2 v[66:67], v[12:13], off offset:1536 nt
	global_load_dwordx2 v[76:77], v[14:15], off offset:1536 nt
	global_load_dwordx4 v[20:23], v3, s[2:3] offset:16
	global_load_dwordx4 v[144:147], v3, s[2:3]
	s_add_u32 s0, s21, s0
	s_addc_u32 s1, s22, s1
	s_waitcnt vmcnt(1)
	v_ashrrev_i32_e32 v165, 31, v20
	s_waitcnt vmcnt(0)
	v_ashrrev_i32_e32 v13, 31, v144
	v_mov_b32_e32 v12, v144
	v_lshlrev_b64 v[12:13], 11, v[12:13]
	v_ashrrev_i32_e32 v15, 31, v145
	v_mov_b32_e32 v14, v145
	v_lshl_add_u64 v[12:13], v[0:1], 0, v[12:13]
	v_ashrrev_i32_e32 v145, 31, v146
	v_mov_b32_e32 v144, v146
	v_ashrrev_i32_e32 v149, 31, v147
	v_mov_b32_e32 v148, v147
	v_mov_b32_e32 v164, v20
	v_ashrrev_i32_e32 v167, 31, v21
	v_mov_b32_e32 v166, v21
	v_ashrrev_i32_e32 v179, 31, v22
	v_mov_b32_e32 v178, v22
	v_ashrrev_i32_e32 v181, 31, v23
	v_mov_b32_e32 v180, v23
	v_lshlrev_b64 v[134:135], 11, v[14:15]
	global_load_dwordx2 v[114:115], v[12:13], off nt
	global_load_dwordx2 v[112:113], v[12:13], off offset:512 nt
	global_load_dwordx2 v[110:111], v[12:13], off offset:1024 nt
	global_load_dwordx2 v[108:109], v[12:13], off offset:1536 nt
	s_nop 0
	global_load_dwordx4 v[12:15], v3, s[0:1] offset:16
	global_load_dwordx4 v[16:19], v3, s[0:1]
	v_lshlrev_b64 v[152:153], 11, v[148:149]
	v_lshlrev_b64 v[144:145], 11, v[144:145]
	v_lshlrev_b64 v[170:171], 11, v[166:167]
	v_lshlrev_b64 v[20:21], 11, v[164:165]
	v_lshlrev_b64 v[184:185], 11, v[180:181]
	v_lshlrev_b64 v[22:23], 11, v[178:179]
	v_lshl_add_u64 v[134:135], v[0:1], 0, v[134:135]
	v_lshl_add_u64 v[144:145], v[0:1], 0, v[144:145]
	v_lshl_add_u64 v[152:153], v[0:1], 0, v[152:153]
	v_lshl_add_u64 v[20:21], v[0:1], 0, v[20:21]
	v_lshl_add_u64 v[170:171], v[0:1], 0, v[170:171]
	v_lshl_add_u64 v[22:23], v[0:1], 0, v[22:23]
	v_lshl_add_u64 v[184:185], v[0:1], 0, v[184:185]
	global_load_dwordx2 v[140:141], v[134:135], off nt
	global_load_dwordx2 v[138:139], v[134:135], off offset:512 nt
	global_load_dwordx2 v[136:137], v[134:135], off offset:1024 nt
	s_nop 0
	global_load_dwordx2 v[134:135], v[134:135], off offset:1536 nt
	s_nop 0
	global_load_dwordx2 v[150:151], v[144:145], off nt
	global_load_dwordx2 v[148:149], v[144:145], off offset:512 nt
	global_load_dwordx2 v[146:147], v[144:145], off offset:1024 nt
	s_nop 0
	global_load_dwordx2 v[144:145], v[144:145], off offset:1536 nt
	s_nop 0
	global_load_dwordx2 v[158:159], v[152:153], off nt
	global_load_dwordx2 v[156:157], v[152:153], off offset:512 nt
	global_load_dwordx2 v[154:155], v[152:153], off offset:1024 nt
	s_nop 0
	global_load_dwordx2 v[152:153], v[152:153], off offset:1536 nt
	s_nop 0
	global_load_dwordx2 v[168:169], v[20:21], off nt
	global_load_dwordx2 v[166:167], v[20:21], off offset:512 nt
	global_load_dwordx2 v[164:165], v[20:21], off offset:1024 nt
	s_nop 0
	global_load_dwordx2 v[20:21], v[20:21], off offset:1536 nt
	s_nop 0
	global_load_dwordx2 v[176:177], v[170:171], off nt
	global_load_dwordx2 v[174:175], v[170:171], off offset:512 nt
	global_load_dwordx2 v[172:173], v[170:171], off offset:1024 nt
	s_nop 0
	global_load_dwordx2 v[170:171], v[170:171], off offset:1536 nt
	s_nop 0
	global_load_dwordx2 v[182:183], v[22:23], off nt
	global_load_dwordx2 v[180:181], v[22:23], off offset:512 nt
	global_load_dwordx2 v[178:179], v[22:23], off offset:1024 nt
	s_nop 0
	global_load_dwordx2 v[22:23], v[22:23], off offset:1536 nt
	s_nop 0
	global_load_dwordx2 v[190:191], v[184:185], off nt
	global_load_dwordx2 v[188:189], v[184:185], off offset:512 nt
	global_load_dwordx2 v[186:187], v[184:185], off offset:1024 nt
	s_nop 0
	global_load_dwordx2 v[184:185], v[184:185], off offset:1536 nt
.LBB0_3198:
	v_lshlrev_b32_e32 v196, 16, v80
	v_and_b32_e32 v197, 0xffff0000, v80
	v_lshlrev_b32_e32 v80, 16, v81
	v_and_b32_e32 v81, 0xffff0000, v81
	v_lshlrev_b32_e32 v198, 16, v72
	v_and_b32_e32 v199, 0xffff0000, v72
	v_lshlrev_b32_e32 v72, 16, v73
	v_and_b32_e32 v73, 0xffff0000, v73
	s_mov_b32 s0, 0x3fb504f3
	v_pk_fma_f32 v[204:205], v[72:73], s[0:1], v[80:81] op_sel_hi:[1,0,1]
	v_lshlrev_b32_e32 v72, 16, v58
	v_and_b32_e32 v73, 0xffff0000, v58
	v_lshlrev_b32_e32 v58, 16, v59
	v_and_b32_e32 v59, 0xffff0000, v59
	v_lshlrev_b32_e32 v80, 16, v54
	v_and_b32_e32 v81, 0xffff0000, v54
	v_lshlrev_b32_e32 v54, 16, v55
	v_and_b32_e32 v55, 0xffff0000, v55
	v_pk_fma_f32 v[54:55], v[54:55], s[0:1], v[58:59] op_sel_hi:[1,0,1]
	v_pk_fma_f32 v[58:59], v[80:81], s[0:1], v[72:73] op_sel_hi:[1,0,1]
	v_lshlrev_b32_e32 v72, 16, v50
	v_and_b32_e32 v73, 0xffff0000, v50
	v_lshlrev_b32_e32 v50, 16, v51
	v_and_b32_e32 v51, 0xffff0000, v51
	v_lshlrev_b32_e32 v80, 16, v46
	v_and_b32_e32 v81, 0xffff0000, v46
	v_lshlrev_b32_e32 v46, 16, v47
	v_and_b32_e32 v47, 0xffff0000, v47
	v_pk_fma_f32 v[196:197], v[198:199], s[0:1], v[196:197] op_sel_hi:[1,0,1]
	v_pk_fma_f32 v[198:199], v[46:47], s[0:1], v[50:51] op_sel_hi:[1,0,1]
	v_lshlrev_b32_e32 v46, 16, v44
	v_and_b32_e32 v47, 0xffff0000, v44
	v_lshlrev_b32_e32 v44, 16, v45
	v_and_b32_e32 v45, 0xffff0000, v45
	v_lshlrev_b32_e32 v50, 16, v42
	v_and_b32_e32 v51, 0xffff0000, v42
	v_lshlrev_b32_e32 v42, 16, v43
	v_and_b32_e32 v43, 0xffff0000, v43
	v_pk_fma_f32 v[208:209], v[80:81], s[0:1], v[72:73] op_sel_hi:[1,0,1]
	v_pk_fma_f32 v[72:73], v[42:43], s[0:1], v[44:45] op_sel_hi:[1,0,1]
	v_lshlrev_b32_e32 v42, 16, v92
	v_and_b32_e32 v43, 0xffff0000, v92
	v_pk_fma_f32 v[210:211], v[50:51], s[0:1], v[46:47] op_sel_hi:[1,0,1]
	v_pk_fma_f32 v[42:43], v[8:9], v[42:43], v[196:197] op_sel_hi:[0,1,1]
	v_lshlrev_b32_e32 v46, 16, v106
	v_and_b32_e32 v47, 0xffff0000, v106
	v_pk_fma_f32 v[42:43], v[8:9], v[46:47], v[42:43] op_sel:[1,0,0]
	v_lshlrev_b32_e32 v46, 16, v126
	v_and_b32_e32 v47, 0xffff0000, v126
	v_pk_fma_f32 v[42:43], v[10:11], v[46:47], v[42:43] op_sel_hi:[0,1,1]
	v_lshlrev_b32_e32 v46, 16, v122
	v_and_b32_e32 v47, 0xffff0000, v122
	v_pk_fma_f32 v[42:43], v[10:11], v[46:47], v[42:43] op_sel:[1,0,0]
	v_lshlrev_b32_e32 v46, 16, v130
	v_and_b32_e32 v47, 0xffff0000, v130
	v_pk_fma_f32 v[42:43], v[4:5], v[46:47], v[42:43] op_sel_hi:[0,1,1]
	v_lshlrev_b32_e32 v46, 16, v128
	v_and_b32_e32 v47, 0xffff0000, v128
	v_pk_fma_f32 v[42:43], v[4:5], v[46:47], v[42:43] op_sel:[1,0,0]
	v_lshlrev_b32_e32 v46, 16, v160
	v_and_b32_e32 v47, 0xffff0000, v160
	v_lshlrev_b32_e32 v44, 16, v93
	v_and_b32_e32 v45, 0xffff0000, v93
	v_pk_fma_f32 v[42:43], v[6:7], v[46:47], v[42:43] op_sel_hi:[0,1,1]
	v_lshlrev_b32_e32 v46, 16, v162
	v_and_b32_e32 v47, 0xffff0000, v162
	v_pk_fma_f32 v[42:43], v[6:7], v[46:47], v[42:43] op_sel:[1,0,0]
	v_pk_fma_f32 v[44:45], v[8:9], v[44:45], v[204:205] op_sel_hi:[0,1,1]
	v_lshlrev_b32_e32 v46, 16, v107
	v_and_b32_e32 v47, 0xffff0000, v107
	v_pk_fma_f32 v[44:45], v[8:9], v[46:47], v[44:45] op_sel:[1,0,0]
	v_lshlrev_b32_e32 v46, 16, v127
	v_and_b32_e32 v47, 0xffff0000, v127
	v_pk_fma_f32 v[44:45], v[10:11], v[46:47], v[44:45] op_sel_hi:[0,1,1]
	v_lshlrev_b32_e32 v46, 16, v123
	v_and_b32_e32 v47, 0xffff0000, v123
	v_pk_fma_f32 v[44:45], v[10:11], v[46:47], v[44:45] op_sel:[1,0,0]
	v_lshlrev_b32_e32 v46, 16, v131
	v_and_b32_e32 v47, 0xffff0000, v131
	v_pk_fma_f32 v[44:45], v[4:5], v[46:47], v[44:45] op_sel_hi:[0,1,1]
	v_lshlrev_b32_e32 v46, 16, v129
	v_and_b32_e32 v47, 0xffff0000, v129
	v_pk_fma_f32 v[44:45], v[4:5], v[46:47], v[44:45] op_sel:[1,0,0]
	v_lshlrev_b32_e32 v46, 16, v161
	v_and_b32_e32 v47, 0xffff0000, v161
	v_lshlrev_b32_e32 v50, 16, v90
	v_and_b32_e32 v51, 0xffff0000, v90
	v_pk_fma_f32 v[44:45], v[6:7], v[46:47], v[44:45] op_sel_hi:[0,1,1]
	v_lshlrev_b32_e32 v46, 16, v163
	v_and_b32_e32 v47, 0xffff0000, v163
	v_pk_fma_f32 v[46:47], v[6:7], v[46:47], v[44:45] op_sel:[1,0,0]
	v_pk_fma_f32 v[44:45], v[8:9], v[50:51], v[58:59] op_sel_hi:[0,1,1]
	v_lshlrev_b32_e32 v50, 16, v88
	v_and_b32_e32 v51, 0xffff0000, v88
	v_pk_fma_f32 v[44:45], v[8:9], v[50:51], v[44:45] op_sel:[1,0,0]
	v_lshlrev_b32_e32 v50, 16, v102
	v_and_b32_e32 v51, 0xffff0000, v102
	v_pk_fma_f32 v[44:45], v[10:11], v[50:51], v[44:45] op_sel_hi:[0,1,1]
	v_lshlrev_b32_e32 v50, 16, v100
	v_and_b32_e32 v51, 0xffff0000, v100
	v_pk_fma_f32 v[44:45], v[10:11], v[50:51], v[44:45] op_sel:[1,0,0]
	v_lshlrev_b32_e32 v50, 16, v118
	v_and_b32_e32 v51, 0xffff0000, v118
	v_pk_fma_f32 v[44:45], v[4:5], v[50:51], v[44:45] op_sel_hi:[0,1,1]
	v_lshlrev_b32_e32 v50, 16, v116
	v_and_b32_e32 v51, 0xffff0000, v116
	v_pk_fma_f32 v[44:45], v[4:5], v[50:51], v[44:45] op_sel:[1,0,0]
	v_lshlrev_b32_e32 v50, 16, v132
	v_and_b32_e32 v51, 0xffff0000, v132
	v_lshlrev_b32_e32 v90, 16, v91
	v_and_b32_e32 v91, 0xffff0000, v91
	v_pk_fma_f32 v[44:45], v[6:7], v[50:51], v[44:45] op_sel_hi:[0,1,1]
	v_lshlrev_b32_e32 v50, 16, v142
	v_and_b32_e32 v51, 0xffff0000, v142
	v_pk_fma_f32 v[44:45], v[6:7], v[50:51], v[44:45] op_sel:[1,0,0]
	v_pk_fma_f32 v[50:51], v[8:9], v[90:91], v[54:55] op_sel_hi:[0,1,1]
	v_lshlrev_b32_e32 v54, 16, v89
	v_and_b32_e32 v55, 0xffff0000, v89
	v_pk_fma_f32 v[50:51], v[8:9], v[54:55], v[50:51] op_sel:[1,0,0]
	v_lshlrev_b32_e32 v54, 16, v103
	v_and_b32_e32 v55, 0xffff0000, v103
	v_pk_fma_f32 v[50:51], v[10:11], v[54:55], v[50:51] op_sel_hi:[0,1,1]
	v_lshlrev_b32_e32 v54, 16, v101
	v_and_b32_e32 v55, 0xffff0000, v101
	v_pk_fma_f32 v[50:51], v[10:11], v[54:55], v[50:51] op_sel:[1,0,0]
	v_lshlrev_b32_e32 v54, 16, v119
	v_and_b32_e32 v55, 0xffff0000, v119
	v_pk_fma_f32 v[50:51], v[4:5], v[54:55], v[50:51] op_sel_hi:[0,1,1]
	v_lshlrev_b32_e32 v54, 16, v117
	v_and_b32_e32 v55, 0xffff0000, v117
	v_pk_fma_f32 v[50:51], v[4:5], v[54:55], v[50:51] op_sel:[1,0,0]
	v_lshlrev_b32_e32 v54, 16, v133
	v_and_b32_e32 v55, 0xffff0000, v133
	v_lshlrev_b32_e32 v92, 16, v86
	v_and_b32_e32 v93, 0xffff0000, v86
	v_pk_fma_f32 v[50:51], v[6:7], v[54:55], v[50:51] op_sel_hi:[0,1,1]
	v_lshlrev_b32_e32 v54, 16, v143
	v_and_b32_e32 v55, 0xffff0000, v143
	v_pk_fma_f32 v[50:51], v[6:7], v[54:55], v[50:51] op_sel:[1,0,0]
	v_pk_fma_f32 v[54:55], v[8:9], v[92:93], v[208:209] op_sel_hi:[0,1,1]
	v_lshlrev_b32_e32 v58, 16, v48
	v_and_b32_e32 v59, 0xffff0000, v48
	v_pk_fma_f32 v[54:55], v[8:9], v[58:59], v[54:55] op_sel:[1,0,0]
	v_lshlrev_b32_e32 v58, 16, v82
	v_and_b32_e32 v59, 0xffff0000, v82
	v_pk_fma_f32 v[54:55], v[10:11], v[58:59], v[54:55] op_sel_hi:[0,1,1]
	v_lshlrev_b32_e32 v58, 16, v78
	v_and_b32_e32 v59, 0xffff0000, v78
	v_pk_fma_f32 v[54:55], v[10:11], v[58:59], v[54:55] op_sel:[1,0,0]
	v_lshlrev_b32_e32 v58, 16, v96
	v_and_b32_e32 v59, 0xffff0000, v96
	v_pk_fma_f32 v[54:55], v[4:5], v[58:59], v[54:55] op_sel_hi:[0,1,1]
	v_lshlrev_b32_e32 v58, 16, v94
	v_and_b32_e32 v59, 0xffff0000, v94
	v_pk_fma_f32 v[54:55], v[4:5], v[58:59], v[54:55] op_sel:[1,0,0]
	v_lshlrev_b32_e32 v58, 16, v120
	v_and_b32_e32 v59, 0xffff0000, v120
	v_lshlrev_b32_e32 v86, 16, v87
	v_and_b32_e32 v87, 0xffff0000, v87
	v_pk_fma_f32 v[54:55], v[6:7], v[58:59], v[54:55] op_sel_hi:[0,1,1]
	v_lshlrev_b32_e32 v58, 16, v124
	v_and_b32_e32 v59, 0xffff0000, v124
	v_pk_fma_f32 v[54:55], v[6:7], v[58:59], v[54:55] op_sel:[1,0,0]
	v_pk_fma_f32 v[58:59], v[8:9], v[86:87], v[198:199] op_sel_hi:[0,1,1]
	v_lshlrev_b32_e32 v48, 16, v49
	v_and_b32_e32 v49, 0xffff0000, v49
	v_pk_fma_f32 v[48:49], v[8:9], v[48:49], v[58:59] op_sel:[1,0,0]
	v_lshlrev_b32_e32 v58, 16, v83
	v_and_b32_e32 v59, 0xffff0000, v83
	v_pk_fma_f32 v[48:49], v[10:11], v[58:59], v[48:49] op_sel_hi:[0,1,1]
	v_lshlrev_b32_e32 v58, 16, v79
	v_and_b32_e32 v59, 0xffff0000, v79
	v_pk_fma_f32 v[48:49], v[10:11], v[58:59], v[48:49] op_sel:[1,0,0]
	v_lshlrev_b32_e32 v58, 16, v97
	v_and_b32_e32 v59, 0xffff0000, v97
	v_pk_fma_f32 v[48:49], v[4:5], v[58:59], v[48:49] op_sel_hi:[0,1,1]
	v_lshlrev_b32_e32 v58, 16, v95
	v_and_b32_e32 v59, 0xffff0000, v95
	v_pk_fma_f32 v[48:49], v[4:5], v[58:59], v[48:49] op_sel:[1,0,0]
	v_lshlrev_b32_e32 v58, 16, v121
	v_and_b32_e32 v59, 0xffff0000, v121
	v_lshlrev_b32_e32 v212, 16, v84
	v_and_b32_e32 v213, 0xffff0000, v84
	v_lshlrev_b32_e32 v80, 16, v85
	v_and_b32_e32 v81, 0xffff0000, v85
	v_pk_fma_f32 v[48:49], v[6:7], v[58:59], v[48:49] op_sel_hi:[0,1,1]
	v_lshlrev_b32_e32 v58, 16, v125
	v_and_b32_e32 v59, 0xffff0000, v125
	v_pk_fma_f32 v[48:49], v[6:7], v[58:59], v[48:49] op_sel:[1,0,0]
	v_pk_fma_f32 v[58:59], v[8:9], v[212:213], v[210:211] op_sel_hi:[0,1,1]
	v_lshlrev_b32_e32 v78, 16, v36
	v_and_b32_e32 v79, 0xffff0000, v36
	v_pk_fma_f32 v[72:73], v[8:9], v[80:81], v[72:73] op_sel_hi:[0,1,1]
	v_lshlrev_b32_e32 v36, 16, v37
	v_and_b32_e32 v37, 0xffff0000, v37
	v_pk_fma_f32 v[58:59], v[8:9], v[78:79], v[58:59] op_sel:[1,0,0]
	v_lshlrev_b32_e32 v78, 16, v40
	v_and_b32_e32 v79, 0xffff0000, v40
	v_pk_fma_f32 v[8:9], v[8:9], v[36:37], v[72:73] op_sel:[1,0,0]
	v_lshlrev_b32_e32 v36, 16, v41
	v_and_b32_e32 v37, 0xffff0000, v41
	v_pk_fma_f32 v[58:59], v[10:11], v[78:79], v[58:59] op_sel_hi:[0,1,1]
	v_lshlrev_b32_e32 v78, 16, v38
	v_and_b32_e32 v79, 0xffff0000, v38
	v_pk_fma_f32 v[8:9], v[10:11], v[36:37], v[8:9] op_sel_hi:[0,1,1]
	v_lshlrev_b32_e32 v36, 16, v39
	v_and_b32_e32 v37, 0xffff0000, v39
	v_pk_fma_f32 v[58:59], v[10:11], v[78:79], v[58:59] op_sel:[1,0,0]
	v_lshlrev_b32_e32 v78, 16, v56
	v_and_b32_e32 v79, 0xffff0000, v56
	v_pk_fma_f32 v[8:9], v[10:11], v[36:37], v[8:9] op_sel:[1,0,0]
	v_lshlrev_b32_e32 v10, 16, v57
	v_and_b32_e32 v11, 0xffff0000, v57
	v_pk_fma_f32 v[58:59], v[4:5], v[78:79], v[58:59] op_sel_hi:[0,1,1]
	v_lshlrev_b32_e32 v78, 16, v52
	v_and_b32_e32 v79, 0xffff0000, v52
	v_pk_fma_f32 v[8:9], v[4:5], v[10:11], v[8:9] op_sel_hi:[0,1,1]
	v_lshlrev_b32_e32 v10, 16, v53
	v_and_b32_e32 v11, 0xffff0000, v53
	v_pk_fma_f32 v[58:59], v[4:5], v[78:79], v[58:59] op_sel:[1,0,0]
	v_lshlrev_b32_e32 v78, 16, v98
	v_and_b32_e32 v79, 0xffff0000, v98
	v_pk_fma_f32 v[4:5], v[4:5], v[10:11], v[8:9] op_sel:[1,0,0]
	v_lshlrev_b32_e32 v8, 16, v99
	v_and_b32_e32 v9, 0xffff0000, v99
	v_pk_fma_f32 v[58:59], v[6:7], v[78:79], v[58:59] op_sel_hi:[0,1,1]
	v_lshlrev_b32_e32 v78, 16, v104
	v_and_b32_e32 v79, 0xffff0000, v104
	v_pk_fma_f32 v[4:5], v[6:7], v[8:9], v[4:5] op_sel_hi:[0,1,1]
	v_lshlrev_b32_e32 v8, 16, v105
	v_and_b32_e32 v9, 0xffff0000, v105
	v_pk_fma_f32 v[58:59], v[6:7], v[78:79], v[58:59] op_sel:[1,0,0]
	v_pk_fma_f32 v[8:9], v[6:7], v[8:9], v[4:5] op_sel:[1,0,0]
	v_mov_b32_e32 v4, v42
	v_mov_b32_e32 v5, v46
	v_mov_b32_e32 v6, v43
	v_mov_b32_e32 v7, v47
	v_pk_add_f32 v[4:5], v[4:5], v[6:7]
	v_mov_b32_e32 v6, v44
	v_mov_b32_e32 v7, v50
	v_mov_b32_e32 v10, v45
	v_mov_b32_e32 v11, v51
	v_pk_add_f32 v[6:7], v[6:7], v[10:11]
	v_add_f32_e32 v4, v4, v5
	v_pk_add_f32 v[6:7], v[6:7], v[6:7] op_sel_hi:[0,1]
	v_pk_add_f32 v[10:11], v[54:55], v[54:55] op_sel_hi:[0,1]
	v_pk_add_f32 v[36:37], v[48:49], v[48:49] op_sel_hi:[0,1]
	v_add_f32_e32 v5, 0, v4
	v_mov_b32_e32 v10, v58
	v_mov_b32_e32 v36, v59
	v_mov_b32_e32 v6, v8
	v_mov_b32_e32 v4, v9
	v_pk_add_f32 v[10:11], v[10:11], v[36:37]
	v_pk_add_f32 v[4:5], v[6:7], v[4:5]
	s_mov_b32 s0, 0xf800000
	v_pk_add_f32 v[4:5], v[10:11], v[4:5]
	s_nop 0
	v_add_f32_e32 v4, v4, v5
	ds_bpermute_b32 v5, v2, v4
	s_waitcnt lgkmcnt(0)
	v_add_f32_e32 v4, v4, v5
	ds_bpermute_b32 v5, v192, v4
	s_waitcnt lgkmcnt(0)
	v_add_f32_e32 v4, v4, v5
	ds_bpermute_b32 v5, v193, v4
	s_waitcnt lgkmcnt(0)
	v_add_f32_e32 v4, v4, v5
	ds_bpermute_b32 v5, v194, v4
	s_waitcnt lgkmcnt(0)
	v_add_f32_e32 v4, v4, v5
	ds_bpermute_b32 v5, v195, v4
	s_waitcnt lgkmcnt(0)
	v_add_f32_e32 v4, v4, v5
	ds_bpermute_b32 v5, v221, v4
	s_waitcnt lgkmcnt(0)
	v_add_f32_e32 v38, v4, v5
	v_fmamk_f32 v43, v38, 0xba800000, v43
	v_fmac_f32_e32 v42, 0xba800000, v38
	v_fmamk_f32 v47, v38, 0xba800000, v47
	v_fmac_f32_e32 v46, 0xba800000, v38
	v_pk_mul_f32 v[4:5], v[46:47], v[46:47]
	v_pk_mul_f32 v[6:7], v[42:43], v[42:43]
	v_fmamk_f32 v51, v38, 0xba800000, v51
	v_pk_mov_b32 v[10:11], v[6:7], v[4:5] op_sel:[1,0]
	v_mov_b32_e32 v7, v5
	v_pk_add_f32 v[4:5], v[10:11], v[6:7]
	v_fmac_f32_e32 v50, 0xba800000, v38
	v_fmamk_f32 v45, v38, 0xba800000, v45
	v_fmac_f32_e32 v44, 0xba800000, v38
	v_pk_add_f32 v[10:11], v[4:5], v[4:5] op_sel_hi:[0,1]
	v_pk_mul_f32 v[4:5], v[50:51], v[50:51]
	v_pk_mul_f32 v[6:7], v[44:45], v[44:45]
	v_fmac_f32_e32 v54, 0xba800000, v38
	v_pk_mov_b32 v[36:37], v[6:7], v[4:5] op_sel:[1,0]
	v_mov_b32_e32 v7, v5
	v_pk_add_f32 v[4:5], v[36:37], v[6:7]
	v_fmac_f32_e32 v48, 0xba800000, v38
	v_pk_add_f32 v[40:41], v[4:5], v[4:5] op_sel_hi:[0,1]
	v_fmamk_f32 v55, v38, 0xba800000, v55
	v_mul_f32_e32 v4, v54, v54
	v_fmamk_f32 v49, v38, 0xba800000, v49
	v_pk_fma_f32 v[52:53], v[54:55], v[54:55], v[4:5] op_sel_hi:[1,1,0]
	v_mul_f32_e32 v4, v48, v48
	v_pk_fma_f32 v[56:57], v[48:49], v[48:49], v[4:5] op_sel_hi:[1,1,0]
	v_fmamk_f32 v9, v38, 0xba800000, v9
	v_fmac_f32_e32 v8, 0xba800000, v38
	v_fmamk_f32 v59, v38, 0xba800000, v59
	v_fmac_f32_e32 v58, 0xba800000, v38
	global_load_dwordx4 v[4:7], v[28:29], off
	global_load_dwordx4 v[36:39], v[30:31], off
	v_mul_f32_e32 v52, v58, v58
	v_mul_f32_e32 v56, v59, v59
	v_mul_f32_e32 v10, v8, v8
	v_mul_f32_e32 v40, v9, v9
	v_pk_add_f32 v[52:53], v[52:53], v[56:57]
	v_pk_add_f32 v[10:11], v[10:11], v[40:41]
	s_nop 0
	v_pk_add_f32 v[10:11], v[52:53], v[10:11]
	s_nop 0
	v_add_f32_e32 v10, v10, v11
	ds_bpermute_b32 v11, v2, v10
	s_waitcnt lgkmcnt(0)
	v_add_f32_e32 v10, v10, v11
	ds_bpermute_b32 v11, v192, v10
	s_waitcnt lgkmcnt(0)
	v_add_f32_e32 v10, v10, v11
	ds_bpermute_b32 v11, v193, v10
	s_waitcnt lgkmcnt(0)
	v_add_f32_e32 v10, v10, v11
	ds_bpermute_b32 v11, v194, v10
	s_waitcnt lgkmcnt(0)
	v_add_f32_e32 v10, v10, v11
	ds_bpermute_b32 v11, v195, v10
	s_waitcnt lgkmcnt(0)
	v_add_f32_e32 v10, v10, v11
	ds_bpermute_b32 v11, v221, v10
	s_waitcnt lgkmcnt(0)
	v_add_f32_e32 v10, v10, v11
	v_fmamk_f32 v10, v10, 0x3a800000, v214
	v_mul_f32_e32 v11, 0x4f800000, v10
	v_cmp_gt_f32_e32 vcc, s0, v10
	s_nop 1
	v_cndmask_b32_e32 v10, v10, v11, vcc
	v_sqrt_f32_e32 v11, v10
	s_nop 0
	v_add_u32_e32 v40, -1, v11
	v_fma_f32 v41, -v40, v11, v10
	v_cmp_ge_f32_e64 s[34:35], 0, v41
	v_add_u32_e32 v41, 1, v11
	s_nop 0
	v_cndmask_b32_e64 v40, v11, v40, s[34:35]
	v_fma_f32 v11, -v41, v11, v10
	v_cmp_lt_f32_e64 s[34:35], 0, v11
	s_nop 1
	v_cndmask_b32_e64 v11, v40, v41, s[34:35]
	v_mul_f32_e32 v40, 0x37800000, v11
	v_cndmask_b32_e32 v11, v11, v40, vcc
	v_cmp_class_f32_e32 vcc, v10, v215
	s_nop 1
	v_cndmask_b32_e32 v10, v11, v10, vcc
	v_div_scale_f32 v11, s[0:1], v10, v10, 1.0
	v_rcp_f32_e32 v40, v11
	s_nop 0
	v_fma_f32 v41, -v11, v40, 1.0
	v_fmac_f32_e32 v40, v41, v40
	v_div_scale_f32 v41, vcc, 1.0, v10, 1.0
	v_mul_f32_e32 v52, v41, v40
	v_fma_f32 v53, -v11, v52, v41
	v_fmac_f32_e32 v52, v53, v40
	v_fma_f32 v11, -v11, v52, v41
	v_div_fmas_f32 v11, v11, v40, v52
	v_div_fixup_f32 v10, v11, v10, 1.0
	v_pk_mul_f32 v[40:41], v[42:43], v[10:11] op_sel_hi:[1,0]
	v_pk_mul_f32 v[42:43], v[46:47], v[10:11] op_sel_hi:[1,0]
	v_cndmask_b32_e64 v11, 0, 1, s[8:9]
	s_waitcnt vmcnt(0)
	v_pk_fma_f32 v[6:7], v[6:7], v[42:43], v[38:39]
	v_cmp_ne_u32_e64 s[36:37], 1, v11
	s_andn2_b64 vcc, exec, s[8:9]
	v_pk_fma_f32 v[4:5], v[4:5], v[40:41], v[36:37]
	s_cbranch_vccnz .LBB0_3200
	global_store_dwordx4 v[34:35], v[4:7], off offset:-3072 nt

.LBB0_3202:
	global_load_dwordx4 v[4:7], v[28:29], off offset:1024
	s_nop 0
	global_load_dwordx4 v[36:39], v[30:31], off offset:1024
	v_mov_b32_e32 v11, v10
	v_mov_b32_e32 v40, v10
	v_mov_b32_e32 v41, v10
	v_pk_mul_f32 v[40:41], v[50:51], v[40:41]
	v_pk_mul_f32 v[42:43], v[44:45], v[10:11]
	s_and_b64 vcc, exec, s[36:37]
	v_mov_b32_e32 v208, v220
	v_mov_b32_e32 v209, v222
	v_mov_b32_e32 v210, v223
	v_mov_b32_e32 v211, v224
	v_mov_b32_e32 v212, v225
	v_mov_b32_e32 v213, v226
	s_waitcnt vmcnt(0)
	v_pk_fma_f32 v[6:7], v[40:41], v[6:7], v[38:39]
	v_pk_fma_f32 v[4:5], v[42:43], v[4:5], v[36:37]
	s_cbranch_vccnz .LBB0_3204
	global_store_dwordx4 v[34:35], v[4:7], off offset:-2048 nt

.LBB0_3206:
	global_load_dwordx4 v[4:7], v[28:29], off offset:2048
	s_nop 0
	global_load_dwordx4 v[36:39], v[30:31], off offset:2048
	v_mov_b32_e32 v40, v10
	v_mov_b32_e32 v41, v10
	v_pk_mul_f32 v[42:43], v[54:55], v[10:11]
	v_pk_mul_f32 v[40:41], v[48:49], v[40:41]
	s_and_b64 vcc, exec, s[36:37]
	s_waitcnt vmcnt(0)
	v_pk_fma_f32 v[6:7], v[40:41], v[6:7], v[38:39]
	v_pk_fma_f32 v[4:5], v[42:43], v[4:5], v[36:37]
	s_cbranch_vccnz .LBB0_3208
	global_store_dwordx4 v[34:35], v[4:7], off offset:-1024 nt

.LBB0_3210:
	global_load_dwordx4 v[4:7], v[28:29], off offset:3072
	s_nop 0
	global_load_dwordx4 v[36:39], v[30:31], off offset:3072
	v_mov_b32_e32 v40, v10
	v_mov_b32_e32 v41, v10
	v_pk_mul_f32 v[10:11], v[58:59], v[10:11]
	v_pk_mul_f32 v[8:9], v[8:9], v[40:41]
	s_and_b64 vcc, exec, s[36:37]
	s_waitcnt vmcnt(0)
	v_pk_fma_f32 v[6:7], v[8:9], v[6:7], v[38:39]
	v_pk_fma_f32 v[4:5], v[10:11], v[4:5], v[36:37]
	s_cbranch_vccnz .LBB0_3212
	global_store_dwordx4 v[34:35], v[4:7], off nt
